# attention epilogues: lane^1 / lane^2 ds_swizzle exchanges replaced by DPP quad_perm moves (no LDS round trip)
# speedup vs baseline: 1.0072x; 1.0066x over previous
; #define SBAR() __builtin_amdgcn_sched_barrier(0)
; __device__ __forceinline__ int crow(int r, int hi) { return (r & 3) + 8 * (r >> 2) + 4 * hi; }
; #define FIN(PY0_, PY1_, alY_) do { if constexpr (F8) finishSM8(PY0_, PY1_, alY_, l_reg, pa8); else finishSM(PY0_, PY1_, alY_, l_reg, pa0, pa1, pa2, pa3); } while (0)
; #define PVT(VB_) do { if constexpr (F8) PV8(VB_); else pv_tile<VB_, false>(o, vb0, pa0, pa1, pa2, pa3, true); } while (0)
; #define PSM(P0_, P1_, mn_, al_) partialSM<F8 ? 8 : 0, F8 ? 2 : 8, F8 ? 5 : 0>(P0_, P1_, m_reg, mn_, al_, dead_)
; __device__ __forceinline__ void finishSM8(f32x16& p0, f32x16& p1, float alpha, float& l_reg, i32x8& pa) {
;     for (int r = 0; r < 16; ++r) p1[r] = __builtin_amdgcn_exp2f(p1[r]);
;     float ps;
;     { float s0 = p0[0] + p0[1], s1 = p0[2] + p0[3], s2 = p1[0] + p1[1], s3 = p1[2] + p1[3];
; #pragma unroll
;       for (int r = 4; r < 16; r += 4) { s0 += p0[r]; s0 += p0[r + 1]; s1 += p0[r + 2]; s1 += p0[r + 3]; s2 += p1[r]; s2 += p1[r + 1]; s3 += p1[r + 2]; s3 += p1[r + 3]; }
;       ps = (s0 + s1) + (s2 + s3); }
;     { auto rr = __builtin_amdgcn_permlane32_swap(__float_as_uint(ps), __float_as_uint(ps), false, false);
;       ps = __uint_as_float(rr[0]) + __uint_as_float(rr[1]); }
;     l_reg = l_reg * alpha + ps;
; #pragma unroll
;     for (int d = 0; d < 4; ++d) { int w0 = 0, w1 = 0;
;         w0 = __builtin_amdgcn_cvt_pk_fp8_f32(p0[4 * d], p0[4 * d + 1], w0, false); w0 = __builtin_amdgcn_cvt_pk_fp8_f32(p0[4 * d + 2], p0[4 * d + 3], w0, true);
;         w1 = __builtin_amdgcn_cvt_pk_fp8_f32(p1[4 * d], p1[4 * d + 1], w1, false); w1 = __builtin_amdgcn_cvt_pk_fp8_f32(p1[4 * d + 2], p1[4 * d + 3], w1, true);
;         pa[d] = w0; pa[4 + d] = w1; }
; }
; template <class Epi, bool F8 = false>
; __device__ __forceinline__ void block(const BlockRef& cur, int skv, char* lds, Seam& S, bool moba, unsigned selmask, const Epi& E) {
;     ...
;     FIN(pA0, pA1, alA); SBAR();
;     PVT(0);
;     if (even) { MASKT(pB0, pB1, NT - 1); PSM(pB0, pB1, mnB, alB); __syncthreads(); RESC(alB);
;         FIN(pB0, pB1, alB); SBAR(); PVT(1); }
;     SBAR();
;     if (hi == 0) li_l[r32] = l_reg; asm volatile("s_waitcnt lgkmcnt(0)" ::: "memory");
;     float rli[16];
; #pragma unroll
;     for (int r = 0; r < 16; ++r) rli[r] = __builtin_amdgcn_rcpf(li_l[crow(r, hi)]) * (F8 ? 1.0f / 16.0f : 1.0f);
.LBB0_1068:
	v_cndmask_b32_e64 v7, v7, v163, s[8:9]
	v_fmamk_f32 v7, v7, 0xba0293ee, v1
	v_cndmask_b32_e64 v7, v7, v210, s[6:7]
	v_fmamk_f32 v8, v98, 0x3a0293ee, v7
	v_fmamk_f32 v9, v99, 0x3a0293ee, v7
	v_fmamk_f32 v10, v100, 0x3a0293ee, v7
	v_fmamk_f32 v11, v101, 0x3a0293ee, v7
	v_fmamk_f32 v98, v82, 0x3a0293ee, v7
	v_fmamk_f32 v99, v83, 0x3a0293ee, v7
	v_fmamk_f32 v100, v84, 0x3a0293ee, v7
	v_fmamk_f32 v101, v85, 0x3a0293ee, v7
	v_fmamk_f32 v12, v102, 0x3a0293ee, v7
	v_fmamk_f32 v13, v103, 0x3a0293ee, v7
	v_fmamk_f32 v15, v104, 0x3a0293ee, v7
	v_fmamk_f32 v17, v105, 0x3a0293ee, v7
	v_fmamk_f32 v104, v106, 0x3a0293ee, v7
	v_fmamk_f32 v105, v107, 0x3a0293ee, v7
	v_fmamk_f32 v106, v108, 0x3a0293ee, v7
	v_fmamk_f32 v107, v109, 0x3a0293ee, v7
	v_fmamk_f32 v108, v110, 0x3a0293ee, v7
	v_fmamk_f32 v109, v111, 0x3a0293ee, v7
	v_fmamk_f32 v110, v112, 0x3a0293ee, v7
	v_fmamk_f32 v111, v113, 0x3a0293ee, v7
	v_fmamk_f32 v102, v86, 0x3a0293ee, v7
	v_fmamk_f32 v103, v87, 0x3a0293ee, v7
	v_fmamk_f32 v88, v88, 0x3a0293ee, v7
	v_fmamk_f32 v89, v89, 0x3a0293ee, v7
	v_fmamk_f32 v90, v90, 0x3a0293ee, v7
	v_fmamk_f32 v91, v91, 0x3a0293ee, v7
	v_fmamk_f32 v92, v92, 0x3a0293ee, v7
	v_fmamk_f32 v93, v93, 0x3a0293ee, v7
	v_fmamk_f32 v94, v94, 0x3a0293ee, v7
	v_exp_f32_e32 v86, v8
	v_exp_f32_e32 v87, v9
	v_exp_f32_e32 v14, v10
	v_exp_f32_e32 v16, v11
	v_fmamk_f32 v95, v95, 0x3a0293ee, v7
	v_fmamk_f32 v96, v96, 0x3a0293ee, v7
	v_fmac_f32_e32 v7, 0x3a0293ee, v97
	v_exp_f32_e32 v97, v98
	v_exp_f32_e32 v98, v99
	v_exp_f32_e32 v99, v100
	v_exp_f32_e32 v100, v101
	v_exp_f32_e32 v84, v12
	v_exp_f32_e32 v82, v15
	v_exp_f32_e32 v101, v102
	v_exp_f32_e32 v102, v103
	v_exp_f32_e32 v103, v88
	v_exp_f32_e32 v85, v13
	v_exp_f32_e32 v83, v17
	v_exp_f32_e32 v15, v104
	v_exp_f32_e32 v104, v89
	v_exp_f32_e32 v17, v105
	v_exp_f32_e32 v8, v106
	v_exp_f32_e32 v105, v90
	v_exp_f32_e32 v106, v92
	v_exp_f32_e32 v9, v107
	v_exp_f32_e32 v10, v110
	v_exp_f32_e32 v91, v91
	v_exp_f32_e32 v107, v93
	v_exp_f32_e32 v110, v7
	v_add_f32_e32 v7, v86, v87
	v_add_f32_e32 v88, v14, v16
	v_add_f32_e32 v89, v97, v98
	v_add_f32_e32 v90, v99, v100
	v_exp_f32_e32 v12, v108
	v_exp_f32_e32 v108, v94
	v_exp_f32_e32 v96, v96
	v_add_f32_e32 v7, v84, v7
	v_add_f32_e32 v88, v82, v88
	v_add_f32_e32 v89, v101, v89
	v_add_f32_e32 v90, v103, v90
	v_exp_f32_e32 v13, v109
	v_exp_f32_e32 v11, v111
	v_exp_f32_e32 v109, v95
	v_add_f32_e32 v7, v85, v7
	v_add_f32_e32 v88, v83, v88
	v_add_f32_e32 v89, v102, v89
	v_add_f32_e32 v90, v104, v90
	v_add_f32_e32 v7, v15, v7
	v_add_f32_e32 v88, v8, v88
	v_add_f32_e32 v89, v105, v89
	v_add_f32_e32 v90, v106, v90
	v_add_f32_e32 v7, v17, v7
	v_add_f32_e32 v88, v9, v88
	v_add_f32_e32 v89, v91, v89
	v_add_f32_e32 v90, v107, v90
	v_add_f32_e32 v7, v12, v7
	v_add_f32_e32 v88, v10, v88
	v_add_f32_e32 v89, v108, v89
	v_add_f32_e32 v90, v96, v90
	v_add_f32_e32 v7, v13, v7
	v_add_f32_e32 v88, v11, v88
	v_add_f32_e32 v89, v109, v89
	v_add_f32_e32 v90, v110, v90
	v_add_f32_e32 v7, v88, v7
	v_add_f32_e32 v88, v89, v90
	v_mov_b32_e32 v90, v3
	v_cvt_pk_fp8_f32 v90, v15, v17
	v_mov_b32_e32 v94, v3
	v_add_f32_e32 v7, v88, v7
	v_mov_b32_e32 v88, v3
	v_mov_b32_e32 v92, v3
	v_mov_b32_e32 v89, v3
	v_mov_b32_e32 v93, v3
	v_cvt_pk_fp8_f32 v94, v105, v91
	v_mov_b32_e32 v91, v3
	v_mov_b32_e32 v95, v3
	v_cvt_pk_fp8_f32 v88, v86, v87
	v_cvt_pk_fp8_f32 v92, v97, v98
	v_cvt_pk_fp8_f32 v89, v84, v85
	v_cvt_pk_fp8_f32 v93, v101, v102
	v_cvt_pk_fp8_f32 v91, v12, v13
	v_cvt_pk_fp8_f32 v95, v108, v109
	v_cvt_pk_fp8_f32 v90, v8, v9 op_sel:[0,0,1]
	v_mov_b32_e32 v8, v7
	s_nop 1
	v_permlane32_swap_b32_e32 v7, v8
	v_cvt_pk_fp8_f32 v88, v14, v16 op_sel:[0,0,1]
	v_cvt_pk_fp8_f32 v92, v99, v100 op_sel:[0,0,1]
	v_cvt_pk_fp8_f32 v89, v82, v83 op_sel:[0,0,1]
	v_cvt_pk_fp8_f32 v93, v103, v104 op_sel:[0,0,1]
	v_cvt_pk_fp8_f32 v94, v106, v107 op_sel:[0,0,1]
	v_cvt_pk_fp8_f32 v91, v10, v11 op_sel:[0,0,1]
	v_cvt_pk_fp8_f32 v95, v96, v110 op_sel:[0,0,1]
	ds_read_b128 v[10:13], v157 offset:16384
	ds_read_b128 v[96:99], v157 offset:18432
	ds_read_b128 v[14:17], v158 offset:16384
	ds_read_b128 v[100:103], v158 offset:18432
	s_waitcnt lgkmcnt(1)
	v_mfma_f32_32x32x64_f8f6f4 v[34:49], v[88:95], v[10:17], v[34:49]
	ds_read_b128 v[10:13], v157 offset:20480
	ds_read_b128 v[14:17], v158 offset:20480
	s_waitcnt lgkmcnt(2)
	v_mfma_f32_32x32x64_f8f6f4 v[50:65], v[88:95], v[96:103], v[50:65]
	ds_read_b128 v[96:99], v157 offset:22528
	ds_read_b128 v[100:103], v158 offset:22528
	s_waitcnt lgkmcnt(2)
	v_mfma_f32_32x32x64_f8f6f4 v[18:33], v[88:95], v[10:17], v[18:33]
	s_waitcnt lgkmcnt(0)
	v_mfma_f32_32x32x64_f8f6f4 v[66:81], v[88:95], v[96:103], v[66:81]
	s_nop 15
	s_nop 15
	s_and_saveexec_b64 s[6:7], s[4:5]
	v_add_f32_e32 v2, v2, v5
	v_fmac_f32_e32 v2, v156, v4
	v_add_f32_e32 v4, v7, v8
	v_fmac_f32_e32 v4, v2, v6
	ds_write_b32 v155, v4
	s_or_b64 exec, exec, s[6:7]
	s_waitcnt lgkmcnt(0)
	v_add_u32_e32 v2, s73, v154
	ds_read_b128 v[4:7], v2
	ds_read_b128 v[8:11], v2 offset:32
	s_brev_b32 s10, 60
	s_mov_b32 s53, 0x800000
	s_lshl_b32 s4, s29, 8
	s_waitcnt lgkmcnt(1)
	v_rcp_f32_e32 v4, v4
	s_and_b32 s4, s4, 0x3000
	s_or_b32 s4, s72, s4
	s_lshl_b32 s4, s4, 12
	v_mul_f32_e32 v88, 0x3d800000, v4
	v_rcp_f32_e32 v4, v5
	v_readlane_b32 s6, v252, 34
	v_readlane_b32 s7, v252, 35
	s_add_u32 s4, s6, s4
	v_mul_f32_e32 v92, 0x3d800000, v4
	v_rcp_f32_e32 v4, v6
	s_addc_u32 s5, s7, 0
	s_lshl_b32 s6, s29, 7
	s_and_b32 s6, s6, 0x780
	v_mul_f32_e32 v86, 0x3d800000, v4
	v_rcp_f32_e32 v4, v7
	v_readlane_b32 s12, v253, 30
	s_add_u32 s8, s4, s6
	v_readlane_b32 s13, v253, 31
	v_mul_f32_e32 v84, 0x3d800000, v4
	s_waitcnt lgkmcnt(0)
; __device__ __forceinline__ float half_sum(float s) {
;     s += swz_xor<1>(s); s += swz_xor<2>(s); s += swz_xor<4>(s); s += swz_xor<8>(s); s += swz_xor<16>(s); return s;
; }
;     __device__ __forceinline__ void operator()(f32x16 (&o)[4], const float (&rli)[16], int wid, int lane, int r32, int hi) const {
;     ...
;             for (int r = 0; r < 16; ++r) { float s = 0.f;
; #pragma unroll
;                 for (int d0 = 0; d0 < 4; ++d0) { const float v = o[d0][r] * rli[r]; o[d0][r] = v; s += v * v; }
;                 s = half_sum(s); rn[r] = rsqrtf(s * (1.0f / 128.0f) + 1e-5f); }
	v_rcp_f32_e32 v4, v8
	v_readlane_b32 s20, v253, 38
	v_readlane_b32 s21, v253, 39
	s_addc_u32 s9, s5, 0
	v_mul_f32_e32 v82, 0x3d800000, v4
	v_rcp_f32_e32 v4, v9
	s_lshl_b32 s4, s6, 2
	s_mov_b64 s[12:13], s[20:21]
	s_add_u32 s6, s12, s4
	v_mul_f32_e32 v106, 0x3d800000, v4
	v_rcp_f32_e32 v4, v10
	ds_read_b128 v[96:99], v2 offset:96
	s_addc_u32 s7, s13, 0
	s_ashr_i32 s89, s88, 31
	v_mul_f32_e32 v94, 0x3d800000, v4
	v_rcp_f32_e32 v4, v11
	s_lshl_b64 s[4:5], s[88:89], 12
	s_add_u32 s8, s8, s4
	s_addc_u32 s9, s9, s5
	v_mul_f32_e32 v90, 0x3d800000, v4
	ds_read_b128 v[4:7], v2 offset:64
	s_waitcnt lgkmcnt(1)
	v_rcp_f32_e32 v2, v96
	v_mov_b32_e32 v96, v34
	v_readlane_b32 s14, v253, 32
	s_waitcnt lgkmcnt(0)
	v_rcp_f32_e32 v4, v4
	v_mul_f32_e32 v8, 0x3d800000, v2
	v_rcp_f32_e32 v2, v97
	v_mov_b32_e32 v97, v50
	v_mul_f32_e32 v16, 0x3d800000, v4
	v_rcp_f32_e32 v4, v5
	v_mov_b32_e32 v50, v35
	v_pk_mul_f32 v[110:111], v[96:97], v[88:89] op_sel_hi:[1,0]
	v_mov_b32_e32 v96, v66
	v_mul_f32_e32 v14, 0x3d800000, v4
	v_rcp_f32_e32 v4, v6
	v_mul_f32_e32 v6, 0x3d800000, v2
	v_rcp_f32_e32 v2, v98
	v_mov_b32_e32 v97, v18
	v_mul_f32_e32 v12, 0x3d800000, v4
	v_rcp_f32_e32 v4, v7
	v_mov_b32_e32 v18, v67
	v_pk_mul_f32 v[100:101], v[110:111], v[110:111]
	v_pk_mul_f32 v[104:105], v[96:97], v[88:89] op_sel_hi:[1,0]
	v_mul_f32_e32 v10, 0x3d800000, v4
	v_mul_f32_e32 v4, 0x3d800000, v2
	v_rcp_f32_e32 v2, v99
	v_pk_mul_f32 v[98:99], v[50:51], v[92:93] op_sel_hi:[1,0]
	v_pk_mul_f32 v[96:97], v[18:19], v[92:93] op_sel_hi:[1,0]
	v_pk_mul_f32 v[34:35], v[98:99], v[98:99]
	v_pk_mul_f32 v[88:89], v[104:105], v[104:105]
	v_pk_mul_f32 v[18:19], v[96:97], v[96:97]
	v_mov_b32_e32 v50, v34
	v_mov_b32_e32 v51, v100
	v_mov_b32_e32 v100, v35
	v_pk_add_f32 v[34:35], v[50:51], v[100:101]
	v_mov_b32_e32 v50, v19
	v_mov_b32_e32 v51, v89
	v_pk_add_f32 v[34:35], v[50:51], v[34:35]
	v_mov_b32_e32 v19, v88
	v_pk_add_f32 v[18:19], v[18:19], v[34:35]
	s_nop 1
	v_mov_b32_dpp v35, v19 quad_perm:[1,0,3,2] row_mask:0xf bank_mask:0xf
	s_nop 1
	v_mov_b32_dpp v34, v18 quad_perm:[1,0,3,2] row_mask:0xf bank_mask:0xf
	v_mul_f32_e32 v2, 0x3d800000, v2
	v_ashrrev_i32_e32 v131, 31, v130
	v_readlane_b32 s15, v253, 33
	v_readlane_b32 s16, v253, 34
	s_waitcnt lgkmcnt(0)
	v_pk_add_f32 v[18:19], v[18:19], v[34:35]
	s_nop 1
	v_mov_b32_dpp v35, v19 quad_perm:[2,3,0,1] row_mask:0xf bank_mask:0xf
	s_nop 1
	v_mov_b32_dpp v34, v18 quad_perm:[2,3,0,1] row_mask:0xf bank_mask:0xf
	v_readlane_b32 s17, v253, 35
	v_readlane_b32 s18, v253, 36
	v_readlane_b32 s19, v253, 37
	v_readlane_b32 s22, v253, 40
	s_waitcnt lgkmcnt(0)
	v_pk_add_f32 v[18:19], v[18:19], v[34:35]
	ds_swizzle_b32 v35, v19 offset:swizzle(SWAP,4)
	ds_swizzle_b32 v34, v18 offset:swizzle(SWAP,4)
	v_readlane_b32 s23, v253, 41
	v_readlane_b32 s24, v253, 42
	v_readlane_b32 s25, v253, 43
	v_readlane_b32 s26, v253, 44
	s_waitcnt lgkmcnt(0)
	v_pk_add_f32 v[18:19], v[18:19], v[34:35]
	ds_swizzle_b32 v35, v19 offset:swizzle(SWAP,8)
	ds_swizzle_b32 v34, v18 offset:swizzle(SWAP,8)
	v_readlane_b32 s27, v253, 45
	s_waitcnt lgkmcnt(0)
	v_pk_add_f32 v[18:19], v[18:19], v[34:35]
	ds_swizzle_b32 v35, v19 offset:swizzle(SWAP,16)
	ds_swizzle_b32 v34, v18 offset:swizzle(SWAP,16)
	s_waitcnt lgkmcnt(0)
	v_pk_add_f32 v[18:19], v[18:19], v[34:35]
	s_nop 0
	v_pk_fma_f32 v[116:117], v[18:19], s[10:11], v[198:199] op_sel_hi:[1,0,0]
	v_mov_b32_e32 v18, v36
	v_mov_b32_e32 v19, v52
	v_mov_b32_e32 v52, v37
	v_pk_mul_f32 v[102:103], v[18:19], v[86:87] op_sel_hi:[1,0]
	v_mov_b32_e32 v34, v68
	v_mov_b32_e32 v35, v20
	v_pk_mul_f32 v[92:93], v[52:53], v[84:85] op_sel_hi:[1,0]
	v_mov_b32_e32 v20, v69
	v_pk_mul_f32 v[18:19], v[102:103], v[102:103]
	v_pk_mul_f32 v[100:101], v[34:35], v[86:87] op_sel_hi:[1,0]
	v_pk_mul_f32 v[36:37], v[92:93], v[92:93]
	v_pk_mul_f32 v[86:87], v[20:21], v[84:85] op_sel_hi:[1,0]
	v_pk_mul_f32 v[34:35], v[100:101], v[100:101]
	v_pk_mul_f32 v[20:21], v[86:87], v[86:87]
	v_mov_b32_e32 v50, v36
	v_mov_b32_e32 v51, v18
	v_mov_b32_e32 v18, v37
	v_pk_add_f32 v[18:19], v[50:51], v[18:19]
	v_mov_b32_e32 v36, v21
	v_mov_b32_e32 v37, v35
	v_pk_add_f32 v[18:19], v[36:37], v[18:19]
	v_mov_b32_e32 v21, v34
	v_pk_add_f32 v[18:19], v[20:21], v[18:19]
	s_nop 1
	v_mov_b32_dpp v21, v19 quad_perm:[1,0,3,2] row_mask:0xf bank_mask:0xf
	s_nop 1
	v_mov_b32_dpp v20, v18 quad_perm:[1,0,3,2] row_mask:0xf bank_mask:0xf
	v_mul_f32_e32 v5, 0x4b800000, v117
	v_cmp_gt_f32_e32 vcc, s53, v117
	v_cmp_gt_f32_e64 s[4:5], s53, v116
	s_waitcnt lgkmcnt(0)
	v_pk_add_f32 v[18:19], v[18:19], v[20:21]
	s_nop 1
	v_mov_b32_dpp v21, v19 quad_perm:[2,3,0,1] row_mask:0xf bank_mask:0xf
	s_nop 1
	v_mov_b32_dpp v20, v18 quad_perm:[2,3,0,1] row_mask:0xf bank_mask:0xf
	v_cndmask_b32_e32 v5, v117, v5, vcc
	v_rsq_f32_e32 v5, v5
	s_waitcnt lgkmcnt(0)
	v_pk_add_f32 v[18:19], v[18:19], v[20:21]
	ds_swizzle_b32 v21, v19 offset:swizzle(SWAP,4)
	ds_swizzle_b32 v20, v18 offset:swizzle(SWAP,4)
	v_mul_f32_e32 v7, 0x45800000, v5
	v_cndmask_b32_e32 v117, v5, v7, vcc
	s_waitcnt lgkmcnt(0)
	v_pk_add_f32 v[18:19], v[18:19], v[20:21]
	ds_swizzle_b32 v21, v19 offset:swizzle(SWAP,8)
	ds_swizzle_b32 v20, v18 offset:swizzle(SWAP,8)
	s_waitcnt lgkmcnt(0)
; __device__ __forceinline__ float half_sum(float s) {
;     s += swz_xor<1>(s); s += swz_xor<2>(s); s += swz_xor<4>(s); s += swz_xor<8>(s); s += swz_xor<16>(s); return s;
; }
;     __device__ __forceinline__ void operator()(f32x16 (&o)[4], const float (&rli)[16], int wid, int lane, int r32, int hi) const {
;     ...
;             for (int r = 0; r < 16; ++r) { float s = 0.f;
; #pragma unroll
;                 for (int d0 = 0; d0 < 4; ++d0) { const float v = o[d0][r] * rli[r]; o[d0][r] = v; s += v * v; }
;                 s = half_sum(s); rn[r] = rsqrtf(s * (1.0f / 128.0f) + 1e-5f); }
	v_pk_add_f32 v[112:113], v[18:19], v[20:21]
	v_mov_b32_e32 v18, v38
	v_mov_b32_e32 v19, v54
	v_mov_b32_e32 v20, v70
	v_mov_b32_e32 v21, v22
	v_mov_b32_e32 v54, v39
	v_pk_mul_f32 v[88:89], v[18:19], v[82:83] op_sel_hi:[1,0]
	v_pk_mul_f32 v[84:85], v[20:21], v[82:83] op_sel_hi:[1,0]
	v_pk_mul_f32 v[82:83], v[54:55], v[106:107] op_sel_hi:[1,0]
	v_mov_b32_e32 v22, v71
	v_pk_mul_f32 v[18:19], v[88:89], v[88:89]
	v_pk_mul_f32 v[34:35], v[82:83], v[82:83]
	v_pk_mul_f32 v[66:67], v[22:23], v[106:107] op_sel_hi:[1,0]
	v_pk_mul_f32 v[20:21], v[84:85], v[84:85]
	v_pk_mul_f32 v[22:23], v[66:67], v[66:67]
	v_mov_b32_e32 v36, v34
	v_mov_b32_e32 v37, v18
	v_mov_b32_e32 v18, v35
	v_pk_add_f32 v[18:19], v[36:37], v[18:19]
	v_mov_b32_e32 v34, v23
	v_mov_b32_e32 v35, v21
	v_pk_add_f32 v[18:19], v[34:35], v[18:19]
	v_mov_b32_e32 v23, v20
	v_pk_add_f32 v[18:19], v[22:23], v[18:19]
	s_nop 1
	v_mov_b32_dpp v21, v19 quad_perm:[1,0,3,2] row_mask:0xf bank_mask:0xf
	s_nop 1
	v_mov_b32_dpp v20, v18 quad_perm:[1,0,3,2] row_mask:0xf bank_mask:0xf
	ds_swizzle_b32 v115, v113 offset:swizzle(SWAP,16)
	ds_swizzle_b32 v114, v112 offset:swizzle(SWAP,16)
	s_waitcnt lgkmcnt(0)
	v_pk_add_f32 v[18:19], v[18:19], v[20:21]
	s_nop 1
	v_mov_b32_dpp v21, v19 quad_perm:[2,3,0,1] row_mask:0xf bank_mask:0xf
	s_nop 1
	v_mov_b32_dpp v20, v18 quad_perm:[2,3,0,1] row_mask:0xf bank_mask:0xf
	s_waitcnt lgkmcnt(0)
	v_pk_add_f32 v[18:19], v[18:19], v[20:21]
	ds_swizzle_b32 v21, v19 offset:swizzle(SWAP,4)
	ds_swizzle_b32 v20, v18 offset:swizzle(SWAP,4)
	s_waitcnt lgkmcnt(0)
	v_pk_add_f32 v[18:19], v[18:19], v[20:21]
	ds_swizzle_b32 v21, v19 offset:swizzle(SWAP,8)
	ds_swizzle_b32 v20, v18 offset:swizzle(SWAP,8)
	s_waitcnt lgkmcnt(0)
	v_pk_add_f32 v[106:107], v[18:19], v[20:21]
	v_mov_b32_e32 v18, v40
	v_mov_b32_e32 v19, v56
	v_mov_b32_e32 v56, v41
	v_pk_mul_f32 v[70:71], v[18:19], v[94:95] op_sel_hi:[1,0]
	v_mov_b32_e32 v20, v72
	v_mov_b32_e32 v21, v24
	v_pk_mul_f32 v[54:55], v[56:57], v[90:91] op_sel_hi:[1,0]
	v_mov_b32_e32 v24, v73
	v_pk_mul_f32 v[18:19], v[70:71], v[70:71]
	v_pk_mul_f32 v[68:69], v[20:21], v[94:95] op_sel_hi:[1,0]
	v_pk_mul_f32 v[22:23], v[54:55], v[54:55]
	v_pk_mul_f32 v[50:51], v[24:25], v[90:91] op_sel_hi:[1,0]
	v_pk_mul_f32 v[20:21], v[68:69], v[68:69]
	v_pk_mul_f32 v[24:25], v[50:51], v[50:51]
	v_mov_b32_e32 v34, v22
	v_mov_b32_e32 v35, v18
	v_mov_b32_e32 v18, v23
	v_pk_add_f32 v[18:19], v[34:35], v[18:19]
	v_mov_b32_e32 v22, v25
	v_mov_b32_e32 v23, v21
	v_pk_add_f32 v[18:19], v[22:23], v[18:19]
	v_mov_b32_e32 v25, v20
	v_pk_add_f32 v[18:19], v[24:25], v[18:19]
	s_nop 1
	v_mov_b32_dpp v21, v19 quad_perm:[1,0,3,2] row_mask:0xf bank_mask:0xf
	s_nop 1
	v_mov_b32_dpp v20, v18 quad_perm:[1,0,3,2] row_mask:0xf bank_mask:0xf
	ds_swizzle_b32 v109, v107 offset:swizzle(SWAP,16)
	ds_swizzle_b32 v108, v106 offset:swizzle(SWAP,16)
	s_waitcnt lgkmcnt(0)
	v_pk_add_f32 v[18:19], v[18:19], v[20:21]
	s_nop 1
	v_mov_b32_dpp v21, v19 quad_perm:[2,3,0,1] row_mask:0xf bank_mask:0xf
	s_nop 1
	v_mov_b32_dpp v20, v18 quad_perm:[2,3,0,1] row_mask:0xf bank_mask:0xf
	s_waitcnt lgkmcnt(0)
	v_pk_add_f32 v[18:19], v[18:19], v[20:21]
	ds_swizzle_b32 v21, v19 offset:swizzle(SWAP,4)
	ds_swizzle_b32 v20, v18 offset:swizzle(SWAP,4)
	s_waitcnt lgkmcnt(0)
	v_pk_add_f32 v[18:19], v[18:19], v[20:21]
	ds_swizzle_b32 v21, v19 offset:swizzle(SWAP,8)
	ds_swizzle_b32 v20, v18 offset:swizzle(SWAP,8)
	s_waitcnt lgkmcnt(0)
	v_pk_add_f32 v[90:91], v[18:19], v[20:21]
	v_mov_b32_e32 v18, v42
	v_mov_b32_e32 v19, v58
	v_mov_b32_e32 v58, v43
	v_pk_mul_f32 v[56:57], v[18:19], v[16:17] op_sel_hi:[1,0]
	v_mov_b32_e32 v20, v74
	v_mov_b32_e32 v21, v26
	v_pk_mul_f32 v[38:39], v[58:59], v[14:15] op_sel_hi:[1,0]
	v_mov_b32_e32 v26, v75
	v_pk_mul_f32 v[18:19], v[56:57], v[56:57]
	v_pk_mul_f32 v[52:53], v[20:21], v[16:17] op_sel_hi:[1,0]
	v_pk_mul_f32 v[20:21], v[38:39], v[38:39]
	v_pk_mul_f32 v[34:35], v[26:27], v[14:15] op_sel_hi:[1,0]
	v_pk_mul_f32 v[16:17], v[52:53], v[52:53]
	v_pk_mul_f32 v[14:15], v[34:35], v[34:35]
	v_mov_b32_e32 v22, v20
	v_mov_b32_e32 v23, v18
	v_mov_b32_e32 v18, v21
	v_pk_add_f32 v[18:19], v[22:23], v[18:19]
	v_mov_b32_e32 v20, v15
	v_mov_b32_e32 v21, v17
	v_pk_add_f32 v[18:19], v[20:21], v[18:19]
	v_mov_b32_e32 v15, v16
	v_pk_add_f32 v[14:15], v[14:15], v[18:19]
	s_nop 1
	v_mov_b32_dpp v17, v15 quad_perm:[1,0,3,2] row_mask:0xf bank_mask:0xf
	s_nop 1
	v_mov_b32_dpp v16, v14 quad_perm:[1,0,3,2] row_mask:0xf bank_mask:0xf
	ds_swizzle_b32 v95, v91 offset:swizzle(SWAP,16)
	ds_swizzle_b32 v94, v90 offset:swizzle(SWAP,16)
	s_waitcnt lgkmcnt(0)
	v_pk_add_f32 v[14:15], v[14:15], v[16:17]
	s_nop 1
	v_mov_b32_dpp v17, v15 quad_perm:[2,3,0,1] row_mask:0xf bank_mask:0xf
	s_nop 1
	v_mov_b32_dpp v16, v14 quad_perm:[2,3,0,1] row_mask:0xf bank_mask:0xf
	s_waitcnt lgkmcnt(0)
	v_pk_add_f32 v[14:15], v[14:15], v[16:17]
	ds_swizzle_b32 v17, v15 offset:swizzle(SWAP,4)
	ds_swizzle_b32 v16, v14 offset:swizzle(SWAP,4)
	s_waitcnt lgkmcnt(0)
	v_pk_add_f32 v[14:15], v[14:15], v[16:17]
	ds_swizzle_b32 v17, v15 offset:swizzle(SWAP,8)
	ds_swizzle_b32 v16, v14 offset:swizzle(SWAP,8)
	s_waitcnt lgkmcnt(0)
; __device__ __forceinline__ int crow(int r, int hi) { return (r & 3) + 8 * (r >> 2) + 4 * hi; }
; __device__ __forceinline__ void store_quad8(unsigned char* p, float v, int r32) {
;     v = fminf(fmaxf(v, -448.f), 448.f);
;     const float v1 = swz_xor<1>(v);
;     const int w = __builtin_amdgcn_cvt_pk_fp8_f32(v, v1, 0, false);
;     const int w2 = __builtin_amdgcn_ds_swizzle(w, (2 << 10) | 0x1f);
;     if ((r32 & 3) == 0) *(unsigned*)p = ((unsigned)w & 0xffffu) | ((unsigned)w2 << 16);
; }
;     __device__ __forceinline__ void operator()(f32x16 (&o)[4], const float (&rli)[16], int wid, int lane, int r32, int hi) const {
;     ...
;             for (int r = 0; r < 16; ++r) { float s = 0.f;
; #pragma unroll
;                 for (int d0 = 0; d0 < 4; ++d0) { const float v = o[d0][r] * rli[r]; o[d0][r] = v; s += v * v; }
;                 s = half_sum(s); rn[r] = rsqrtf(s * (1.0f / 128.0f) + 1e-5f); }
;             float g[4];
; #pragma unroll
;             for (int d0 = 0; d0 < 4; ++d0) g[d0] = gain[d0 * 32 + r32];
; #pragma unroll
;             for (int r = 0; r < 16; ++r)
; #pragma unroll
;                 for (int d0 = 0; d0 < 4; ++d0) store_quad8(base + (size_t)crow(r, hi) * 4096 + d0 * 32 + r32, o[d0][r] * rn[r] * g[d0], r32);
	v_pk_add_f32 v[72:73], v[14:15], v[16:17]
	v_mov_b32_e32 v14, v44
	v_mov_b32_e32 v15, v60
	v_mov_b32_e32 v60, v45
	v_pk_mul_f32 v[40:41], v[14:15], v[12:13] op_sel_hi:[1,0]
	v_mov_b32_e32 v16, v76
	v_mov_b32_e32 v17, v28
	v_pk_mul_f32 v[24:25], v[60:61], v[10:11] op_sel_hi:[1,0]
	v_mov_b32_e32 v28, v77
	v_pk_mul_f32 v[14:15], v[40:41], v[40:41]
	v_pk_mul_f32 v[36:37], v[16:17], v[12:13] op_sel_hi:[1,0]
	v_pk_mul_f32 v[16:17], v[24:25], v[24:25]
	v_pk_mul_f32 v[20:21], v[28:29], v[10:11] op_sel_hi:[1,0]
	v_pk_mul_f32 v[12:13], v[36:37], v[36:37]
	v_pk_mul_f32 v[10:11], v[20:21], v[20:21]
	v_mov_b32_e32 v18, v16
	v_mov_b32_e32 v19, v14
	v_mov_b32_e32 v14, v17
	v_pk_add_f32 v[14:15], v[18:19], v[14:15]
	v_mov_b32_e32 v16, v11
	v_mov_b32_e32 v17, v13
	v_pk_add_f32 v[14:15], v[16:17], v[14:15]
	v_mov_b32_e32 v11, v12
	v_pk_add_f32 v[10:11], v[10:11], v[14:15]
	s_nop 1
	v_mov_b32_dpp v13, v11 quad_perm:[1,0,3,2] row_mask:0xf bank_mask:0xf
	s_nop 1
	v_mov_b32_dpp v12, v10 quad_perm:[1,0,3,2] row_mask:0xf bank_mask:0xf
	ds_swizzle_b32 v75, v73 offset:swizzle(SWAP,16)
	ds_swizzle_b32 v74, v72 offset:swizzle(SWAP,16)
	s_waitcnt lgkmcnt(0)
	v_pk_add_f32 v[10:11], v[10:11], v[12:13]
	s_nop 1
	v_mov_b32_dpp v13, v11 quad_perm:[2,3,0,1] row_mask:0xf bank_mask:0xf
	s_nop 1
	v_mov_b32_dpp v12, v10 quad_perm:[2,3,0,1] row_mask:0xf bank_mask:0xf
	s_waitcnt lgkmcnt(0)
	v_pk_add_f32 v[10:11], v[10:11], v[12:13]
	ds_swizzle_b32 v13, v11 offset:swizzle(SWAP,4)
	ds_swizzle_b32 v12, v10 offset:swizzle(SWAP,4)
	s_waitcnt lgkmcnt(0)
	v_pk_add_f32 v[10:11], v[10:11], v[12:13]
	ds_swizzle_b32 v13, v11 offset:swizzle(SWAP,8)
	ds_swizzle_b32 v12, v10 offset:swizzle(SWAP,8)
	s_waitcnt lgkmcnt(0)
	v_pk_add_f32 v[44:45], v[10:11], v[12:13]
	v_mov_b32_e32 v10, v46
	v_mov_b32_e32 v11, v62
	v_mov_b32_e32 v62, v47
	v_pk_mul_f32 v[26:27], v[10:11], v[8:9] op_sel_hi:[1,0]
	v_mov_b32_e32 v12, v78
	v_mov_b32_e32 v13, v30
	v_pk_mul_f32 v[14:15], v[62:63], v[6:7] op_sel_hi:[1,0]
	v_mov_b32_e32 v30, v79
	v_pk_mul_f32 v[10:11], v[26:27], v[26:27]
	v_pk_mul_f32 v[22:23], v[12:13], v[8:9] op_sel_hi:[1,0]
	v_pk_mul_f32 v[16:17], v[14:15], v[14:15]
	v_pk_mul_f32 v[12:13], v[30:31], v[6:7] op_sel_hi:[1,0]
	v_pk_mul_f32 v[8:9], v[22:23], v[22:23]
	v_pk_mul_f32 v[6:7], v[12:13], v[12:13]
	v_mov_b32_e32 v18, v16
	v_mov_b32_e32 v19, v10
	v_mov_b32_e32 v10, v17
	v_pk_add_f32 v[10:11], v[18:19], v[10:11]
	v_mov_b32_e32 v16, v7
	v_mov_b32_e32 v17, v9
	v_pk_add_f32 v[10:11], v[16:17], v[10:11]
	v_mov_b32_e32 v7, v8
	v_pk_add_f32 v[6:7], v[6:7], v[10:11]
	s_nop 1
	v_mov_b32_dpp v9, v7 quad_perm:[1,0,3,2] row_mask:0xf bank_mask:0xf
	s_nop 1
	v_mov_b32_dpp v8, v6 quad_perm:[1,0,3,2] row_mask:0xf bank_mask:0xf
	ds_swizzle_b32 v59, v45 offset:swizzle(SWAP,16)
	ds_swizzle_b32 v58, v44 offset:swizzle(SWAP,16)
	s_waitcnt lgkmcnt(0)
	v_pk_add_f32 v[6:7], v[6:7], v[8:9]
	s_nop 1
	v_mov_b32_dpp v9, v7 quad_perm:[2,3,0,1] row_mask:0xf bank_mask:0xf
	s_nop 1
	v_mov_b32_dpp v8, v6 quad_perm:[2,3,0,1] row_mask:0xf bank_mask:0xf
	s_waitcnt lgkmcnt(0)
	v_pk_add_f32 v[6:7], v[6:7], v[8:9]
	ds_swizzle_b32 v9, v7 offset:swizzle(SWAP,4)
	ds_swizzle_b32 v8, v6 offset:swizzle(SWAP,4)
	s_waitcnt lgkmcnt(0)
	v_pk_add_f32 v[6:7], v[6:7], v[8:9]
	ds_swizzle_b32 v9, v7 offset:swizzle(SWAP,8)
	ds_swizzle_b32 v8, v6 offset:swizzle(SWAP,8)
	s_waitcnt lgkmcnt(0)
	v_pk_add_f32 v[28:29], v[6:7], v[8:9]
	v_mov_b32_e32 v6, v48
	v_mov_b32_e32 v7, v64
	v_pk_mul_f32 v[10:11], v[6:7], v[4:5] op_sel_hi:[1,0]
	v_mov_b32_e32 v6, v80
	v_mov_b32_e32 v7, v32
	v_mov_b32_e32 v64, v49
	v_pk_mul_f32 v[8:9], v[6:7], v[4:5] op_sel_hi:[1,0]
	v_pk_mul_f32 v[6:7], v[64:65], v[2:3] op_sel_hi:[1,0]
	v_mov_b32_e32 v32, v81
	v_pk_mul_f32 v[16:17], v[10:11], v[10:11]
	v_pk_mul_f32 v[42:43], v[6:7], v[6:7]
	v_pk_mul_f32 v[4:5], v[32:33], v[2:3] op_sel_hi:[1,0]
	v_pk_mul_f32 v[18:19], v[8:9], v[8:9]
	v_pk_mul_f32 v[32:33], v[4:5], v[4:5]
	v_mov_b32_e32 v46, v42
	v_mov_b32_e32 v47, v16
	v_mov_b32_e32 v16, v43
	v_pk_add_f32 v[16:17], v[46:47], v[16:17]
	v_mov_b32_e32 v42, v33
	v_mov_b32_e32 v43, v19
	v_pk_add_f32 v[16:17], v[42:43], v[16:17]
	v_mov_b32_e32 v33, v18
	v_pk_add_f32 v[16:17], v[32:33], v[16:17]
	v_lshl_add_u64 v[32:33], v[130:131], 2, s[6:7]
	global_load_dword v60, v[32:33], off
	global_load_dword v62, v[32:33], off offset:128
	global_load_dword v61, v[32:33], off offset:256
	global_load_dword v2, v[32:33], off offset:384
	s_nop 1
	v_mov_b32_dpp v19, v17 quad_perm:[1,0,3,2] row_mask:0xf bank_mask:0xf
	s_nop 1
	v_mov_b32_dpp v18, v16 quad_perm:[1,0,3,2] row_mask:0xf bank_mask:0xf
	v_lshlrev_b32_e32 v42, 2, v152
	v_ashrrev_i32_e32 v43, 31, v42
	v_lshlrev_b64 v[46:47], 12, v[42:43]
	v_mul_f32_e32 v43, v110, v117
	s_waitcnt lgkmcnt(0)
	v_pk_add_f32 v[16:17], v[16:17], v[18:19]
	s_nop 1
	v_mov_b32_dpp v19, v17 quad_perm:[2,3,0,1] row_mask:0xf bank_mask:0xf
	s_nop 1
	v_mov_b32_dpp v18, v16 quad_perm:[2,3,0,1] row_mask:0xf bank_mask:0xf
	ds_swizzle_b32 v31, v29 offset:swizzle(SWAP,16)
	ds_swizzle_b32 v30, v28 offset:swizzle(SWAP,16)
	v_and_b32_e32 v32, 3, v130
	v_cmp_eq_u32_e32 vcc, 0, v32
	s_waitcnt lgkmcnt(0)
	v_pk_add_f32 v[16:17], v[16:17], v[18:19]
	ds_swizzle_b32 v19, v17 offset:swizzle(SWAP,4)
	ds_swizzle_b32 v18, v16 offset:swizzle(SWAP,4)
	v_lshl_add_u64 v[32:33], s[8:9], 0, v[130:131]
	v_lshl_add_u64 v[46:47], v[32:33], 0, v[46:47]
	s_waitcnt lgkmcnt(0)
	v_pk_add_f32 v[16:17], v[16:17], v[18:19]
	ds_swizzle_b32 v19, v17 offset:swizzle(SWAP,8)
	ds_swizzle_b32 v18, v16 offset:swizzle(SWAP,8)
	s_waitcnt lgkmcnt(0)
	v_pk_add_f32 v[16:17], v[16:17], v[18:19]
	ds_swizzle_b32 v19, v17 offset:swizzle(SWAP,16)
	ds_swizzle_b32 v18, v16 offset:swizzle(SWAP,16)
	s_waitcnt vmcnt(3)
	v_mul_f32_e32 v43, v43, v60
	v_max_f32_e32 v43, 0xc3e00000, v43
	v_min_f32_e32 v48, 0x43e00000, v43
	s_nop 1
	v_mov_b32_dpp v49, v48 quad_perm:[1,0,3,2] row_mask:0xf bank_mask:0xf
	v_mov_b32_e32 v43, v3
	s_waitcnt lgkmcnt(0)
	v_cvt_pk_fp8_f32 v43, v48, v49
	s_nop 1
	v_mov_b32_dpp v48, v43 quad_perm:[2,3,0,1] row_mask:0xf bank_mask:0xf
	s_and_saveexec_b64 s[6:7], vcc
	s_cbranch_execz .LBB0_1072
	v_and_b32_e32 v43, 0xffff, v43
	s_waitcnt lgkmcnt(0)
	v_lshl_or_b32 v43, v48, 16, v43
	global_store_dword v[46:47], v43, off
; __device__ __forceinline__ int crow(int r, int hi) { return (r & 3) + 8 * (r >> 2) + 4 * hi; }
; __device__ __forceinline__ void store_quad8(unsigned char* p, float v, int r32) {
;     v = fminf(fmaxf(v, -448.f), 448.f);
;     const float v1 = swz_xor<1>(v);
;     const int w = __builtin_amdgcn_cvt_pk_fp8_f32(v, v1, 0, false);
;     const int w2 = __builtin_amdgcn_ds_swizzle(w, (2 << 10) | 0x1f);
;     if ((r32 & 3) == 0) *(unsigned*)p = ((unsigned)w & 0xffffu) | ((unsigned)w2 << 16);
; }
;     __device__ __forceinline__ void operator()(f32x16 (&o)[4], const float (&rli)[16], int wid, int lane, int r32, int hi) const {
;     ...
;             for (int r = 0; r < 16; ++r)
; #pragma unroll
;                 for (int d0 = 0; d0 < 4; ++d0) store_quad8(base + (size_t)crow(r, hi) * 4096 + d0 * 32 + r32, o[d0][r] * rn[r] * g[d0], r32);
.LBB0_1072:
	s_or_b64 exec, exec, s[6:7]
	v_mul_f32_e32 v43, v111, v117
	s_waitcnt vmcnt(2)
	v_mul_f32_e32 v43, v43, v62
	v_max_f32_e32 v43, 0xc3e00000, v43
	s_waitcnt lgkmcnt(0)
	v_min_f32_e32 v48, 0x43e00000, v43
	s_nop 1
	v_mov_b32_dpp v49, v48 quad_perm:[1,0,3,2] row_mask:0xf bank_mask:0xf
	v_mov_b32_e32 v43, v3
	s_waitcnt lgkmcnt(0)
	v_cvt_pk_fp8_f32 v43, v48, v49
	s_nop 1
	v_mov_b32_dpp v48, v43 quad_perm:[2,3,0,1] row_mask:0xf bank_mask:0xf
	s_and_saveexec_b64 s[6:7], vcc
	s_cbranch_execz .LBB0_1074
	v_and_b32_e32 v43, 0xffff, v43
	s_waitcnt lgkmcnt(0)
	v_lshl_or_b32 v43, v48, 16, v43
	global_store_dword v[46:47], v43, off offset:32
.LBB0_1074:
	s_or_b64 exec, exec, s[6:7]
	v_mul_f32_e32 v43, v105, v117
	s_waitcnt vmcnt(1)
	v_mul_f32_e32 v43, v43, v61
	v_max_f32_e32 v43, 0xc3e00000, v43
	s_waitcnt lgkmcnt(0)
	v_min_f32_e32 v48, 0x43e00000, v43
	s_nop 1
	v_mov_b32_dpp v49, v48 quad_perm:[1,0,3,2] row_mask:0xf bank_mask:0xf
	v_mov_b32_e32 v43, v3
	s_waitcnt lgkmcnt(0)
	v_cvt_pk_fp8_f32 v43, v48, v49
	s_nop 1
	v_mov_b32_dpp v48, v43 quad_perm:[2,3,0,1] row_mask:0xf bank_mask:0xf
	s_and_saveexec_b64 s[6:7], vcc
	v_readlane_b32 s88, v252, 34
	v_readlane_b32 s89, v252, 35
	s_cbranch_execz .LBB0_1076
	v_and_b32_e32 v43, 0xffff, v43
	s_waitcnt lgkmcnt(0)
	v_lshl_or_b32 v43, v48, 16, v43
	global_store_dword v[46:47], v43, off offset:64
.LBB0_1076:
	s_or_b64 exec, exec, s[6:7]
	v_mul_f32_e32 v43, v104, v117
	s_waitcnt vmcnt(0)
	v_mul_f32_e32 v43, v43, v2
	v_max_f32_e32 v43, 0xc3e00000, v43
	s_waitcnt lgkmcnt(0)
	v_min_f32_e32 v48, 0x43e00000, v43
	s_nop 1
	v_mov_b32_dpp v49, v48 quad_perm:[1,0,3,2] row_mask:0xf bank_mask:0xf
	v_mov_b32_e32 v43, v3
	s_waitcnt lgkmcnt(0)
	v_cvt_pk_fp8_f32 v43, v48, v49
	s_nop 1
	v_mov_b32_dpp v48, v43 quad_perm:[2,3,0,1] row_mask:0xf bank_mask:0xf
	s_and_saveexec_b64 s[6:7], vcc
	s_cbranch_execz .LBB0_1078
	v_and_b32_e32 v43, 0xffff, v43
	s_waitcnt lgkmcnt(0)
	v_lshl_or_b32 v43, v48, 16, v43
	global_store_dword v[46:47], v43, off offset:96
.LBB0_1078:
	s_or_b64 exec, exec, s[6:7]
	v_mul_f32_e32 v43, 0x4b800000, v116
	v_cndmask_b32_e64 v43, v116, v43, s[4:5]
	v_rsq_f32_e32 v43, v43
	s_nop 0
	v_mul_f32_e32 v46, 0x45800000, v43
	v_cndmask_b32_e64 v43, v43, v46, s[4:5]
	s_waitcnt lgkmcnt(0)
	v_mul_f32_e32 v48, v98, v43
	v_mul_f32_e32 v48, v48, v60
	v_max_f32_e32 v48, 0xc3e00000, v48
	v_min_f32_e32 v49, 0x43e00000, v48
	s_nop 1
	v_mov_b32_dpp v63, v49 quad_perm:[1,0,3,2] row_mask:0xf bank_mask:0xf
	v_mov_b32_e32 v48, v3
	v_or_b32_e32 v46, 1, v42
	v_ashrrev_i32_e32 v47, 31, v46
	v_lshlrev_b64 v[46:47], 12, v[46:47]
	s_waitcnt lgkmcnt(0)
	v_cvt_pk_fp8_f32 v48, v49, v63
	v_lshl_add_u64 v[46:47], v[32:33], 0, v[46:47]
	s_nop 1
	v_mov_b32_dpp v49, v48 quad_perm:[2,3,0,1] row_mask:0xf bank_mask:0xf
	s_and_saveexec_b64 s[4:5], vcc
	s_cbranch_execz .LBB0_1080
	v_and_b32_e32 v48, 0xffff, v48
	s_waitcnt lgkmcnt(0)
	v_lshl_or_b32 v48, v49, 16, v48
	global_store_dword v[46:47], v48, off
.LBB0_1080:
	s_or_b64 exec, exec, s[4:5]
	v_mul_f32_e32 v48, v99, v43
	v_mul_f32_e32 v48, v48, v62
	v_max_f32_e32 v48, 0xc3e00000, v48
	s_waitcnt lgkmcnt(0)
	v_min_f32_e32 v49, 0x43e00000, v48
	s_nop 1
	v_mov_b32_dpp v63, v49 quad_perm:[1,0,3,2] row_mask:0xf bank_mask:0xf
	v_mov_b32_e32 v48, v3
	s_waitcnt lgkmcnt(0)
	v_cvt_pk_fp8_f32 v48, v49, v63
	s_nop 1
	v_mov_b32_dpp v49, v48 quad_perm:[2,3,0,1] row_mask:0xf bank_mask:0xf
	s_and_saveexec_b64 s[4:5], vcc
	s_cbranch_execz .LBB0_1082
	v_and_b32_e32 v48, 0xffff, v48
	s_waitcnt lgkmcnt(0)
	v_lshl_or_b32 v48, v49, 16, v48
	global_store_dword v[46:47], v48, off offset:32
.LBB0_1082:
	s_or_b64 exec, exec, s[4:5]
	v_mul_f32_e32 v48, v97, v43
	v_mul_f32_e32 v48, v48, v61
	v_max_f32_e32 v48, 0xc3e00000, v48
	s_waitcnt lgkmcnt(0)
	v_min_f32_e32 v49, 0x43e00000, v48
	s_nop 1
	v_mov_b32_dpp v63, v49 quad_perm:[1,0,3,2] row_mask:0xf bank_mask:0xf
	v_mov_b32_e32 v48, v3
	s_waitcnt lgkmcnt(0)
	v_cvt_pk_fp8_f32 v48, v49, v63
	s_nop 1
	v_mov_b32_dpp v49, v48 quad_perm:[2,3,0,1] row_mask:0xf bank_mask:0xf
	s_and_saveexec_b64 s[4:5], vcc
	s_cbranch_execz .LBB0_1084
	v_and_b32_e32 v48, 0xffff, v48
	s_waitcnt lgkmcnt(0)
	v_lshl_or_b32 v48, v49, 16, v48
	global_store_dword v[46:47], v48, off offset:64
.LBB0_1084:
	s_or_b64 exec, exec, s[4:5]
	v_mul_f32_e32 v43, v96, v43
	v_mul_f32_e32 v43, v43, v2
	v_max_f32_e32 v43, 0xc3e00000, v43
	v_min_f32_e32 v48, 0x43e00000, v43
	s_waitcnt lgkmcnt(0)
	s_nop 1
	v_mov_b32_dpp v49, v48 quad_perm:[1,0,3,2] row_mask:0xf bank_mask:0xf
	v_mov_b32_e32 v43, v3
	s_waitcnt lgkmcnt(0)
	v_cvt_pk_fp8_f32 v43, v48, v49
	s_nop 1
	v_mov_b32_dpp v48, v43 quad_perm:[2,3,0,1] row_mask:0xf bank_mask:0xf
	s_and_saveexec_b64 s[4:5], vcc
	s_cbranch_execz .LBB0_1086
	v_and_b32_e32 v43, 0xffff, v43
	s_waitcnt lgkmcnt(0)
	v_lshl_or_b32 v43, v48, 16, v43
	global_store_dword v[46:47], v43, off offset:96
.LBB0_1086:
	s_or_b64 exec, exec, s[4:5]
	v_pk_add_f32 v[46:47], v[112:113], v[114:115]
	s_nop 0
	v_pk_fma_f32 v[46:47], v[46:47], s[10:11], v[198:199] op_sel_hi:[1,0,0]
	s_nop 0
	v_mul_f32_e32 v43, 0x4b800000, v47
	v_cmp_gt_f32_e64 s[4:5], s53, v47
	s_nop 1
	v_cndmask_b32_e64 v43, v47, v43, s[4:5]
	v_rsq_f32_e32 v43, v43
	s_nop 0
	v_mul_f32_e32 v47, 0x45800000, v43
	v_cndmask_b32_e64 v43, v43, v47, s[4:5]
	v_mul_f32_e32 v47, v102, v43
	v_mul_f32_e32 v47, v47, v60
	v_max_f32_e32 v47, 0xc3e00000, v47
	s_waitcnt lgkmcnt(0)
	v_min_f32_e32 v48, 0x43e00000, v47
	s_nop 1
	v_mov_b32_dpp v49, v48 quad_perm:[1,0,3,2] row_mask:0xf bank_mask:0xf
	v_mov_b32_e32 v47, v3
	v_cmp_gt_f32_e64 s[4:5], s53, v46
	s_waitcnt lgkmcnt(0)
	v_cvt_pk_fp8_f32 v47, v48, v49
	v_or_b32_e32 v48, 2, v42
	v_ashrrev_i32_e32 v49, 31, v48
	v_lshlrev_b64 v[48:49], 12, v[48:49]
	s_nop 1
	v_mov_b32_dpp v63, v47 quad_perm:[2,3,0,1] row_mask:0xf bank_mask:0xf
	v_lshl_add_u64 v[48:49], v[32:33], 0, v[48:49]
	s_and_saveexec_b64 s[6:7], vcc
	s_cbranch_execz .LBB0_1088
	v_and_b32_e32 v47, 0xffff, v47
	s_waitcnt lgkmcnt(0)
	v_lshl_or_b32 v47, v63, 16, v47
	global_store_dword v[48:49], v47, off
; __device__ __forceinline__ int crow(int r, int hi) { return (r & 3) + 8 * (r >> 2) + 4 * hi; }
; __device__ __forceinline__ void store_quad8(unsigned char* p, float v, int r32) {
;     v = fminf(fmaxf(v, -448.f), 448.f);
;     const float v1 = swz_xor<1>(v);
;     const int w = __builtin_amdgcn_cvt_pk_fp8_f32(v, v1, 0, false);
;     const int w2 = __builtin_amdgcn_ds_swizzle(w, (2 << 10) | 0x1f);
;     if ((r32 & 3) == 0) *(unsigned*)p = ((unsigned)w & 0xffffu) | ((unsigned)w2 << 16);
; }
;     __device__ __forceinline__ void operator()(f32x16 (&o)[4], const float (&rli)[16], int wid, int lane, int r32, int hi) const {
;     ...
;             for (int r = 0; r < 16; ++r)
; #pragma unroll
;                 for (int d0 = 0; d0 < 4; ++d0) store_quad8(base + (size_t)crow(r, hi) * 4096 + d0 * 32 + r32, o[d0][r] * rn[r] * g[d0], r32);
.LBB0_1088:
	s_or_b64 exec, exec, s[6:7]
	v_mul_f32_e32 v47, v103, v43
	v_mul_f32_e32 v47, v47, v62
	v_max_f32_e32 v47, 0xc3e00000, v47
	s_waitcnt lgkmcnt(0)
	v_min_f32_e32 v63, 0x43e00000, v47
	s_nop 1
	v_mov_b32_dpp v64, v63 quad_perm:[1,0,3,2] row_mask:0xf bank_mask:0xf
	v_mov_b32_e32 v47, v3
	s_waitcnt lgkmcnt(0)
	v_cvt_pk_fp8_f32 v47, v63, v64
	s_nop 1
	v_mov_b32_dpp v63, v47 quad_perm:[2,3,0,1] row_mask:0xf bank_mask:0xf
	s_and_saveexec_b64 s[6:7], vcc
	s_cbranch_execz .LBB0_1090
	v_and_b32_e32 v47, 0xffff, v47
	s_waitcnt lgkmcnt(0)
	v_lshl_or_b32 v47, v63, 16, v47
	global_store_dword v[48:49], v47, off offset:32
.LBB0_1090:
	s_or_b64 exec, exec, s[6:7]
	v_mul_f32_e32 v47, v101, v43
	v_mul_f32_e32 v47, v47, v61
	v_max_f32_e32 v47, 0xc3e00000, v47
	s_waitcnt lgkmcnt(0)
	v_min_f32_e32 v63, 0x43e00000, v47
	s_nop 1
	v_mov_b32_dpp v64, v63 quad_perm:[1,0,3,2] row_mask:0xf bank_mask:0xf
	v_mov_b32_e32 v47, v3
	s_waitcnt lgkmcnt(0)
	v_cvt_pk_fp8_f32 v47, v63, v64
	s_nop 1
	v_mov_b32_dpp v63, v47 quad_perm:[2,3,0,1] row_mask:0xf bank_mask:0xf
	s_and_saveexec_b64 s[6:7], vcc
	s_cbranch_execz .LBB0_1092
	v_and_b32_e32 v47, 0xffff, v47
	s_waitcnt lgkmcnt(0)
	v_lshl_or_b32 v47, v63, 16, v47
	global_store_dword v[48:49], v47, off offset:64
.LBB0_1092:
	s_or_b64 exec, exec, s[6:7]
	v_mul_f32_e32 v43, v100, v43
	v_mul_f32_e32 v43, v43, v2
	v_max_f32_e32 v43, 0xc3e00000, v43
	v_min_f32_e32 v47, 0x43e00000, v43
	s_waitcnt lgkmcnt(0)
	s_nop 1
	v_mov_b32_dpp v63, v47 quad_perm:[1,0,3,2] row_mask:0xf bank_mask:0xf
	v_mov_b32_e32 v43, v3
	s_waitcnt lgkmcnt(0)
	v_cvt_pk_fp8_f32 v43, v47, v63
	s_nop 1
	v_mov_b32_dpp v47, v43 quad_perm:[2,3,0,1] row_mask:0xf bank_mask:0xf
	s_and_saveexec_b64 s[6:7], vcc
	s_cbranch_execz .LBB0_1094
	v_and_b32_e32 v43, 0xffff, v43
	s_waitcnt lgkmcnt(0)
	v_lshl_or_b32 v43, v47, 16, v43
	global_store_dword v[48:49], v43, off offset:96
.LBB0_1094:
	s_or_b64 exec, exec, s[6:7]
	v_mul_f32_e32 v43, 0x4b800000, v46
	v_cndmask_b32_e64 v43, v46, v43, s[4:5]
	v_rsq_f32_e32 v43, v43
	s_nop 0
	v_mul_f32_e32 v46, 0x45800000, v43
	v_cndmask_b32_e64 v43, v43, v46, s[4:5]
	v_mul_f32_e32 v48, v92, v43
	v_mul_f32_e32 v48, v48, v60
	v_max_f32_e32 v48, 0xc3e00000, v48
	v_min_f32_e32 v49, 0x43e00000, v48
	s_nop 1
	v_mov_b32_dpp v63, v49 quad_perm:[1,0,3,2] row_mask:0xf bank_mask:0xf
	v_mov_b32_e32 v48, v3
	v_or_b32_e32 v46, 3, v42
	s_waitcnt lgkmcnt(0)
	v_ashrrev_i32_e32 v47, 31, v46
	v_lshlrev_b64 v[46:47], 12, v[46:47]
	s_waitcnt lgkmcnt(0)
	v_cvt_pk_fp8_f32 v48, v49, v63
	v_lshl_add_u64 v[46:47], v[32:33], 0, v[46:47]
	s_nop 1
	v_mov_b32_dpp v49, v48 quad_perm:[2,3,0,1] row_mask:0xf bank_mask:0xf
	s_and_saveexec_b64 s[4:5], vcc
	s_cbranch_execz .LBB0_1096
	v_and_b32_e32 v48, 0xffff, v48
	s_waitcnt lgkmcnt(0)
	v_lshl_or_b32 v48, v49, 16, v48
	global_store_dword v[46:47], v48, off
.LBB0_1096:
	s_or_b64 exec, exec, s[4:5]
	v_mul_f32_e32 v48, v93, v43
	v_mul_f32_e32 v48, v48, v62
	v_max_f32_e32 v48, 0xc3e00000, v48
	s_waitcnt lgkmcnt(0)
	v_min_f32_e32 v49, 0x43e00000, v48
	s_nop 1
	v_mov_b32_dpp v63, v49 quad_perm:[1,0,3,2] row_mask:0xf bank_mask:0xf
	v_mov_b32_e32 v48, v3
	s_waitcnt lgkmcnt(0)
	v_cvt_pk_fp8_f32 v48, v49, v63
	s_nop 1
	v_mov_b32_dpp v49, v48 quad_perm:[2,3,0,1] row_mask:0xf bank_mask:0xf
	s_and_saveexec_b64 s[4:5], vcc
	s_cbranch_execz .LBB0_1098
	v_and_b32_e32 v48, 0xffff, v48
	s_waitcnt lgkmcnt(0)
	v_lshl_or_b32 v48, v49, 16, v48
	global_store_dword v[46:47], v48, off offset:32
.LBB0_1098:
	s_or_b64 exec, exec, s[4:5]
	v_mul_f32_e32 v48, v87, v43
	v_mul_f32_e32 v48, v48, v61
	v_max_f32_e32 v48, 0xc3e00000, v48
	s_waitcnt lgkmcnt(0)
	v_min_f32_e32 v49, 0x43e00000, v48
	s_nop 1
	v_mov_b32_dpp v63, v49 quad_perm:[1,0,3,2] row_mask:0xf bank_mask:0xf
	v_mov_b32_e32 v48, v3
	s_waitcnt lgkmcnt(0)
	v_cvt_pk_fp8_f32 v48, v49, v63
	s_nop 1
	v_mov_b32_dpp v49, v48 quad_perm:[2,3,0,1] row_mask:0xf bank_mask:0xf
	s_and_saveexec_b64 s[4:5], vcc
	s_cbranch_execz .LBB0_1100
	v_and_b32_e32 v48, 0xffff, v48
	s_waitcnt lgkmcnt(0)
	v_lshl_or_b32 v48, v49, 16, v48
	global_store_dword v[46:47], v48, off offset:64
.LBB0_1100:
	s_or_b64 exec, exec, s[4:5]
	v_mul_f32_e32 v43, v86, v43
	v_mul_f32_e32 v43, v43, v2
	v_max_f32_e32 v43, 0xc3e00000, v43
	v_min_f32_e32 v48, 0x43e00000, v43
	s_waitcnt lgkmcnt(0)
	s_nop 1
	v_mov_b32_dpp v49, v48 quad_perm:[1,0,3,2] row_mask:0xf bank_mask:0xf
	v_mov_b32_e32 v43, v3
	s_waitcnt lgkmcnt(0)
	v_cvt_pk_fp8_f32 v43, v48, v49
	s_nop 1
	v_mov_b32_dpp v48, v43 quad_perm:[2,3,0,1] row_mask:0xf bank_mask:0xf
	s_and_saveexec_b64 s[4:5], vcc
	s_cbranch_execz .LBB0_1102
	v_and_b32_e32 v43, 0xffff, v43
	s_waitcnt lgkmcnt(0)
	v_lshl_or_b32 v43, v48, 16, v43
	global_store_dword v[46:47], v43, off offset:96
.LBB0_1102:
	s_or_b64 exec, exec, s[4:5]
	v_pk_add_f32 v[46:47], v[106:107], v[108:109]
	s_nop 0
	v_pk_fma_f32 v[46:47], v[46:47], s[10:11], v[198:199] op_sel_hi:[1,0,0]
	s_nop 0
	v_mul_f32_e32 v43, 0x4b800000, v47
	v_cmp_gt_f32_e64 s[4:5], s53, v47
	s_nop 1
	v_cndmask_b32_e64 v43, v47, v43, s[4:5]
	v_rsq_f32_e32 v43, v43
	s_nop 0
	v_mul_f32_e32 v47, 0x45800000, v43
	v_cndmask_b32_e64 v43, v43, v47, s[4:5]
	v_mul_f32_e32 v47, v88, v43
	v_mul_f32_e32 v47, v47, v60
	v_max_f32_e32 v47, 0xc3e00000, v47
	s_waitcnt lgkmcnt(0)
	v_min_f32_e32 v48, 0x43e00000, v47
	s_nop 1
	v_mov_b32_dpp v49, v48 quad_perm:[1,0,3,2] row_mask:0xf bank_mask:0xf
	v_mov_b32_e32 v47, v3
	v_cmp_gt_f32_e64 s[4:5], s53, v46
	s_waitcnt lgkmcnt(0)
	v_cvt_pk_fp8_f32 v47, v48, v49
	v_add_u32_e32 v48, 8, v42
	v_ashrrev_i32_e32 v49, 31, v48
	v_lshlrev_b64 v[48:49], 12, v[48:49]
	s_nop 1
	v_mov_b32_dpp v63, v47 quad_perm:[2,3,0,1] row_mask:0xf bank_mask:0xf
	v_lshl_add_u64 v[48:49], v[32:33], 0, v[48:49]
	s_and_saveexec_b64 s[6:7], vcc
	s_cbranch_execz .LBB0_1104
	v_and_b32_e32 v47, 0xffff, v47
	s_waitcnt lgkmcnt(0)
	v_lshl_or_b32 v47, v63, 16, v47
	global_store_dword v[48:49], v47, off
; __device__ __forceinline__ int crow(int r, int hi) { return (r & 3) + 8 * (r >> 2) + 4 * hi; }
; __device__ __forceinline__ void store_quad8(unsigned char* p, float v, int r32) {
;     v = fminf(fmaxf(v, -448.f), 448.f);
;     const float v1 = swz_xor<1>(v);
;     const int w = __builtin_amdgcn_cvt_pk_fp8_f32(v, v1, 0, false);
;     const int w2 = __builtin_amdgcn_ds_swizzle(w, (2 << 10) | 0x1f);
;     if ((r32 & 3) == 0) *(unsigned*)p = ((unsigned)w & 0xffffu) | ((unsigned)w2 << 16);
; }
;     __device__ __forceinline__ void operator()(f32x16 (&o)[4], const float (&rli)[16], int wid, int lane, int r32, int hi) const {
;     ...
;             for (int r = 0; r < 16; ++r)
; #pragma unroll
;                 for (int d0 = 0; d0 < 4; ++d0) store_quad8(base + (size_t)crow(r, hi) * 4096 + d0 * 32 + r32, o[d0][r] * rn[r] * g[d0], r32);
.LBB0_1104:
	s_or_b64 exec, exec, s[6:7]
	v_mul_f32_e32 v47, v89, v43
	v_mul_f32_e32 v47, v47, v62
	v_max_f32_e32 v47, 0xc3e00000, v47
	s_waitcnt lgkmcnt(0)
	v_min_f32_e32 v63, 0x43e00000, v47
	s_nop 1
	v_mov_b32_dpp v64, v63 quad_perm:[1,0,3,2] row_mask:0xf bank_mask:0xf
	v_mov_b32_e32 v47, v3
	s_waitcnt lgkmcnt(0)
	v_cvt_pk_fp8_f32 v47, v63, v64
	s_nop 1
	v_mov_b32_dpp v63, v47 quad_perm:[2,3,0,1] row_mask:0xf bank_mask:0xf
	s_and_saveexec_b64 s[6:7], vcc
	s_cbranch_execz .LBB0_1106
	v_and_b32_e32 v47, 0xffff, v47
	s_waitcnt lgkmcnt(0)
	v_lshl_or_b32 v47, v63, 16, v47
	global_store_dword v[48:49], v47, off offset:32
.LBB0_1106:
	s_or_b64 exec, exec, s[6:7]
	v_mul_f32_e32 v47, v85, v43
	v_mul_f32_e32 v47, v47, v61
	v_max_f32_e32 v47, 0xc3e00000, v47
	s_waitcnt lgkmcnt(0)
	v_min_f32_e32 v63, 0x43e00000, v47
	s_nop 1
	v_mov_b32_dpp v64, v63 quad_perm:[1,0,3,2] row_mask:0xf bank_mask:0xf
	v_mov_b32_e32 v47, v3
	s_waitcnt lgkmcnt(0)
	v_cvt_pk_fp8_f32 v47, v63, v64
	s_nop 1
	v_mov_b32_dpp v63, v47 quad_perm:[2,3,0,1] row_mask:0xf bank_mask:0xf
	s_and_saveexec_b64 s[6:7], vcc
	s_cbranch_execz .LBB0_1108
	v_and_b32_e32 v47, 0xffff, v47
	s_waitcnt lgkmcnt(0)
	v_lshl_or_b32 v47, v63, 16, v47
	global_store_dword v[48:49], v47, off offset:64
.LBB0_1108:
	s_or_b64 exec, exec, s[6:7]
	v_mul_f32_e32 v43, v84, v43
	v_mul_f32_e32 v43, v43, v2
	v_max_f32_e32 v43, 0xc3e00000, v43
	v_min_f32_e32 v47, 0x43e00000, v43
	s_waitcnt lgkmcnt(0)
	s_nop 1
	v_mov_b32_dpp v63, v47 quad_perm:[1,0,3,2] row_mask:0xf bank_mask:0xf
	v_mov_b32_e32 v43, v3
	s_waitcnt lgkmcnt(0)
	v_cvt_pk_fp8_f32 v43, v47, v63
	s_nop 1
	v_mov_b32_dpp v47, v43 quad_perm:[2,3,0,1] row_mask:0xf bank_mask:0xf
	s_and_saveexec_b64 s[6:7], vcc
	s_cbranch_execz .LBB0_1110
	v_and_b32_e32 v43, 0xffff, v43
	s_waitcnt lgkmcnt(0)
	v_lshl_or_b32 v43, v47, 16, v43
	global_store_dword v[48:49], v43, off offset:96
.LBB0_1110:
	s_or_b64 exec, exec, s[6:7]
	v_mul_f32_e32 v43, 0x4b800000, v46
	v_cndmask_b32_e64 v43, v46, v43, s[4:5]
	v_rsq_f32_e32 v43, v43
	s_nop 0
	v_mul_f32_e32 v46, 0x45800000, v43
	v_cndmask_b32_e64 v43, v43, v46, s[4:5]
	v_mul_f32_e32 v48, v82, v43
	v_mul_f32_e32 v48, v48, v60
	v_max_f32_e32 v48, 0xc3e00000, v48
	v_min_f32_e32 v49, 0x43e00000, v48
	s_nop 1
	v_mov_b32_dpp v63, v49 quad_perm:[1,0,3,2] row_mask:0xf bank_mask:0xf
	v_mov_b32_e32 v48, v3
	v_add_u32_e32 v46, 9, v42
	s_waitcnt lgkmcnt(0)
	v_ashrrev_i32_e32 v47, 31, v46
	v_lshlrev_b64 v[46:47], 12, v[46:47]
	s_waitcnt lgkmcnt(0)
	v_cvt_pk_fp8_f32 v48, v49, v63
	v_lshl_add_u64 v[46:47], v[32:33], 0, v[46:47]
	s_nop 1
	v_mov_b32_dpp v49, v48 quad_perm:[2,3,0,1] row_mask:0xf bank_mask:0xf
	s_and_saveexec_b64 s[4:5], vcc
	s_cbranch_execz .LBB0_1112
	v_and_b32_e32 v48, 0xffff, v48
	s_waitcnt lgkmcnt(0)
	v_lshl_or_b32 v48, v49, 16, v48
	global_store_dword v[46:47], v48, off
.LBB0_1112:
	s_or_b64 exec, exec, s[4:5]
	v_mul_f32_e32 v48, v83, v43
	v_mul_f32_e32 v48, v48, v62
	v_max_f32_e32 v48, 0xc3e00000, v48
	s_waitcnt lgkmcnt(0)
	v_min_f32_e32 v49, 0x43e00000, v48
	s_nop 1
	v_mov_b32_dpp v63, v49 quad_perm:[1,0,3,2] row_mask:0xf bank_mask:0xf
	v_mov_b32_e32 v48, v3
	s_waitcnt lgkmcnt(0)
	v_cvt_pk_fp8_f32 v48, v49, v63
	s_nop 1
	v_mov_b32_dpp v49, v48 quad_perm:[2,3,0,1] row_mask:0xf bank_mask:0xf
	s_and_saveexec_b64 s[4:5], vcc
	s_cbranch_execz .LBB0_1114
	v_and_b32_e32 v48, 0xffff, v48
	s_waitcnt lgkmcnt(0)
	v_lshl_or_b32 v48, v49, 16, v48
	global_store_dword v[46:47], v48, off offset:32
.LBB0_1114:
	s_or_b64 exec, exec, s[4:5]
	v_mul_f32_e32 v48, v67, v43
	v_mul_f32_e32 v48, v48, v61
	v_max_f32_e32 v48, 0xc3e00000, v48
	s_waitcnt lgkmcnt(0)
	v_min_f32_e32 v49, 0x43e00000, v48
	s_nop 1
	v_mov_b32_dpp v63, v49 quad_perm:[1,0,3,2] row_mask:0xf bank_mask:0xf
	v_mov_b32_e32 v48, v3
	s_waitcnt lgkmcnt(0)
	v_cvt_pk_fp8_f32 v48, v49, v63
	s_nop 1
	v_mov_b32_dpp v49, v48 quad_perm:[2,3,0,1] row_mask:0xf bank_mask:0xf
	s_and_saveexec_b64 s[4:5], vcc
	s_cbranch_execz .LBB0_1116
	v_and_b32_e32 v48, 0xffff, v48
	s_waitcnt lgkmcnt(0)
	v_lshl_or_b32 v48, v49, 16, v48
	global_store_dword v[46:47], v48, off offset:64
.LBB0_1116:
	s_or_b64 exec, exec, s[4:5]
	v_mul_f32_e32 v43, v66, v43
	v_mul_f32_e32 v43, v43, v2
	v_max_f32_e32 v43, 0xc3e00000, v43
	v_min_f32_e32 v48, 0x43e00000, v43
	s_waitcnt lgkmcnt(0)
	s_nop 1
	v_mov_b32_dpp v49, v48 quad_perm:[1,0,3,2] row_mask:0xf bank_mask:0xf
	v_mov_b32_e32 v43, v3
	s_waitcnt lgkmcnt(0)
	v_cvt_pk_fp8_f32 v43, v48, v49
	s_nop 1
	v_mov_b32_dpp v48, v43 quad_perm:[2,3,0,1] row_mask:0xf bank_mask:0xf
	s_and_saveexec_b64 s[4:5], vcc
	s_cbranch_execz .LBB0_1118
	v_and_b32_e32 v43, 0xffff, v43
	s_waitcnt lgkmcnt(0)
	v_lshl_or_b32 v43, v48, 16, v43
	global_store_dword v[46:47], v43, off offset:96
.LBB0_1118:
	s_or_b64 exec, exec, s[4:5]
	v_pk_add_f32 v[46:47], v[90:91], v[94:95]
	s_nop 0
	v_pk_fma_f32 v[46:47], v[46:47], s[10:11], v[198:199] op_sel_hi:[1,0,0]
	s_nop 0
	v_mul_f32_e32 v43, 0x4b800000, v47
	v_cmp_gt_f32_e64 s[4:5], s53, v47
	s_nop 1
	v_cndmask_b32_e64 v43, v47, v43, s[4:5]
	v_rsq_f32_e32 v43, v43
	s_nop 0
	v_mul_f32_e32 v47, 0x45800000, v43
	v_cndmask_b32_e64 v43, v43, v47, s[4:5]
	v_mul_f32_e32 v47, v70, v43
	v_mul_f32_e32 v47, v47, v60
	v_max_f32_e32 v47, 0xc3e00000, v47
	s_waitcnt lgkmcnt(0)
	v_min_f32_e32 v48, 0x43e00000, v47
	s_nop 1
	v_mov_b32_dpp v49, v48 quad_perm:[1,0,3,2] row_mask:0xf bank_mask:0xf
	v_mov_b32_e32 v47, v3
	v_cmp_gt_f32_e64 s[4:5], s53, v46
	s_waitcnt lgkmcnt(0)
	v_cvt_pk_fp8_f32 v47, v48, v49
	v_add_u32_e32 v48, 10, v42
	v_ashrrev_i32_e32 v49, 31, v48
	v_lshlrev_b64 v[48:49], 12, v[48:49]
	s_nop 1
	v_mov_b32_dpp v63, v47 quad_perm:[2,3,0,1] row_mask:0xf bank_mask:0xf
	v_lshl_add_u64 v[48:49], v[32:33], 0, v[48:49]
	s_and_saveexec_b64 s[6:7], vcc
	s_cbranch_execz .LBB0_1120
	v_and_b32_e32 v47, 0xffff, v47
	s_waitcnt lgkmcnt(0)
	v_lshl_or_b32 v47, v63, 16, v47
	global_store_dword v[48:49], v47, off
; __device__ __forceinline__ int crow(int r, int hi) { return (r & 3) + 8 * (r >> 2) + 4 * hi; }
; __device__ __forceinline__ void store_quad8(unsigned char* p, float v, int r32) {
;     v = fminf(fmaxf(v, -448.f), 448.f);
;     const float v1 = swz_xor<1>(v);
;     const int w = __builtin_amdgcn_cvt_pk_fp8_f32(v, v1, 0, false);
;     const int w2 = __builtin_amdgcn_ds_swizzle(w, (2 << 10) | 0x1f);
;     if ((r32 & 3) == 0) *(unsigned*)p = ((unsigned)w & 0xffffu) | ((unsigned)w2 << 16);
; }
;     __device__ __forceinline__ void operator()(f32x16 (&o)[4], const float (&rli)[16], int wid, int lane, int r32, int hi) const {
;     ...
;             for (int r = 0; r < 16; ++r)
; #pragma unroll
;                 for (int d0 = 0; d0 < 4; ++d0) store_quad8(base + (size_t)crow(r, hi) * 4096 + d0 * 32 + r32, o[d0][r] * rn[r] * g[d0], r32);
.LBB0_1120:
	s_or_b64 exec, exec, s[6:7]
	v_mul_f32_e32 v47, v71, v43
	v_mul_f32_e32 v47, v47, v62
	v_max_f32_e32 v47, 0xc3e00000, v47
	s_waitcnt lgkmcnt(0)
	v_min_f32_e32 v63, 0x43e00000, v47
	s_nop 1
	v_mov_b32_dpp v64, v63 quad_perm:[1,0,3,2] row_mask:0xf bank_mask:0xf
	v_mov_b32_e32 v47, v3
	s_waitcnt lgkmcnt(0)
	v_cvt_pk_fp8_f32 v47, v63, v64
	s_nop 1
	v_mov_b32_dpp v63, v47 quad_perm:[2,3,0,1] row_mask:0xf bank_mask:0xf
	s_and_saveexec_b64 s[6:7], vcc
	s_cbranch_execz .LBB0_1122
	v_and_b32_e32 v47, 0xffff, v47
	s_waitcnt lgkmcnt(0)
	v_lshl_or_b32 v47, v63, 16, v47
	global_store_dword v[48:49], v47, off offset:32
.LBB0_1122:
	s_or_b64 exec, exec, s[6:7]
	v_mul_f32_e32 v47, v69, v43
	v_mul_f32_e32 v47, v47, v61
	v_max_f32_e32 v47, 0xc3e00000, v47
	s_waitcnt lgkmcnt(0)
	v_min_f32_e32 v63, 0x43e00000, v47
	s_nop 1
	v_mov_b32_dpp v64, v63 quad_perm:[1,0,3,2] row_mask:0xf bank_mask:0xf
	v_mov_b32_e32 v47, v3
	s_waitcnt lgkmcnt(0)
	v_cvt_pk_fp8_f32 v47, v63, v64
	s_nop 1
	v_mov_b32_dpp v63, v47 quad_perm:[2,3,0,1] row_mask:0xf bank_mask:0xf
	s_and_saveexec_b64 s[6:7], vcc
	s_cbranch_execz .LBB0_1124
	v_and_b32_e32 v47, 0xffff, v47
	s_waitcnt lgkmcnt(0)
	v_lshl_or_b32 v47, v63, 16, v47
	global_store_dword v[48:49], v47, off offset:64
.LBB0_1124:
	s_or_b64 exec, exec, s[6:7]
	v_mul_f32_e32 v43, v68, v43
	v_mul_f32_e32 v43, v43, v2
	v_max_f32_e32 v43, 0xc3e00000, v43
	v_min_f32_e32 v47, 0x43e00000, v43
	s_waitcnt lgkmcnt(0)
	s_nop 1
	v_mov_b32_dpp v63, v47 quad_perm:[1,0,3,2] row_mask:0xf bank_mask:0xf
	v_mov_b32_e32 v43, v3
	s_waitcnt lgkmcnt(0)
	v_cvt_pk_fp8_f32 v43, v47, v63
	s_nop 1
	v_mov_b32_dpp v47, v43 quad_perm:[2,3,0,1] row_mask:0xf bank_mask:0xf
	s_and_saveexec_b64 s[6:7], vcc
	s_cbranch_execz .LBB0_1126
	v_and_b32_e32 v43, 0xffff, v43
	s_waitcnt lgkmcnt(0)
	v_lshl_or_b32 v43, v47, 16, v43
	global_store_dword v[48:49], v43, off offset:96
.LBB0_1126:
	s_or_b64 exec, exec, s[6:7]
	v_mul_f32_e32 v43, 0x4b800000, v46
	v_cndmask_b32_e64 v43, v46, v43, s[4:5]
	v_rsq_f32_e32 v43, v43
	s_nop 0
	v_mul_f32_e32 v46, 0x45800000, v43
	v_cndmask_b32_e64 v43, v43, v46, s[4:5]
	v_mul_f32_e32 v48, v54, v43
	v_mul_f32_e32 v48, v48, v60
	v_max_f32_e32 v48, 0xc3e00000, v48
	v_min_f32_e32 v49, 0x43e00000, v48
	s_nop 1
	v_mov_b32_dpp v54, v49 quad_perm:[1,0,3,2] row_mask:0xf bank_mask:0xf
	v_mov_b32_e32 v48, v3
	v_add_u32_e32 v46, 11, v42
	s_waitcnt lgkmcnt(0)
	v_ashrrev_i32_e32 v47, 31, v46
	v_lshlrev_b64 v[46:47], 12, v[46:47]
	s_waitcnt lgkmcnt(0)
	v_cvt_pk_fp8_f32 v48, v49, v54
	v_lshl_add_u64 v[46:47], v[32:33], 0, v[46:47]
	s_nop 1
	v_mov_b32_dpp v49, v48 quad_perm:[2,3,0,1] row_mask:0xf bank_mask:0xf
	s_and_saveexec_b64 s[4:5], vcc
	s_cbranch_execz .LBB0_1128
	v_and_b32_e32 v48, 0xffff, v48
	s_waitcnt lgkmcnt(0)
	v_lshl_or_b32 v48, v49, 16, v48
	global_store_dword v[46:47], v48, off
.LBB0_1128:
	s_or_b64 exec, exec, s[4:5]
	v_mul_f32_e32 v48, v55, v43
	v_mul_f32_e32 v48, v48, v62
	v_max_f32_e32 v48, 0xc3e00000, v48
	s_waitcnt lgkmcnt(0)
	v_min_f32_e32 v49, 0x43e00000, v48
	s_nop 1
	v_mov_b32_dpp v54, v49 quad_perm:[1,0,3,2] row_mask:0xf bank_mask:0xf
	v_mov_b32_e32 v48, v3
	s_waitcnt lgkmcnt(0)
	v_cvt_pk_fp8_f32 v48, v49, v54
	s_nop 1
	v_mov_b32_dpp v49, v48 quad_perm:[2,3,0,1] row_mask:0xf bank_mask:0xf
	s_and_saveexec_b64 s[4:5], vcc
	s_cbranch_execz .LBB0_1130
	v_and_b32_e32 v48, 0xffff, v48
	s_waitcnt lgkmcnt(0)
	v_lshl_or_b32 v48, v49, 16, v48
	global_store_dword v[46:47], v48, off offset:32
.LBB0_1130:
	s_or_b64 exec, exec, s[4:5]
	v_mul_f32_e32 v48, v51, v43
	v_mul_f32_e32 v48, v48, v61
	v_max_f32_e32 v48, 0xc3e00000, v48
	s_waitcnt lgkmcnt(0)
	v_min_f32_e32 v49, 0x43e00000, v48
	s_nop 1
	v_mov_b32_dpp v51, v49 quad_perm:[1,0,3,2] row_mask:0xf bank_mask:0xf
	v_mov_b32_e32 v48, v3
	s_waitcnt lgkmcnt(0)
	v_cvt_pk_fp8_f32 v48, v49, v51
	s_nop 1
	v_mov_b32_dpp v49, v48 quad_perm:[2,3,0,1] row_mask:0xf bank_mask:0xf
	s_and_saveexec_b64 s[4:5], vcc
	s_cbranch_execz .LBB0_1132
	v_and_b32_e32 v48, 0xffff, v48
	s_waitcnt lgkmcnt(0)
	v_lshl_or_b32 v48, v49, 16, v48
	global_store_dword v[46:47], v48, off offset:64
.LBB0_1132:
	s_or_b64 exec, exec, s[4:5]
	v_mul_f32_e32 v43, v50, v43
	v_mul_f32_e32 v43, v43, v2
	v_max_f32_e32 v43, 0xc3e00000, v43
	v_min_f32_e32 v48, 0x43e00000, v43
	s_waitcnt lgkmcnt(0)
	s_nop 1
	v_mov_b32_dpp v49, v48 quad_perm:[1,0,3,2] row_mask:0xf bank_mask:0xf
	v_mov_b32_e32 v43, v3
	s_waitcnt lgkmcnt(0)
	v_cvt_pk_fp8_f32 v43, v48, v49
	s_nop 1
	v_mov_b32_dpp v48, v43 quad_perm:[2,3,0,1] row_mask:0xf bank_mask:0xf
	s_and_saveexec_b64 s[4:5], vcc
	s_cbranch_execz .LBB0_1134
	v_and_b32_e32 v43, 0xffff, v43
	s_waitcnt lgkmcnt(0)
	v_lshl_or_b32 v43, v48, 16, v43
	global_store_dword v[46:47], v43, off offset:96
.LBB0_1134:
	s_or_b64 exec, exec, s[4:5]
	v_pk_add_f32 v[46:47], v[72:73], v[74:75]
	s_nop 0
	v_pk_fma_f32 v[46:47], v[46:47], s[10:11], v[198:199] op_sel_hi:[1,0,0]
	s_nop 0
	v_mul_f32_e32 v43, 0x4b800000, v47
	v_cmp_gt_f32_e64 s[4:5], s53, v47
	s_nop 1
	v_cndmask_b32_e64 v43, v47, v43, s[4:5]
	v_rsq_f32_e32 v43, v43
	s_nop 0
	v_mul_f32_e32 v47, 0x45800000, v43
	v_cndmask_b32_e64 v43, v43, v47, s[4:5]
	v_mul_f32_e32 v47, v56, v43
	v_mul_f32_e32 v47, v47, v60
	v_max_f32_e32 v47, 0xc3e00000, v47
	s_waitcnt lgkmcnt(0)
	v_min_f32_e32 v48, 0x43e00000, v47
	s_nop 1
	v_mov_b32_dpp v49, v48 quad_perm:[1,0,3,2] row_mask:0xf bank_mask:0xf
	v_mov_b32_e32 v47, v3
	v_cmp_gt_f32_e64 s[4:5], s53, v46
	s_waitcnt lgkmcnt(0)
	v_cvt_pk_fp8_f32 v47, v48, v49
	v_add_u32_e32 v48, 16, v42
	v_ashrrev_i32_e32 v49, 31, v48
	v_lshlrev_b64 v[48:49], 12, v[48:49]
	s_nop 1
	v_mov_b32_dpp v50, v47 quad_perm:[2,3,0,1] row_mask:0xf bank_mask:0xf
	v_lshl_add_u64 v[48:49], v[32:33], 0, v[48:49]
	s_and_saveexec_b64 s[6:7], vcc
	s_cbranch_execz .LBB0_1136
	v_and_b32_e32 v47, 0xffff, v47
	s_waitcnt lgkmcnt(0)
	v_lshl_or_b32 v47, v50, 16, v47
	global_store_dword v[48:49], v47, off
; __device__ __forceinline__ int crow(int r, int hi) { return (r & 3) + 8 * (r >> 2) + 4 * hi; }
; __device__ __forceinline__ void store_quad8(unsigned char* p, float v, int r32) {
;     v = fminf(fmaxf(v, -448.f), 448.f);
;     const float v1 = swz_xor<1>(v);
;     const int w = __builtin_amdgcn_cvt_pk_fp8_f32(v, v1, 0, false);
;     const int w2 = __builtin_amdgcn_ds_swizzle(w, (2 << 10) | 0x1f);
;     if ((r32 & 3) == 0) *(unsigned*)p = ((unsigned)w & 0xffffu) | ((unsigned)w2 << 16);
; }
;     __device__ __forceinline__ void operator()(f32x16 (&o)[4], const float (&rli)[16], int wid, int lane, int r32, int hi) const {
;     ...
;             for (int r = 0; r < 16; ++r)
; #pragma unroll
;                 for (int d0 = 0; d0 < 4; ++d0) store_quad8(base + (size_t)crow(r, hi) * 4096 + d0 * 32 + r32, o[d0][r] * rn[r] * g[d0], r32);
.LBB0_1136:
	s_or_b64 exec, exec, s[6:7]
	v_mul_f32_e32 v47, v57, v43
	v_mul_f32_e32 v47, v47, v62
	v_max_f32_e32 v47, 0xc3e00000, v47
	s_waitcnt lgkmcnt(0)
	v_min_f32_e32 v50, 0x43e00000, v47
	s_nop 1
	v_mov_b32_dpp v51, v50 quad_perm:[1,0,3,2] row_mask:0xf bank_mask:0xf
	v_mov_b32_e32 v47, v3
	s_waitcnt lgkmcnt(0)
	v_cvt_pk_fp8_f32 v47, v50, v51
	s_nop 1
	v_mov_b32_dpp v50, v47 quad_perm:[2,3,0,1] row_mask:0xf bank_mask:0xf
	s_and_saveexec_b64 s[6:7], vcc
	s_cbranch_execz .LBB0_1138
	v_and_b32_e32 v47, 0xffff, v47
	s_waitcnt lgkmcnt(0)
	v_lshl_or_b32 v47, v50, 16, v47
	global_store_dword v[48:49], v47, off offset:32
.LBB0_1138:
	s_or_b64 exec, exec, s[6:7]
	v_mul_f32_e32 v47, v53, v43
	v_mul_f32_e32 v47, v47, v61
	v_max_f32_e32 v47, 0xc3e00000, v47
	s_waitcnt lgkmcnt(0)
	v_min_f32_e32 v50, 0x43e00000, v47
	s_nop 1
	v_mov_b32_dpp v51, v50 quad_perm:[1,0,3,2] row_mask:0xf bank_mask:0xf
	v_mov_b32_e32 v47, v3
	s_waitcnt lgkmcnt(0)
	v_cvt_pk_fp8_f32 v47, v50, v51
	s_nop 1
	v_mov_b32_dpp v50, v47 quad_perm:[2,3,0,1] row_mask:0xf bank_mask:0xf
	s_and_saveexec_b64 s[6:7], vcc
	s_cbranch_execz .LBB0_1140
	v_and_b32_e32 v47, 0xffff, v47
	s_waitcnt lgkmcnt(0)
	v_lshl_or_b32 v47, v50, 16, v47
	global_store_dword v[48:49], v47, off offset:64
.LBB0_1140:
	s_or_b64 exec, exec, s[6:7]
	v_mul_f32_e32 v43, v52, v43
	v_mul_f32_e32 v43, v43, v2
	v_max_f32_e32 v43, 0xc3e00000, v43
	v_min_f32_e32 v47, 0x43e00000, v43
	s_waitcnt lgkmcnt(0)
	s_nop 1
	v_mov_b32_dpp v50, v47 quad_perm:[1,0,3,2] row_mask:0xf bank_mask:0xf
	v_mov_b32_e32 v43, v3
	s_waitcnt lgkmcnt(0)
	v_cvt_pk_fp8_f32 v43, v47, v50
	s_nop 1
	v_mov_b32_dpp v47, v43 quad_perm:[2,3,0,1] row_mask:0xf bank_mask:0xf
	s_and_saveexec_b64 s[6:7], vcc
	s_cbranch_execz .LBB0_1142
	v_and_b32_e32 v43, 0xffff, v43
	s_waitcnt lgkmcnt(0)
	v_lshl_or_b32 v43, v47, 16, v43
	global_store_dword v[48:49], v43, off offset:96
.LBB0_1142:
	s_or_b64 exec, exec, s[6:7]
	v_mul_f32_e32 v43, 0x4b800000, v46
	v_cndmask_b32_e64 v43, v46, v43, s[4:5]
	v_rsq_f32_e32 v43, v43
	s_nop 0
	v_mul_f32_e32 v46, 0x45800000, v43
	v_cndmask_b32_e64 v43, v43, v46, s[4:5]
	v_mul_f32_e32 v38, v38, v43
	v_mul_f32_e32 v38, v38, v60
	v_max_f32_e32 v38, 0xc3e00000, v38
	v_min_f32_e32 v48, 0x43e00000, v38
	s_nop 1
	v_mov_b32_dpp v49, v48 quad_perm:[1,0,3,2] row_mask:0xf bank_mask:0xf
	v_mov_b32_e32 v38, v3
	v_add_u32_e32 v46, 17, v42
	s_waitcnt lgkmcnt(0)
	v_ashrrev_i32_e32 v47, 31, v46
	v_lshlrev_b64 v[46:47], 12, v[46:47]
	s_waitcnt lgkmcnt(0)
	v_cvt_pk_fp8_f32 v38, v48, v49
	v_lshl_add_u64 v[46:47], v[32:33], 0, v[46:47]
	s_nop 1
	v_mov_b32_dpp v48, v38 quad_perm:[2,3,0,1] row_mask:0xf bank_mask:0xf
	s_and_saveexec_b64 s[4:5], vcc
	s_cbranch_execz .LBB0_1144
	v_and_b32_e32 v38, 0xffff, v38
	s_waitcnt lgkmcnt(0)
	v_lshl_or_b32 v38, v48, 16, v38
	global_store_dword v[46:47], v38, off
.LBB0_1144:
	s_or_b64 exec, exec, s[4:5]
	v_mul_f32_e32 v38, v39, v43
	v_mul_f32_e32 v38, v38, v62
	v_max_f32_e32 v38, 0xc3e00000, v38
	v_min_f32_e32 v39, 0x43e00000, v38
	s_waitcnt lgkmcnt(0)
	s_nop 1
	v_mov_b32_dpp v48, v39 quad_perm:[1,0,3,2] row_mask:0xf bank_mask:0xf
	v_mov_b32_e32 v38, v3
	s_waitcnt lgkmcnt(0)
	v_cvt_pk_fp8_f32 v38, v39, v48
	s_nop 1
	v_mov_b32_dpp v39, v38 quad_perm:[2,3,0,1] row_mask:0xf bank_mask:0xf
	s_and_saveexec_b64 s[4:5], vcc
	s_cbranch_execz .LBB0_1146
	v_and_b32_e32 v38, 0xffff, v38
	s_waitcnt lgkmcnt(0)
	v_lshl_or_b32 v38, v39, 16, v38
	global_store_dword v[46:47], v38, off offset:32
.LBB0_1146:
	s_or_b64 exec, exec, s[4:5]
	v_mul_f32_e32 v35, v35, v43
	v_mul_f32_e32 v35, v35, v61
	v_max_f32_e32 v35, 0xc3e00000, v35
	v_min_f32_e32 v38, 0x43e00000, v35
	s_waitcnt lgkmcnt(0)
	s_nop 1
	v_mov_b32_dpp v39, v38 quad_perm:[1,0,3,2] row_mask:0xf bank_mask:0xf
	v_mov_b32_e32 v35, v3
	s_waitcnt lgkmcnt(0)
	v_cvt_pk_fp8_f32 v35, v38, v39
	s_nop 1
	v_mov_b32_dpp v38, v35 quad_perm:[2,3,0,1] row_mask:0xf bank_mask:0xf
	s_and_saveexec_b64 s[4:5], vcc
	s_cbranch_execz .LBB0_1148
	v_and_b32_e32 v35, 0xffff, v35
	s_waitcnt lgkmcnt(0)
	v_lshl_or_b32 v35, v38, 16, v35
	global_store_dword v[46:47], v35, off offset:64
.LBB0_1148:
	s_or_b64 exec, exec, s[4:5]
	v_mul_f32_e32 v34, v34, v43
	v_mul_f32_e32 v34, v34, v2
	v_max_f32_e32 v34, 0xc3e00000, v34
	v_min_f32_e32 v35, 0x43e00000, v34
	s_waitcnt lgkmcnt(0)
	s_nop 1
	v_mov_b32_dpp v38, v35 quad_perm:[1,0,3,2] row_mask:0xf bank_mask:0xf
	v_mov_b32_e32 v34, v3
	s_waitcnt lgkmcnt(0)
	v_cvt_pk_fp8_f32 v34, v35, v38
	s_nop 1
	v_mov_b32_dpp v35, v34 quad_perm:[2,3,0,1] row_mask:0xf bank_mask:0xf
	s_and_saveexec_b64 s[4:5], vcc
	s_cbranch_execz .LBB0_1150
	v_and_b32_e32 v34, 0xffff, v34
	s_waitcnt lgkmcnt(0)
	v_lshl_or_b32 v34, v35, 16, v34
	global_store_dword v[46:47], v34, off offset:96
.LBB0_1150:
	s_or_b64 exec, exec, s[4:5]
	s_waitcnt lgkmcnt(0)
	v_pk_add_f32 v[34:35], v[44:45], v[58:59]
	s_nop 0
	v_pk_fma_f32 v[34:35], v[34:35], s[10:11], v[198:199] op_sel_hi:[1,0,0]
	s_nop 0
	v_mul_f32_e32 v38, 0x4b800000, v35
	v_cmp_gt_f32_e64 s[4:5], s53, v35
	s_nop 1
	v_cndmask_b32_e64 v35, v35, v38, s[4:5]
	v_rsq_f32_e32 v35, v35
	s_nop 0
	v_mul_f32_e32 v38, 0x45800000, v35
	v_cndmask_b32_e64 v35, v35, v38, s[4:5]
	v_mul_f32_e32 v38, v40, v35
	v_mul_f32_e32 v38, v38, v60
	v_max_f32_e32 v38, 0xc3e00000, v38
	v_min_f32_e32 v38, 0x43e00000, v38
	s_nop 1
	v_mov_b32_dpp v39, v38 quad_perm:[1,0,3,2] row_mask:0xf bank_mask:0xf
	v_mov_b32_e32 v40, v3
	v_cmp_gt_f32_e64 s[4:5], s53, v34
	s_waitcnt lgkmcnt(0)
	v_cvt_pk_fp8_f32 v40, v38, v39
	v_add_u32_e32 v38, 18, v42
	v_ashrrev_i32_e32 v39, 31, v38
	v_lshlrev_b64 v[38:39], 12, v[38:39]
	s_nop 1
	v_mov_b32_dpp v43, v40 quad_perm:[2,3,0,1] row_mask:0xf bank_mask:0xf
	v_lshl_add_u64 v[38:39], v[32:33], 0, v[38:39]
	s_and_saveexec_b64 s[6:7], vcc
	s_cbranch_execz .LBB0_1152
	v_and_b32_e32 v40, 0xffff, v40
	s_waitcnt lgkmcnt(0)
	v_lshl_or_b32 v40, v43, 16, v40
	global_store_dword v[38:39], v40, off
; __device__ __forceinline__ int crow(int r, int hi) { return (r & 3) + 8 * (r >> 2) + 4 * hi; }
; __device__ __forceinline__ void store_quad8(unsigned char* p, float v, int r32) {
;     v = fminf(fmaxf(v, -448.f), 448.f);
;     const float v1 = swz_xor<1>(v);
;     const int w = __builtin_amdgcn_cvt_pk_fp8_f32(v, v1, 0, false);
;     const int w2 = __builtin_amdgcn_ds_swizzle(w, (2 << 10) | 0x1f);
;     if ((r32 & 3) == 0) *(unsigned*)p = ((unsigned)w & 0xffffu) | ((unsigned)w2 << 16);
; }
;     __device__ __forceinline__ void operator()(f32x16 (&o)[4], const float (&rli)[16], int wid, int lane, int r32, int hi) const {
;     ...
;             for (int r = 0; r < 16; ++r)
; #pragma unroll
;                 for (int d0 = 0; d0 < 4; ++d0) store_quad8(base + (size_t)crow(r, hi) * 4096 + d0 * 32 + r32, o[d0][r] * rn[r] * g[d0], r32);
.LBB0_1152:
	s_or_b64 exec, exec, s[6:7]
	v_mul_f32_e32 v40, v41, v35
	v_mul_f32_e32 v40, v40, v62
	v_max_f32_e32 v40, 0xc3e00000, v40
	v_min_f32_e32 v41, 0x43e00000, v40
	s_waitcnt lgkmcnt(0)
	s_nop 1
	v_mov_b32_dpp v43, v41 quad_perm:[1,0,3,2] row_mask:0xf bank_mask:0xf
	v_mov_b32_e32 v40, v3
	s_waitcnt lgkmcnt(0)
	v_cvt_pk_fp8_f32 v40, v41, v43
	s_nop 1
	v_mov_b32_dpp v41, v40 quad_perm:[2,3,0,1] row_mask:0xf bank_mask:0xf
	s_and_saveexec_b64 s[6:7], vcc
	s_cbranch_execz .LBB0_1154
	v_and_b32_e32 v40, 0xffff, v40
	s_waitcnt lgkmcnt(0)
	v_lshl_or_b32 v40, v41, 16, v40
	global_store_dword v[38:39], v40, off offset:32
.LBB0_1154:
	s_or_b64 exec, exec, s[6:7]
	v_mul_f32_e32 v37, v37, v35
	v_mul_f32_e32 v37, v37, v61
	v_max_f32_e32 v37, 0xc3e00000, v37
	v_min_f32_e32 v40, 0x43e00000, v37
	s_waitcnt lgkmcnt(0)
	s_nop 1
	v_mov_b32_dpp v41, v40 quad_perm:[1,0,3,2] row_mask:0xf bank_mask:0xf
	v_mov_b32_e32 v37, v3
	s_waitcnt lgkmcnt(0)
	v_cvt_pk_fp8_f32 v37, v40, v41
	s_nop 1
	v_mov_b32_dpp v40, v37 quad_perm:[2,3,0,1] row_mask:0xf bank_mask:0xf
	s_and_saveexec_b64 s[6:7], vcc
	s_cbranch_execz .LBB0_1156
	v_and_b32_e32 v37, 0xffff, v37
	s_waitcnt lgkmcnt(0)
	v_lshl_or_b32 v37, v40, 16, v37
	global_store_dword v[38:39], v37, off offset:64
.LBB0_1156:
	s_or_b64 exec, exec, s[6:7]
	v_mul_f32_e32 v35, v36, v35
	v_mul_f32_e32 v35, v35, v2
	v_max_f32_e32 v35, 0xc3e00000, v35
	v_min_f32_e32 v36, 0x43e00000, v35
	s_nop 1
	v_mov_b32_dpp v37, v36 quad_perm:[1,0,3,2] row_mask:0xf bank_mask:0xf
	v_mov_b32_e32 v35, v3
	s_waitcnt lgkmcnt(0)
	v_cvt_pk_fp8_f32 v35, v36, v37
	s_nop 1
	v_mov_b32_dpp v36, v35 quad_perm:[2,3,0,1] row_mask:0xf bank_mask:0xf
	s_and_saveexec_b64 s[6:7], vcc
	s_cbranch_execz .LBB0_1158
	v_and_b32_e32 v35, 0xffff, v35
	s_waitcnt lgkmcnt(0)
	v_lshl_or_b32 v35, v36, 16, v35
	global_store_dword v[38:39], v35, off offset:96
.LBB0_1158:
	s_or_b64 exec, exec, s[6:7]
	v_mul_f32_e32 v35, 0x4b800000, v34
	v_cndmask_b32_e64 v34, v34, v35, s[4:5]
	v_rsq_f32_e32 v34, v34
	s_nop 0
	v_mul_f32_e32 v35, 0x45800000, v34
	s_waitcnt lgkmcnt(0)
	v_cndmask_b32_e64 v36, v34, v35, s[4:5]
	v_mul_f32_e32 v24, v24, v36
	v_mul_f32_e32 v24, v24, v60
	v_max_f32_e32 v24, 0xc3e00000, v24
	v_min_f32_e32 v37, 0x43e00000, v24
	s_nop 1
	v_mov_b32_dpp v38, v37 quad_perm:[1,0,3,2] row_mask:0xf bank_mask:0xf
	v_mov_b32_e32 v24, v3
	v_add_u32_e32 v34, 19, v42
	v_ashrrev_i32_e32 v35, 31, v34
	v_lshlrev_b64 v[34:35], 12, v[34:35]
	s_waitcnt lgkmcnt(0)
	v_cvt_pk_fp8_f32 v24, v37, v38
	v_lshl_add_u64 v[34:35], v[32:33], 0, v[34:35]
	s_nop 1
	v_mov_b32_dpp v37, v24 quad_perm:[2,3,0,1] row_mask:0xf bank_mask:0xf
	s_and_saveexec_b64 s[4:5], vcc
	s_cbranch_execz .LBB0_1160
	v_and_b32_e32 v24, 0xffff, v24
	s_waitcnt lgkmcnt(0)
	v_lshl_or_b32 v24, v37, 16, v24
	global_store_dword v[34:35], v24, off
.LBB0_1160:
	s_or_b64 exec, exec, s[4:5]
	v_mul_f32_e32 v24, v25, v36
	v_mul_f32_e32 v24, v24, v62
	v_max_f32_e32 v24, 0xc3e00000, v24
	v_min_f32_e32 v25, 0x43e00000, v24
	s_waitcnt lgkmcnt(0)
	s_nop 1
	v_mov_b32_dpp v37, v25 quad_perm:[1,0,3,2] row_mask:0xf bank_mask:0xf
	v_mov_b32_e32 v24, v3
	s_waitcnt lgkmcnt(0)
	v_cvt_pk_fp8_f32 v24, v25, v37
	s_nop 1
	v_mov_b32_dpp v25, v24 quad_perm:[2,3,0,1] row_mask:0xf bank_mask:0xf
	s_and_saveexec_b64 s[4:5], vcc
	s_cbranch_execz .LBB0_1162
	v_and_b32_e32 v24, 0xffff, v24
	s_waitcnt lgkmcnt(0)
	v_lshl_or_b32 v24, v25, 16, v24
	global_store_dword v[34:35], v24, off offset:32
.LBB0_1162:
	s_or_b64 exec, exec, s[4:5]
	v_mul_f32_e32 v21, v21, v36
	v_mul_f32_e32 v21, v21, v61
	v_max_f32_e32 v21, 0xc3e00000, v21
	v_min_f32_e32 v24, 0x43e00000, v21
	s_waitcnt lgkmcnt(0)
	s_nop 1
	v_mov_b32_dpp v25, v24 quad_perm:[1,0,3,2] row_mask:0xf bank_mask:0xf
	v_mov_b32_e32 v21, v3
	s_waitcnt lgkmcnt(0)
	v_cvt_pk_fp8_f32 v21, v24, v25
	s_nop 1
	v_mov_b32_dpp v24, v21 quad_perm:[2,3,0,1] row_mask:0xf bank_mask:0xf
	s_and_saveexec_b64 s[4:5], vcc
	s_cbranch_execz .LBB0_1164
	v_and_b32_e32 v21, 0xffff, v21
	s_waitcnt lgkmcnt(0)
	v_lshl_or_b32 v21, v24, 16, v21
	global_store_dword v[34:35], v21, off offset:64
.LBB0_1164:
	s_or_b64 exec, exec, s[4:5]
	v_mul_f32_e32 v20, v20, v36
	v_mul_f32_e32 v20, v20, v2
	v_max_f32_e32 v20, 0xc3e00000, v20
	v_min_f32_e32 v21, 0x43e00000, v20
	s_waitcnt lgkmcnt(0)
	s_nop 1
	v_mov_b32_dpp v24, v21 quad_perm:[1,0,3,2] row_mask:0xf bank_mask:0xf
	v_mov_b32_e32 v20, v3
	s_waitcnt lgkmcnt(0)
	v_cvt_pk_fp8_f32 v20, v21, v24
	s_nop 1
	v_mov_b32_dpp v21, v20 quad_perm:[2,3,0,1] row_mask:0xf bank_mask:0xf
	s_and_saveexec_b64 s[4:5], vcc
	s_cbranch_execz .LBB0_1166
	v_and_b32_e32 v20, 0xffff, v20
	s_waitcnt lgkmcnt(0)
	v_lshl_or_b32 v20, v21, 16, v20
	global_store_dword v[34:35], v20, off offset:96
.LBB0_1166:
	s_or_b64 exec, exec, s[4:5]
	s_waitcnt lgkmcnt(0)
	v_pk_add_f32 v[20:21], v[28:29], v[30:31]
	s_nop 0
	v_pk_fma_f32 v[20:21], v[20:21], s[10:11], v[198:199] op_sel_hi:[1,0,0]
	s_nop 0
	v_mul_f32_e32 v24, 0x4b800000, v21
	v_cmp_gt_f32_e64 s[4:5], s53, v21
	s_nop 1
	v_cndmask_b32_e64 v21, v21, v24, s[4:5]
	v_rsq_f32_e32 v21, v21
	s_nop 0
	v_mul_f32_e32 v24, 0x45800000, v21
	v_cndmask_b32_e64 v21, v21, v24, s[4:5]
	v_mul_f32_e32 v24, v26, v21
	v_mul_f32_e32 v24, v24, v60
	v_max_f32_e32 v24, 0xc3e00000, v24
	v_min_f32_e32 v24, 0x43e00000, v24
	s_nop 1
	v_mov_b32_dpp v25, v24 quad_perm:[1,0,3,2] row_mask:0xf bank_mask:0xf
	v_mov_b32_e32 v26, v3
	v_cmp_gt_f32_e64 s[4:5], s53, v20
	s_waitcnt lgkmcnt(0)
	v_cvt_pk_fp8_f32 v26, v24, v25
	v_add_u32_e32 v24, 24, v42
	v_ashrrev_i32_e32 v25, 31, v24
	v_lshlrev_b64 v[24:25], 12, v[24:25]
	s_nop 1
	v_mov_b32_dpp v28, v26 quad_perm:[2,3,0,1] row_mask:0xf bank_mask:0xf
	v_lshl_add_u64 v[24:25], v[32:33], 0, v[24:25]
	s_and_saveexec_b64 s[6:7], vcc
	s_cbranch_execz .LBB0_1168
	v_and_b32_e32 v26, 0xffff, v26
	s_waitcnt lgkmcnt(0)
	v_lshl_or_b32 v26, v28, 16, v26
	global_store_dword v[24:25], v26, off
; __device__ __forceinline__ int crow(int r, int hi) { return (r & 3) + 8 * (r >> 2) + 4 * hi; }
; __device__ __forceinline__ void store_quad8(unsigned char* p, float v, int r32) {
;     v = fminf(fmaxf(v, -448.f), 448.f);
;     const float v1 = swz_xor<1>(v);
;     const int w = __builtin_amdgcn_cvt_pk_fp8_f32(v, v1, 0, false);
;     const int w2 = __builtin_amdgcn_ds_swizzle(w, (2 << 10) | 0x1f);
;     if ((r32 & 3) == 0) *(unsigned*)p = ((unsigned)w & 0xffffu) | ((unsigned)w2 << 16);
; }
;     __device__ __forceinline__ void operator()(f32x16 (&o)[4], const float (&rli)[16], int wid, int lane, int r32, int hi) const {
;     ...
;             for (int r = 0; r < 16; ++r)
; #pragma unroll
;                 for (int d0 = 0; d0 < 4; ++d0) store_quad8(base + (size_t)crow(r, hi) * 4096 + d0 * 32 + r32, o[d0][r] * rn[r] * g[d0], r32);
.LBB0_1168:
	s_or_b64 exec, exec, s[6:7]
	v_mul_f32_e32 v26, v27, v21
	v_mul_f32_e32 v26, v26, v62
	v_max_f32_e32 v26, 0xc3e00000, v26
	v_min_f32_e32 v27, 0x43e00000, v26
	s_waitcnt lgkmcnt(0)
	s_nop 1
	v_mov_b32_dpp v28, v27 quad_perm:[1,0,3,2] row_mask:0xf bank_mask:0xf
	v_mov_b32_e32 v26, v3
	s_waitcnt lgkmcnt(0)
	v_cvt_pk_fp8_f32 v26, v27, v28
	s_nop 1
	v_mov_b32_dpp v27, v26 quad_perm:[2,3,0,1] row_mask:0xf bank_mask:0xf
	s_and_saveexec_b64 s[6:7], vcc
	s_cbranch_execz .LBB0_1170
	v_and_b32_e32 v26, 0xffff, v26
	s_waitcnt lgkmcnt(0)
	v_lshl_or_b32 v26, v27, 16, v26
	global_store_dword v[24:25], v26, off offset:32
.LBB0_1170:
	s_or_b64 exec, exec, s[6:7]
	v_mul_f32_e32 v23, v23, v21
	v_mul_f32_e32 v23, v23, v61
	v_max_f32_e32 v23, 0xc3e00000, v23
	v_min_f32_e32 v26, 0x43e00000, v23
	s_waitcnt lgkmcnt(0)
	s_nop 1
	v_mov_b32_dpp v27, v26 quad_perm:[1,0,3,2] row_mask:0xf bank_mask:0xf
	v_mov_b32_e32 v23, v3
	s_waitcnt lgkmcnt(0)
	v_cvt_pk_fp8_f32 v23, v26, v27
	s_nop 1
	v_mov_b32_dpp v26, v23 quad_perm:[2,3,0,1] row_mask:0xf bank_mask:0xf
	s_and_saveexec_b64 s[6:7], vcc
	s_cbranch_execz .LBB0_1172
	v_and_b32_e32 v23, 0xffff, v23
	s_waitcnt lgkmcnt(0)
	v_lshl_or_b32 v23, v26, 16, v23
	global_store_dword v[24:25], v23, off offset:64
.LBB0_1172:
	s_or_b64 exec, exec, s[6:7]
	v_mul_f32_e32 v21, v22, v21
	v_mul_f32_e32 v21, v21, v2
	v_max_f32_e32 v21, 0xc3e00000, v21
	v_min_f32_e32 v22, 0x43e00000, v21
	s_nop 1
	v_mov_b32_dpp v23, v22 quad_perm:[1,0,3,2] row_mask:0xf bank_mask:0xf
	v_mov_b32_e32 v21, v3
	s_waitcnt lgkmcnt(0)
	v_cvt_pk_fp8_f32 v21, v22, v23
	s_nop 1
	v_mov_b32_dpp v22, v21 quad_perm:[2,3,0,1] row_mask:0xf bank_mask:0xf
	s_and_saveexec_b64 s[6:7], vcc
	s_cbranch_execz .LBB0_1174
	v_and_b32_e32 v21, 0xffff, v21
	s_waitcnt lgkmcnt(0)
	v_lshl_or_b32 v21, v22, 16, v21
	global_store_dword v[24:25], v21, off offset:96
.LBB0_1174:
	s_or_b64 exec, exec, s[6:7]
	v_mul_f32_e32 v21, 0x4b800000, v20
	v_cndmask_b32_e64 v20, v20, v21, s[4:5]
	v_rsq_f32_e32 v20, v20
	s_nop 0
	v_mul_f32_e32 v21, 0x45800000, v20
	s_waitcnt lgkmcnt(0)
	v_cndmask_b32_e64 v22, v20, v21, s[4:5]
	v_mul_f32_e32 v14, v14, v22
	v_mul_f32_e32 v14, v14, v60
	v_max_f32_e32 v14, 0xc3e00000, v14
	v_min_f32_e32 v23, 0x43e00000, v14
	s_nop 1
	v_mov_b32_dpp v24, v23 quad_perm:[1,0,3,2] row_mask:0xf bank_mask:0xf
	v_mov_b32_e32 v14, v3
	v_add_u32_e32 v20, 25, v42
	v_ashrrev_i32_e32 v21, 31, v20
	v_lshlrev_b64 v[20:21], 12, v[20:21]
	s_waitcnt lgkmcnt(0)
	v_cvt_pk_fp8_f32 v14, v23, v24
	v_lshl_add_u64 v[20:21], v[32:33], 0, v[20:21]
	s_nop 1
	v_mov_b32_dpp v23, v14 quad_perm:[2,3,0,1] row_mask:0xf bank_mask:0xf
	s_and_saveexec_b64 s[4:5], vcc
	s_cbranch_execz .LBB0_1176
	v_and_b32_e32 v14, 0xffff, v14
	s_waitcnt lgkmcnt(0)
	v_lshl_or_b32 v14, v23, 16, v14
	global_store_dword v[20:21], v14, off
.LBB0_1176:
	s_or_b64 exec, exec, s[4:5]
	v_mul_f32_e32 v14, v15, v22
	v_mul_f32_e32 v14, v14, v62
	v_max_f32_e32 v14, 0xc3e00000, v14
	v_min_f32_e32 v15, 0x43e00000, v14
	s_waitcnt lgkmcnt(0)
	s_nop 1
	v_mov_b32_dpp v23, v15 quad_perm:[1,0,3,2] row_mask:0xf bank_mask:0xf
	v_mov_b32_e32 v14, v3
	s_waitcnt lgkmcnt(0)
	v_cvt_pk_fp8_f32 v14, v15, v23
	s_nop 1
	v_mov_b32_dpp v15, v14 quad_perm:[2,3,0,1] row_mask:0xf bank_mask:0xf
	s_and_saveexec_b64 s[4:5], vcc
	s_cbranch_execz .LBB0_1178
	v_and_b32_e32 v14, 0xffff, v14
	s_waitcnt lgkmcnt(0)
	v_lshl_or_b32 v14, v15, 16, v14
	global_store_dword v[20:21], v14, off offset:32
.LBB0_1178:
	s_or_b64 exec, exec, s[4:5]
	v_mul_f32_e32 v13, v13, v22
	v_mul_f32_e32 v13, v13, v61
	v_max_f32_e32 v13, 0xc3e00000, v13
	v_min_f32_e32 v14, 0x43e00000, v13
	s_waitcnt lgkmcnt(0)
	s_nop 1
	v_mov_b32_dpp v15, v14 quad_perm:[1,0,3,2] row_mask:0xf bank_mask:0xf
	v_mov_b32_e32 v13, v3
	s_waitcnt lgkmcnt(0)
	v_cvt_pk_fp8_f32 v13, v14, v15
	s_nop 1
	v_mov_b32_dpp v14, v13 quad_perm:[2,3,0,1] row_mask:0xf bank_mask:0xf
	s_and_saveexec_b64 s[4:5], vcc
	s_cbranch_execz .LBB0_1180
	v_and_b32_e32 v13, 0xffff, v13
	s_waitcnt lgkmcnt(0)
	v_lshl_or_b32 v13, v14, 16, v13
	global_store_dword v[20:21], v13, off offset:64
.LBB0_1180:
	s_or_b64 exec, exec, s[4:5]
	v_mul_f32_e32 v12, v12, v22
	v_mul_f32_e32 v12, v12, v2
	v_max_f32_e32 v12, 0xc3e00000, v12
	v_min_f32_e32 v13, 0x43e00000, v12
	s_waitcnt lgkmcnt(0)
	s_nop 1
	v_mov_b32_dpp v14, v13 quad_perm:[1,0,3,2] row_mask:0xf bank_mask:0xf
	v_mov_b32_e32 v12, v3
	s_waitcnt lgkmcnt(0)
	v_cvt_pk_fp8_f32 v12, v13, v14
	s_nop 1
	v_mov_b32_dpp v13, v12 quad_perm:[2,3,0,1] row_mask:0xf bank_mask:0xf
	s_and_saveexec_b64 s[4:5], vcc
	s_cbranch_execz .LBB0_1182
	v_and_b32_e32 v12, 0xffff, v12
	s_waitcnt lgkmcnt(0)
	v_lshl_or_b32 v12, v13, 16, v12
	global_store_dword v[20:21], v12, off offset:96
; __device__ __forceinline__ int crow(int r, int hi) { return (r & 3) + 8 * (r >> 2) + 4 * hi; }
; __device__ __forceinline__ void store_quad8(unsigned char* p, float v, int r32) {
;     v = fminf(fmaxf(v, -448.f), 448.f);
;     const float v1 = swz_xor<1>(v);
;     const int w = __builtin_amdgcn_cvt_pk_fp8_f32(v, v1, 0, false);
;     const int w2 = __builtin_amdgcn_ds_swizzle(w, (2 << 10) | 0x1f);
;     if ((r32 & 3) == 0) *(unsigned*)p = ((unsigned)w & 0xffffu) | ((unsigned)w2 << 16);
; }
;     __device__ __forceinline__ void operator()(f32x16 (&o)[4], const float (&rli)[16], int wid, int lane, int r32, int hi) const {
;     ...
;             for (int r = 0; r < 16; ++r)
; #pragma unroll
;                 for (int d0 = 0; d0 < 4; ++d0) store_quad8(base + (size_t)crow(r, hi) * 4096 + d0 * 32 + r32, o[d0][r] * rn[r] * g[d0], r32);
.LBB0_1182:
	s_or_b64 exec, exec, s[4:5]
	s_waitcnt lgkmcnt(0)
	v_pk_add_f32 v[12:13], v[16:17], v[18:19]
	s_nop 0
	v_pk_fma_f32 v[12:13], v[12:13], s[10:11], v[198:199] op_sel_hi:[1,0,0]
	s_nop 0
	v_mul_f32_e32 v14, 0x4b800000, v13
	v_cmp_gt_f32_e64 s[4:5], s53, v13
	s_nop 1
	v_cndmask_b32_e64 v13, v13, v14, s[4:5]
	v_rsq_f32_e32 v13, v13
	s_nop 0
	v_mul_f32_e32 v14, 0x45800000, v13
	v_cndmask_b32_e64 v13, v13, v14, s[4:5]
	v_mul_f32_e32 v10, v10, v13
	v_mul_f32_e32 v10, v60, v10
	v_max_f32_e32 v10, 0xc3e00000, v10
	v_min_f32_e32 v14, 0x43e00000, v10
	s_nop 1
	v_mov_b32_dpp v15, v14 quad_perm:[1,0,3,2] row_mask:0xf bank_mask:0xf
	v_mov_b32_e32 v10, v3
	v_cmp_gt_f32_e64 s[4:5], s53, v12
	s_waitcnt lgkmcnt(0)
	v_cvt_pk_fp8_f32 v10, v14, v15
	v_add_u32_e32 v14, 26, v42
	v_ashrrev_i32_e32 v15, 31, v14
	v_lshlrev_b64 v[14:15], 12, v[14:15]
	s_nop 1
	v_mov_b32_dpp v16, v10 quad_perm:[2,3,0,1] row_mask:0xf bank_mask:0xf
	v_lshl_add_u64 v[14:15], v[32:33], 0, v[14:15]
	s_and_saveexec_b64 s[6:7], vcc
	s_cbranch_execz .LBB0_1184
	v_and_b32_e32 v10, 0xffff, v10
	s_waitcnt lgkmcnt(0)
	v_lshl_or_b32 v10, v16, 16, v10
	global_store_dword v[14:15], v10, off
.LBB0_1184:
	s_or_b64 exec, exec, s[6:7]
	v_mul_f32_e32 v10, v11, v13
	v_mul_f32_e32 v10, v62, v10
	v_max_f32_e32 v10, 0xc3e00000, v10
	v_min_f32_e32 v11, 0x43e00000, v10
	s_waitcnt lgkmcnt(0)
	s_nop 1
	v_mov_b32_dpp v16, v11 quad_perm:[1,0,3,2] row_mask:0xf bank_mask:0xf
	v_mov_b32_e32 v10, v3
	s_waitcnt lgkmcnt(0)
	v_cvt_pk_fp8_f32 v10, v11, v16
	s_nop 1
	v_mov_b32_dpp v11, v10 quad_perm:[2,3,0,1] row_mask:0xf bank_mask:0xf
	s_and_saveexec_b64 s[6:7], vcc
	s_cbranch_execz .LBB0_1186
	v_and_b32_e32 v10, 0xffff, v10
	s_waitcnt lgkmcnt(0)
	v_lshl_or_b32 v10, v11, 16, v10
	global_store_dword v[14:15], v10, off offset:32
.LBB0_1186:
	s_or_b64 exec, exec, s[6:7]
	v_mul_f32_e32 v9, v9, v13
	v_mul_f32_e32 v9, v61, v9
	v_max_f32_e32 v9, 0xc3e00000, v9
	v_min_f32_e32 v10, 0x43e00000, v9
	s_waitcnt lgkmcnt(0)
	s_nop 1
	v_mov_b32_dpp v11, v10 quad_perm:[1,0,3,2] row_mask:0xf bank_mask:0xf
	v_mov_b32_e32 v9, v3
	s_waitcnt lgkmcnt(0)
	v_cvt_pk_fp8_f32 v9, v10, v11
	s_nop 1
	v_mov_b32_dpp v10, v9 quad_perm:[2,3,0,1] row_mask:0xf bank_mask:0xf
	s_and_saveexec_b64 s[6:7], vcc
	s_cbranch_execz .LBB0_1188
	v_and_b32_e32 v9, 0xffff, v9
	s_waitcnt lgkmcnt(0)
	v_lshl_or_b32 v9, v10, 16, v9
	global_store_dword v[14:15], v9, off offset:64
.LBB0_1188:
	s_or_b64 exec, exec, s[6:7]
	v_mul_f32_e32 v8, v8, v13
	v_mul_f32_e32 v8, v2, v8
	v_max_f32_e32 v8, 0xc3e00000, v8
	v_min_f32_e32 v9, 0x43e00000, v8
	s_waitcnt lgkmcnt(0)
	s_nop 1
	v_mov_b32_dpp v10, v9 quad_perm:[1,0,3,2] row_mask:0xf bank_mask:0xf
	v_mov_b32_e32 v8, v3
	s_waitcnt lgkmcnt(0)
	v_cvt_pk_fp8_f32 v8, v9, v10
	s_nop 1
	v_mov_b32_dpp v9, v8 quad_perm:[2,3,0,1] row_mask:0xf bank_mask:0xf
	s_and_saveexec_b64 s[6:7], vcc
	s_cbranch_execz .LBB0_1190
	v_and_b32_e32 v8, 0xffff, v8
	s_waitcnt lgkmcnt(0)
	v_lshl_or_b32 v8, v9, 16, v8
	global_store_dword v[14:15], v8, off offset:96
.LBB0_1190:
	s_or_b64 exec, exec, s[6:7]
	v_mul_f32_e32 v8, 0x4b800000, v12
	v_cndmask_b32_e64 v8, v12, v8, s[4:5]
	v_rsq_f32_e32 v8, v8
	s_waitcnt lgkmcnt(0)
	v_mul_f32_e32 v9, 0x45800000, v8
	v_cndmask_b32_e64 v10, v8, v9, s[4:5]
	v_mul_f32_e32 v6, v6, v10
	v_mul_f32_e32 v6, v60, v6
	v_max_f32_e32 v6, 0xc3e00000, v6
	v_min_f32_e32 v8, 0x43e00000, v6
	s_nop 1
	v_mov_b32_dpp v9, v8 quad_perm:[1,0,3,2] row_mask:0xf bank_mask:0xf
	v_mov_b32_e32 v6, v3
	s_waitcnt lgkmcnt(0)
	v_cvt_pk_fp8_f32 v6, v8, v9
	v_add_u32_e32 v8, 27, v42
	v_ashrrev_i32_e32 v9, 31, v8
	v_lshlrev_b64 v[8:9], 12, v[8:9]
	s_nop 1
	v_mov_b32_dpp v11, v6 quad_perm:[2,3,0,1] row_mask:0xf bank_mask:0xf
	v_lshl_add_u64 v[8:9], v[32:33], 0, v[8:9]
	s_and_saveexec_b64 s[4:5], vcc
	s_cbranch_execz .LBB0_1192
	v_and_b32_e32 v6, 0xffff, v6
	s_waitcnt lgkmcnt(0)
	v_lshl_or_b32 v6, v11, 16, v6
	global_store_dword v[8:9], v6, off
.LBB0_1192:
	s_or_b64 exec, exec, s[4:5]
	v_mul_f32_e32 v6, v7, v10
	v_mul_f32_e32 v6, v62, v6
	v_max_f32_e32 v6, 0xc3e00000, v6
	v_min_f32_e32 v7, 0x43e00000, v6
	s_waitcnt lgkmcnt(0)
	s_nop 1
	v_mov_b32_dpp v11, v7 quad_perm:[1,0,3,2] row_mask:0xf bank_mask:0xf
	v_mov_b32_e32 v6, v3
	s_waitcnt lgkmcnt(0)
	v_cvt_pk_fp8_f32 v6, v7, v11
	s_nop 1
	v_mov_b32_dpp v7, v6 quad_perm:[2,3,0,1] row_mask:0xf bank_mask:0xf
	s_and_saveexec_b64 s[4:5], vcc
	s_cbranch_execz .LBB0_1194
	v_and_b32_e32 v6, 0xffff, v6
	s_waitcnt lgkmcnt(0)
	v_lshl_or_b32 v6, v7, 16, v6
	global_store_dword v[8:9], v6, off offset:32
.LBB0_1194:
	s_or_b64 exec, exec, s[4:5]
	v_mul_f32_e32 v5, v5, v10
	v_mul_f32_e32 v5, v61, v5
	v_max_f32_e32 v5, 0xc3e00000, v5
	v_min_f32_e32 v6, 0x43e00000, v5
	s_waitcnt lgkmcnt(0)
	s_nop 1
	v_mov_b32_dpp v7, v6 quad_perm:[1,0,3,2] row_mask:0xf bank_mask:0xf
	v_mov_b32_e32 v5, v3
	s_waitcnt lgkmcnt(0)
	v_cvt_pk_fp8_f32 v5, v6, v7
	s_nop 1
	v_mov_b32_dpp v6, v5 quad_perm:[2,3,0,1] row_mask:0xf bank_mask:0xf
	s_and_saveexec_b64 s[4:5], vcc
	s_cbranch_execz .LBB0_1196
	v_and_b32_e32 v5, 0xffff, v5
	s_waitcnt lgkmcnt(0)
	v_lshl_or_b32 v5, v6, 16, v5
	global_store_dword v[8:9], v5, off offset:64
.LBB0_1196:
	s_or_b64 exec, exec, s[4:5]
	v_mul_f32_e32 v4, v4, v10
	v_mul_f32_e32 v2, v2, v4
	v_max_f32_e32 v2, 0xc3e00000, v2
	v_min_f32_e32 v4, 0x43e00000, v2
	s_nop 1
	v_mov_b32_dpp v5, v4 quad_perm:[1,0,3,2] row_mask:0xf bank_mask:0xf
	v_mov_b32_e32 v2, v3
	s_waitcnt lgkmcnt(0)
	v_cvt_pk_fp8_f32 v2, v4, v5
	s_nop 1
	v_mov_b32_dpp v4, v2 quad_perm:[2,3,0,1] row_mask:0xf bank_mask:0xf
	s_and_saveexec_b64 s[4:5], vcc
	s_cbranch_execz .LBB0_1198
	v_and_b32_e32 v2, 0xffff, v2
	s_waitcnt lgkmcnt(0)
	v_lshl_or_b32 v2, v4, 16, v2
	global_store_dword v[8:9], v2, off offset:96

; #define SBAR() __builtin_amdgcn_sched_barrier(0)
; __device__ __forceinline__ int crow(int r, int hi) { return (r & 3) + 8 * (r >> 2) + 4 * hi; }
; __device__ __forceinline__ float mul_ns(float a, float b) { float r; asm("v_mul_f32 %0, %1, %2" : "=v"(r) : "v"(a), "v"(b)); return r; }
; __device__ __forceinline__ float fma_ns(float a, float b, float c) { float r; asm("v_fma_f32 %0, %1, %2, %3" : "=v"(r) : "v"(a), "v"(b), "v"(c)); return r; }
; template <class Epi>
; __device__ __forceinline__ void block_wide8(const BlockRef& cur, const bf16* V2, int skv, char* lds, Seam& S, const Epi& E) {
;     ...
;     if (hi == 0) li_l[r32] = l_reg; asm volatile("s_waitcnt lgkmcnt(0)" ::: "memory");
;     float rli[16];
; #pragma unroll
;     for (int r = 0; r < 16; ++r) rli[r] = __builtin_amdgcn_rcpf(li_l[crow(r, hi)]) * (1.0f / 16.0f);
;     __device__ __forceinline__ void operator()(f32x16 (&o)[8], const float (&rli)[16], int wid, int lane, int r32, int hi) const {
;     ...
;             for (int rb = 0; rb < 16; rb += 4) { unsigned tw[4][4];
; #pragma unroll
;                 for (int q = 0; q < 4; ++q)
; #pragma unroll
;                     for (int k = 0; k < 4; ++k) tw[q][k] = (scw + ((rb + q) * 4 + k) * 64)[ul];
;                 asm volatile("" ::: "memory"); SBAR();
; #pragma unroll
;                 for (int q = 0; q < 4; ++q) { const int r = rb + q; float s = 0.f;
; #pragma unroll
;                     for (int d0 = 0; d0 < 8; ++d0) { const float t = __uint_as_float((d0 & 1) ? (tw[q][d0 >> 1] & 0xffff0000u) : (tw[q][d0 >> 1] << 16));
;                         const float dd = fma_ns(nlam, mul_ns(o[d0][r], rli[r]), t); s = fma_ns(dd, dd, s); }
;                     s = half_sum(s); rn[r] = rsqrtf(s * (1.0f / 256.0f) + 1e-5f) * 0.8f; }
.LBB0_1290:
	v_cmp_gt_u32_e32 vcc, 32, v200
	s_and_saveexec_b64 s[4:5], vcc
	v_readlane_b32 s88, v252, 34
	v_readlane_b32 s89, v252, 35
	s_mov_b32 s54, 0x3b800000
	s_mov_b32 s29, s77
	v_lshl_add_u32 v2, v202, 2, s93
	ds_write_b32 v2, v215
	s_or_b64 exec, exec, s[4:5]
	s_waitcnt lgkmcnt(0)
	v_lshl_add_u32 v2, v213, 4, s93
	ds_read_b128 v[4:7], v2
	ds_read_b128 v[8:11], v2 offset:32
	v_readlane_b32 s76, v252, 36
	s_cmp_lg_u32 s30, 0
	v_readlane_b32 s77, v252, 37
	s_waitcnt lgkmcnt(0)
	v_rcp_f32_e32 v4, v4
	v_rcp_f32_e32 v5, v5
	v_rcp_f32_e32 v6, v6
	v_rcp_f32_e32 v7, v7
	v_rcp_f32_e32 v8, v8
	v_mul_f32_e32 v183, 0x3d800000, v4
	v_mul_f32_e32 v182, 0x3d800000, v5
	v_mul_f32_e32 v181, 0x3d800000, v6
	v_mul_f32_e32 v180, 0x3d800000, v7
	v_mul_f32_e32 v179, 0x3d800000, v8
	v_rcp_f32_e32 v8, v9
	v_rcp_f32_e32 v9, v10
	v_rcp_f32_e32 v10, v11
	ds_read_b128 v[4:7], v2 offset:64
	v_mul_f32_e32 v178, 0x3d800000, v8
	v_mul_f32_e32 v177, 0x3d800000, v9
	v_mul_f32_e32 v176, 0x3d800000, v10
	ds_read_b128 v[8:11], v2 offset:96
	s_waitcnt lgkmcnt(0)
	v_rcp_f32_e32 v2, v4
	v_rcp_f32_e32 v4, v5
	v_rcp_f32_e32 v5, v6
	v_rcp_f32_e32 v6, v7
	v_mul_f32_e32 v175, 0x3d800000, v2
	v_mul_f32_e32 v174, 0x3d800000, v4
	v_mul_f32_e32 v173, 0x3d800000, v5
	v_mul_f32_e32 v172, 0x3d800000, v6
	v_rcp_f32_e32 v2, v8
	v_rcp_f32_e32 v4, v9
	v_rcp_f32_e32 v5, v10
	v_rcp_f32_e32 v6, v11
	v_mul_f32_e32 v171, 0x3d800000, v2
	v_mul_f32_e32 v170, 0x3d800000, v4
	v_mul_f32_e32 v169, 0x3d800000, v5
	v_mul_f32_e32 v168, 0x3d800000, v6
	s_cbranch_scc0 .LBB0_1550
	v_readlane_b32 s4, v252, 4
	v_mov_b32_e32 v201, v3
	v_readlane_b32 s5, v252, 5
	s_nop 1
	v_lshl_add_u64 v[4:5], v[200:201], 2, s[4:5]
	global_load_dword v2, v[4:5], off
	global_load_dword v6, v[4:5], off offset:256
	global_load_dword v7, v[4:5], off offset:512
	global_load_dword v8, v[4:5], off offset:768
	global_load_dword v10, v[4:5], off offset:1024
	global_load_dword v11, v[4:5], off offset:1280
	global_load_dword v12, v[4:5], off offset:1536
	global_load_dword v13, v[4:5], off offset:1792
	global_load_dword v14, v[4:5], off offset:2048
	global_load_dword v15, v[4:5], off offset:2304
	global_load_dword v16, v[4:5], off offset:2560
	global_load_dword v17, v[4:5], off offset:2816
	global_load_dword v146, v[4:5], off offset:3072
	global_load_dword v147, v[4:5], off offset:3328
	global_load_dword v148, v[4:5], off offset:3584
	global_load_dword v149, v[4:5], off offset:3840
	s_lshl_b32 s4, s16, 12
	s_add_i32 s86, s4, s86
	s_lshl_b64 s[4:5], s[86:87], 12
	s_add_u32 s4, s88, s4
	s_addc_u32 s5, s89, s5
	s_lshl_b32 s6, s15, 8
	s_add_u32 s8, s4, s6
	s_addc_u32 s9, s5, 0
	v_readlane_b32 s4, v252, 38
	v_readlane_b32 s5, v252, 39
	s_ashr_i32 s5, s4, 31
	s_lshl_b64 s[6:7], s[4:5], 12
	s_waitcnt vmcnt(0)
	v_lshlrev_b32_e32 v9, 16, v2
	v_mul_f32 v192, v130, v183
	v_and_b32_e32 v2, 0xffff0000, v2
	v_fma_f32 v9, v212, v192, v9
	v_mul_f32 v150, v114, v183
	s_nop 0
	v_fma_f32 v9, v9, v9, v3
	v_fma_f32 v2, v212, v150, v2
	v_mul_f32 v150, v98, v183
	s_nop 0
	v_fma_f32 v2, v2, v2, v9
	v_lshlrev_b32_e32 v9, 16, v6
	v_fma_f32 v9, v212, v150, v9
	v_and_b32_e32 v6, 0xffff0000, v6
	v_fma_f32 v2, v9, v9, v2
	v_mul_f32 v9, v82, v183
	s_nop 0
	v_fma_f32 v6, v212, v9, v6
	v_mul_f32 v9, v66, v183
	s_nop 0
	v_fma_f32 v2, v6, v6, v2
	v_lshlrev_b32_e32 v6, 16, v7
	v_fma_f32 v6, v212, v9, v6
	s_nop 0
	v_fma_f32 v2, v6, v6, v2
	v_and_b32_e32 v6, 0xffff0000, v7
	v_mul_f32 v7, v50, v183
	s_nop 0
	v_fma_f32 v6, v212, v7, v6
	v_mul_f32 v7, v34, v183
	s_nop 0
	v_fma_f32 v2, v6, v6, v2
	v_lshlrev_b32_e32 v6, 16, v8
	v_fma_f32 v6, v212, v7, v6
	v_mul_f32 v7, v18, v183
	s_nop 0
	v_fma_f32 v2, v6, v6, v2
	v_and_b32_e32 v6, 0xffff0000, v8
	v_fma_f32 v6, v212, v7, v6
	v_mul_f32 v8, v115, v182
	s_nop 0
	v_fma_f32 v7, v6, v6, v2
	v_lshlrev_b32_e32 v2, 16, v10
	v_mul_f32 v6, v131, v182
	s_nop 1
	v_mov_b32_dpp v9, v7 quad_perm:[1,0,3,2] row_mask:0xf bank_mask:0xf
	v_fma_f32 v2, v212, v6, v2
	v_and_b32_e32 v6, 0xffff0000, v10
	v_fma_f32 v2, v2, v2, v3
	v_fma_f32 v6, v212, v8, v6
	v_mul_f32 v8, v99, v182
	s_nop 0
	v_fma_f32 v2, v6, v6, v2
	v_lshlrev_b32_e32 v6, 16, v11
	v_fma_f32 v6, v212, v8, v6
	v_mul_f32 v8, v83, v182
	s_nop 0
	v_fma_f32 v2, v6, v6, v2
	v_and_b32_e32 v6, 0xffff0000, v11
	v_fma_f32 v6, v212, v8, v6
	v_mul_f32 v8, v67, v182
	s_nop 0
	v_fma_f32 v2, v6, v6, v2
	v_lshlrev_b32_e32 v6, 16, v12
	v_fma_f32 v6, v212, v8, v6
	v_mul_f32 v8, v51, v182
	s_nop 0
	v_fma_f32 v2, v6, v6, v2
	v_and_b32_e32 v6, 0xffff0000, v12
	v_fma_f32 v6, v212, v8, v6
	v_mul_f32 v8, v35, v182
	s_nop 0
	v_fma_f32 v2, v6, v6, v2
	v_lshlrev_b32_e32 v6, 16, v13
	v_fma_f32 v6, v212, v8, v6
	v_mul_f32 v8, v19, v182
	s_nop 0
	v_fma_f32 v2, v6, v6, v2
	v_and_b32_e32 v6, 0xffff0000, v13
	v_fma_f32 v6, v212, v8, v6
	s_nop 0
	v_fma_f32 v6, v6, v6, v2
	s_nop 1
	v_mov_b32_dpp v8, v6 quad_perm:[1,0,3,2] row_mask:0xf bank_mask:0xf
	s_waitcnt lgkmcnt(0)
	v_pk_add_f32 v[6:7], v[6:7], v[8:9]
	s_nop 1
	v_mov_b32_dpp v9, v7 quad_perm:[2,3,0,1] row_mask:0xf bank_mask:0xf
	s_nop 1
	v_mov_b32_dpp v8, v6 quad_perm:[2,3,0,1] row_mask:0xf bank_mask:0xf
	s_waitcnt lgkmcnt(0)
	v_pk_add_f32 v[6:7], v[6:7], v[8:9]
	ds_swizzle_b32 v9, v7 offset:swizzle(SWAP,4)
	ds_swizzle_b32 v8, v6 offset:swizzle(SWAP,4)
	s_waitcnt lgkmcnt(0)
	v_pk_add_f32 v[6:7], v[6:7], v[8:9]
	ds_swizzle_b32 v9, v7 offset:swizzle(SWAP,8)
	ds_swizzle_b32 v8, v6 offset:swizzle(SWAP,8)
	s_waitcnt lgkmcnt(0)
	v_pk_add_f32 v[6:7], v[6:7], v[8:9]
	ds_swizzle_b32 v9, v7 offset:swizzle(SWAP,16)
	ds_swizzle_b32 v8, v6 offset:swizzle(SWAP,16)
	s_waitcnt lgkmcnt(0)
; #define SBAR() __builtin_amdgcn_sched_barrier(0)
; __device__ __forceinline__ float mul_ns(float a, float b) { float r; asm("v_mul_f32 %0, %1, %2" : "=v"(r) : "v"(a), "v"(b)); return r; }
; __device__ __forceinline__ float fma_ns(float a, float b, float c) { float r; asm("v_fma_f32 %0, %1, %2, %3" : "=v"(r) : "v"(a), "v"(b), "v"(c)); return r; }
; __device__ __forceinline__ float half_sum(float s) {
;     s += swz_xor<1>(s); s += swz_xor<2>(s); s += swz_xor<4>(s); s += swz_xor<8>(s); s += swz_xor<16>(s); return s;
; }
;     __device__ __forceinline__ void operator()(f32x16 (&o)[8], const float (&rli)[16], int wid, int lane, int r32, int hi) const {
;     ...
;             for (int rb = 0; rb < 16; rb += 4) { unsigned tw[4][4];
; #pragma unroll
;                 for (int q = 0; q < 4; ++q)
; #pragma unroll
;                     for (int k = 0; k < 4; ++k) tw[q][k] = (scw + ((rb + q) * 4 + k) * 64)[ul];
;                 asm volatile("" ::: "memory"); SBAR();
; #pragma unroll
;                 for (int q = 0; q < 4; ++q) { const int r = rb + q; float s = 0.f;
; #pragma unroll
;                     for (int d0 = 0; d0 < 8; ++d0) { const float t = __uint_as_float((d0 & 1) ? (tw[q][d0 >> 1] & 0xffff0000u) : (tw[q][d0 >> 1] << 16));
;                         const float dd = fma_ns(nlam, mul_ns(o[d0][r], rli[r]), t); s = fma_ns(dd, dd, s); }
;                     s = half_sum(s); rn[r] = rsqrtf(s * (1.0f / 256.0f) + 1e-5f) * 0.8f; }
	v_pk_add_f32 v[6:7], v[6:7], v[8:9]
	s_nop 0
	v_pk_fma_f32 v[164:165], v[6:7], s[54:55], v[198:199] op_sel_hi:[1,0,0]
	v_mul_f32 v7, v116, v181
	v_mul_f32 v8, v117, v180
	s_nop 0
	v_mul_f32_e32 v2, 0x4b800000, v165
	v_cmp_gt_f32_e64 s[4:5], s53, v165
	v_cmp_gt_f32_e32 vcc, s53, v164
	s_nop 0
	v_cndmask_b32_e64 v2, v165, v2, s[4:5]
	v_rsq_f32_e32 v2, v2
	s_nop 0
	v_mul_f32_e32 v6, 0x45800000, v2
	v_cndmask_b32_e64 v2, v2, v6, s[4:5]
	v_mul_f32_e32 v191, 0x3f4ccccd, v2
	v_lshlrev_b32_e32 v2, 16, v14
	v_mul_f32 v6, v132, v181
	s_nop 0
	v_fma_f32 v2, v212, v6, v2
	v_and_b32_e32 v6, 0xffff0000, v14
	v_fma_f32 v2, v2, v2, v3
	v_fma_f32 v6, v212, v7, v6
	v_mul_f32 v7, v100, v181
	s_nop 0
	v_fma_f32 v2, v6, v6, v2
	v_lshlrev_b32_e32 v6, 16, v15
	v_fma_f32 v6, v212, v7, v6
	v_mul_f32 v7, v84, v181
	s_nop 0
	v_fma_f32 v2, v6, v6, v2
	v_and_b32_e32 v6, 0xffff0000, v15
	v_fma_f32 v6, v212, v7, v6
	v_mul_f32 v7, v68, v181
	s_nop 0
	v_fma_f32 v2, v6, v6, v2
	v_lshlrev_b32_e32 v6, 16, v16
	v_fma_f32 v6, v212, v7, v6
	v_mul_f32 v7, v52, v181
	s_nop 0
	v_fma_f32 v2, v6, v6, v2
	v_and_b32_e32 v6, 0xffff0000, v16
	v_fma_f32 v6, v212, v7, v6
	v_mul_f32 v7, v36, v181
	s_nop 0
	v_fma_f32 v2, v6, v6, v2
	v_lshlrev_b32_e32 v6, 16, v17
	v_fma_f32 v6, v212, v7, v6
	v_mul_f32 v7, v20, v181
	s_nop 0
	v_fma_f32 v2, v6, v6, v2
	v_and_b32_e32 v6, 0xffff0000, v17
	v_fma_f32 v6, v212, v7, v6
	s_nop 0
	v_fma_f32 v7, v6, v6, v2
	v_lshlrev_b32_e32 v2, 16, v146
	v_mul_f32 v6, v133, v180
	s_nop 1
	v_mov_b32_dpp v9, v7 quad_perm:[1,0,3,2] row_mask:0xf bank_mask:0xf
	v_fma_f32 v2, v212, v6, v2
	v_and_b32_e32 v6, 0xffff0000, v146
	v_fma_f32 v2, v2, v2, v3
	v_fma_f32 v6, v212, v8, v6
	v_mul_f32 v8, v101, v180
	s_nop 0
	v_fma_f32 v2, v6, v6, v2
	v_lshlrev_b32_e32 v6, 16, v147
	v_fma_f32 v6, v212, v8, v6
	v_mul_f32 v8, v85, v180
	s_nop 0
	v_fma_f32 v2, v6, v6, v2
	v_and_b32_e32 v6, 0xffff0000, v147
	v_fma_f32 v6, v212, v8, v6
	v_mul_f32 v8, v69, v180
	s_nop 0
	v_fma_f32 v2, v6, v6, v2
	v_lshlrev_b32_e32 v6, 16, v148
	v_fma_f32 v6, v212, v8, v6
	v_mul_f32 v8, v53, v180
	s_nop 0
	v_fma_f32 v2, v6, v6, v2
	v_and_b32_e32 v6, 0xffff0000, v148
	v_fma_f32 v6, v212, v8, v6
	v_mul_f32 v8, v37, v180
	s_nop 0
	v_fma_f32 v2, v6, v6, v2
	v_lshlrev_b32_e32 v6, 16, v149
	v_fma_f32 v6, v212, v8, v6
	v_mul_f32 v8, v21, v180
	s_nop 0
	v_fma_f32 v2, v6, v6, v2
	v_and_b32_e32 v6, 0xffff0000, v149
	v_fma_f32 v6, v212, v8, v6
	s_nop 0
	v_fma_f32 v6, v6, v6, v2
	s_nop 1
	v_mov_b32_dpp v8, v6 quad_perm:[1,0,3,2] row_mask:0xf bank_mask:0xf
	s_waitcnt lgkmcnt(0)
	v_pk_add_f32 v[6:7], v[6:7], v[8:9]
	s_nop 1
	v_mov_b32_dpp v9, v7 quad_perm:[2,3,0,1] row_mask:0xf bank_mask:0xf
	s_nop 1
	v_mov_b32_dpp v8, v6 quad_perm:[2,3,0,1] row_mask:0xf bank_mask:0xf
	s_waitcnt lgkmcnt(0)
	v_pk_add_f32 v[6:7], v[6:7], v[8:9]
	ds_swizzle_b32 v9, v7 offset:swizzle(SWAP,4)
	ds_swizzle_b32 v8, v6 offset:swizzle(SWAP,4)
	s_waitcnt lgkmcnt(0)
	v_pk_add_f32 v[6:7], v[6:7], v[8:9]
	ds_swizzle_b32 v9, v7 offset:swizzle(SWAP,8)
	ds_swizzle_b32 v8, v6 offset:swizzle(SWAP,8)
	s_waitcnt lgkmcnt(0)
	v_pk_add_f32 v[160:161], v[6:7], v[8:9]
	ds_swizzle_b32 v163, v161 offset:swizzle(SWAP,16)
	ds_swizzle_b32 v162, v160 offset:swizzle(SWAP,16)
	s_movk_i32 s4, 0x1000
	v_add_co_u32_e64 v8, s[4:5], s4, v4
	s_nop 1
	v_addc_co_u32_e64 v9, s[4:5], 0, v5, s[4:5]
	s_movk_i32 s4, 0x2000
	s_nop 0
	v_add_co_u32_e64 v6, s[4:5], s4, v4
	s_nop 1
	v_addc_co_u32_e64 v7, s[4:5], 0, v5, s[4:5]
	global_load_dword v2, v[8:9], off offset:256
	global_load_dword v10, v[8:9], off offset:512
	global_load_dword v11, v[8:9], off offset:768
	global_load_dword v12, v[8:9], off offset:1024
	global_load_dword v13, v[8:9], off offset:1280
	global_load_dword v14, v[8:9], off offset:1536
	global_load_dword v15, v[8:9], off offset:1792
	global_load_dword v16, v[8:9], off offset:2048
	global_load_dword v17, v[6:7], off offset:-4096
	global_load_dword v146, v[8:9], off offset:2304
	global_load_dword v147, v[8:9], off offset:2560
	global_load_dword v148, v[8:9], off offset:2816
	global_load_dword v149, v[8:9], off offset:3072
	global_load_dword v150, v[8:9], off offset:3328
	global_load_dword v151, v[8:9], off offset:3584
	global_load_dword v152, v[8:9], off offset:3840
	s_waitcnt vmcnt(7)
	v_lshlrev_b32_e32 v8, 16, v17
	v_mul_f32 v9, v134, v179
	s_nop 0
	v_fma_f32 v8, v212, v9, v8
	v_and_b32_e32 v9, 0xffff0000, v17
	v_fma_f32 v8, v8, v8, v3
	v_mul_f32 v17, v118, v179
	s_nop 0
	v_fma_f32 v9, v212, v17, v9
	v_mul_f32 v17, v102, v179
	s_nop 0
	v_fma_f32 v8, v9, v9, v8
	v_lshlrev_b32_e32 v9, 16, v2
	v_fma_f32 v9, v212, v17, v9
	v_and_b32_e32 v2, 0xffff0000, v2
	v_fma_f32 v8, v9, v9, v8
	v_mul_f32 v9, v86, v179
	s_nop 0
	v_fma_f32 v2, v212, v9, v2
	v_mul_f32 v9, v70, v179
	s_nop 0
	v_fma_f32 v2, v2, v2, v8
	v_lshlrev_b32_e32 v8, 16, v10
	v_fma_f32 v8, v212, v9, v8
	v_mul_f32 v9, v54, v179
	s_nop 0
	v_fma_f32 v2, v8, v8, v2
	v_and_b32_e32 v8, 0xffff0000, v10
	v_fma_f32 v8, v212, v9, v8
	v_mul_f32 v9, v38, v179
	v_mul_f32 v10, v119, v178
	s_nop 0
	v_fma_f32 v2, v8, v8, v2
	v_lshlrev_b32_e32 v8, 16, v11
	v_fma_f32 v8, v212, v9, v8
	v_mul_f32 v9, v22, v179
	s_nop 0
	v_fma_f32 v2, v8, v8, v2
	v_and_b32_e32 v8, 0xffff0000, v11
	v_fma_f32 v8, v212, v9, v8
	s_nop 0
	v_fma_f32 v9, v8, v8, v2
	v_lshlrev_b32_e32 v2, 16, v12
	v_mul_f32 v8, v135, v178
	s_nop 1
	v_mov_b32_dpp v11, v9 quad_perm:[1,0,3,2] row_mask:0xf bank_mask:0xf
	v_fma_f32 v2, v212, v8, v2
	v_and_b32_e32 v8, 0xffff0000, v12
	v_fma_f32 v2, v2, v2, v3
	v_fma_f32 v8, v212, v10, v8
	v_mul_f32 v10, v103, v178
	v_mul_f32 v12, v136, v177
	s_nop 0
	v_fma_f32 v2, v8, v8, v2
	v_lshlrev_b32_e32 v8, 16, v13
	v_fma_f32 v8, v212, v10, v8
	v_mul_f32 v10, v87, v178
	s_nop 0
	v_fma_f32 v2, v8, v8, v2
	v_and_b32_e32 v8, 0xffff0000, v13
	v_fma_f32 v8, v212, v10, v8
	v_mul_f32 v10, v71, v178
	v_mul_f32 v13, v120, v177
	s_nop 0
	v_fma_f32 v2, v8, v8, v2
	v_lshlrev_b32_e32 v8, 16, v14
	v_fma_f32 v8, v212, v10, v8
	v_mul_f32 v10, v55, v178
	s_nop 0
	v_fma_f32 v2, v8, v8, v2
	v_and_b32_e32 v8, 0xffff0000, v14
	v_fma_f32 v8, v212, v10, v8
	v_mul_f32 v10, v39, v178
	v_mul_f32 v14, v121, v176
	s_nop 0
	v_fma_f32 v2, v8, v8, v2
	v_lshlrev_b32_e32 v8, 16, v15
	v_fma_f32 v8, v212, v10, v8
	v_mul_f32 v10, v23, v178
	s_nop 0
	v_fma_f32 v2, v8, v8, v2
	v_and_b32_e32 v8, 0xffff0000, v15
	v_fma_f32 v8, v212, v10, v8
	s_nop 0
	v_fma_f32 v8, v8, v8, v2
	v_lshlrev_b32_e32 v2, 16, v16
	v_fma_f32 v2, v212, v12, v2
	v_and_b32_e32 v12, 0xffff0000, v16
	v_fma_f32 v2, v2, v2, v3
	v_fma_f32 v12, v212, v13, v12
	v_mul_f32 v13, v104, v177
	s_nop 1
	v_mov_b32_dpp v10, v8 quad_perm:[1,0,3,2] row_mask:0xf bank_mask:0xf
	v_fma_f32 v2, v12, v12, v2
	s_waitcnt vmcnt(6)
; #define SBAR() __builtin_amdgcn_sched_barrier(0)
; __device__ __forceinline__ float mul_ns(float a, float b) { float r; asm("v_mul_f32 %0, %1, %2" : "=v"(r) : "v"(a), "v"(b)); return r; }
; __device__ __forceinline__ float fma_ns(float a, float b, float c) { float r; asm("v_fma_f32 %0, %1, %2, %3" : "=v"(r) : "v"(a), "v"(b), "v"(c)); return r; }
; __device__ __forceinline__ float half_sum(float s) {
;     s += swz_xor<1>(s); s += swz_xor<2>(s); s += swz_xor<4>(s); s += swz_xor<8>(s); s += swz_xor<16>(s); return s;
; }
;     __device__ __forceinline__ void operator()(f32x16 (&o)[8], const float (&rli)[16], int wid, int lane, int r32, int hi) const {
;     ...
;             for (int rb = 0; rb < 16; rb += 4) { unsigned tw[4][4];
; #pragma unroll
;                 for (int q = 0; q < 4; ++q)
; #pragma unroll
;                     for (int k = 0; k < 4; ++k) tw[q][k] = (scw + ((rb + q) * 4 + k) * 64)[ul];
;                 asm volatile("" ::: "memory"); SBAR();
; #pragma unroll
;                 for (int q = 0; q < 4; ++q) { const int r = rb + q; float s = 0.f;
; #pragma unroll
;                     for (int d0 = 0; d0 < 8; ++d0) { const float t = __uint_as_float((d0 & 1) ? (tw[q][d0 >> 1] & 0xffff0000u) : (tw[q][d0 >> 1] << 16));
;                         const float dd = fma_ns(nlam, mul_ns(o[d0][r], rli[r]), t); s = fma_ns(dd, dd, s); }
;                     s = half_sum(s); rn[r] = rsqrtf(s * (1.0f / 256.0f) + 1e-5f) * 0.8f; }
;                 asm volatile("" ::: "memory"); SBAR(); }
	v_lshlrev_b32_e32 v12, 16, v146
	v_fma_f32 v12, v212, v13, v12
	v_mul_f32 v13, v88, v177
	s_waitcnt lgkmcnt(0)
	v_pk_add_f32 v[8:9], v[8:9], v[10:11]
	v_fma_f32 v2, v12, v12, v2
	v_and_b32_e32 v12, 0xffff0000, v146
	v_fma_f32 v12, v212, v13, v12
	v_mul_f32 v13, v72, v177
	s_nop 1
	v_mov_b32_dpp v11, v9 quad_perm:[2,3,0,1] row_mask:0xf bank_mask:0xf
	v_fma_f32 v2, v12, v12, v2
	s_waitcnt vmcnt(5)
	v_lshlrev_b32_e32 v12, 16, v147
	v_fma_f32 v12, v212, v13, v12
	v_mul_f32 v13, v56, v177
	s_nop 1
	v_mov_b32_dpp v10, v8 quad_perm:[2,3,0,1] row_mask:0xf bank_mask:0xf
	v_fma_f32 v2, v12, v12, v2
	v_and_b32_e32 v12, 0xffff0000, v147
	v_fma_f32 v12, v212, v13, v12
	v_mul_f32 v13, v40, v177
	s_waitcnt lgkmcnt(0)
	v_pk_add_f32 v[8:9], v[8:9], v[10:11]
	v_fma_f32 v2, v12, v12, v2
	s_waitcnt vmcnt(4)
	v_lshlrev_b32_e32 v12, 16, v148
	v_fma_f32 v12, v212, v13, v12
	v_mul_f32 v13, v24, v177
	ds_swizzle_b32 v11, v9 offset:swizzle(SWAP,4)
	v_fma_f32 v2, v12, v12, v2
	v_and_b32_e32 v12, 0xffff0000, v148
	v_fma_f32 v12, v212, v13, v12
	ds_swizzle_b32 v10, v8 offset:swizzle(SWAP,4)
	v_fma_f32 v13, v12, v12, v2
	s_waitcnt vmcnt(3)
	v_lshlrev_b32_e32 v2, 16, v149
	v_mul_f32 v12, v137, v176
	s_nop 1
	v_mov_b32_dpp v15, v13 quad_perm:[1,0,3,2] row_mask:0xf bank_mask:0xf
	v_fma_f32 v2, v212, v12, v2
	v_and_b32_e32 v12, 0xffff0000, v149
	v_fma_f32 v2, v2, v2, v3
	v_fma_f32 v12, v212, v14, v12
	v_mul_f32 v14, v105, v176
	s_waitcnt lgkmcnt(0)
	v_pk_add_f32 v[8:9], v[8:9], v[10:11]
	v_fma_f32 v2, v12, v12, v2
	s_waitcnt vmcnt(2)
	v_lshlrev_b32_e32 v12, 16, v150
	v_fma_f32 v12, v212, v14, v12
	v_mul_f32 v14, v89, v176
	ds_swizzle_b32 v11, v9 offset:swizzle(SWAP,8)
	v_fma_f32 v2, v12, v12, v2
	v_and_b32_e32 v12, 0xffff0000, v150
	v_fma_f32 v12, v212, v14, v12
	v_mul_f32 v14, v73, v176
	ds_swizzle_b32 v10, v8 offset:swizzle(SWAP,8)
	v_fma_f32 v2, v12, v12, v2
	s_waitcnt vmcnt(1)
	v_lshlrev_b32_e32 v12, 16, v151
	v_fma_f32 v12, v212, v14, v12
	v_mul_f32 v14, v57, v176
	s_waitcnt lgkmcnt(0)
	v_pk_add_f32 v[156:157], v[8:9], v[10:11]
	v_fma_f32 v2, v12, v12, v2
	v_and_b32_e32 v12, 0xffff0000, v151
	v_fma_f32 v12, v212, v14, v12
	v_mul_f32 v14, v41, v176
	ds_swizzle_b32 v159, v157 offset:swizzle(SWAP,16)
	v_fma_f32 v2, v12, v12, v2
	s_waitcnt vmcnt(0)
	v_lshlrev_b32_e32 v12, 16, v152
	v_fma_f32 v12, v212, v14, v12
	v_mul_f32 v14, v25, v176
	ds_swizzle_b32 v158, v156 offset:swizzle(SWAP,16)
	v_fma_f32 v2, v12, v12, v2
	v_and_b32_e32 v12, 0xffff0000, v152
	v_fma_f32 v12, v212, v14, v12
	s_nop 0
	v_fma_f32 v12, v12, v12, v2
	s_nop 1
	v_mov_b32_dpp v14, v12 quad_perm:[1,0,3,2] row_mask:0xf bank_mask:0xf
	s_waitcnt lgkmcnt(0)
	v_pk_add_f32 v[12:13], v[12:13], v[14:15]
	s_nop 1
	v_mov_b32_dpp v15, v13 quad_perm:[2,3,0,1] row_mask:0xf bank_mask:0xf
	s_nop 1
	v_mov_b32_dpp v14, v12 quad_perm:[2,3,0,1] row_mask:0xf bank_mask:0xf
	s_waitcnt lgkmcnt(0)
	v_pk_add_f32 v[12:13], v[12:13], v[14:15]
	ds_swizzle_b32 v15, v13 offset:swizzle(SWAP,4)
	ds_swizzle_b32 v14, v12 offset:swizzle(SWAP,4)
	s_waitcnt lgkmcnt(0)
	v_pk_add_f32 v[12:13], v[12:13], v[14:15]
	ds_swizzle_b32 v15, v13 offset:swizzle(SWAP,8)
	ds_swizzle_b32 v14, v12 offset:swizzle(SWAP,8)
	s_waitcnt lgkmcnt(0)
	v_pk_add_f32 v[152:153], v[12:13], v[14:15]
	ds_swizzle_b32 v155, v153 offset:swizzle(SWAP,16)
	ds_swizzle_b32 v154, v152 offset:swizzle(SWAP,16)
	global_load_dword v2, v[6:7], off
	global_load_dword v8, v[6:7], off offset:256
	global_load_dword v9, v[6:7], off offset:512
	global_load_dword v10, v[6:7], off offset:768
	global_load_dword v11, v[6:7], off offset:1024
	global_load_dword v12, v[6:7], off offset:1280
	global_load_dword v13, v[6:7], off offset:1536
	global_load_dword v14, v[6:7], off offset:1792
	global_load_dword v15, v[6:7], off offset:2048
	global_load_dword v16, v[6:7], off offset:2304
	global_load_dword v17, v[6:7], off offset:2560
	global_load_dword v146, v[6:7], off offset:2816
	global_load_dword v147, v[6:7], off offset:3072
	global_load_dword v148, v[6:7], off offset:3328
	global_load_dword v149, v[6:7], off offset:3584
	global_load_dword v150, v[6:7], off offset:3840
	s_waitcnt vmcnt(15)
	v_lshlrev_b32_e32 v6, 16, v2
	v_mul_f32 v7, v138, v175
	v_and_b32_e32 v2, 0xffff0000, v2
	v_fma_f32 v6, v212, v7, v6
	v_mul_f32 v7, v122, v175
	s_nop 0
	v_fma_f32 v6, v6, v6, v3
	v_fma_f32 v2, v212, v7, v2
	v_mul_f32 v7, v106, v175
	s_nop 0
	v_fma_f32 v2, v2, v2, v6
	s_waitcnt vmcnt(14)
	v_lshlrev_b32_e32 v6, 16, v8
	v_fma_f32 v6, v212, v7, v6
	v_mul_f32 v7, v90, v175
	s_nop 0
	v_fma_f32 v2, v6, v6, v2
	v_and_b32_e32 v6, 0xffff0000, v8
	v_fma_f32 v6, v212, v7, v6
	v_mul_f32 v7, v74, v175
	v_mul_f32 v8, v123, v174
	s_nop 0
	v_fma_f32 v2, v6, v6, v2
	s_waitcnt vmcnt(13)
	v_lshlrev_b32_e32 v6, 16, v9
	v_fma_f32 v6, v212, v7, v6
	v_mul_f32 v7, v58, v175
	s_nop 0
	v_fma_f32 v2, v6, v6, v2
	v_and_b32_e32 v6, 0xffff0000, v9
	v_fma_f32 v6, v212, v7, v6
	v_mul_f32 v7, v42, v175
	s_nop 0
	v_fma_f32 v2, v6, v6, v2
	s_waitcnt vmcnt(12)
	v_lshlrev_b32_e32 v6, 16, v10
	v_fma_f32 v6, v212, v7, v6
	v_mul_f32 v7, v26, v175
	s_nop 0
	v_fma_f32 v2, v6, v6, v2
	v_and_b32_e32 v6, 0xffff0000, v10
	v_fma_f32 v6, v212, v7, v6
	v_mul_f32 v10, v140, v173
	s_nop 0
	v_fma_f32 v7, v6, v6, v2
	s_waitcnt vmcnt(11)
	v_lshlrev_b32_e32 v2, 16, v11
	v_mul_f32 v6, v139, v174
	s_nop 1
	v_mov_b32_dpp v9, v7 quad_perm:[1,0,3,2] row_mask:0xf bank_mask:0xf
	v_fma_f32 v2, v212, v6, v2
	v_and_b32_e32 v6, 0xffff0000, v11
	v_fma_f32 v2, v2, v2, v3
	v_fma_f32 v6, v212, v8, v6
	v_mul_f32 v8, v107, v174
	v_mul_f32 v11, v124, v173
	s_nop 0
	v_fma_f32 v2, v6, v6, v2
	s_waitcnt vmcnt(10)
; #define SBAR() __builtin_amdgcn_sched_barrier(0)
; __device__ __forceinline__ float mul_ns(float a, float b) { float r; asm("v_mul_f32 %0, %1, %2" : "=v"(r) : "v"(a), "v"(b)); return r; }
; __device__ __forceinline__ float fma_ns(float a, float b, float c) { float r; asm("v_fma_f32 %0, %1, %2, %3" : "=v"(r) : "v"(a), "v"(b), "v"(c)); return r; }
; __device__ __forceinline__ float half_sum(float s) {
;     s += swz_xor<1>(s); s += swz_xor<2>(s); s += swz_xor<4>(s); s += swz_xor<8>(s); s += swz_xor<16>(s); return s;
; }
;     __device__ __forceinline__ void operator()(f32x16 (&o)[8], const float (&rli)[16], int wid, int lane, int r32, int hi) const {
;     ...
;             for (int rb = 0; rb < 16; rb += 4) { unsigned tw[4][4];
; #pragma unroll
;                 for (int q = 0; q < 4; ++q)
; #pragma unroll
;                     for (int k = 0; k < 4; ++k) tw[q][k] = (scw + ((rb + q) * 4 + k) * 64)[ul];
;                 asm volatile("" ::: "memory"); SBAR();
; #pragma unroll
;                 for (int q = 0; q < 4; ++q) { const int r = rb + q; float s = 0.f;
; #pragma unroll
;                     for (int d0 = 0; d0 < 8; ++d0) { const float t = __uint_as_float((d0 & 1) ? (tw[q][d0 >> 1] & 0xffff0000u) : (tw[q][d0 >> 1] << 16));
;                         const float dd = fma_ns(nlam, mul_ns(o[d0][r], rli[r]), t); s = fma_ns(dd, dd, s); }
;                     s = half_sum(s); rn[r] = rsqrtf(s * (1.0f / 256.0f) + 1e-5f) * 0.8f; }
;                 asm volatile("" ::: "memory"); SBAR(); }
	v_lshlrev_b32_e32 v6, 16, v12
	v_fma_f32 v6, v212, v8, v6
	v_mul_f32 v8, v91, v174
	s_nop 0
	v_fma_f32 v2, v6, v6, v2
	v_and_b32_e32 v6, 0xffff0000, v12
	v_fma_f32 v6, v212, v8, v6
	v_mul_f32 v8, v75, v174
	v_mul_f32 v12, v125, v172
	s_nop 0
	v_fma_f32 v2, v6, v6, v2
	s_waitcnt vmcnt(9)
	v_lshlrev_b32_e32 v6, 16, v13
	v_fma_f32 v6, v212, v8, v6
	v_mul_f32 v8, v59, v174
	s_nop 0
	v_fma_f32 v2, v6, v6, v2
	v_and_b32_e32 v6, 0xffff0000, v13
	v_fma_f32 v6, v212, v8, v6
	v_mul_f32 v8, v43, v174
	s_nop 0
	v_fma_f32 v2, v6, v6, v2
	s_waitcnt vmcnt(8)
	v_lshlrev_b32_e32 v6, 16, v14
	v_fma_f32 v6, v212, v8, v6
	v_mul_f32 v8, v27, v174
	s_nop 0
	v_fma_f32 v2, v6, v6, v2
	v_and_b32_e32 v6, 0xffff0000, v14
	v_fma_f32 v6, v212, v8, v6
	s_nop 0
	v_fma_f32 v6, v6, v6, v2
	s_waitcnt vmcnt(7)
	v_lshlrev_b32_e32 v2, 16, v15
	v_fma_f32 v2, v212, v10, v2
	v_and_b32_e32 v10, 0xffff0000, v15
	v_fma_f32 v2, v2, v2, v3
	v_fma_f32 v10, v212, v11, v10
	v_mul_f32 v11, v108, v173
	s_nop 1
	v_mov_b32_dpp v8, v6 quad_perm:[1,0,3,2] row_mask:0xf bank_mask:0xf
	v_fma_f32 v2, v10, v10, v2
	s_waitcnt vmcnt(6)
	v_lshlrev_b32_e32 v10, 16, v16
	v_fma_f32 v10, v212, v11, v10
	v_mul_f32 v11, v92, v173
	s_waitcnt lgkmcnt(0)
	v_pk_add_f32 v[6:7], v[6:7], v[8:9]
	v_fma_f32 v2, v10, v10, v2
	v_and_b32_e32 v10, 0xffff0000, v16
	v_fma_f32 v10, v212, v11, v10
	v_mul_f32 v11, v76, v173
	s_nop 1
	v_mov_b32_dpp v9, v7 quad_perm:[2,3,0,1] row_mask:0xf bank_mask:0xf
	v_fma_f32 v2, v10, v10, v2
	s_waitcnt vmcnt(5)
	v_lshlrev_b32_e32 v10, 16, v17
	v_fma_f32 v10, v212, v11, v10
	v_mul_f32 v11, v60, v173
	s_nop 1
	v_mov_b32_dpp v8, v6 quad_perm:[2,3,0,1] row_mask:0xf bank_mask:0xf
	v_fma_f32 v2, v10, v10, v2
	v_and_b32_e32 v10, 0xffff0000, v17
	v_fma_f32 v10, v212, v11, v10
	v_mul_f32 v11, v44, v173
	s_waitcnt lgkmcnt(0)
	v_pk_add_f32 v[6:7], v[6:7], v[8:9]
	v_fma_f32 v2, v10, v10, v2
	s_waitcnt vmcnt(4)
	v_lshlrev_b32_e32 v10, 16, v146
	v_fma_f32 v10, v212, v11, v10
	v_mul_f32 v11, v28, v173
	ds_swizzle_b32 v9, v7 offset:swizzle(SWAP,4)
	v_fma_f32 v2, v10, v10, v2
	v_and_b32_e32 v10, 0xffff0000, v146
	v_fma_f32 v10, v212, v11, v10
	ds_swizzle_b32 v8, v6 offset:swizzle(SWAP,4)
	v_fma_f32 v11, v10, v10, v2
	s_waitcnt vmcnt(3)
	v_lshlrev_b32_e32 v2, 16, v147
	v_mul_f32 v10, v141, v172
	s_nop 1
	v_mov_b32_dpp v13, v11 quad_perm:[1,0,3,2] row_mask:0xf bank_mask:0xf
	v_fma_f32 v2, v212, v10, v2
	v_and_b32_e32 v10, 0xffff0000, v147
	v_fma_f32 v2, v2, v2, v3
	v_fma_f32 v10, v212, v12, v10
	v_mul_f32 v12, v109, v172
	s_waitcnt lgkmcnt(0)
	v_pk_add_f32 v[6:7], v[6:7], v[8:9]
	v_fma_f32 v2, v10, v10, v2
	s_waitcnt vmcnt(2)
	v_lshlrev_b32_e32 v10, 16, v148
	v_fma_f32 v10, v212, v12, v10
	v_mul_f32 v12, v93, v172
	ds_swizzle_b32 v9, v7 offset:swizzle(SWAP,8)
	v_fma_f32 v2, v10, v10, v2
	v_and_b32_e32 v10, 0xffff0000, v148
	v_fma_f32 v10, v212, v12, v10
	v_mul_f32 v12, v77, v172
	ds_swizzle_b32 v8, v6 offset:swizzle(SWAP,8)
	v_fma_f32 v2, v10, v10, v2
	s_waitcnt vmcnt(1)
	v_lshlrev_b32_e32 v10, 16, v149
	v_fma_f32 v10, v212, v12, v10
	v_mul_f32 v12, v61, v172
	s_nop 0
	v_fma_f32 v2, v10, v10, v2
	v_and_b32_e32 v10, 0xffff0000, v149
	v_fma_f32 v10, v212, v12, v10
	v_mul_f32 v12, v45, v172
	s_waitcnt lgkmcnt(0)
	v_pk_add_f32 v[148:149], v[6:7], v[8:9]
	v_fma_f32 v2, v10, v10, v2
	s_waitcnt vmcnt(0)
	v_lshlrev_b32_e32 v10, 16, v150
	v_fma_f32 v10, v212, v12, v10
	v_mul_f32 v12, v29, v172
	ds_swizzle_b32 v151, v149 offset:swizzle(SWAP,16)
	v_fma_f32 v2, v10, v10, v2
	v_and_b32_e32 v10, 0xffff0000, v150
	v_fma_f32 v10, v212, v12, v10
	ds_swizzle_b32 v150, v148 offset:swizzle(SWAP,16)
	v_fma_f32 v10, v10, v10, v2
	s_nop 1
	v_mov_b32_dpp v12, v10 quad_perm:[1,0,3,2] row_mask:0xf bank_mask:0xf
	s_waitcnt lgkmcnt(0)
	v_pk_add_f32 v[10:11], v[10:11], v[12:13]
	s_nop 1
	v_mov_b32_dpp v13, v11 quad_perm:[2,3,0,1] row_mask:0xf bank_mask:0xf
	s_nop 1
	v_mov_b32_dpp v12, v10 quad_perm:[2,3,0,1] row_mask:0xf bank_mask:0xf
	s_waitcnt lgkmcnt(0)
	v_pk_add_f32 v[10:11], v[10:11], v[12:13]
	ds_swizzle_b32 v13, v11 offset:swizzle(SWAP,4)
	ds_swizzle_b32 v12, v10 offset:swizzle(SWAP,4)
	s_waitcnt lgkmcnt(0)
	v_pk_add_f32 v[10:11], v[10:11], v[12:13]
	ds_swizzle_b32 v13, v11 offset:swizzle(SWAP,8)
	ds_swizzle_b32 v12, v10 offset:swizzle(SWAP,8)
	s_waitcnt lgkmcnt(0)
	v_pk_add_f32 v[16:17], v[10:11], v[12:13]
	ds_swizzle_b32 v147, v17 offset:swizzle(SWAP,16)
	ds_swizzle_b32 v146, v16 offset:swizzle(SWAP,16)
	s_movk_i32 s4, 0x3000
	v_add_co_u32_e64 v6, s[4:5], s4, v4
	s_nop 1
	v_addc_co_u32_e64 v7, s[4:5], 0, v5, s[4:5]
	global_load_dword v2, v[6:7], off
	global_load_dword v8, v[6:7], off offset:256
	global_load_dword v9, v[6:7], off offset:512
	global_load_dword v10, v[6:7], off offset:768
	global_load_dword v11, v[6:7], off offset:1024
	global_load_dword v12, v[6:7], off offset:1280
	global_load_dword v13, v[6:7], off offset:1536
	global_load_dword v14, v[6:7], off offset:1792
	global_load_dword v15, v[6:7], off offset:2048
	global_load_dword v165, v[6:7], off offset:2304
	global_load_dword v166, v[6:7], off offset:2560
	global_load_dword v167, v[6:7], off offset:2816
	global_load_dword v184, v[6:7], off offset:3072
	global_load_dword v185, v[6:7], off offset:3328
	global_load_dword v186, v[6:7], off offset:3584
	global_load_dword v187, v[6:7], off offset:3840
	s_waitcnt vmcnt(15)
	v_lshlrev_b32_e32 v6, 16, v2
	v_mul_f32 v7, v142, v171
	v_and_b32_e32 v2, 0xffff0000, v2
	v_fma_f32 v6, v212, v7, v6
	v_mul_f32 v7, v126, v171
	s_nop 0
	v_fma_f32 v6, v6, v6, v3
	v_fma_f32 v2, v212, v7, v2
	v_mul_f32 v7, v110, v171
	s_nop 0
	v_fma_f32 v2, v2, v2, v6
	s_waitcnt vmcnt(14)
; #define SBAR() __builtin_amdgcn_sched_barrier(0)
; __device__ __forceinline__ float mul_ns(float a, float b) { float r; asm("v_mul_f32 %0, %1, %2" : "=v"(r) : "v"(a), "v"(b)); return r; }
; __device__ __forceinline__ float fma_ns(float a, float b, float c) { float r; asm("v_fma_f32 %0, %1, %2, %3" : "=v"(r) : "v"(a), "v"(b), "v"(c)); return r; }
; __device__ __forceinline__ float half_sum(float s) {
;     s += swz_xor<1>(s); s += swz_xor<2>(s); s += swz_xor<4>(s); s += swz_xor<8>(s); s += swz_xor<16>(s); return s;
; }
;     __device__ __forceinline__ void operator()(f32x16 (&o)[8], const float (&rli)[16], int wid, int lane, int r32, int hi) const {
;     ...
;             for (int rb = 0; rb < 16; rb += 4) { unsigned tw[4][4];
; #pragma unroll
;                 for (int q = 0; q < 4; ++q)
; #pragma unroll
;                     for (int k = 0; k < 4; ++k) tw[q][k] = (scw + ((rb + q) * 4 + k) * 64)[ul];
;                 asm volatile("" ::: "memory"); SBAR();
; #pragma unroll
;                 for (int q = 0; q < 4; ++q) { const int r = rb + q; float s = 0.f;
; #pragma unroll
;                     for (int d0 = 0; d0 < 8; ++d0) { const float t = __uint_as_float((d0 & 1) ? (tw[q][d0 >> 1] & 0xffff0000u) : (tw[q][d0 >> 1] << 16));
;                         const float dd = fma_ns(nlam, mul_ns(o[d0][r], rli[r]), t); s = fma_ns(dd, dd, s); }
;                     s = half_sum(s); rn[r] = rsqrtf(s * (1.0f / 256.0f) + 1e-5f) * 0.8f; }
;                 asm volatile("" ::: "memory"); SBAR(); }
	v_lshlrev_b32_e32 v6, 16, v8
	v_fma_f32 v6, v212, v7, v6
	v_mul_f32 v7, v94, v171
	s_nop 0
	v_fma_f32 v2, v6, v6, v2
	v_and_b32_e32 v6, 0xffff0000, v8
	v_fma_f32 v6, v212, v7, v6
	v_mul_f32 v7, v78, v171
	v_mul_f32 v8, v127, v170
	s_nop 0
	v_fma_f32 v2, v6, v6, v2
	s_waitcnt vmcnt(13)
	v_lshlrev_b32_e32 v6, 16, v9
	v_fma_f32 v6, v212, v7, v6
	v_mul_f32 v7, v62, v171
	s_nop 0
	v_fma_f32 v2, v6, v6, v2
	v_and_b32_e32 v6, 0xffff0000, v9
	v_fma_f32 v6, v212, v7, v6
	v_mul_f32 v7, v46, v171
	s_nop 0
	v_fma_f32 v2, v6, v6, v2
	s_waitcnt vmcnt(12)
	v_lshlrev_b32_e32 v6, 16, v10
	v_fma_f32 v6, v212, v7, v6
	v_mul_f32 v7, v30, v171
	s_nop 0
	v_fma_f32 v2, v6, v6, v2
	v_and_b32_e32 v6, 0xffff0000, v10
	v_fma_f32 v6, v212, v7, v6
	v_mul_f32 v10, v144, v169
	s_nop 0
	v_fma_f32 v7, v6, v6, v2
	s_waitcnt vmcnt(11)
	v_lshlrev_b32_e32 v2, 16, v11
	v_mul_f32 v6, v143, v170
	s_nop 1
	v_mov_b32_dpp v9, v7 quad_perm:[1,0,3,2] row_mask:0xf bank_mask:0xf
	v_fma_f32 v2, v212, v6, v2
	v_and_b32_e32 v6, 0xffff0000, v11
	v_fma_f32 v2, v2, v2, v3
	v_fma_f32 v6, v212, v8, v6
	v_mul_f32 v8, v111, v170
	v_mul_f32 v11, v128, v169
	s_nop 0
	v_fma_f32 v2, v6, v6, v2
	s_waitcnt vmcnt(10)
	v_lshlrev_b32_e32 v6, 16, v12
	v_fma_f32 v6, v212, v8, v6
	v_mul_f32 v8, v95, v170
	s_nop 0
	v_fma_f32 v2, v6, v6, v2
	v_and_b32_e32 v6, 0xffff0000, v12
	v_fma_f32 v6, v212, v8, v6
	v_mul_f32 v8, v79, v170
	v_mul_f32 v12, v129, v168
	s_nop 0
	v_fma_f32 v2, v6, v6, v2
	s_waitcnt vmcnt(9)
	v_lshlrev_b32_e32 v6, 16, v13
	v_fma_f32 v6, v212, v8, v6
	v_mul_f32 v8, v63, v170
	s_nop 0
	v_fma_f32 v2, v6, v6, v2
	v_and_b32_e32 v6, 0xffff0000, v13
	v_fma_f32 v6, v212, v8, v6
	v_mul_f32 v8, v47, v170
	s_nop 0
	v_fma_f32 v2, v6, v6, v2
	s_waitcnt vmcnt(8)
	v_lshlrev_b32_e32 v6, 16, v14
	v_fma_f32 v6, v212, v8, v6
	v_mul_f32 v8, v31, v170
	s_nop 0
	v_fma_f32 v2, v6, v6, v2
	v_and_b32_e32 v6, 0xffff0000, v14
	v_fma_f32 v6, v212, v8, v6
	s_nop 0
	v_fma_f32 v6, v6, v6, v2
	s_waitcnt vmcnt(7)
	v_lshlrev_b32_e32 v2, 16, v15
	v_fma_f32 v2, v212, v10, v2
	v_and_b32_e32 v10, 0xffff0000, v15
	v_fma_f32 v2, v2, v2, v3
	v_fma_f32 v10, v212, v11, v10
	v_mul_f32 v11, v112, v169
	s_nop 1
	v_mov_b32_dpp v8, v6 quad_perm:[1,0,3,2] row_mask:0xf bank_mask:0xf
	v_fma_f32 v2, v10, v10, v2
	s_waitcnt vmcnt(6)
	v_lshlrev_b32_e32 v10, 16, v165
	v_fma_f32 v10, v212, v11, v10
	v_mul_f32 v11, v96, v169
	s_waitcnt lgkmcnt(0)
	v_pk_add_f32 v[6:7], v[6:7], v[8:9]
	v_fma_f32 v2, v10, v10, v2
	v_and_b32_e32 v10, 0xffff0000, v165
	v_fma_f32 v10, v212, v11, v10
	v_mul_f32 v11, v80, v169
	s_nop 1
	v_mov_b32_dpp v9, v7 quad_perm:[2,3,0,1] row_mask:0xf bank_mask:0xf
	v_fma_f32 v2, v10, v10, v2
	s_waitcnt vmcnt(5)
	v_lshlrev_b32_e32 v10, 16, v166
	v_fma_f32 v10, v212, v11, v10
	v_mul_f32 v11, v64, v169
	s_nop 1
	v_mov_b32_dpp v8, v6 quad_perm:[2,3,0,1] row_mask:0xf bank_mask:0xf
	v_fma_f32 v2, v10, v10, v2
	v_and_b32_e32 v10, 0xffff0000, v166
	v_fma_f32 v10, v212, v11, v10
	v_mul_f32 v11, v48, v169
	s_waitcnt lgkmcnt(0)
	v_pk_add_f32 v[6:7], v[6:7], v[8:9]
	v_fma_f32 v2, v10, v10, v2
	s_waitcnt vmcnt(4)
	v_lshlrev_b32_e32 v10, 16, v167
	v_fma_f32 v10, v212, v11, v10
	v_mul_f32 v11, v32, v169
	ds_swizzle_b32 v9, v7 offset:swizzle(SWAP,4)
	v_fma_f32 v2, v10, v10, v2
	v_and_b32_e32 v10, 0xffff0000, v167
	v_fma_f32 v10, v212, v11, v10
	ds_swizzle_b32 v8, v6 offset:swizzle(SWAP,4)
	v_fma_f32 v11, v10, v10, v2
	s_waitcnt vmcnt(3)
	v_lshlrev_b32_e32 v2, 16, v184
	v_mul_f32 v10, v145, v168
	s_nop 1
	v_mov_b32_dpp v13, v11 quad_perm:[1,0,3,2] row_mask:0xf bank_mask:0xf
	v_fma_f32 v2, v212, v10, v2
	v_and_b32_e32 v10, 0xffff0000, v184
	v_fma_f32 v2, v2, v2, v3
	v_fma_f32 v10, v212, v12, v10
	v_mul_f32 v12, v113, v168
	s_waitcnt lgkmcnt(0)
	v_pk_add_f32 v[6:7], v[6:7], v[8:9]
	v_fma_f32 v2, v10, v10, v2
	s_waitcnt vmcnt(2)
	v_lshlrev_b32_e32 v10, 16, v185
	v_fma_f32 v10, v212, v12, v10
	v_mul_f32 v12, v97, v168
	ds_swizzle_b32 v9, v7 offset:swizzle(SWAP,8)
	v_fma_f32 v2, v10, v10, v2
	v_and_b32_e32 v10, 0xffff0000, v185
	v_fma_f32 v10, v212, v12, v10
	v_mul_f32 v12, v81, v168
	ds_swizzle_b32 v8, v6 offset:swizzle(SWAP,8)
	v_fma_f32 v2, v10, v10, v2
	s_waitcnt vmcnt(1)
	v_lshlrev_b32_e32 v10, 16, v186
	v_fma_f32 v10, v212, v12, v10
	v_mul_f32 v12, v65, v168
	s_nop 0
	v_fma_f32 v2, v10, v10, v2
	v_and_b32_e32 v10, 0xffff0000, v186
	v_fma_f32 v10, v212, v12, v10
	v_mul_f32 v12, v49, v168
	s_nop 0
	v_fma_f32 v2, v10, v10, v2
	s_waitcnt vmcnt(0)
	v_lshlrev_b32_e32 v10, 16, v187
	v_fma_f32 v10, v212, v12, v10
	v_mul_f32 v12, v33, v168
	s_nop 0
	v_fma_f32 v2, v10, v10, v2
	v_and_b32_e32 v10, 0xffff0000, v187
	v_fma_f32 v10, v212, v12, v10
	s_nop 0
	v_fma_f32 v10, v10, v10, v2
	s_nop 1
	v_mov_b32_dpp v12, v10 quad_perm:[1,0,3,2] row_mask:0xf bank_mask:0xf
	s_waitcnt lgkmcnt(0)
	v_pk_add_f32 v[10:11], v[10:11], v[12:13]
	s_nop 1
	v_mov_b32_dpp v13, v11 quad_perm:[2,3,0,1] row_mask:0xf bank_mask:0xf
	s_nop 1
	v_mov_b32_dpp v12, v10 quad_perm:[2,3,0,1] row_mask:0xf bank_mask:0xf
	s_waitcnt lgkmcnt(0)
	v_pk_add_f32 v[10:11], v[10:11], v[12:13]
	ds_swizzle_b32 v13, v11 offset:swizzle(SWAP,4)
	ds_swizzle_b32 v12, v10 offset:swizzle(SWAP,4)
	s_waitcnt lgkmcnt(0)
	v_pk_add_f32 v[10:11], v[10:11], v[12:13]
	ds_swizzle_b32 v167, v11 offset:swizzle(SWAP,8)
	ds_swizzle_b32 v166, v10 offset:swizzle(SWAP,8)
	v_pk_add_f32 v[12:13], v[6:7], v[8:9]
	ds_swizzle_b32 v15, v13 offset:swizzle(SWAP,16)
	ds_swizzle_b32 v14, v12 offset:swizzle(SWAP,16)
	s_waitcnt lgkmcnt(0)
; #define SBAR() __builtin_amdgcn_sched_barrier(0)
; __device__ __forceinline__ int crow(int r, int hi) { return (r & 3) + 8 * (r >> 2) + 4 * hi; }
; __device__ __forceinline__ float mul_ns(float a, float b) { float r; asm("v_mul_f32 %0, %1, %2" : "=v"(r) : "v"(a), "v"(b)); return r; }
; __device__ __forceinline__ float fma_ns(float a, float b, float c) { float r; asm("v_fma_f32 %0, %1, %2, %3" : "=v"(r) : "v"(a), "v"(b), "v"(c)); return r; }
; __device__ __forceinline__ void store_quad8(unsigned char* p, float v, int r32) {
;     v = fminf(fmaxf(v, -448.f), 448.f);
;     const float v1 = swz_xor<1>(v);
;     const int w = __builtin_amdgcn_cvt_pk_fp8_f32(v, v1, 0, false);
;     const int w2 = __builtin_amdgcn_ds_swizzle(w, (2 << 10) | 0x1f);
;     if ((r32 & 3) == 0) *(unsigned*)p = ((unsigned)w & 0xffffu) | ((unsigned)w2 << 16);
; }
;     __device__ __forceinline__ void operator()(f32x16 (&o)[8], const float (&rli)[16], int wid, int lane, int r32, int hi) const {
;     ...
;             float g[8];
; #pragma unroll
;             for (int d0 = 0; d0 < 8; ++d0) g[d0] = gain[d0 * 32 + r32];
; #pragma unroll
;             for (int rb = 0; rb < 16; rb += 4) { unsigned tw[4][4];
; #pragma unroll
;                 for (int q = 0; q < 4; ++q)
; #pragma unroll
;                     for (int k = 0; k < 4; ++k) tw[q][k] = (scw + ((rb + q) * 4 + k) * 64)[ul];
;                 asm volatile("" ::: "memory"); SBAR();
; #pragma unroll
;                 for (int q = 0; q < 4; ++q) { const int r = rb + q;
; #pragma unroll
;                     for (int d0 = 0; d0 < 8; ++d0) { const float t = __uint_as_float((d0 & 1) ? (tw[q][d0 >> 1] & 0xffff0000u) : (tw[q][d0 >> 1] << 16));
;                         const float dd = fma_ns(nlam, mul_ns(o[d0][r], rli[r]), t);
;                         store_quad8(base + (crow(r, 0) * 4096 + d0 * 32) + uo, mul_ns(mul_ns(dd, rn[r]), g[d0]), r32); } }
	v_pk_add_f32 v[8:9], v[10:11], v[166:167]
	ds_swizzle_b32 v11, v9 offset:swizzle(SWAP,16)
	ds_swizzle_b32 v10, v8 offset:swizzle(SWAP,16)
	v_readlane_b32 s12, v253, 10
	v_ashrrev_i32_e32 v203, 31, v202
	v_readlane_b32 s14, v253, 12
	v_readlane_b32 s15, v253, 13
	s_add_u32 s6, s8, s6
	s_addc_u32 s7, s9, s7
	v_lshl_add_u64 v[6:7], v[202:203], 2, s[14:15]
	global_load_dword v190, v[6:7], off
	global_load_dword v189, v[6:7], off offset:128
	global_load_dword v188, v[6:7], off offset:256
	global_load_dword v187, v[6:7], off offset:384
	global_load_dword v186, v[6:7], off offset:512
	global_load_dword v185, v[6:7], off offset:640
	global_load_dword v184, v[6:7], off offset:768
	global_load_dword v165, v[6:7], off offset:896
	global_load_dword v217, v[4:5], off
	global_load_dword v215, v[4:5], off offset:256
	global_load_dword v214, v[4:5], off offset:512
	global_load_dword v209, v[4:5], off offset:768
	global_load_dword v208, v[4:5], off offset:1024
	global_load_dword v207, v[4:5], off offset:1280
	global_load_dword v206, v[4:5], off offset:1536
	global_load_dword v205, v[4:5], off offset:1792
	global_load_dword v204, v[4:5], off offset:2048
	global_load_dword v203, v[4:5], off offset:2304
	global_load_dword v201, v[4:5], off offset:2560
	global_load_dword v197, v[4:5], off offset:2816
	global_load_dword v196, v[4:5], off offset:3072
	global_load_dword v195, v[4:5], off offset:3328
	global_load_dword v194, v[4:5], off offset:3584
	global_load_dword v193, v[4:5], off offset:3840
	v_lshl_add_u32 v2, v213, 14, v202
	v_and_b32_e32 v6, 3, v202
	v_lshl_add_u64 v[166:167], s[6:7], 0, v[2:3]
	s_mov_b64 s[6:7], 0x800
	v_cmp_eq_u32_e64 s[4:5], 0, v6
	v_lshl_add_u64 v[6:7], v[166:167], 0, s[6:7]
	v_readlane_b32 s13, v253, 11
	v_readlane_b32 s16, v253, 14
	v_readlane_b32 s17, v253, 15
	v_readlane_b32 s18, v253, 16
	v_readlane_b32 s19, v253, 17
	v_readlane_b32 s20, v253, 18
	v_readlane_b32 s21, v253, 19
	v_readlane_b32 s22, v253, 20
	v_readlane_b32 s23, v253, 21
	v_readlane_b32 s24, v253, 22
	v_readlane_b32 s25, v253, 23
	v_readlane_b32 s26, v253, 24
	v_readlane_b32 s27, v253, 25
	s_waitcnt vmcnt(15)
	v_lshlrev_b32_e32 v2, 16, v217
	v_fma_f32 v2, v212, v192, v2
	s_nop 0
	v_mul_f32 v2, v2, v191
	s_nop 0
	v_mul_f32 v2, v2, v190
	s_nop 0
	v_max_f32_e32 v2, v2, v2
	v_max_f32_e32 v2, 0xc3e00000, v2
	v_min_f32_e32 v192, 0x43e00000, v2
	s_nop 1
	v_mov_b32_dpp v202, v192 quad_perm:[1,0,3,2] row_mask:0xf bank_mask:0xf
	v_mov_b32_e32 v2, v3
	s_waitcnt lgkmcnt(0)
	v_cvt_pk_fp8_f32 v2, v192, v202
	s_nop 1
	v_mov_b32_dpp v192, v2 quad_perm:[2,3,0,1] row_mask:0xf bank_mask:0xf
	s_and_saveexec_b64 s[6:7], s[4:5]
	s_cbranch_execz .LBB0_1295
	v_and_b32_e32 v2, 0xffff, v2
	s_waitcnt lgkmcnt(0)
	v_lshl_or_b32 v2, v192, 16, v2
	global_store_dword v[6:7], v2, off
.LBB0_1295:
	s_or_b64 exec, exec, s[6:7]
	v_and_b32_e32 v2, 0xffff0000, v217
	s_waitcnt lgkmcnt(0)
	v_mul_f32 v192, v114, v183
	s_nop 0
	v_fma_f32 v2, v212, v192, v2
	s_nop 0
	v_mul_f32 v2, v2, v191
	s_nop 0
	v_mul_f32 v2, v2, v189
	s_nop 0
	v_max_f32_e32 v2, v2, v2
	v_max_f32_e32 v2, 0xc3e00000, v2
	v_min_f32_e32 v192, 0x43e00000, v2
	s_nop 1
	v_mov_b32_dpp v202, v192 quad_perm:[1,0,3,2] row_mask:0xf bank_mask:0xf
	v_mov_b32_e32 v2, v3
	s_waitcnt lgkmcnt(0)
	v_cvt_pk_fp8_f32 v2, v192, v202
	s_nop 1
	v_mov_b32_dpp v192, v2 quad_perm:[2,3,0,1] row_mask:0xf bank_mask:0xf
	s_and_saveexec_b64 s[6:7], s[4:5]
	s_cbranch_execz .LBB0_1297
	v_and_b32_e32 v2, 0xffff, v2
	s_waitcnt lgkmcnt(0)
	v_lshl_or_b32 v2, v192, 16, v2
	global_store_dword v[166:167], v2, off offset:2080
.LBB0_1297:
	s_or_b64 exec, exec, s[6:7]
	s_waitcnt vmcnt(14)
	v_lshlrev_b32_e32 v2, 16, v215
	s_waitcnt lgkmcnt(0)
	v_mul_f32 v192, v98, v183
	s_nop 0
	v_fma_f32 v2, v212, v192, v2
	s_nop 0
	v_mul_f32 v2, v2, v191
	s_nop 0
	v_mul_f32 v2, v2, v188
	s_nop 0
	v_max_f32_e32 v2, v2, v2
	v_max_f32_e32 v2, 0xc3e00000, v2
	v_min_f32_e32 v192, 0x43e00000, v2
	s_nop 1
	v_mov_b32_dpp v202, v192 quad_perm:[1,0,3,2] row_mask:0xf bank_mask:0xf
	v_mov_b32_e32 v2, v3
	s_waitcnt lgkmcnt(0)
	v_cvt_pk_fp8_f32 v2, v192, v202
	s_nop 1
	v_mov_b32_dpp v192, v2 quad_perm:[2,3,0,1] row_mask:0xf bank_mask:0xf
	s_and_saveexec_b64 s[6:7], s[4:5]
	s_cbranch_execz .LBB0_1299
	v_and_b32_e32 v2, 0xffff, v2
	s_waitcnt lgkmcnt(0)
	v_lshl_or_b32 v2, v192, 16, v2
	global_store_dword v[166:167], v2, off offset:2112
.LBB0_1299:
	s_or_b64 exec, exec, s[6:7]
	v_and_b32_e32 v2, 0xffff0000, v215
	s_waitcnt lgkmcnt(0)
	v_mul_f32 v192, v82, v183
	s_nop 0
	v_fma_f32 v2, v212, v192, v2
	s_nop 0
	v_mul_f32 v2, v2, v191
	s_nop 0
	v_mul_f32 v2, v2, v187
	s_nop 0
	v_max_f32_e32 v2, v2, v2
	v_max_f32_e32 v2, 0xc3e00000, v2
	v_min_f32_e32 v192, 0x43e00000, v2
	s_nop 1
	v_mov_b32_dpp v202, v192 quad_perm:[1,0,3,2] row_mask:0xf bank_mask:0xf
	v_mov_b32_e32 v2, v3
	s_waitcnt lgkmcnt(0)
	v_cvt_pk_fp8_f32 v2, v192, v202
	s_nop 1
	v_mov_b32_dpp v192, v2 quad_perm:[2,3,0,1] row_mask:0xf bank_mask:0xf
	s_and_saveexec_b64 s[6:7], s[4:5]
	s_cbranch_execz .LBB0_1301
	v_and_b32_e32 v2, 0xffff, v2
	s_waitcnt lgkmcnt(0)
	v_lshl_or_b32 v2, v192, 16, v2
	global_store_dword v[166:167], v2, off offset:2144
.LBB0_1301:
	s_or_b64 exec, exec, s[6:7]
	s_waitcnt vmcnt(13)
	v_lshlrev_b32_e32 v2, 16, v214
	s_waitcnt lgkmcnt(0)
	v_mul_f32 v192, v66, v183
	s_nop 0
	v_fma_f32 v2, v212, v192, v2
	s_nop 0
	v_mul_f32 v2, v2, v191
	s_nop 0
	v_mul_f32 v2, v2, v186
	s_nop 0
	v_max_f32_e32 v2, v2, v2
	v_max_f32_e32 v2, 0xc3e00000, v2
	v_min_f32_e32 v192, 0x43e00000, v2
	s_nop 1
	v_mov_b32_dpp v202, v192 quad_perm:[1,0,3,2] row_mask:0xf bank_mask:0xf
	v_mov_b32_e32 v2, v3
	s_waitcnt lgkmcnt(0)
	v_cvt_pk_fp8_f32 v2, v192, v202
	s_nop 1
	v_mov_b32_dpp v192, v2 quad_perm:[2,3,0,1] row_mask:0xf bank_mask:0xf
	s_and_saveexec_b64 s[6:7], s[4:5]
	s_cbranch_execz .LBB0_1303
	v_and_b32_e32 v2, 0xffff, v2
	s_waitcnt lgkmcnt(0)
	v_lshl_or_b32 v2, v192, 16, v2
	global_store_dword v[166:167], v2, off offset:2176
; __device__ __forceinline__ int crow(int r, int hi) { return (r & 3) + 8 * (r >> 2) + 4 * hi; }
; __device__ __forceinline__ float mul_ns(float a, float b) { float r; asm("v_mul_f32 %0, %1, %2" : "=v"(r) : "v"(a), "v"(b)); return r; }
; __device__ __forceinline__ float fma_ns(float a, float b, float c) { float r; asm("v_fma_f32 %0, %1, %2, %3" : "=v"(r) : "v"(a), "v"(b), "v"(c)); return r; }
; __device__ __forceinline__ void store_quad8(unsigned char* p, float v, int r32) {
;     v = fminf(fmaxf(v, -448.f), 448.f);
;     const float v1 = swz_xor<1>(v);
;     const int w = __builtin_amdgcn_cvt_pk_fp8_f32(v, v1, 0, false);
;     const int w2 = __builtin_amdgcn_ds_swizzle(w, (2 << 10) | 0x1f);
;     if ((r32 & 3) == 0) *(unsigned*)p = ((unsigned)w & 0xffffu) | ((unsigned)w2 << 16);
; }
;     __device__ __forceinline__ void operator()(f32x16 (&o)[8], const float (&rli)[16], int wid, int lane, int r32, int hi) const {
;     ...
;                 for (int q = 0; q < 4; ++q) { const int r = rb + q;
; #pragma unroll
;                     for (int d0 = 0; d0 < 8; ++d0) { const float t = __uint_as_float((d0 & 1) ? (tw[q][d0 >> 1] & 0xffff0000u) : (tw[q][d0 >> 1] << 16));
;                         const float dd = fma_ns(nlam, mul_ns(o[d0][r], rli[r]), t);
;                         store_quad8(base + (crow(r, 0) * 4096 + d0 * 32) + uo, mul_ns(mul_ns(dd, rn[r]), g[d0]), r32); } }
.LBB0_1303:
	s_or_b64 exec, exec, s[6:7]
	v_and_b32_e32 v2, 0xffff0000, v214
	s_waitcnt lgkmcnt(0)
	v_mul_f32 v192, v50, v183
	s_nop 0
	v_fma_f32 v2, v212, v192, v2
	s_nop 0
	v_mul_f32 v2, v2, v191
	s_nop 0
	v_mul_f32 v2, v2, v185
	s_nop 0
	v_max_f32_e32 v2, v2, v2
	v_max_f32_e32 v2, 0xc3e00000, v2
	v_min_f32_e32 v192, 0x43e00000, v2
	s_nop 1
	v_mov_b32_dpp v202, v192 quad_perm:[1,0,3,2] row_mask:0xf bank_mask:0xf
	v_mov_b32_e32 v2, v3
	s_waitcnt lgkmcnt(0)
	v_cvt_pk_fp8_f32 v2, v192, v202
	s_nop 1
	v_mov_b32_dpp v192, v2 quad_perm:[2,3,0,1] row_mask:0xf bank_mask:0xf
	s_and_saveexec_b64 s[6:7], s[4:5]
	s_cbranch_execz .LBB0_1305
	v_and_b32_e32 v2, 0xffff, v2
	s_waitcnt lgkmcnt(0)
	v_lshl_or_b32 v2, v192, 16, v2
	global_store_dword v[166:167], v2, off offset:2208
.LBB0_1305:
	s_or_b64 exec, exec, s[6:7]
	s_waitcnt vmcnt(12)
	v_lshlrev_b32_e32 v2, 16, v209
	s_waitcnt lgkmcnt(0)
	v_mul_f32 v192, v34, v183
	s_nop 0
	v_fma_f32 v2, v212, v192, v2
	s_nop 0
	v_mul_f32 v2, v2, v191
	s_nop 0
	v_mul_f32 v2, v2, v184
	s_nop 0
	v_max_f32_e32 v2, v2, v2
	v_max_f32_e32 v2, 0xc3e00000, v2
	v_min_f32_e32 v192, 0x43e00000, v2
	s_nop 1
	v_mov_b32_dpp v202, v192 quad_perm:[1,0,3,2] row_mask:0xf bank_mask:0xf
	v_mov_b32_e32 v2, v3
	s_waitcnt lgkmcnt(0)
	v_cvt_pk_fp8_f32 v2, v192, v202
	s_nop 1
	v_mov_b32_dpp v192, v2 quad_perm:[2,3,0,1] row_mask:0xf bank_mask:0xf
	s_and_saveexec_b64 s[6:7], s[4:5]
	s_cbranch_execz .LBB0_1307
	v_and_b32_e32 v2, 0xffff, v2
	s_waitcnt lgkmcnt(0)
	v_lshl_or_b32 v2, v192, 16, v2
	global_store_dword v[166:167], v2, off offset:2240
.LBB0_1307:
	s_or_b64 exec, exec, s[6:7]
	v_and_b32_e32 v2, 0xffff0000, v209
	s_waitcnt lgkmcnt(0)
	v_mul_f32 v192, v18, v183
	s_nop 0
	v_fma_f32 v2, v212, v192, v2
	s_nop 0
	v_mul_f32 v2, v2, v191
	s_nop 0
	v_mul_f32 v2, v2, v165
	s_nop 0
	v_max_f32_e32 v2, v2, v2
	v_max_f32_e32 v2, 0xc3e00000, v2
	v_min_f32_e32 v191, 0x43e00000, v2
	s_nop 1
	v_mov_b32_dpp v192, v191 quad_perm:[1,0,3,2] row_mask:0xf bank_mask:0xf
	v_mov_b32_e32 v2, v3
	s_waitcnt lgkmcnt(0)
	v_cvt_pk_fp8_f32 v2, v191, v192
	s_nop 1
	v_mov_b32_dpp v191, v2 quad_perm:[2,3,0,1] row_mask:0xf bank_mask:0xf
	s_and_saveexec_b64 s[6:7], s[4:5]
	s_cbranch_execz .LBB0_1309
	v_and_b32_e32 v2, 0xffff, v2
	s_waitcnt lgkmcnt(0)
	v_lshl_or_b32 v2, v191, 16, v2
	global_store_dword v[166:167], v2, off offset:2272
.LBB0_1309:
	s_or_b64 exec, exec, s[6:7]
	v_mul_f32_e32 v2, 0x4b800000, v164
	v_cndmask_b32_e32 v2, v164, v2, vcc
	v_rsq_f32_e32 v2, v2
	v_mul_f32 v166, v131, v182
	s_nop 0
	v_mul_f32_e32 v164, 0x45800000, v2
	v_cndmask_b32_e32 v2, v2, v164, vcc
	s_waitcnt vmcnt(11)
	v_lshlrev_b32_e32 v164, 16, v208
	v_fma_f32 v164, v212, v166, v164
	v_mul_f32_e32 v2, 0x3f4ccccd, v2
	v_mul_f32 v164, v164, v2
	s_nop 0
	v_mul_f32 v164, v164, v190
	s_nop 0
	v_max_f32_e32 v164, v164, v164
	v_max_f32_e32 v164, 0xc3e00000, v164
	v_min_f32_e32 v166, 0x43e00000, v164
	s_nop 1
	v_mov_b32_dpp v167, v166 quad_perm:[1,0,3,2] row_mask:0xf bank_mask:0xf
	v_mov_b32_e32 v164, v3
	s_waitcnt lgkmcnt(0)
	v_cvt_pk_fp8_f32 v164, v166, v167
	s_nop 1
	v_mov_b32_dpp v166, v164 quad_perm:[2,3,0,1] row_mask:0xf bank_mask:0xf
	s_and_saveexec_b64 s[6:7], s[4:5]
	s_cbranch_execz .LBB0_1311
	v_and_b32_e32 v164, 0xffff, v164
	s_waitcnt lgkmcnt(0)
	v_lshl_or_b32 v164, v166, 16, v164
	v_add_co_u32_e32 v166, vcc, 0x1000, v6
	s_nop 1
	v_addc_co_u32_e32 v167, vcc, 0, v7, vcc
	global_store_dword v[166:167], v164, off
.LBB0_1311:
	s_or_b64 exec, exec, s[6:7]
	v_and_b32_e32 v164, 0xffff0000, v208
	s_waitcnt lgkmcnt(0)
	v_mul_f32 v166, v115, v182
	s_nop 0
	v_fma_f32 v164, v212, v166, v164
	s_nop 0
	v_mul_f32 v164, v164, v2
	s_nop 0
	v_mul_f32 v164, v164, v189
	s_nop 0
	v_max_f32_e32 v164, v164, v164
	v_max_f32_e32 v164, 0xc3e00000, v164
	v_min_f32_e32 v166, 0x43e00000, v164
	s_nop 1
	v_mov_b32_dpp v167, v166 quad_perm:[1,0,3,2] row_mask:0xf bank_mask:0xf
	v_mov_b32_e32 v164, v3
	s_waitcnt lgkmcnt(0)
	v_cvt_pk_fp8_f32 v164, v166, v167
	s_nop 1
	v_mov_b32_dpp v166, v164 quad_perm:[2,3,0,1] row_mask:0xf bank_mask:0xf
	s_and_saveexec_b64 s[6:7], s[4:5]
	s_cbranch_execz .LBB0_1313
	v_and_b32_e32 v164, 0xffff, v164
	s_waitcnt lgkmcnt(0)
	v_lshl_or_b32 v164, v166, 16, v164
	v_add_co_u32_e32 v166, vcc, 0x1000, v6
	s_nop 1
	v_addc_co_u32_e32 v167, vcc, 0, v7, vcc
	global_store_dword v[166:167], v164, off offset:32
.LBB0_1313:
	s_or_b64 exec, exec, s[6:7]
	s_waitcnt vmcnt(10)
	v_lshlrev_b32_e32 v164, 16, v207
	s_waitcnt lgkmcnt(0)
	v_mul_f32 v166, v99, v182
	s_nop 0
	v_fma_f32 v164, v212, v166, v164
	s_nop 0
	v_mul_f32 v164, v164, v2
	s_nop 0
	v_mul_f32 v164, v164, v188
	s_nop 0
	v_max_f32_e32 v164, v164, v164
	v_max_f32_e32 v164, 0xc3e00000, v164
	v_min_f32_e32 v166, 0x43e00000, v164
	s_nop 1
	v_mov_b32_dpp v167, v166 quad_perm:[1,0,3,2] row_mask:0xf bank_mask:0xf
	v_mov_b32_e32 v164, v3
	s_waitcnt lgkmcnt(0)
	v_cvt_pk_fp8_f32 v164, v166, v167
	s_nop 1
	v_mov_b32_dpp v166, v164 quad_perm:[2,3,0,1] row_mask:0xf bank_mask:0xf
	s_and_saveexec_b64 s[6:7], s[4:5]
	s_cbranch_execz .LBB0_1315
	v_and_b32_e32 v164, 0xffff, v164
	s_waitcnt lgkmcnt(0)
	v_lshl_or_b32 v164, v166, 16, v164
	v_add_co_u32_e32 v166, vcc, 0x1000, v6
	s_nop 1
	v_addc_co_u32_e32 v167, vcc, 0, v7, vcc
	global_store_dword v[166:167], v164, off offset:64
; __device__ __forceinline__ int crow(int r, int hi) { return (r & 3) + 8 * (r >> 2) + 4 * hi; }
; __device__ __forceinline__ float mul_ns(float a, float b) { float r; asm("v_mul_f32 %0, %1, %2" : "=v"(r) : "v"(a), "v"(b)); return r; }
; __device__ __forceinline__ float fma_ns(float a, float b, float c) { float r; asm("v_fma_f32 %0, %1, %2, %3" : "=v"(r) : "v"(a), "v"(b), "v"(c)); return r; }
; __device__ __forceinline__ void store_quad8(unsigned char* p, float v, int r32) {
;     v = fminf(fmaxf(v, -448.f), 448.f);
;     const float v1 = swz_xor<1>(v);
;     const int w = __builtin_amdgcn_cvt_pk_fp8_f32(v, v1, 0, false);
;     const int w2 = __builtin_amdgcn_ds_swizzle(w, (2 << 10) | 0x1f);
;     if ((r32 & 3) == 0) *(unsigned*)p = ((unsigned)w & 0xffffu) | ((unsigned)w2 << 16);
; }
;     __device__ __forceinline__ void operator()(f32x16 (&o)[8], const float (&rli)[16], int wid, int lane, int r32, int hi) const {
;     ...
;                 for (int q = 0; q < 4; ++q) { const int r = rb + q;
; #pragma unroll
;                     for (int d0 = 0; d0 < 8; ++d0) { const float t = __uint_as_float((d0 & 1) ? (tw[q][d0 >> 1] & 0xffff0000u) : (tw[q][d0 >> 1] << 16));
;                         const float dd = fma_ns(nlam, mul_ns(o[d0][r], rli[r]), t);
;                         store_quad8(base + (crow(r, 0) * 4096 + d0 * 32) + uo, mul_ns(mul_ns(dd, rn[r]), g[d0]), r32); } }
.LBB0_1315:
	s_or_b64 exec, exec, s[6:7]
	v_and_b32_e32 v164, 0xffff0000, v207
	s_waitcnt lgkmcnt(0)
	v_mul_f32 v166, v83, v182
	s_nop 0
	v_fma_f32 v164, v212, v166, v164
	s_nop 0
	v_mul_f32 v164, v164, v2
	s_nop 0
	v_mul_f32 v164, v164, v187
	s_nop 0
	v_max_f32_e32 v164, v164, v164
	v_max_f32_e32 v164, 0xc3e00000, v164
	v_min_f32_e32 v166, 0x43e00000, v164
	s_nop 1
	v_mov_b32_dpp v167, v166 quad_perm:[1,0,3,2] row_mask:0xf bank_mask:0xf
	v_mov_b32_e32 v164, v3
	s_waitcnt lgkmcnt(0)
	v_cvt_pk_fp8_f32 v164, v166, v167
	s_nop 1
	v_mov_b32_dpp v166, v164 quad_perm:[2,3,0,1] row_mask:0xf bank_mask:0xf
	s_and_saveexec_b64 s[6:7], s[4:5]
	s_cbranch_execz .LBB0_1317
	v_and_b32_e32 v164, 0xffff, v164
	s_waitcnt lgkmcnt(0)
	v_lshl_or_b32 v164, v166, 16, v164
	v_add_co_u32_e32 v166, vcc, 0x1000, v6
	s_nop 1
	v_addc_co_u32_e32 v167, vcc, 0, v7, vcc
	global_store_dword v[166:167], v164, off offset:96
.LBB0_1317:
	s_or_b64 exec, exec, s[6:7]
	s_waitcnt vmcnt(9)
	v_lshlrev_b32_e32 v164, 16, v206
	s_waitcnt lgkmcnt(0)
	v_mul_f32 v166, v67, v182
	s_nop 0
	v_fma_f32 v164, v212, v166, v164
	s_nop 0
	v_mul_f32 v164, v164, v2
	s_nop 0
	v_mul_f32 v164, v164, v186
	s_nop 0
	v_max_f32_e32 v164, v164, v164
	v_max_f32_e32 v164, 0xc3e00000, v164
	v_min_f32_e32 v166, 0x43e00000, v164
	s_nop 1
	v_mov_b32_dpp v167, v166 quad_perm:[1,0,3,2] row_mask:0xf bank_mask:0xf
	v_mov_b32_e32 v164, v3
	s_waitcnt lgkmcnt(0)
	v_cvt_pk_fp8_f32 v164, v166, v167
	s_nop 1
	v_mov_b32_dpp v166, v164 quad_perm:[2,3,0,1] row_mask:0xf bank_mask:0xf
	s_and_saveexec_b64 s[6:7], s[4:5]
	s_cbranch_execz .LBB0_1319
	v_and_b32_e32 v164, 0xffff, v164
	s_waitcnt lgkmcnt(0)
	v_lshl_or_b32 v164, v166, 16, v164
	v_add_co_u32_e32 v166, vcc, 0x1000, v6
	s_nop 1
	v_addc_co_u32_e32 v167, vcc, 0, v7, vcc
	global_store_dword v[166:167], v164, off offset:128
.LBB0_1319:
	s_or_b64 exec, exec, s[6:7]
	v_and_b32_e32 v164, 0xffff0000, v206
	s_waitcnt lgkmcnt(0)
	v_mul_f32 v166, v51, v182
	s_nop 0
	v_fma_f32 v164, v212, v166, v164
	s_nop 0
	v_mul_f32 v164, v164, v2
	s_nop 0
	v_mul_f32 v164, v164, v185
	s_nop 0
	v_max_f32_e32 v164, v164, v164
	v_max_f32_e32 v164, 0xc3e00000, v164
	v_min_f32_e32 v166, 0x43e00000, v164
	s_nop 1
	v_mov_b32_dpp v167, v166 quad_perm:[1,0,3,2] row_mask:0xf bank_mask:0xf
	v_mov_b32_e32 v164, v3
	s_waitcnt lgkmcnt(0)
	v_cvt_pk_fp8_f32 v164, v166, v167
	s_nop 1
	v_mov_b32_dpp v166, v164 quad_perm:[2,3,0,1] row_mask:0xf bank_mask:0xf
	s_and_saveexec_b64 s[6:7], s[4:5]
	s_cbranch_execz .LBB0_1321
	v_and_b32_e32 v164, 0xffff, v164
	s_waitcnt lgkmcnt(0)
	v_lshl_or_b32 v164, v166, 16, v164
	v_add_co_u32_e32 v166, vcc, 0x1000, v6
	s_nop 1
	v_addc_co_u32_e32 v167, vcc, 0, v7, vcc
	global_store_dword v[166:167], v164, off offset:160
.LBB0_1321:
	s_or_b64 exec, exec, s[6:7]
	s_waitcnt vmcnt(8)
	v_lshlrev_b32_e32 v164, 16, v205
	s_waitcnt lgkmcnt(0)
	v_mul_f32 v166, v35, v182
	s_nop 0
	v_fma_f32 v164, v212, v166, v164
	s_nop 0
	v_mul_f32 v164, v164, v2
	s_nop 0
	v_mul_f32 v164, v164, v184
	s_nop 0
	v_max_f32_e32 v164, v164, v164
	v_max_f32_e32 v164, 0xc3e00000, v164
	v_min_f32_e32 v166, 0x43e00000, v164
	s_nop 1
	v_mov_b32_dpp v167, v166 quad_perm:[1,0,3,2] row_mask:0xf bank_mask:0xf
	v_mov_b32_e32 v164, v3
	s_waitcnt lgkmcnt(0)
	v_cvt_pk_fp8_f32 v164, v166, v167
	s_nop 1
	v_mov_b32_dpp v166, v164 quad_perm:[2,3,0,1] row_mask:0xf bank_mask:0xf
	s_and_saveexec_b64 s[6:7], s[4:5]
	s_cbranch_execz .LBB0_1323
	v_and_b32_e32 v164, 0xffff, v164
	s_waitcnt lgkmcnt(0)
	v_lshl_or_b32 v164, v166, 16, v164
	v_add_co_u32_e32 v166, vcc, 0x1000, v6
	s_nop 1
	v_addc_co_u32_e32 v167, vcc, 0, v7, vcc
	global_store_dword v[166:167], v164, off offset:192
.LBB0_1323:
	s_or_b64 exec, exec, s[6:7]
	v_and_b32_e32 v164, 0xffff0000, v205
	s_waitcnt lgkmcnt(0)
	v_mul_f32 v166, v19, v182
	s_nop 0
	v_fma_f32 v164, v212, v166, v164
	s_nop 0
	v_mul_f32 v2, v164, v2
	s_nop 0
	v_mul_f32 v2, v2, v165
	s_nop 0
	v_max_f32_e32 v2, v2, v2
	v_max_f32_e32 v2, 0xc3e00000, v2
	v_min_f32_e32 v164, 0x43e00000, v2
	s_nop 1
	v_mov_b32_dpp v166, v164 quad_perm:[1,0,3,2] row_mask:0xf bank_mask:0xf
	v_mov_b32_e32 v2, v3
	s_waitcnt lgkmcnt(0)
	v_cvt_pk_fp8_f32 v2, v164, v166
	s_nop 1
	v_mov_b32_dpp v164, v2 quad_perm:[2,3,0,1] row_mask:0xf bank_mask:0xf
	s_and_saveexec_b64 s[6:7], s[4:5]
	s_cbranch_execz .LBB0_1325
	v_and_b32_e32 v2, 0xffff, v2
	v_add_co_u32_e32 v166, vcc, 0x1000, v6
	s_waitcnt lgkmcnt(0)
	v_lshl_or_b32 v2, v164, 16, v2
	v_addc_co_u32_e32 v167, vcc, 0, v7, vcc
	global_store_dword v[166:167], v2, off offset:224
.LBB0_1325:
	s_or_b64 exec, exec, s[6:7]
	v_pk_add_f32 v[160:161], v[160:161], v[162:163]
	v_mul_f32 v162, v132, v181
	s_nop 0
	v_pk_fma_f32 v[160:161], v[160:161], s[54:55], v[198:199] op_sel_hi:[1,0,0]
	s_nop 0
	v_mul_f32_e32 v2, 0x4b800000, v161
	v_cmp_gt_f32_e32 vcc, s53, v161
	v_cmp_gt_f32_e64 s[6:7], s53, v160
	s_nop 0
	v_cndmask_b32_e32 v2, v161, v2, vcc
	v_rsq_f32_e32 v2, v2
	s_waitcnt vmcnt(7)
	v_lshlrev_b32_e32 v161, 16, v204
	v_fma_f32 v161, v212, v162, v161
	v_mul_f32_e32 v163, 0x45800000, v2
	v_cndmask_b32_e32 v2, v2, v163, vcc
	v_mul_f32_e32 v2, 0x3f4ccccd, v2
	v_mul_f32 v161, v161, v2
	s_nop 0
	v_mul_f32 v161, v161, v190
	s_nop 0
	v_max_f32_e32 v161, v161, v161
	v_max_f32_e32 v161, 0xc3e00000, v161
	v_min_f32_e32 v162, 0x43e00000, v161
	s_nop 1
	v_mov_b32_dpp v163, v162 quad_perm:[1,0,3,2] row_mask:0xf bank_mask:0xf
	v_mov_b32_e32 v161, v3
	s_waitcnt lgkmcnt(0)
	v_cvt_pk_fp8_f32 v161, v162, v163
	s_nop 1
	v_mov_b32_dpp v162, v161 quad_perm:[2,3,0,1] row_mask:0xf bank_mask:0xf
	s_and_saveexec_b64 s[8:9], s[4:5]
	s_cbranch_execz .LBB0_1327
	v_and_b32_e32 v161, 0xffff, v161
	s_waitcnt lgkmcnt(0)
	v_lshl_or_b32 v161, v162, 16, v161
	v_add_co_u32_e32 v162, vcc, 0x2000, v6
	s_nop 1
	v_addc_co_u32_e32 v163, vcc, 0, v7, vcc
	global_store_dword v[162:163], v161, off
; __device__ __forceinline__ int crow(int r, int hi) { return (r & 3) + 8 * (r >> 2) + 4 * hi; }
; __device__ __forceinline__ float mul_ns(float a, float b) { float r; asm("v_mul_f32 %0, %1, %2" : "=v"(r) : "v"(a), "v"(b)); return r; }
; __device__ __forceinline__ float fma_ns(float a, float b, float c) { float r; asm("v_fma_f32 %0, %1, %2, %3" : "=v"(r) : "v"(a), "v"(b), "v"(c)); return r; }
; __device__ __forceinline__ void store_quad8(unsigned char* p, float v, int r32) {
;     v = fminf(fmaxf(v, -448.f), 448.f);
;     const float v1 = swz_xor<1>(v);
;     const int w = __builtin_amdgcn_cvt_pk_fp8_f32(v, v1, 0, false);
;     const int w2 = __builtin_amdgcn_ds_swizzle(w, (2 << 10) | 0x1f);
;     if ((r32 & 3) == 0) *(unsigned*)p = ((unsigned)w & 0xffffu) | ((unsigned)w2 << 16);
; }
;     __device__ __forceinline__ void operator()(f32x16 (&o)[8], const float (&rli)[16], int wid, int lane, int r32, int hi) const {
;     ...
;                 for (int q = 0; q < 4; ++q) { const int r = rb + q;
; #pragma unroll
;                     for (int d0 = 0; d0 < 8; ++d0) { const float t = __uint_as_float((d0 & 1) ? (tw[q][d0 >> 1] & 0xffff0000u) : (tw[q][d0 >> 1] << 16));
;                         const float dd = fma_ns(nlam, mul_ns(o[d0][r], rli[r]), t);
;                         store_quad8(base + (crow(r, 0) * 4096 + d0 * 32) + uo, mul_ns(mul_ns(dd, rn[r]), g[d0]), r32); } }
.LBB0_1327:
	s_or_b64 exec, exec, s[8:9]
	v_and_b32_e32 v161, 0xffff0000, v204
	s_waitcnt lgkmcnt(0)
	v_mul_f32 v162, v116, v181
	s_nop 0
	v_fma_f32 v161, v212, v162, v161
	s_nop 0
	v_mul_f32 v161, v161, v2
	s_nop 0
	v_mul_f32 v161, v161, v189
	s_nop 0
	v_max_f32_e32 v161, v161, v161
	v_max_f32_e32 v161, 0xc3e00000, v161
	v_min_f32_e32 v162, 0x43e00000, v161
	s_nop 1
	v_mov_b32_dpp v163, v162 quad_perm:[1,0,3,2] row_mask:0xf bank_mask:0xf
	v_mov_b32_e32 v161, v3
	s_waitcnt lgkmcnt(0)
	v_cvt_pk_fp8_f32 v161, v162, v163
	s_nop 1
	v_mov_b32_dpp v162, v161 quad_perm:[2,3,0,1] row_mask:0xf bank_mask:0xf
	s_and_saveexec_b64 s[8:9], s[4:5]
	s_cbranch_execz .LBB0_1329
	v_and_b32_e32 v161, 0xffff, v161
	s_waitcnt lgkmcnt(0)
	v_lshl_or_b32 v161, v162, 16, v161
	v_add_co_u32_e32 v162, vcc, 0x2000, v6
	s_nop 1
	v_addc_co_u32_e32 v163, vcc, 0, v7, vcc
	global_store_dword v[162:163], v161, off offset:32
.LBB0_1329:
	s_or_b64 exec, exec, s[8:9]
	s_waitcnt vmcnt(6)
	v_lshlrev_b32_e32 v161, 16, v203
	s_waitcnt lgkmcnt(0)
	v_mul_f32 v162, v100, v181
	s_nop 0
	v_fma_f32 v161, v212, v162, v161
	s_nop 0
	v_mul_f32 v161, v161, v2
	s_nop 0
	v_mul_f32 v161, v161, v188
	s_nop 0
	v_max_f32_e32 v161, v161, v161
	v_max_f32_e32 v161, 0xc3e00000, v161
	v_min_f32_e32 v162, 0x43e00000, v161
	s_nop 1
	v_mov_b32_dpp v163, v162 quad_perm:[1,0,3,2] row_mask:0xf bank_mask:0xf
	v_mov_b32_e32 v161, v3
	s_waitcnt lgkmcnt(0)
	v_cvt_pk_fp8_f32 v161, v162, v163
	s_nop 1
	v_mov_b32_dpp v162, v161 quad_perm:[2,3,0,1] row_mask:0xf bank_mask:0xf
	s_and_saveexec_b64 s[8:9], s[4:5]
	s_cbranch_execz .LBB0_1331
	v_and_b32_e32 v161, 0xffff, v161
	s_waitcnt lgkmcnt(0)
	v_lshl_or_b32 v161, v162, 16, v161
	v_add_co_u32_e32 v162, vcc, 0x2000, v6
	s_nop 1
	v_addc_co_u32_e32 v163, vcc, 0, v7, vcc
	global_store_dword v[162:163], v161, off offset:64
.LBB0_1331:
	s_or_b64 exec, exec, s[8:9]
	v_and_b32_e32 v161, 0xffff0000, v203
	s_waitcnt lgkmcnt(0)
	v_mul_f32 v162, v84, v181
	s_nop 0
	v_fma_f32 v161, v212, v162, v161
	s_nop 0
	v_mul_f32 v161, v161, v2
	s_nop 0
	v_mul_f32 v161, v161, v187
	s_nop 0
	v_max_f32_e32 v161, v161, v161
	v_max_f32_e32 v161, 0xc3e00000, v161
	v_min_f32_e32 v162, 0x43e00000, v161
	s_nop 1
	v_mov_b32_dpp v163, v162 quad_perm:[1,0,3,2] row_mask:0xf bank_mask:0xf
	v_mov_b32_e32 v161, v3
	s_waitcnt lgkmcnt(0)
	v_cvt_pk_fp8_f32 v161, v162, v163
	s_nop 1
	v_mov_b32_dpp v162, v161 quad_perm:[2,3,0,1] row_mask:0xf bank_mask:0xf
	s_and_saveexec_b64 s[8:9], s[4:5]
	s_cbranch_execz .LBB0_1333
	v_and_b32_e32 v161, 0xffff, v161
	s_waitcnt lgkmcnt(0)
	v_lshl_or_b32 v161, v162, 16, v161
	v_add_co_u32_e32 v162, vcc, 0x2000, v6
	s_nop 1
	v_addc_co_u32_e32 v163, vcc, 0, v7, vcc
	global_store_dword v[162:163], v161, off offset:96
.LBB0_1333:
	s_or_b64 exec, exec, s[8:9]
	s_waitcnt vmcnt(5)
	v_lshlrev_b32_e32 v161, 16, v201
	s_waitcnt lgkmcnt(0)
	v_mul_f32 v162, v68, v181
	s_nop 0
	v_fma_f32 v161, v212, v162, v161
	s_nop 0
	v_mul_f32 v161, v161, v2
	s_nop 0
	v_mul_f32 v161, v161, v186
	s_nop 0
	v_max_f32_e32 v161, v161, v161
	v_max_f32_e32 v161, 0xc3e00000, v161
	v_min_f32_e32 v162, 0x43e00000, v161
	s_nop 1
	v_mov_b32_dpp v163, v162 quad_perm:[1,0,3,2] row_mask:0xf bank_mask:0xf
	v_mov_b32_e32 v161, v3
	s_waitcnt lgkmcnt(0)
	v_cvt_pk_fp8_f32 v161, v162, v163
	s_nop 1
	v_mov_b32_dpp v162, v161 quad_perm:[2,3,0,1] row_mask:0xf bank_mask:0xf
	s_and_saveexec_b64 s[8:9], s[4:5]
	s_cbranch_execz .LBB0_1335
	v_and_b32_e32 v161, 0xffff, v161
	s_waitcnt lgkmcnt(0)
	v_lshl_or_b32 v161, v162, 16, v161
	v_add_co_u32_e32 v162, vcc, 0x2000, v6
	s_nop 1
	v_addc_co_u32_e32 v163, vcc, 0, v7, vcc
	global_store_dword v[162:163], v161, off offset:128
.LBB0_1335:
	s_or_b64 exec, exec, s[8:9]
	v_and_b32_e32 v161, 0xffff0000, v201
	s_waitcnt lgkmcnt(0)
	v_mul_f32 v162, v52, v181
	s_nop 0
	v_fma_f32 v161, v212, v162, v161
	s_nop 0
	v_mul_f32 v161, v161, v2
	s_nop 0
	v_mul_f32 v161, v161, v185
	s_nop 0
	v_max_f32_e32 v161, v161, v161
	v_max_f32_e32 v161, 0xc3e00000, v161
	v_min_f32_e32 v162, 0x43e00000, v161
	s_nop 1
	v_mov_b32_dpp v163, v162 quad_perm:[1,0,3,2] row_mask:0xf bank_mask:0xf
	v_mov_b32_e32 v161, v3
	s_waitcnt lgkmcnt(0)
	v_cvt_pk_fp8_f32 v161, v162, v163
	s_nop 1
	v_mov_b32_dpp v162, v161 quad_perm:[2,3,0,1] row_mask:0xf bank_mask:0xf
	s_and_saveexec_b64 s[8:9], s[4:5]
	s_cbranch_execz .LBB0_1337
	v_and_b32_e32 v161, 0xffff, v161
	s_waitcnt lgkmcnt(0)
	v_lshl_or_b32 v161, v162, 16, v161
	v_add_co_u32_e32 v162, vcc, 0x2000, v6
	s_nop 1
	v_addc_co_u32_e32 v163, vcc, 0, v7, vcc
	global_store_dword v[162:163], v161, off offset:160
.LBB0_1337:
	s_or_b64 exec, exec, s[8:9]
	s_waitcnt vmcnt(4)
	v_lshlrev_b32_e32 v161, 16, v197
	s_waitcnt lgkmcnt(0)
	v_mul_f32 v162, v36, v181
	s_nop 0
	v_fma_f32 v161, v212, v162, v161
	s_nop 0
	v_mul_f32 v161, v161, v2
	s_nop 0
	v_mul_f32 v161, v161, v184
	s_nop 0
	v_max_f32_e32 v161, v161, v161
	v_max_f32_e32 v161, 0xc3e00000, v161
	v_min_f32_e32 v162, 0x43e00000, v161
	s_nop 1
	v_mov_b32_dpp v163, v162 quad_perm:[1,0,3,2] row_mask:0xf bank_mask:0xf
	v_mov_b32_e32 v161, v3
	s_waitcnt lgkmcnt(0)
	v_cvt_pk_fp8_f32 v161, v162, v163
	s_nop 1
	v_mov_b32_dpp v162, v161 quad_perm:[2,3,0,1] row_mask:0xf bank_mask:0xf
	s_and_saveexec_b64 s[8:9], s[4:5]
	s_cbranch_execz .LBB0_1339
	v_and_b32_e32 v161, 0xffff, v161
	s_waitcnt lgkmcnt(0)
	v_lshl_or_b32 v161, v162, 16, v161
	v_add_co_u32_e32 v162, vcc, 0x2000, v6
	s_nop 1
	v_addc_co_u32_e32 v163, vcc, 0, v7, vcc
	global_store_dword v[162:163], v161, off offset:192
; __device__ __forceinline__ int crow(int r, int hi) { return (r & 3) + 8 * (r >> 2) + 4 * hi; }
; __device__ __forceinline__ float mul_ns(float a, float b) { float r; asm("v_mul_f32 %0, %1, %2" : "=v"(r) : "v"(a), "v"(b)); return r; }
; __device__ __forceinline__ float fma_ns(float a, float b, float c) { float r; asm("v_fma_f32 %0, %1, %2, %3" : "=v"(r) : "v"(a), "v"(b), "v"(c)); return r; }
; __device__ __forceinline__ void store_quad8(unsigned char* p, float v, int r32) {
;     v = fminf(fmaxf(v, -448.f), 448.f);
;     const float v1 = swz_xor<1>(v);
;     const int w = __builtin_amdgcn_cvt_pk_fp8_f32(v, v1, 0, false);
;     const int w2 = __builtin_amdgcn_ds_swizzle(w, (2 << 10) | 0x1f);
;     if ((r32 & 3) == 0) *(unsigned*)p = ((unsigned)w & 0xffffu) | ((unsigned)w2 << 16);
; }
;     __device__ __forceinline__ void operator()(f32x16 (&o)[8], const float (&rli)[16], int wid, int lane, int r32, int hi) const {
;     ...
;                 for (int q = 0; q < 4; ++q) { const int r = rb + q;
; #pragma unroll
;                     for (int d0 = 0; d0 < 8; ++d0) { const float t = __uint_as_float((d0 & 1) ? (tw[q][d0 >> 1] & 0xffff0000u) : (tw[q][d0 >> 1] << 16));
;                         const float dd = fma_ns(nlam, mul_ns(o[d0][r], rli[r]), t);
;                         store_quad8(base + (crow(r, 0) * 4096 + d0 * 32) + uo, mul_ns(mul_ns(dd, rn[r]), g[d0]), r32); } }
.LBB0_1339:
	s_or_b64 exec, exec, s[8:9]
	v_and_b32_e32 v161, 0xffff0000, v197
	s_waitcnt lgkmcnt(0)
	v_mul_f32 v162, v20, v181
	s_nop 0
	v_fma_f32 v161, v212, v162, v161
	s_nop 0
	v_mul_f32 v2, v161, v2
	s_nop 0
	v_mul_f32 v2, v2, v165
	s_nop 0
	v_max_f32_e32 v2, v2, v2
	v_max_f32_e32 v2, 0xc3e00000, v2
	v_min_f32_e32 v161, 0x43e00000, v2
	s_nop 1
	v_mov_b32_dpp v162, v161 quad_perm:[1,0,3,2] row_mask:0xf bank_mask:0xf
	v_mov_b32_e32 v2, v3
	s_waitcnt lgkmcnt(0)
	v_cvt_pk_fp8_f32 v2, v161, v162
	s_nop 1
	v_mov_b32_dpp v161, v2 quad_perm:[2,3,0,1] row_mask:0xf bank_mask:0xf
	s_and_saveexec_b64 s[8:9], s[4:5]
	s_cbranch_execz .LBB0_1341
	v_and_b32_e32 v2, 0xffff, v2
	v_add_co_u32_e32 v162, vcc, 0x2000, v6
	s_waitcnt lgkmcnt(0)
	v_lshl_or_b32 v2, v161, 16, v2
	v_addc_co_u32_e32 v163, vcc, 0, v7, vcc
	global_store_dword v[162:163], v2, off offset:224
.LBB0_1341:
	s_or_b64 exec, exec, s[8:9]
	v_mul_f32_e32 v2, 0x4b800000, v160
	v_cndmask_b32_e64 v2, v160, v2, s[6:7]
	v_rsq_f32_e32 v2, v2
	s_waitcnt lgkmcnt(0)
	v_mul_f32 v161, v133, v180
	v_mul_f32_e32 v160, 0x45800000, v2
	v_cndmask_b32_e64 v2, v2, v160, s[6:7]
	s_waitcnt vmcnt(3)
	v_lshlrev_b32_e32 v160, 16, v196
	v_fma_f32 v160, v212, v161, v160
	v_mul_f32_e32 v2, 0x3f4ccccd, v2
	v_mul_f32 v160, v160, v2
	s_nop 0
	v_mul_f32 v160, v160, v190
	s_nop 0
	v_max_f32_e32 v160, v160, v160
	v_max_f32_e32 v160, 0xc3e00000, v160
	v_min_f32_e32 v161, 0x43e00000, v160
	s_nop 1
	v_mov_b32_dpp v162, v161 quad_perm:[1,0,3,2] row_mask:0xf bank_mask:0xf
	v_mov_b32_e32 v160, v3
	s_waitcnt lgkmcnt(0)
	v_cvt_pk_fp8_f32 v160, v161, v162
	s_nop 1
	v_mov_b32_dpp v161, v160 quad_perm:[2,3,0,1] row_mask:0xf bank_mask:0xf
	s_and_saveexec_b64 s[6:7], s[4:5]
	s_cbranch_execz .LBB0_1343
	v_and_b32_e32 v160, 0xffff, v160
	s_waitcnt lgkmcnt(0)
	v_lshl_or_b32 v162, v161, 16, v160
	v_add_co_u32_e32 v160, vcc, 0x3000, v6
	s_nop 1
	v_addc_co_u32_e32 v161, vcc, 0, v7, vcc
	global_store_dword v[160:161], v162, off
.LBB0_1343:
	s_or_b64 exec, exec, s[6:7]
	v_and_b32_e32 v160, 0xffff0000, v196
	s_waitcnt lgkmcnt(0)
	v_mul_f32 v161, v117, v180
	s_nop 0
	v_fma_f32 v160, v212, v161, v160
	s_nop 0
	v_mul_f32 v160, v160, v2
	s_nop 0
	v_mul_f32 v160, v160, v189
	s_nop 0
	v_max_f32_e32 v160, v160, v160
	v_max_f32_e32 v160, 0xc3e00000, v160
	v_min_f32_e32 v161, 0x43e00000, v160
	s_nop 1
	v_mov_b32_dpp v162, v161 quad_perm:[1,0,3,2] row_mask:0xf bank_mask:0xf
	v_mov_b32_e32 v160, v3
	s_waitcnt lgkmcnt(0)
	v_cvt_pk_fp8_f32 v160, v161, v162
	s_nop 1
	v_mov_b32_dpp v161, v160 quad_perm:[2,3,0,1] row_mask:0xf bank_mask:0xf
	s_and_saveexec_b64 s[6:7], s[4:5]
	s_cbranch_execz .LBB0_1345
	v_and_b32_e32 v160, 0xffff, v160
	s_waitcnt lgkmcnt(0)
	v_lshl_or_b32 v162, v161, 16, v160
	v_add_co_u32_e32 v160, vcc, 0x3000, v6
	s_nop 1
	v_addc_co_u32_e32 v161, vcc, 0, v7, vcc
	global_store_dword v[160:161], v162, off offset:32
.LBB0_1345:
	s_or_b64 exec, exec, s[6:7]
	s_waitcnt vmcnt(2)
	v_lshlrev_b32_e32 v160, 16, v195
	s_waitcnt lgkmcnt(0)
	v_mul_f32 v161, v101, v180
	s_nop 0
	v_fma_f32 v160, v212, v161, v160
	s_nop 0
	v_mul_f32 v160, v160, v2
	s_nop 0
	v_mul_f32 v160, v160, v188
	s_nop 0
	v_max_f32_e32 v160, v160, v160
	v_max_f32_e32 v160, 0xc3e00000, v160
	v_min_f32_e32 v161, 0x43e00000, v160
	s_nop 1
	v_mov_b32_dpp v162, v161 quad_perm:[1,0,3,2] row_mask:0xf bank_mask:0xf
	v_mov_b32_e32 v160, v3
	s_waitcnt lgkmcnt(0)
	v_cvt_pk_fp8_f32 v160, v161, v162
	s_nop 1
	v_mov_b32_dpp v161, v160 quad_perm:[2,3,0,1] row_mask:0xf bank_mask:0xf
	s_and_saveexec_b64 s[6:7], s[4:5]
	s_cbranch_execz .LBB0_1347
	v_and_b32_e32 v160, 0xffff, v160
	s_waitcnt lgkmcnt(0)
	v_lshl_or_b32 v162, v161, 16, v160
	v_add_co_u32_e32 v160, vcc, 0x3000, v6
	s_nop 1
	v_addc_co_u32_e32 v161, vcc, 0, v7, vcc
	global_store_dword v[160:161], v162, off offset:64
.LBB0_1347:
	s_or_b64 exec, exec, s[6:7]
	v_and_b32_e32 v160, 0xffff0000, v195
	s_waitcnt lgkmcnt(0)
	v_mul_f32 v161, v85, v180
	s_nop 0
	v_fma_f32 v160, v212, v161, v160
	s_nop 0
	v_mul_f32 v160, v160, v2
	s_nop 0
	v_mul_f32 v160, v160, v187
	s_nop 0
	v_max_f32_e32 v160, v160, v160
	v_max_f32_e32 v160, 0xc3e00000, v160
	v_min_f32_e32 v161, 0x43e00000, v160
	s_nop 1
	v_mov_b32_dpp v162, v161 quad_perm:[1,0,3,2] row_mask:0xf bank_mask:0xf
	v_mov_b32_e32 v160, v3
	s_waitcnt lgkmcnt(0)
	v_cvt_pk_fp8_f32 v160, v161, v162
	s_nop 1
	v_mov_b32_dpp v161, v160 quad_perm:[2,3,0,1] row_mask:0xf bank_mask:0xf
	s_and_saveexec_b64 s[6:7], s[4:5]
	s_cbranch_execz .LBB0_1349
	v_and_b32_e32 v160, 0xffff, v160
	s_waitcnt lgkmcnt(0)
	v_lshl_or_b32 v162, v161, 16, v160
	v_add_co_u32_e32 v160, vcc, 0x3000, v6
	s_nop 1
	v_addc_co_u32_e32 v161, vcc, 0, v7, vcc
	global_store_dword v[160:161], v162, off offset:96
.LBB0_1349:
	s_or_b64 exec, exec, s[6:7]
	s_waitcnt vmcnt(1)
	v_lshlrev_b32_e32 v160, 16, v194
	s_waitcnt lgkmcnt(0)
	v_mul_f32 v161, v69, v180
	s_nop 0
	v_fma_f32 v160, v212, v161, v160
	s_nop 0
	v_mul_f32 v160, v160, v2
	s_nop 0
	v_mul_f32 v160, v160, v186
	s_nop 0
	v_max_f32_e32 v160, v160, v160
	v_max_f32_e32 v160, 0xc3e00000, v160
	v_min_f32_e32 v161, 0x43e00000, v160
	s_nop 1
	v_mov_b32_dpp v162, v161 quad_perm:[1,0,3,2] row_mask:0xf bank_mask:0xf
	v_mov_b32_e32 v160, v3
	s_waitcnt lgkmcnt(0)
	v_cvt_pk_fp8_f32 v160, v161, v162
	s_nop 1
	v_mov_b32_dpp v161, v160 quad_perm:[2,3,0,1] row_mask:0xf bank_mask:0xf
	s_and_saveexec_b64 s[6:7], s[4:5]
	s_cbranch_execz .LBB0_1351
	v_and_b32_e32 v160, 0xffff, v160
	s_waitcnt lgkmcnt(0)
	v_lshl_or_b32 v162, v161, 16, v160
	v_add_co_u32_e32 v160, vcc, 0x3000, v6
	s_nop 1
	v_addc_co_u32_e32 v161, vcc, 0, v7, vcc
	global_store_dword v[160:161], v162, off offset:128
; #define SBAR() __builtin_amdgcn_sched_barrier(0)
; __device__ __forceinline__ int crow(int r, int hi) { return (r & 3) + 8 * (r >> 2) + 4 * hi; }
; __device__ __forceinline__ float mul_ns(float a, float b) { float r; asm("v_mul_f32 %0, %1, %2" : "=v"(r) : "v"(a), "v"(b)); return r; }
; __device__ __forceinline__ float fma_ns(float a, float b, float c) { float r; asm("v_fma_f32 %0, %1, %2, %3" : "=v"(r) : "v"(a), "v"(b), "v"(c)); return r; }
; __device__ __forceinline__ void store_quad8(unsigned char* p, float v, int r32) {
;     v = fminf(fmaxf(v, -448.f), 448.f);
;     const float v1 = swz_xor<1>(v);
;     const int w = __builtin_amdgcn_cvt_pk_fp8_f32(v, v1, 0, false);
;     const int w2 = __builtin_amdgcn_ds_swizzle(w, (2 << 10) | 0x1f);
;     if ((r32 & 3) == 0) *(unsigned*)p = ((unsigned)w & 0xffffu) | ((unsigned)w2 << 16);
; }
;     __device__ __forceinline__ void operator()(f32x16 (&o)[8], const float (&rli)[16], int wid, int lane, int r32, int hi) const {
;     ...
;             for (int rb = 0; rb < 16; rb += 4) { unsigned tw[4][4];
; #pragma unroll
;                 for (int q = 0; q < 4; ++q)
; #pragma unroll
;                     for (int k = 0; k < 4; ++k) tw[q][k] = (scw + ((rb + q) * 4 + k) * 64)[ul];
;                 asm volatile("" ::: "memory"); SBAR();
; #pragma unroll
;                 for (int q = 0; q < 4; ++q) { const int r = rb + q;
; #pragma unroll
;                     for (int d0 = 0; d0 < 8; ++d0) { const float t = __uint_as_float((d0 & 1) ? (tw[q][d0 >> 1] & 0xffff0000u) : (tw[q][d0 >> 1] << 16));
;                         const float dd = fma_ns(nlam, mul_ns(o[d0][r], rli[r]), t);
;                         store_quad8(base + (crow(r, 0) * 4096 + d0 * 32) + uo, mul_ns(mul_ns(dd, rn[r]), g[d0]), r32); } }
.LBB0_1351:
	s_or_b64 exec, exec, s[6:7]
	v_and_b32_e32 v160, 0xffff0000, v194
	s_waitcnt lgkmcnt(0)
	v_mul_f32 v161, v53, v180
	s_nop 0
	v_fma_f32 v160, v212, v161, v160
	s_nop 0
	v_mul_f32 v160, v160, v2
	s_nop 0
	v_mul_f32 v160, v160, v185
	s_nop 0
	v_max_f32_e32 v160, v160, v160
	v_max_f32_e32 v160, 0xc3e00000, v160
	v_min_f32_e32 v161, 0x43e00000, v160
	s_nop 1
	v_mov_b32_dpp v162, v161 quad_perm:[1,0,3,2] row_mask:0xf bank_mask:0xf
	v_mov_b32_e32 v160, v3
	s_waitcnt lgkmcnt(0)
	v_cvt_pk_fp8_f32 v160, v161, v162
	s_nop 1
	v_mov_b32_dpp v161, v160 quad_perm:[2,3,0,1] row_mask:0xf bank_mask:0xf
	s_and_saveexec_b64 s[6:7], s[4:5]
	s_cbranch_execz .LBB0_1353
	v_and_b32_e32 v160, 0xffff, v160
	s_waitcnt lgkmcnt(0)
	v_lshl_or_b32 v162, v161, 16, v160
	v_add_co_u32_e32 v160, vcc, 0x3000, v6
	s_nop 1
	v_addc_co_u32_e32 v161, vcc, 0, v7, vcc
	global_store_dword v[160:161], v162, off offset:160
.LBB0_1353:
	s_or_b64 exec, exec, s[6:7]
	s_waitcnt vmcnt(0)
	v_lshlrev_b32_e32 v160, 16, v193
	s_waitcnt lgkmcnt(0)
	v_mul_f32 v161, v37, v180
	s_nop 0
	v_fma_f32 v160, v212, v161, v160
	s_nop 0
	v_mul_f32 v160, v160, v2
	s_nop 0
	v_mul_f32 v160, v160, v184
	s_nop 0
	v_max_f32_e32 v160, v160, v160
	v_max_f32_e32 v160, 0xc3e00000, v160
	v_min_f32_e32 v161, 0x43e00000, v160
	s_nop 1
	v_mov_b32_dpp v162, v161 quad_perm:[1,0,3,2] row_mask:0xf bank_mask:0xf
	v_mov_b32_e32 v160, v3
	s_waitcnt lgkmcnt(0)
	v_cvt_pk_fp8_f32 v160, v161, v162
	s_nop 1
	v_mov_b32_dpp v161, v160 quad_perm:[2,3,0,1] row_mask:0xf bank_mask:0xf
	s_and_saveexec_b64 s[6:7], s[4:5]
	s_cbranch_execz .LBB0_1355
	v_and_b32_e32 v160, 0xffff, v160
	s_waitcnt lgkmcnt(0)
	v_lshl_or_b32 v162, v161, 16, v160
	v_add_co_u32_e32 v160, vcc, 0x3000, v6
	s_nop 1
	v_addc_co_u32_e32 v161, vcc, 0, v7, vcc
	global_store_dword v[160:161], v162, off offset:192
.LBB0_1355:
	s_or_b64 exec, exec, s[6:7]
	v_and_b32_e32 v160, 0xffff0000, v193
	s_waitcnt lgkmcnt(0)
	v_mul_f32 v161, v21, v180
	s_nop 0
	v_fma_f32 v160, v212, v161, v160
	s_nop 0
	v_mul_f32 v2, v160, v2
	s_nop 0
	v_mul_f32 v2, v2, v165
	s_nop 0
	v_max_f32_e32 v2, v2, v2
	v_max_f32_e32 v2, 0xc3e00000, v2
	v_min_f32_e32 v160, 0x43e00000, v2
	s_nop 1
	v_mov_b32_dpp v161, v160 quad_perm:[1,0,3,2] row_mask:0xf bank_mask:0xf
	v_mov_b32_e32 v2, v3
	s_waitcnt lgkmcnt(0)
	v_cvt_pk_fp8_f32 v2, v160, v161
	s_nop 1
	v_mov_b32_dpp v160, v2 quad_perm:[2,3,0,1] row_mask:0xf bank_mask:0xf
	s_and_saveexec_b64 s[6:7], s[4:5]
	s_cbranch_execz .LBB0_1357
	v_and_b32_e32 v2, 0xffff, v2
	s_waitcnt lgkmcnt(0)
	v_lshl_or_b32 v2, v160, 16, v2
	v_add_co_u32_e32 v160, vcc, 0x3000, v6
	s_nop 1
	v_addc_co_u32_e32 v161, vcc, 0, v7, vcc
	global_store_dword v[160:161], v2, off offset:224
.LBB0_1357:
	s_or_b64 exec, exec, s[6:7]
	s_mov_b64 s[6:7], 0x1000
	s_waitcnt lgkmcnt(0)
	v_lshl_add_u64 v[160:161], v[4:5], 0, s[6:7]
	s_mov_b64 s[6:7], 0x1100
	v_lshl_add_u64 v[162:163], v[4:5], 0, s[6:7]
	s_mov_b64 s[6:7], 0x1200
	v_lshl_add_u64 v[166:167], v[4:5], 0, s[6:7]
	s_mov_b64 s[6:7], 0x1300
	v_lshl_add_u64 v[202:203], v[4:5], 0, s[6:7]
	s_mov_b64 s[6:7], 0x1400
	v_lshl_add_u64 v[204:205], v[4:5], 0, s[6:7]
	s_mov_b64 s[6:7], 0x1500
	v_lshl_add_u64 v[206:207], v[4:5], 0, s[6:7]
	s_mov_b64 s[6:7], 0x1600
	v_pk_add_f32 v[156:157], v[156:157], v[158:159]
	v_lshl_add_u64 v[208:209], v[4:5], 0, s[6:7]
	s_mov_b64 s[6:7], 0x1700
	v_pk_fma_f32 v[156:157], v[156:157], s[54:55], v[198:199] op_sel_hi:[1,0,0]
	v_lshl_add_u64 v[214:215], v[4:5], 0, s[6:7]
	s_mov_b64 s[6:7], 0x1800
	v_mul_f32_e32 v2, 0x4b800000, v157
	v_cmp_gt_f32_e32 vcc, s53, v157
	v_lshl_add_u64 v[218:219], v[4:5], 0, s[6:7]
	s_mov_b64 s[6:7], 0x1900
	v_cndmask_b32_e32 v2, v157, v2, vcc
	v_lshl_add_u64 v[220:221], v[4:5], 0, s[6:7]
	s_mov_b64 s[6:7], 0x1a00
	v_rsq_f32_e32 v2, v2
	v_lshl_add_u64 v[222:223], v[4:5], 0, s[6:7]
	s_mov_b64 s[6:7], 0x1b00
	v_lshl_add_u64 v[224:225], v[4:5], 0, s[6:7]
	s_mov_b64 s[6:7], 0x1c00
	v_lshl_add_u64 v[226:227], v[4:5], 0, s[6:7]
	s_mov_b64 s[6:7], 0x1d00
	v_lshl_add_u64 v[228:229], v[4:5], 0, s[6:7]
	s_mov_b64 s[6:7], 0x1e00
	v_mul_f32_e32 v157, 0x45800000, v2
	v_lshl_add_u64 v[230:231], v[4:5], 0, s[6:7]
	s_mov_b64 s[6:7], 0x1f00
	v_cndmask_b32_e32 v2, v2, v157, vcc
	v_lshl_add_u64 v[232:233], v[4:5], 0, s[6:7]
	v_cmp_gt_f32_e64 s[6:7], s53, v156
	v_mul_f32_e32 v192, 0x3f4ccccd, v2
	global_load_dword v196, v[160:161], off
	global_load_dword v195, v[162:163], off
	global_load_dword v194, v[166:167], off
	global_load_dword v193, v[202:203], off
	global_load_dword v191, v[204:205], off
	s_nop 0
	global_load_dword v167, v[206:207], off
	global_load_dword v166, v[208:209], off
	global_load_dword v164, v[214:215], off
	global_load_dword v163, v[218:219], off
	global_load_dword v162, v[220:221], off
	global_load_dword v161, v[222:223], off
	global_load_dword v160, v[224:225], off
	global_load_dword v159, v[226:227], off
	global_load_dword v158, v[228:229], off
	global_load_dword v157, v[230:231], off
	global_load_dword v2, v[232:233], off
	s_waitcnt vmcnt(15)
	v_lshlrev_b32_e32 v197, 16, v196
	v_mul_f32 v201, v134, v179
	s_nop 0
	v_fma_f32 v197, v212, v201, v197
	s_nop 0
	v_mul_f32 v197, v197, v192
	s_nop 0
	v_mul_f32 v197, v197, v190
	s_nop 0
	v_max_f32_e32 v197, v197, v197
	v_max_f32_e32 v197, 0xc3e00000, v197
	v_min_f32_e32 v201, 0x43e00000, v197
	s_nop 1
	v_mov_b32_dpp v202, v201 quad_perm:[1,0,3,2] row_mask:0xf bank_mask:0xf
	v_mov_b32_e32 v197, v3
	s_waitcnt lgkmcnt(0)
	v_cvt_pk_fp8_f32 v197, v201, v202
	s_nop 1
	v_mov_b32_dpp v201, v197 quad_perm:[2,3,0,1] row_mask:0xf bank_mask:0xf
	s_and_saveexec_b64 s[8:9], s[4:5]
	s_cbranch_execz .LBB0_1359
	v_and_b32_e32 v197, 0xffff, v197
	v_add_co_u32_e32 v202, vcc, 0x8000, v6
	s_waitcnt lgkmcnt(0)
	v_lshl_or_b32 v197, v201, 16, v197
	v_addc_co_u32_e32 v203, vcc, 0, v7, vcc
	global_store_dword v[202:203], v197, off
; __device__ __forceinline__ int crow(int r, int hi) { return (r & 3) + 8 * (r >> 2) + 4 * hi; }
; __device__ __forceinline__ float mul_ns(float a, float b) { float r; asm("v_mul_f32 %0, %1, %2" : "=v"(r) : "v"(a), "v"(b)); return r; }
; __device__ __forceinline__ float fma_ns(float a, float b, float c) { float r; asm("v_fma_f32 %0, %1, %2, %3" : "=v"(r) : "v"(a), "v"(b), "v"(c)); return r; }
; __device__ __forceinline__ void store_quad8(unsigned char* p, float v, int r32) {
;     v = fminf(fmaxf(v, -448.f), 448.f);
;     const float v1 = swz_xor<1>(v);
;     const int w = __builtin_amdgcn_cvt_pk_fp8_f32(v, v1, 0, false);
;     const int w2 = __builtin_amdgcn_ds_swizzle(w, (2 << 10) | 0x1f);
;     if ((r32 & 3) == 0) *(unsigned*)p = ((unsigned)w & 0xffffu) | ((unsigned)w2 << 16);
; }
;     __device__ __forceinline__ void operator()(f32x16 (&o)[8], const float (&rli)[16], int wid, int lane, int r32, int hi) const {
;     ...
;                 for (int q = 0; q < 4; ++q) { const int r = rb + q;
; #pragma unroll
;                     for (int d0 = 0; d0 < 8; ++d0) { const float t = __uint_as_float((d0 & 1) ? (tw[q][d0 >> 1] & 0xffff0000u) : (tw[q][d0 >> 1] << 16));
;                         const float dd = fma_ns(nlam, mul_ns(o[d0][r], rli[r]), t);
;                         store_quad8(base + (crow(r, 0) * 4096 + d0 * 32) + uo, mul_ns(mul_ns(dd, rn[r]), g[d0]), r32); } }
.LBB0_1359:
	s_or_b64 exec, exec, s[8:9]
	v_and_b32_e32 v196, 0xffff0000, v196
	v_mul_f32 v197, v118, v179
	s_nop 0
	v_fma_f32 v196, v212, v197, v196
	s_nop 0
	v_mul_f32 v196, v196, v192
	s_nop 0
	v_mul_f32 v196, v196, v189
	s_nop 0
	v_max_f32_e32 v196, v196, v196
	v_max_f32_e32 v196, 0xc3e00000, v196
	v_min_f32_e32 v197, 0x43e00000, v196
	s_waitcnt lgkmcnt(0)
	s_nop 1
	v_mov_b32_dpp v201, v197 quad_perm:[1,0,3,2] row_mask:0xf bank_mask:0xf
	v_mov_b32_e32 v196, v3
	s_waitcnt lgkmcnt(0)
	v_cvt_pk_fp8_f32 v196, v197, v201
	s_nop 1
	v_mov_b32_dpp v197, v196 quad_perm:[2,3,0,1] row_mask:0xf bank_mask:0xf
	s_and_saveexec_b64 s[8:9], s[4:5]
	s_cbranch_execz .LBB0_1361
	v_and_b32_e32 v196, 0xffff, v196
	s_waitcnt lgkmcnt(0)
	v_lshl_or_b32 v201, v197, 16, v196
	v_add_co_u32_e32 v196, vcc, 0x8000, v6
	s_nop 1
	v_addc_co_u32_e32 v197, vcc, 0, v7, vcc
	global_store_dword v[196:197], v201, off offset:32
.LBB0_1361:
	s_or_b64 exec, exec, s[8:9]
	s_waitcnt vmcnt(14)
	v_lshlrev_b32_e32 v196, 16, v195
	s_waitcnt lgkmcnt(0)
	v_mul_f32 v197, v102, v179
	s_nop 0
	v_fma_f32 v196, v212, v197, v196
	s_nop 0
	v_mul_f32 v196, v196, v192
	s_nop 0
	v_mul_f32 v196, v196, v188
	s_nop 0
	v_max_f32_e32 v196, v196, v196
	v_max_f32_e32 v196, 0xc3e00000, v196
	v_min_f32_e32 v197, 0x43e00000, v196
	s_nop 1
	v_mov_b32_dpp v201, v197 quad_perm:[1,0,3,2] row_mask:0xf bank_mask:0xf
	v_mov_b32_e32 v196, v3
	s_waitcnt lgkmcnt(0)
	v_cvt_pk_fp8_f32 v196, v197, v201
	s_nop 1
	v_mov_b32_dpp v197, v196 quad_perm:[2,3,0,1] row_mask:0xf bank_mask:0xf
	s_and_saveexec_b64 s[8:9], s[4:5]
	s_cbranch_execz .LBB0_1363
	v_and_b32_e32 v196, 0xffff, v196
	s_waitcnt lgkmcnt(0)
	v_lshl_or_b32 v201, v197, 16, v196
	v_add_co_u32_e32 v196, vcc, 0x8000, v6
	s_nop 1
	v_addc_co_u32_e32 v197, vcc, 0, v7, vcc
	global_store_dword v[196:197], v201, off offset:64
.LBB0_1363:
	s_or_b64 exec, exec, s[8:9]
	v_and_b32_e32 v195, 0xffff0000, v195
	v_mul_f32 v196, v86, v179
	s_nop 0
	v_fma_f32 v195, v212, v196, v195
	s_nop 0
	v_mul_f32 v195, v195, v192
	s_nop 0
	v_mul_f32 v195, v195, v187
	s_nop 0
	v_max_f32_e32 v195, v195, v195
	v_max_f32_e32 v195, 0xc3e00000, v195
	v_min_f32_e32 v196, 0x43e00000, v195
	s_waitcnt lgkmcnt(0)
	s_nop 1
	v_mov_b32_dpp v197, v196 quad_perm:[1,0,3,2] row_mask:0xf bank_mask:0xf
	v_mov_b32_e32 v195, v3
	s_waitcnt lgkmcnt(0)
	v_cvt_pk_fp8_f32 v195, v196, v197
	s_nop 1
	v_mov_b32_dpp v196, v195 quad_perm:[2,3,0,1] row_mask:0xf bank_mask:0xf
	s_and_saveexec_b64 s[8:9], s[4:5]
	s_cbranch_execz .LBB0_1365
	v_and_b32_e32 v195, 0xffff, v195
	s_waitcnt lgkmcnt(0)
	v_lshl_or_b32 v195, v196, 16, v195
	v_add_co_u32_e32 v196, vcc, 0x8000, v6
	s_nop 1
	v_addc_co_u32_e32 v197, vcc, 0, v7, vcc
	global_store_dword v[196:197], v195, off offset:96
.LBB0_1365:
	s_or_b64 exec, exec, s[8:9]
	s_waitcnt vmcnt(13)
	v_lshlrev_b32_e32 v195, 16, v194
	s_waitcnt lgkmcnt(0)
	v_mul_f32 v196, v70, v179
	s_nop 0
	v_fma_f32 v195, v212, v196, v195
	s_nop 0
	v_mul_f32 v195, v195, v192
	s_nop 0
	v_mul_f32 v195, v195, v186
	s_nop 0
	v_max_f32_e32 v195, v195, v195
	v_max_f32_e32 v195, 0xc3e00000, v195
	v_min_f32_e32 v196, 0x43e00000, v195
	s_nop 1
	v_mov_b32_dpp v197, v196 quad_perm:[1,0,3,2] row_mask:0xf bank_mask:0xf
	v_mov_b32_e32 v195, v3
	s_waitcnt lgkmcnt(0)
	v_cvt_pk_fp8_f32 v195, v196, v197
	s_nop 1
	v_mov_b32_dpp v196, v195 quad_perm:[2,3,0,1] row_mask:0xf bank_mask:0xf
	s_and_saveexec_b64 s[8:9], s[4:5]
	s_cbranch_execz .LBB0_1367
	v_and_b32_e32 v195, 0xffff, v195
	s_waitcnt lgkmcnt(0)
	v_lshl_or_b32 v195, v196, 16, v195
	v_add_co_u32_e32 v196, vcc, 0x8000, v6
	s_nop 1
	v_addc_co_u32_e32 v197, vcc, 0, v7, vcc
	global_store_dword v[196:197], v195, off offset:128
.LBB0_1367:
	s_or_b64 exec, exec, s[8:9]
	v_and_b32_e32 v194, 0xffff0000, v194
	v_mul_f32 v195, v54, v179
	s_nop 0
	v_fma_f32 v194, v212, v195, v194
	s_nop 0
	v_mul_f32 v194, v194, v192
	s_nop 0
	v_mul_f32 v194, v194, v185
	s_nop 0
	v_max_f32_e32 v194, v194, v194
	v_max_f32_e32 v194, 0xc3e00000, v194
	v_min_f32_e32 v195, 0x43e00000, v194
	s_waitcnt lgkmcnt(0)
	s_nop 1
	v_mov_b32_dpp v196, v195 quad_perm:[1,0,3,2] row_mask:0xf bank_mask:0xf
	v_mov_b32_e32 v194, v3
	s_waitcnt lgkmcnt(0)
	v_cvt_pk_fp8_f32 v194, v195, v196
	s_nop 1
	v_mov_b32_dpp v195, v194 quad_perm:[2,3,0,1] row_mask:0xf bank_mask:0xf
	s_and_saveexec_b64 s[8:9], s[4:5]
	s_cbranch_execz .LBB0_1369
	v_and_b32_e32 v194, 0xffff, v194
	s_waitcnt lgkmcnt(0)
	v_lshl_or_b32 v196, v195, 16, v194
	v_add_co_u32_e32 v194, vcc, 0x8000, v6
	s_nop 1
	v_addc_co_u32_e32 v195, vcc, 0, v7, vcc
	global_store_dword v[194:195], v196, off offset:160
.LBB0_1369:
	s_or_b64 exec, exec, s[8:9]
	s_waitcnt vmcnt(12)
	v_lshlrev_b32_e32 v194, 16, v193
	s_waitcnt lgkmcnt(0)
	v_mul_f32 v195, v38, v179
	s_nop 0
	v_fma_f32 v194, v212, v195, v194
	s_nop 0
	v_mul_f32 v194, v194, v192
	s_nop 0
	v_mul_f32 v194, v194, v184
	s_nop 0
	v_max_f32_e32 v194, v194, v194
	v_max_f32_e32 v194, 0xc3e00000, v194
	v_min_f32_e32 v195, 0x43e00000, v194
	s_nop 1
	v_mov_b32_dpp v196, v195 quad_perm:[1,0,3,2] row_mask:0xf bank_mask:0xf
	v_mov_b32_e32 v194, v3
	s_waitcnt lgkmcnt(0)
	v_cvt_pk_fp8_f32 v194, v195, v196
	s_nop 1
	v_mov_b32_dpp v195, v194 quad_perm:[2,3,0,1] row_mask:0xf bank_mask:0xf
	s_and_saveexec_b64 s[8:9], s[4:5]
	s_cbranch_execz .LBB0_1371
	v_and_b32_e32 v194, 0xffff, v194
	s_waitcnt lgkmcnt(0)
	v_lshl_or_b32 v196, v195, 16, v194
	v_add_co_u32_e32 v194, vcc, 0x8000, v6
	s_nop 1
	v_addc_co_u32_e32 v195, vcc, 0, v7, vcc
	global_store_dword v[194:195], v196, off offset:192
; __device__ __forceinline__ int crow(int r, int hi) { return (r & 3) + 8 * (r >> 2) + 4 * hi; }
; __device__ __forceinline__ float mul_ns(float a, float b) { float r; asm("v_mul_f32 %0, %1, %2" : "=v"(r) : "v"(a), "v"(b)); return r; }
; __device__ __forceinline__ float fma_ns(float a, float b, float c) { float r; asm("v_fma_f32 %0, %1, %2, %3" : "=v"(r) : "v"(a), "v"(b), "v"(c)); return r; }
; __device__ __forceinline__ void store_quad8(unsigned char* p, float v, int r32) {
;     v = fminf(fmaxf(v, -448.f), 448.f);
;     const float v1 = swz_xor<1>(v);
;     const int w = __builtin_amdgcn_cvt_pk_fp8_f32(v, v1, 0, false);
;     const int w2 = __builtin_amdgcn_ds_swizzle(w, (2 << 10) | 0x1f);
;     if ((r32 & 3) == 0) *(unsigned*)p = ((unsigned)w & 0xffffu) | ((unsigned)w2 << 16);
; }
;     __device__ __forceinline__ void operator()(f32x16 (&o)[8], const float (&rli)[16], int wid, int lane, int r32, int hi) const {
;     ...
;                 for (int q = 0; q < 4; ++q) { const int r = rb + q;
; #pragma unroll
;                     for (int d0 = 0; d0 < 8; ++d0) { const float t = __uint_as_float((d0 & 1) ? (tw[q][d0 >> 1] & 0xffff0000u) : (tw[q][d0 >> 1] << 16));
;                         const float dd = fma_ns(nlam, mul_ns(o[d0][r], rli[r]), t);
;                         store_quad8(base + (crow(r, 0) * 4096 + d0 * 32) + uo, mul_ns(mul_ns(dd, rn[r]), g[d0]), r32); } }
.LBB0_1371:
	s_or_b64 exec, exec, s[8:9]
	v_and_b32_e32 v193, 0xffff0000, v193
	v_mul_f32 v194, v22, v179
	s_nop 0
	v_fma_f32 v193, v212, v194, v193
	s_nop 0
	v_mul_f32 v192, v193, v192
	s_nop 0
	v_mul_f32 v192, v192, v165
	s_nop 0
	v_max_f32_e32 v192, v192, v192
	v_max_f32_e32 v192, 0xc3e00000, v192
	v_min_f32_e32 v193, 0x43e00000, v192
	s_nop 1
	v_mov_b32_dpp v194, v193 quad_perm:[1,0,3,2] row_mask:0xf bank_mask:0xf
	v_mov_b32_e32 v192, v3
	s_waitcnt lgkmcnt(0)
	v_cvt_pk_fp8_f32 v192, v193, v194
	s_nop 1
	v_mov_b32_dpp v193, v192 quad_perm:[2,3,0,1] row_mask:0xf bank_mask:0xf
	s_and_saveexec_b64 s[8:9], s[4:5]
	s_cbranch_execz .LBB0_1373
	v_and_b32_e32 v192, 0xffff, v192
	s_waitcnt lgkmcnt(0)
	v_lshl_or_b32 v194, v193, 16, v192
	v_add_co_u32_e32 v192, vcc, 0x8000, v6
	s_nop 1
	v_addc_co_u32_e32 v193, vcc, 0, v7, vcc
	global_store_dword v[192:193], v194, off offset:224
.LBB0_1373:
	s_or_b64 exec, exec, s[8:9]
	v_mul_f32_e32 v192, 0x4b800000, v156
	v_cndmask_b32_e64 v156, v156, v192, s[6:7]
	v_rsq_f32_e32 v156, v156
	s_waitcnt lgkmcnt(0)
	v_mul_f32 v193, v135, v178
	v_mul_f32_e32 v192, 0x45800000, v156
	v_cndmask_b32_e64 v156, v156, v192, s[6:7]
	s_waitcnt vmcnt(11)
	v_lshlrev_b32_e32 v192, 16, v191
	v_fma_f32 v192, v212, v193, v192
	v_mul_f32_e32 v156, 0x3f4ccccd, v156
	v_mul_f32 v192, v192, v156
	s_nop 0
	v_mul_f32 v192, v192, v190
	s_nop 0
	v_max_f32_e32 v192, v192, v192
	v_max_f32_e32 v192, 0xc3e00000, v192
	v_min_f32_e32 v193, 0x43e00000, v192
	s_nop 1
	v_mov_b32_dpp v194, v193 quad_perm:[1,0,3,2] row_mask:0xf bank_mask:0xf
	v_mov_b32_e32 v192, v3
	s_waitcnt lgkmcnt(0)
	v_cvt_pk_fp8_f32 v192, v193, v194
	s_nop 1
	v_mov_b32_dpp v193, v192 quad_perm:[2,3,0,1] row_mask:0xf bank_mask:0xf
	s_and_saveexec_b64 s[6:7], s[4:5]
	s_cbranch_execz .LBB0_1375
	v_and_b32_e32 v192, 0xffff, v192
	s_waitcnt lgkmcnt(0)
	v_lshl_or_b32 v194, v193, 16, v192
	v_add_co_u32_e32 v192, vcc, 0x9000, v6
	s_nop 1
	v_addc_co_u32_e32 v193, vcc, 0, v7, vcc
	global_store_dword v[192:193], v194, off
.LBB0_1375:
	s_or_b64 exec, exec, s[6:7]
	v_and_b32_e32 v191, 0xffff0000, v191
	v_mul_f32 v192, v119, v178
	s_nop 0
	v_fma_f32 v191, v212, v192, v191
	s_nop 0
	v_mul_f32 v191, v191, v156
	s_nop 0
	v_mul_f32 v191, v191, v189
	s_nop 0
	v_max_f32_e32 v191, v191, v191
	v_max_f32_e32 v191, 0xc3e00000, v191
	v_min_f32_e32 v192, 0x43e00000, v191
	s_waitcnt lgkmcnt(0)
	s_nop 1
	v_mov_b32_dpp v193, v192 quad_perm:[1,0,3,2] row_mask:0xf bank_mask:0xf
	v_mov_b32_e32 v191, v3
	s_waitcnt lgkmcnt(0)
	v_cvt_pk_fp8_f32 v191, v192, v193
	s_nop 1
	v_mov_b32_dpp v192, v191 quad_perm:[2,3,0,1] row_mask:0xf bank_mask:0xf
	s_and_saveexec_b64 s[6:7], s[4:5]
	s_cbranch_execz .LBB0_1377
	v_and_b32_e32 v191, 0xffff, v191
	s_waitcnt lgkmcnt(0)
	v_lshl_or_b32 v191, v192, 16, v191
	v_add_co_u32_e32 v192, vcc, 0x9000, v6
	s_nop 1
	v_addc_co_u32_e32 v193, vcc, 0, v7, vcc
	global_store_dword v[192:193], v191, off offset:32
.LBB0_1377:
	s_or_b64 exec, exec, s[6:7]
	s_waitcnt vmcnt(10)
	v_lshlrev_b32_e32 v191, 16, v167
	s_waitcnt lgkmcnt(0)
	v_mul_f32 v192, v103, v178
	s_nop 0
	v_fma_f32 v191, v212, v192, v191
	s_nop 0
	v_mul_f32 v191, v191, v156
	s_nop 0
	v_mul_f32 v191, v191, v188
	s_nop 0
	v_max_f32_e32 v191, v191, v191
	v_max_f32_e32 v191, 0xc3e00000, v191
	v_min_f32_e32 v192, 0x43e00000, v191
	s_nop 1
	v_mov_b32_dpp v193, v192 quad_perm:[1,0,3,2] row_mask:0xf bank_mask:0xf
	v_mov_b32_e32 v191, v3
	s_waitcnt lgkmcnt(0)
	v_cvt_pk_fp8_f32 v191, v192, v193
	s_nop 1
	v_mov_b32_dpp v192, v191 quad_perm:[2,3,0,1] row_mask:0xf bank_mask:0xf
	s_and_saveexec_b64 s[6:7], s[4:5]
	s_cbranch_execz .LBB0_1379
	v_and_b32_e32 v191, 0xffff, v191
	s_waitcnt lgkmcnt(0)
	v_lshl_or_b32 v191, v192, 16, v191
	v_add_co_u32_e32 v192, vcc, 0x9000, v6
	s_nop 1
	v_addc_co_u32_e32 v193, vcc, 0, v7, vcc
	global_store_dword v[192:193], v191, off offset:64
.LBB0_1379:
	s_or_b64 exec, exec, s[6:7]
	v_and_b32_e32 v167, 0xffff0000, v167
	v_mul_f32 v191, v87, v178
	s_nop 0
	v_fma_f32 v167, v212, v191, v167
	s_nop 0
	v_mul_f32 v167, v167, v156
	s_nop 0
	v_mul_f32 v167, v167, v187
	s_nop 0
	v_max_f32_e32 v167, v167, v167
	v_max_f32_e32 v167, 0xc3e00000, v167
	v_min_f32_e32 v191, 0x43e00000, v167
	s_waitcnt lgkmcnt(0)
	s_nop 1
	v_mov_b32_dpp v192, v191 quad_perm:[1,0,3,2] row_mask:0xf bank_mask:0xf
	v_mov_b32_e32 v167, v3
	s_waitcnt lgkmcnt(0)
	v_cvt_pk_fp8_f32 v167, v191, v192
	s_nop 1
	v_mov_b32_dpp v191, v167 quad_perm:[2,3,0,1] row_mask:0xf bank_mask:0xf
	s_and_saveexec_b64 s[6:7], s[4:5]
	s_cbranch_execz .LBB0_1381
	v_and_b32_e32 v167, 0xffff, v167
	v_add_co_u32_e32 v192, vcc, 0x9000, v6
	s_waitcnt lgkmcnt(0)
	v_lshl_or_b32 v167, v191, 16, v167
	v_addc_co_u32_e32 v193, vcc, 0, v7, vcc
	global_store_dword v[192:193], v167, off offset:96
.LBB0_1381:
	s_or_b64 exec, exec, s[6:7]
	s_waitcnt vmcnt(9)
	v_lshlrev_b32_e32 v167, 16, v166
	s_waitcnt lgkmcnt(0)
	v_mul_f32 v191, v71, v178
	s_nop 0
	v_fma_f32 v167, v212, v191, v167
	s_nop 0
	v_mul_f32 v167, v167, v156
	s_nop 0
	v_mul_f32 v167, v167, v186
	s_nop 0
	v_max_f32_e32 v167, v167, v167
	v_max_f32_e32 v167, 0xc3e00000, v167
	v_min_f32_e32 v191, 0x43e00000, v167
	s_nop 1
	v_mov_b32_dpp v192, v191 quad_perm:[1,0,3,2] row_mask:0xf bank_mask:0xf
	v_mov_b32_e32 v167, v3
	s_waitcnt lgkmcnt(0)
	v_cvt_pk_fp8_f32 v167, v191, v192
	s_nop 1
	v_mov_b32_dpp v191, v167 quad_perm:[2,3,0,1] row_mask:0xf bank_mask:0xf
	s_and_saveexec_b64 s[6:7], s[4:5]
	s_cbranch_execz .LBB0_1383
	v_and_b32_e32 v167, 0xffff, v167
	v_add_co_u32_e32 v192, vcc, 0x9000, v6
	s_waitcnt lgkmcnt(0)
	v_lshl_or_b32 v167, v191, 16, v167
	v_addc_co_u32_e32 v193, vcc, 0, v7, vcc
	global_store_dword v[192:193], v167, off offset:128
; __device__ __forceinline__ int crow(int r, int hi) { return (r & 3) + 8 * (r >> 2) + 4 * hi; }
; __device__ __forceinline__ float mul_ns(float a, float b) { float r; asm("v_mul_f32 %0, %1, %2" : "=v"(r) : "v"(a), "v"(b)); return r; }
; __device__ __forceinline__ float fma_ns(float a, float b, float c) { float r; asm("v_fma_f32 %0, %1, %2, %3" : "=v"(r) : "v"(a), "v"(b), "v"(c)); return r; }
; __device__ __forceinline__ void store_quad8(unsigned char* p, float v, int r32) {
;     v = fminf(fmaxf(v, -448.f), 448.f);
;     const float v1 = swz_xor<1>(v);
;     const int w = __builtin_amdgcn_cvt_pk_fp8_f32(v, v1, 0, false);
;     const int w2 = __builtin_amdgcn_ds_swizzle(w, (2 << 10) | 0x1f);
;     if ((r32 & 3) == 0) *(unsigned*)p = ((unsigned)w & 0xffffu) | ((unsigned)w2 << 16);
; }
;     __device__ __forceinline__ void operator()(f32x16 (&o)[8], const float (&rli)[16], int wid, int lane, int r32, int hi) const {
;     ...
;                 for (int q = 0; q < 4; ++q) { const int r = rb + q;
; #pragma unroll
;                     for (int d0 = 0; d0 < 8; ++d0) { const float t = __uint_as_float((d0 & 1) ? (tw[q][d0 >> 1] & 0xffff0000u) : (tw[q][d0 >> 1] << 16));
;                         const float dd = fma_ns(nlam, mul_ns(o[d0][r], rli[r]), t);
;                         store_quad8(base + (crow(r, 0) * 4096 + d0 * 32) + uo, mul_ns(mul_ns(dd, rn[r]), g[d0]), r32); } }
.LBB0_1383:
	s_or_b64 exec, exec, s[6:7]
	v_and_b32_e32 v166, 0xffff0000, v166
	v_mul_f32 v167, v55, v178
	s_nop 0
	v_fma_f32 v166, v212, v167, v166
	s_nop 0
	v_mul_f32 v166, v166, v156
	s_nop 0
	v_mul_f32 v166, v166, v185
	s_nop 0
	v_max_f32_e32 v166, v166, v166
	v_max_f32_e32 v166, 0xc3e00000, v166
	v_min_f32_e32 v167, 0x43e00000, v166
	s_waitcnt lgkmcnt(0)
	s_nop 1
	v_mov_b32_dpp v191, v167 quad_perm:[1,0,3,2] row_mask:0xf bank_mask:0xf
	v_mov_b32_e32 v166, v3
	s_waitcnt lgkmcnt(0)
	v_cvt_pk_fp8_f32 v166, v167, v191
	s_nop 1
	v_mov_b32_dpp v167, v166 quad_perm:[2,3,0,1] row_mask:0xf bank_mask:0xf
	s_and_saveexec_b64 s[6:7], s[4:5]
	s_cbranch_execz .LBB0_1385
	v_and_b32_e32 v166, 0xffff, v166
	s_waitcnt lgkmcnt(0)
	v_lshl_or_b32 v191, v167, 16, v166
	v_add_co_u32_e32 v166, vcc, 0x9000, v6
	s_nop 1
	v_addc_co_u32_e32 v167, vcc, 0, v7, vcc
	global_store_dword v[166:167], v191, off offset:160
.LBB0_1385:
	s_or_b64 exec, exec, s[6:7]
	s_waitcnt vmcnt(8)
	v_lshlrev_b32_e32 v166, 16, v164
	s_waitcnt lgkmcnt(0)
	v_mul_f32 v167, v39, v178
	s_nop 0
	v_fma_f32 v166, v212, v167, v166
	s_nop 0
	v_mul_f32 v166, v166, v156
	s_nop 0
	v_mul_f32 v166, v166, v184
	s_nop 0
	v_max_f32_e32 v166, v166, v166
	v_max_f32_e32 v166, 0xc3e00000, v166
	v_min_f32_e32 v167, 0x43e00000, v166
	s_nop 1
	v_mov_b32_dpp v191, v167 quad_perm:[1,0,3,2] row_mask:0xf bank_mask:0xf
	v_mov_b32_e32 v166, v3
	s_waitcnt lgkmcnt(0)
	v_cvt_pk_fp8_f32 v166, v167, v191
	s_nop 1
	v_mov_b32_dpp v167, v166 quad_perm:[2,3,0,1] row_mask:0xf bank_mask:0xf
	s_and_saveexec_b64 s[6:7], s[4:5]
	s_cbranch_execz .LBB0_1387
	v_and_b32_e32 v166, 0xffff, v166
	s_waitcnt lgkmcnt(0)
	v_lshl_or_b32 v191, v167, 16, v166
	v_add_co_u32_e32 v166, vcc, 0x9000, v6
	s_nop 1
	v_addc_co_u32_e32 v167, vcc, 0, v7, vcc
	global_store_dword v[166:167], v191, off offset:192
.LBB0_1387:
	s_or_b64 exec, exec, s[6:7]
	v_and_b32_e32 v164, 0xffff0000, v164
	v_mul_f32 v166, v23, v178
	s_nop 0
	v_fma_f32 v164, v212, v166, v164
	s_nop 0
	v_mul_f32 v156, v164, v156
	s_nop 0
	v_mul_f32 v156, v156, v165
	s_nop 0
	v_max_f32_e32 v156, v156, v156
	v_max_f32_e32 v156, 0xc3e00000, v156
	v_min_f32_e32 v164, 0x43e00000, v156
	s_nop 1
	v_mov_b32_dpp v166, v164 quad_perm:[1,0,3,2] row_mask:0xf bank_mask:0xf
	v_mov_b32_e32 v156, v3
	s_waitcnt lgkmcnt(0)
	v_cvt_pk_fp8_f32 v156, v164, v166
	s_nop 1
	v_mov_b32_dpp v164, v156 quad_perm:[2,3,0,1] row_mask:0xf bank_mask:0xf
	s_and_saveexec_b64 s[6:7], s[4:5]
	s_cbranch_execz .LBB0_1389
	v_and_b32_e32 v156, 0xffff, v156
	v_add_co_u32_e32 v166, vcc, 0x9000, v6
	s_waitcnt lgkmcnt(0)
	v_lshl_or_b32 v156, v164, 16, v156
	v_addc_co_u32_e32 v167, vcc, 0, v7, vcc
	global_store_dword v[166:167], v156, off offset:224
.LBB0_1389:
	s_or_b64 exec, exec, s[6:7]
	v_pk_add_f32 v[152:153], v[152:153], v[154:155]
	v_mul_f32 v155, v136, v177
	s_nop 0
	v_pk_fma_f32 v[152:153], v[152:153], s[54:55], v[198:199] op_sel_hi:[1,0,0]
	s_nop 0
	v_mul_f32_e32 v154, 0x4b800000, v153
	v_cmp_gt_f32_e32 vcc, s53, v153
	v_cmp_gt_f32_e64 s[6:7], s53, v152
	s_nop 0
	v_cndmask_b32_e32 v153, v153, v154, vcc
	v_rsq_f32_e32 v153, v153
	s_waitcnt vmcnt(7)
	v_lshlrev_b32_e32 v154, 16, v163
	v_fma_f32 v154, v212, v155, v154
	v_mul_f32_e32 v156, 0x45800000, v153
	v_cndmask_b32_e32 v153, v153, v156, vcc
	v_mul_f32_e32 v153, 0x3f4ccccd, v153
	v_mul_f32 v154, v154, v153
	s_nop 0
	v_mul_f32 v154, v154, v190
	s_nop 0
	v_max_f32_e32 v154, v154, v154
	v_max_f32_e32 v154, 0xc3e00000, v154
	v_min_f32_e32 v155, 0x43e00000, v154
	s_nop 1
	v_mov_b32_dpp v156, v155 quad_perm:[1,0,3,2] row_mask:0xf bank_mask:0xf
	v_mov_b32_e32 v154, v3
	s_waitcnt lgkmcnt(0)
	v_cvt_pk_fp8_f32 v154, v155, v156
	s_nop 1
	v_mov_b32_dpp v155, v154 quad_perm:[2,3,0,1] row_mask:0xf bank_mask:0xf
	s_and_saveexec_b64 s[8:9], s[4:5]
	s_cbranch_execz .LBB0_1391
	v_and_b32_e32 v154, 0xffff, v154
	s_waitcnt lgkmcnt(0)
	v_lshl_or_b32 v156, v155, 16, v154
	v_add_co_u32_e32 v154, vcc, 0xa000, v6
	s_nop 1
	v_addc_co_u32_e32 v155, vcc, 0, v7, vcc
	global_store_dword v[154:155], v156, off
.LBB0_1391:
	s_or_b64 exec, exec, s[8:9]
	v_and_b32_e32 v154, 0xffff0000, v163
	s_waitcnt lgkmcnt(0)
	v_mul_f32 v155, v120, v177
	s_nop 0
	v_fma_f32 v154, v212, v155, v154
	s_nop 0
	v_mul_f32 v154, v154, v153
	s_nop 0
	v_mul_f32 v154, v154, v189
	s_nop 0
	v_max_f32_e32 v154, v154, v154
	v_max_f32_e32 v154, 0xc3e00000, v154
	v_min_f32_e32 v155, 0x43e00000, v154
	s_nop 1
	v_mov_b32_dpp v156, v155 quad_perm:[1,0,3,2] row_mask:0xf bank_mask:0xf
	v_mov_b32_e32 v154, v3
	s_waitcnt lgkmcnt(0)
	v_cvt_pk_fp8_f32 v154, v155, v156
	s_nop 1
	v_mov_b32_dpp v155, v154 quad_perm:[2,3,0,1] row_mask:0xf bank_mask:0xf
	s_and_saveexec_b64 s[8:9], s[4:5]
	s_cbranch_execz .LBB0_1393
	v_and_b32_e32 v154, 0xffff, v154
	s_waitcnt lgkmcnt(0)
	v_lshl_or_b32 v156, v155, 16, v154
	v_add_co_u32_e32 v154, vcc, 0xa000, v6
	s_nop 1
	v_addc_co_u32_e32 v155, vcc, 0, v7, vcc
	global_store_dword v[154:155], v156, off offset:32
.LBB0_1393:
	s_or_b64 exec, exec, s[8:9]
	s_waitcnt vmcnt(6)
	v_lshlrev_b32_e32 v154, 16, v162
	s_waitcnt lgkmcnt(0)
	v_mul_f32 v155, v104, v177
	s_nop 0
	v_fma_f32 v154, v212, v155, v154
	s_nop 0
	v_mul_f32 v154, v154, v153
	s_nop 0
	v_mul_f32 v154, v154, v188
	s_nop 0
	v_max_f32_e32 v154, v154, v154
	v_max_f32_e32 v154, 0xc3e00000, v154
	v_min_f32_e32 v155, 0x43e00000, v154
	s_nop 1
	v_mov_b32_dpp v156, v155 quad_perm:[1,0,3,2] row_mask:0xf bank_mask:0xf
	v_mov_b32_e32 v154, v3
	s_waitcnt lgkmcnt(0)
	v_cvt_pk_fp8_f32 v154, v155, v156
	s_nop 1
	v_mov_b32_dpp v155, v154 quad_perm:[2,3,0,1] row_mask:0xf bank_mask:0xf
	s_and_saveexec_b64 s[8:9], s[4:5]
	s_cbranch_execz .LBB0_1395
	v_and_b32_e32 v154, 0xffff, v154
	s_waitcnt lgkmcnt(0)
	v_lshl_or_b32 v156, v155, 16, v154
	v_add_co_u32_e32 v154, vcc, 0xa000, v6
	s_nop 1
	v_addc_co_u32_e32 v155, vcc, 0, v7, vcc
	global_store_dword v[154:155], v156, off offset:64
; __device__ __forceinline__ int crow(int r, int hi) { return (r & 3) + 8 * (r >> 2) + 4 * hi; }
; __device__ __forceinline__ float mul_ns(float a, float b) { float r; asm("v_mul_f32 %0, %1, %2" : "=v"(r) : "v"(a), "v"(b)); return r; }
; __device__ __forceinline__ float fma_ns(float a, float b, float c) { float r; asm("v_fma_f32 %0, %1, %2, %3" : "=v"(r) : "v"(a), "v"(b), "v"(c)); return r; }
; __device__ __forceinline__ void store_quad8(unsigned char* p, float v, int r32) {
;     v = fminf(fmaxf(v, -448.f), 448.f);
;     const float v1 = swz_xor<1>(v);
;     const int w = __builtin_amdgcn_cvt_pk_fp8_f32(v, v1, 0, false);
;     const int w2 = __builtin_amdgcn_ds_swizzle(w, (2 << 10) | 0x1f);
;     if ((r32 & 3) == 0) *(unsigned*)p = ((unsigned)w & 0xffffu) | ((unsigned)w2 << 16);
; }
;     __device__ __forceinline__ void operator()(f32x16 (&o)[8], const float (&rli)[16], int wid, int lane, int r32, int hi) const {
;     ...
;                 for (int q = 0; q < 4; ++q) { const int r = rb + q;
; #pragma unroll
;                     for (int d0 = 0; d0 < 8; ++d0) { const float t = __uint_as_float((d0 & 1) ? (tw[q][d0 >> 1] & 0xffff0000u) : (tw[q][d0 >> 1] << 16));
;                         const float dd = fma_ns(nlam, mul_ns(o[d0][r], rli[r]), t);
;                         store_quad8(base + (crow(r, 0) * 4096 + d0 * 32) + uo, mul_ns(mul_ns(dd, rn[r]), g[d0]), r32); } }
.LBB0_1395:
	s_or_b64 exec, exec, s[8:9]
	v_and_b32_e32 v154, 0xffff0000, v162
	s_waitcnt lgkmcnt(0)
	v_mul_f32 v155, v88, v177
	s_nop 0
	v_fma_f32 v154, v212, v155, v154
	s_nop 0
	v_mul_f32 v154, v154, v153
	s_nop 0
	v_mul_f32 v154, v154, v187
	s_nop 0
	v_max_f32_e32 v154, v154, v154
	v_max_f32_e32 v154, 0xc3e00000, v154
	v_min_f32_e32 v155, 0x43e00000, v154
	s_nop 1
	v_mov_b32_dpp v156, v155 quad_perm:[1,0,3,2] row_mask:0xf bank_mask:0xf
	v_mov_b32_e32 v154, v3
	s_waitcnt lgkmcnt(0)
	v_cvt_pk_fp8_f32 v154, v155, v156
	s_nop 1
	v_mov_b32_dpp v155, v154 quad_perm:[2,3,0,1] row_mask:0xf bank_mask:0xf
	s_and_saveexec_b64 s[8:9], s[4:5]
	s_cbranch_execz .LBB0_1397
	v_and_b32_e32 v154, 0xffff, v154
	s_waitcnt lgkmcnt(0)
	v_lshl_or_b32 v156, v155, 16, v154
	v_add_co_u32_e32 v154, vcc, 0xa000, v6
	s_nop 1
	v_addc_co_u32_e32 v155, vcc, 0, v7, vcc
	global_store_dword v[154:155], v156, off offset:96
.LBB0_1397:
	s_or_b64 exec, exec, s[8:9]
	s_waitcnt vmcnt(5)
	v_lshlrev_b32_e32 v154, 16, v161
	s_waitcnt lgkmcnt(0)
	v_mul_f32 v155, v72, v177
	s_nop 0
	v_fma_f32 v154, v212, v155, v154
	s_nop 0
	v_mul_f32 v154, v154, v153
	s_nop 0
	v_mul_f32 v154, v154, v186
	s_nop 0
	v_max_f32_e32 v154, v154, v154
	v_max_f32_e32 v154, 0xc3e00000, v154
	v_min_f32_e32 v155, 0x43e00000, v154
	s_nop 1
	v_mov_b32_dpp v156, v155 quad_perm:[1,0,3,2] row_mask:0xf bank_mask:0xf
	v_mov_b32_e32 v154, v3
	s_waitcnt lgkmcnt(0)
	v_cvt_pk_fp8_f32 v154, v155, v156
	s_nop 1
	v_mov_b32_dpp v155, v154 quad_perm:[2,3,0,1] row_mask:0xf bank_mask:0xf
	s_and_saveexec_b64 s[8:9], s[4:5]
	s_cbranch_execz .LBB0_1399
	v_and_b32_e32 v154, 0xffff, v154
	s_waitcnt lgkmcnt(0)
	v_lshl_or_b32 v156, v155, 16, v154
	v_add_co_u32_e32 v154, vcc, 0xa000, v6
	s_nop 1
	v_addc_co_u32_e32 v155, vcc, 0, v7, vcc
	global_store_dword v[154:155], v156, off offset:128
.LBB0_1399:
	s_or_b64 exec, exec, s[8:9]
	v_and_b32_e32 v154, 0xffff0000, v161
	s_waitcnt lgkmcnt(0)
	v_mul_f32 v155, v56, v177
	s_nop 0
	v_fma_f32 v154, v212, v155, v154
	s_nop 0
	v_mul_f32 v154, v154, v153
	s_nop 0
	v_mul_f32 v154, v154, v185
	s_nop 0
	v_max_f32_e32 v154, v154, v154
	v_max_f32_e32 v154, 0xc3e00000, v154
	v_min_f32_e32 v155, 0x43e00000, v154
	s_nop 1
	v_mov_b32_dpp v156, v155 quad_perm:[1,0,3,2] row_mask:0xf bank_mask:0xf
	v_mov_b32_e32 v154, v3
	s_waitcnt lgkmcnt(0)
	v_cvt_pk_fp8_f32 v154, v155, v156
	s_nop 1
	v_mov_b32_dpp v155, v154 quad_perm:[2,3,0,1] row_mask:0xf bank_mask:0xf
	s_and_saveexec_b64 s[8:9], s[4:5]
	s_cbranch_execz .LBB0_1401
	v_and_b32_e32 v154, 0xffff, v154
	s_waitcnt lgkmcnt(0)
	v_lshl_or_b32 v156, v155, 16, v154
	v_add_co_u32_e32 v154, vcc, 0xa000, v6
	s_nop 1
	v_addc_co_u32_e32 v155, vcc, 0, v7, vcc
	global_store_dword v[154:155], v156, off offset:160
.LBB0_1401:
	s_or_b64 exec, exec, s[8:9]
	s_waitcnt vmcnt(4)
	v_lshlrev_b32_e32 v154, 16, v160
	s_waitcnt lgkmcnt(0)
	v_mul_f32 v155, v40, v177
	s_nop 0
	v_fma_f32 v154, v212, v155, v154
	s_nop 0
	v_mul_f32 v154, v154, v153
	s_nop 0
	v_mul_f32 v154, v154, v184
	s_nop 0
	v_max_f32_e32 v154, v154, v154
	v_max_f32_e32 v154, 0xc3e00000, v154
	v_min_f32_e32 v155, 0x43e00000, v154
	s_nop 1
	v_mov_b32_dpp v156, v155 quad_perm:[1,0,3,2] row_mask:0xf bank_mask:0xf
	v_mov_b32_e32 v154, v3
	s_waitcnt lgkmcnt(0)
	v_cvt_pk_fp8_f32 v154, v155, v156
	s_nop 1
	v_mov_b32_dpp v155, v154 quad_perm:[2,3,0,1] row_mask:0xf bank_mask:0xf
	s_and_saveexec_b64 s[8:9], s[4:5]
	s_cbranch_execz .LBB0_1403
	v_and_b32_e32 v154, 0xffff, v154
	s_waitcnt lgkmcnt(0)
	v_lshl_or_b32 v156, v155, 16, v154
	v_add_co_u32_e32 v154, vcc, 0xa000, v6
	s_nop 1
	v_addc_co_u32_e32 v155, vcc, 0, v7, vcc
	global_store_dword v[154:155], v156, off offset:192
.LBB0_1403:
	s_or_b64 exec, exec, s[8:9]
	v_and_b32_e32 v154, 0xffff0000, v160
	s_waitcnt lgkmcnt(0)
	v_mul_f32 v155, v24, v177
	s_nop 0
	v_fma_f32 v154, v212, v155, v154
	s_nop 0
	v_mul_f32 v153, v154, v153
	s_nop 0
	v_mul_f32 v153, v153, v165
	s_nop 0
	v_max_f32_e32 v153, v153, v153
	v_max_f32_e32 v153, 0xc3e00000, v153
	v_min_f32_e32 v154, 0x43e00000, v153
	s_nop 1
	v_mov_b32_dpp v155, v154 quad_perm:[1,0,3,2] row_mask:0xf bank_mask:0xf
	v_mov_b32_e32 v153, v3
	s_waitcnt lgkmcnt(0)
	v_cvt_pk_fp8_f32 v153, v154, v155
	s_nop 1
	v_mov_b32_dpp v154, v153 quad_perm:[2,3,0,1] row_mask:0xf bank_mask:0xf
	s_and_saveexec_b64 s[8:9], s[4:5]
	s_cbranch_execz .LBB0_1405
	v_and_b32_e32 v153, 0xffff, v153
	s_waitcnt lgkmcnt(0)
	v_lshl_or_b32 v153, v154, 16, v153
	v_add_co_u32_e32 v154, vcc, 0xa000, v6
	s_nop 1
	v_addc_co_u32_e32 v155, vcc, 0, v7, vcc
	global_store_dword v[154:155], v153, off offset:224
.LBB0_1405:
	s_or_b64 exec, exec, s[8:9]
	v_mul_f32_e32 v153, 0x4b800000, v152
	v_cndmask_b32_e64 v152, v152, v153, s[6:7]
	v_rsq_f32_e32 v152, v152
	s_waitcnt lgkmcnt(0)
	v_mul_f32 v154, v137, v176
	v_mul_f32_e32 v153, 0x45800000, v152
	v_cndmask_b32_e64 v152, v152, v153, s[6:7]
	s_waitcnt vmcnt(3)
	v_lshlrev_b32_e32 v153, 16, v159
	v_fma_f32 v153, v212, v154, v153
	v_mul_f32_e32 v152, 0x3f4ccccd, v152
	v_mul_f32 v153, v153, v152
	s_nop 0
	v_mul_f32 v153, v153, v190
	s_nop 0
	v_max_f32_e32 v153, v153, v153
	v_max_f32_e32 v153, 0xc3e00000, v153
	v_min_f32_e32 v154, 0x43e00000, v153
	s_nop 1
	v_mov_b32_dpp v155, v154 quad_perm:[1,0,3,2] row_mask:0xf bank_mask:0xf
	v_mov_b32_e32 v153, v3
	s_waitcnt lgkmcnt(0)
	v_cvt_pk_fp8_f32 v153, v154, v155
	s_nop 1
	v_mov_b32_dpp v154, v153 quad_perm:[2,3,0,1] row_mask:0xf bank_mask:0xf
	s_and_saveexec_b64 s[6:7], s[4:5]
	s_cbranch_execz .LBB0_1407
	v_and_b32_e32 v153, 0xffff, v153
	s_waitcnt lgkmcnt(0)
	v_lshl_or_b32 v153, v154, 16, v153
	v_add_co_u32_e32 v154, vcc, 0xb000, v6
	s_nop 1
	v_addc_co_u32_e32 v155, vcc, 0, v7, vcc
	global_store_dword v[154:155], v153, off
; __device__ __forceinline__ int crow(int r, int hi) { return (r & 3) + 8 * (r >> 2) + 4 * hi; }
; __device__ __forceinline__ float mul_ns(float a, float b) { float r; asm("v_mul_f32 %0, %1, %2" : "=v"(r) : "v"(a), "v"(b)); return r; }
; __device__ __forceinline__ float fma_ns(float a, float b, float c) { float r; asm("v_fma_f32 %0, %1, %2, %3" : "=v"(r) : "v"(a), "v"(b), "v"(c)); return r; }
; __device__ __forceinline__ void store_quad8(unsigned char* p, float v, int r32) {
;     v = fminf(fmaxf(v, -448.f), 448.f);
;     const float v1 = swz_xor<1>(v);
;     const int w = __builtin_amdgcn_cvt_pk_fp8_f32(v, v1, 0, false);
;     const int w2 = __builtin_amdgcn_ds_swizzle(w, (2 << 10) | 0x1f);
;     if ((r32 & 3) == 0) *(unsigned*)p = ((unsigned)w & 0xffffu) | ((unsigned)w2 << 16);
; }
;     __device__ __forceinline__ void operator()(f32x16 (&o)[8], const float (&rli)[16], int wid, int lane, int r32, int hi) const {
;     ...
;                 for (int q = 0; q < 4; ++q) { const int r = rb + q;
; #pragma unroll
;                     for (int d0 = 0; d0 < 8; ++d0) { const float t = __uint_as_float((d0 & 1) ? (tw[q][d0 >> 1] & 0xffff0000u) : (tw[q][d0 >> 1] << 16));
;                         const float dd = fma_ns(nlam, mul_ns(o[d0][r], rli[r]), t);
;                         store_quad8(base + (crow(r, 0) * 4096 + d0 * 32) + uo, mul_ns(mul_ns(dd, rn[r]), g[d0]), r32); } }
.LBB0_1407:
	s_or_b64 exec, exec, s[6:7]
	v_and_b32_e32 v153, 0xffff0000, v159
	s_waitcnt lgkmcnt(0)
	v_mul_f32 v154, v121, v176
	s_nop 0
	v_fma_f32 v153, v212, v154, v153
	s_nop 0
	v_mul_f32 v153, v153, v152
	s_nop 0
	v_mul_f32 v153, v153, v189
	s_nop 0
	v_max_f32_e32 v153, v153, v153
	v_max_f32_e32 v153, 0xc3e00000, v153
	v_min_f32_e32 v154, 0x43e00000, v153
	s_nop 1
	v_mov_b32_dpp v155, v154 quad_perm:[1,0,3,2] row_mask:0xf bank_mask:0xf
	v_mov_b32_e32 v153, v3
	s_waitcnt lgkmcnt(0)
	v_cvt_pk_fp8_f32 v153, v154, v155
	s_nop 1
	v_mov_b32_dpp v154, v153 quad_perm:[2,3,0,1] row_mask:0xf bank_mask:0xf
	s_and_saveexec_b64 s[6:7], s[4:5]
	s_cbranch_execz .LBB0_1409
	v_and_b32_e32 v153, 0xffff, v153
	s_waitcnt lgkmcnt(0)
	v_lshl_or_b32 v153, v154, 16, v153
	v_add_co_u32_e32 v154, vcc, 0xb000, v6
	s_nop 1
	v_addc_co_u32_e32 v155, vcc, 0, v7, vcc
	global_store_dword v[154:155], v153, off offset:32
.LBB0_1409:
	s_or_b64 exec, exec, s[6:7]
	s_waitcnt vmcnt(2)
	v_lshlrev_b32_e32 v153, 16, v158
	s_waitcnt lgkmcnt(0)
	v_mul_f32 v154, v105, v176
	s_nop 0
	v_fma_f32 v153, v212, v154, v153
	s_nop 0
	v_mul_f32 v153, v153, v152
	s_nop 0
	v_mul_f32 v153, v153, v188
	s_nop 0
	v_max_f32_e32 v153, v153, v153
	v_max_f32_e32 v153, 0xc3e00000, v153
	v_min_f32_e32 v154, 0x43e00000, v153
	s_nop 1
	v_mov_b32_dpp v155, v154 quad_perm:[1,0,3,2] row_mask:0xf bank_mask:0xf
	v_mov_b32_e32 v153, v3
	s_waitcnt lgkmcnt(0)
	v_cvt_pk_fp8_f32 v153, v154, v155
	s_nop 1
	v_mov_b32_dpp v154, v153 quad_perm:[2,3,0,1] row_mask:0xf bank_mask:0xf
	s_and_saveexec_b64 s[6:7], s[4:5]
	s_cbranch_execz .LBB0_1411
	v_and_b32_e32 v153, 0xffff, v153
	s_waitcnt lgkmcnt(0)
	v_lshl_or_b32 v153, v154, 16, v153
	v_add_co_u32_e32 v154, vcc, 0xb000, v6
	s_nop 1
	v_addc_co_u32_e32 v155, vcc, 0, v7, vcc
	global_store_dword v[154:155], v153, off offset:64
.LBB0_1411:
	s_or_b64 exec, exec, s[6:7]
	v_and_b32_e32 v153, 0xffff0000, v158
	s_waitcnt lgkmcnt(0)
	v_mul_f32 v154, v89, v176
	s_nop 0
	v_fma_f32 v153, v212, v154, v153
	s_nop 0
	v_mul_f32 v153, v153, v152
	s_nop 0
	v_mul_f32 v153, v153, v187
	s_nop 0
	v_max_f32_e32 v153, v153, v153
	v_max_f32_e32 v153, 0xc3e00000, v153
	v_min_f32_e32 v154, 0x43e00000, v153
	s_nop 1
	v_mov_b32_dpp v155, v154 quad_perm:[1,0,3,2] row_mask:0xf bank_mask:0xf
	v_mov_b32_e32 v153, v3
	s_waitcnt lgkmcnt(0)
	v_cvt_pk_fp8_f32 v153, v154, v155
	s_nop 1
	v_mov_b32_dpp v154, v153 quad_perm:[2,3,0,1] row_mask:0xf bank_mask:0xf
	s_and_saveexec_b64 s[6:7], s[4:5]
	s_cbranch_execz .LBB0_1413
	v_and_b32_e32 v153, 0xffff, v153
	s_waitcnt lgkmcnt(0)
	v_lshl_or_b32 v153, v154, 16, v153
	v_add_co_u32_e32 v154, vcc, 0xb000, v6
	s_nop 1
	v_addc_co_u32_e32 v155, vcc, 0, v7, vcc
	global_store_dword v[154:155], v153, off offset:96
.LBB0_1413:
	s_or_b64 exec, exec, s[6:7]
	s_waitcnt vmcnt(1)
	v_lshlrev_b32_e32 v153, 16, v157
	s_waitcnt lgkmcnt(0)
	v_mul_f32 v154, v73, v176
	s_nop 0
	v_fma_f32 v153, v212, v154, v153
	s_nop 0
	v_mul_f32 v153, v153, v152
	s_nop 0
	v_mul_f32 v153, v153, v186
	s_nop 0
	v_max_f32_e32 v153, v153, v153
	v_max_f32_e32 v153, 0xc3e00000, v153
	v_min_f32_e32 v154, 0x43e00000, v153
	s_nop 1
	v_mov_b32_dpp v155, v154 quad_perm:[1,0,3,2] row_mask:0xf bank_mask:0xf
	v_mov_b32_e32 v153, v3
	s_waitcnt lgkmcnt(0)
	v_cvt_pk_fp8_f32 v153, v154, v155
	s_nop 1
	v_mov_b32_dpp v154, v153 quad_perm:[2,3,0,1] row_mask:0xf bank_mask:0xf
	s_and_saveexec_b64 s[6:7], s[4:5]
	s_cbranch_execz .LBB0_1415
	v_and_b32_e32 v153, 0xffff, v153
	s_waitcnt lgkmcnt(0)
	v_lshl_or_b32 v153, v154, 16, v153
	v_add_co_u32_e32 v154, vcc, 0xb000, v6
	s_nop 1
	v_addc_co_u32_e32 v155, vcc, 0, v7, vcc
	global_store_dword v[154:155], v153, off offset:128
.LBB0_1415:
	s_or_b64 exec, exec, s[6:7]
	v_and_b32_e32 v153, 0xffff0000, v157
	s_waitcnt lgkmcnt(0)
	v_mul_f32 v154, v57, v176
	s_nop 0
	v_fma_f32 v153, v212, v154, v153
	s_nop 0
	v_mul_f32 v153, v153, v152
	s_nop 0
	v_mul_f32 v153, v153, v185
	s_nop 0
	v_max_f32_e32 v153, v153, v153
	v_max_f32_e32 v153, 0xc3e00000, v153
	v_min_f32_e32 v154, 0x43e00000, v153
	s_nop 1
	v_mov_b32_dpp v155, v154 quad_perm:[1,0,3,2] row_mask:0xf bank_mask:0xf
	v_mov_b32_e32 v153, v3
	s_waitcnt lgkmcnt(0)
	v_cvt_pk_fp8_f32 v153, v154, v155
	s_nop 1
	v_mov_b32_dpp v154, v153 quad_perm:[2,3,0,1] row_mask:0xf bank_mask:0xf
	s_and_saveexec_b64 s[6:7], s[4:5]
	s_cbranch_execz .LBB0_1417
	v_and_b32_e32 v153, 0xffff, v153
	s_waitcnt lgkmcnt(0)
	v_lshl_or_b32 v153, v154, 16, v153
	v_add_co_u32_e32 v154, vcc, 0xb000, v6
	s_nop 1
	v_addc_co_u32_e32 v155, vcc, 0, v7, vcc
	global_store_dword v[154:155], v153, off offset:160
.LBB0_1417:
	s_or_b64 exec, exec, s[6:7]
	s_waitcnt vmcnt(0)
	v_lshlrev_b32_e32 v153, 16, v2
	s_waitcnt lgkmcnt(0)
	v_mul_f32 v154, v41, v176
	s_nop 0
	v_fma_f32 v153, v212, v154, v153
	s_nop 0
	v_mul_f32 v153, v153, v152
	s_nop 0
	v_mul_f32 v153, v153, v184
	s_nop 0
	v_max_f32_e32 v153, v153, v153
	v_max_f32_e32 v153, 0xc3e00000, v153
	v_min_f32_e32 v154, 0x43e00000, v153
	s_nop 1
	v_mov_b32_dpp v155, v154 quad_perm:[1,0,3,2] row_mask:0xf bank_mask:0xf
	v_mov_b32_e32 v153, v3
	s_waitcnt lgkmcnt(0)
	v_cvt_pk_fp8_f32 v153, v154, v155
	s_nop 1
	v_mov_b32_dpp v154, v153 quad_perm:[2,3,0,1] row_mask:0xf bank_mask:0xf
	s_and_saveexec_b64 s[6:7], s[4:5]
	s_cbranch_execz .LBB0_1419
	v_and_b32_e32 v153, 0xffff, v153
	s_waitcnt lgkmcnt(0)
	v_lshl_or_b32 v153, v154, 16, v153
	v_add_co_u32_e32 v154, vcc, 0xb000, v6
	s_nop 1
	v_addc_co_u32_e32 v155, vcc, 0, v7, vcc
	global_store_dword v[154:155], v153, off offset:192
; #define SBAR() __builtin_amdgcn_sched_barrier(0)
; __device__ __forceinline__ int crow(int r, int hi) { return (r & 3) + 8 * (r >> 2) + 4 * hi; }
; __device__ __forceinline__ float mul_ns(float a, float b) { float r; asm("v_mul_f32 %0, %1, %2" : "=v"(r) : "v"(a), "v"(b)); return r; }
; __device__ __forceinline__ float fma_ns(float a, float b, float c) { float r; asm("v_fma_f32 %0, %1, %2, %3" : "=v"(r) : "v"(a), "v"(b), "v"(c)); return r; }
; __device__ __forceinline__ void store_quad8(unsigned char* p, float v, int r32) {
;     v = fminf(fmaxf(v, -448.f), 448.f);
;     const float v1 = swz_xor<1>(v);
;     const int w = __builtin_amdgcn_cvt_pk_fp8_f32(v, v1, 0, false);
;     const int w2 = __builtin_amdgcn_ds_swizzle(w, (2 << 10) | 0x1f);
;     if ((r32 & 3) == 0) *(unsigned*)p = ((unsigned)w & 0xffffu) | ((unsigned)w2 << 16);
; }
;     __device__ __forceinline__ void operator()(f32x16 (&o)[8], const float (&rli)[16], int wid, int lane, int r32, int hi) const {
;     ...
;             for (int rb = 0; rb < 16; rb += 4) { unsigned tw[4][4];
; #pragma unroll
;                 for (int q = 0; q < 4; ++q)
; #pragma unroll
;                     for (int k = 0; k < 4; ++k) tw[q][k] = (scw + ((rb + q) * 4 + k) * 64)[ul];
;                 asm volatile("" ::: "memory"); SBAR();
; #pragma unroll
;                 for (int q = 0; q < 4; ++q) { const int r = rb + q;
; #pragma unroll
;                     for (int d0 = 0; d0 < 8; ++d0) { const float t = __uint_as_float((d0 & 1) ? (tw[q][d0 >> 1] & 0xffff0000u) : (tw[q][d0 >> 1] << 16));
;                         const float dd = fma_ns(nlam, mul_ns(o[d0][r], rli[r]), t);
;                         store_quad8(base + (crow(r, 0) * 4096 + d0 * 32) + uo, mul_ns(mul_ns(dd, rn[r]), g[d0]), r32); } }
.LBB0_1419:
	s_or_b64 exec, exec, s[6:7]
	v_and_b32_e32 v2, 0xffff0000, v2
	v_mul_f32 v153, v25, v176
	s_nop 0
	v_fma_f32 v2, v212, v153, v2
	s_nop 0
	v_mul_f32 v2, v2, v152
	s_nop 0
	v_mul_f32 v2, v2, v165
	s_nop 0
	v_max_f32_e32 v2, v2, v2
	v_max_f32_e32 v2, 0xc3e00000, v2
	v_min_f32_e32 v152, 0x43e00000, v2
	s_nop 1
	v_mov_b32_dpp v153, v152 quad_perm:[1,0,3,2] row_mask:0xf bank_mask:0xf
	v_mov_b32_e32 v2, v3
	s_waitcnt lgkmcnt(0)
	v_cvt_pk_fp8_f32 v2, v152, v153
	s_nop 1
	v_mov_b32_dpp v152, v2 quad_perm:[2,3,0,1] row_mask:0xf bank_mask:0xf
	s_and_saveexec_b64 s[6:7], s[4:5]
	s_cbranch_execz .LBB0_1421
	v_and_b32_e32 v2, 0xffff, v2
	s_waitcnt lgkmcnt(0)
	v_lshl_or_b32 v2, v152, 16, v2
	v_add_co_u32_e32 v152, vcc, 0xb000, v6
	s_nop 1
	v_addc_co_u32_e32 v153, vcc, 0, v7, vcc
	global_store_dword v[152:153], v2, off offset:224
.LBB0_1421:
	s_or_b64 exec, exec, s[6:7]
	s_mov_b64 s[6:7], 0x2000
	s_waitcnt lgkmcnt(0)
	v_lshl_add_u64 v[152:153], v[4:5], 0, s[6:7]
	s_mov_b64 s[6:7], 0x2100
	v_lshl_add_u64 v[154:155], v[4:5], 0, s[6:7]
	s_mov_b64 s[6:7], 0x2200
	v_lshl_add_u64 v[156:157], v[4:5], 0, s[6:7]
	s_mov_b64 s[6:7], 0x2300
	v_lshl_add_u64 v[158:159], v[4:5], 0, s[6:7]
	s_mov_b64 s[6:7], 0x2400
	v_lshl_add_u64 v[166:167], v[4:5], 0, s[6:7]
	s_mov_b64 s[6:7], 0x2500
	v_lshl_add_u64 v[192:193], v[4:5], 0, s[6:7]
	s_mov_b64 s[6:7], 0x2600
	v_pk_add_f32 v[148:149], v[148:149], v[150:151]
	v_lshl_add_u64 v[194:195], v[4:5], 0, s[6:7]
	s_mov_b64 s[6:7], 0x2700
	v_pk_fma_f32 v[148:149], v[148:149], s[54:55], v[198:199] op_sel_hi:[1,0,0]
	v_lshl_add_u64 v[196:197], v[4:5], 0, s[6:7]
	s_mov_b64 s[6:7], 0x2800
	v_mul_f32_e32 v2, 0x4b800000, v149
	v_cmp_gt_f32_e32 vcc, s53, v149
	v_lshl_add_u64 v[202:203], v[4:5], 0, s[6:7]
	s_mov_b64 s[6:7], 0x2900
	v_cndmask_b32_e32 v2, v149, v2, vcc
	v_lshl_add_u64 v[204:205], v[4:5], 0, s[6:7]
	s_mov_b64 s[6:7], 0x2a00
	v_rsq_f32_e32 v2, v2
	v_lshl_add_u64 v[206:207], v[4:5], 0, s[6:7]
	s_mov_b64 s[6:7], 0x2b00
	v_lshl_add_u64 v[208:209], v[4:5], 0, s[6:7]
	s_mov_b64 s[6:7], 0x2c00
	v_lshl_add_u64 v[214:215], v[4:5], 0, s[6:7]
	s_mov_b64 s[6:7], 0x2d00
	v_lshl_add_u64 v[218:219], v[4:5], 0, s[6:7]
	s_mov_b64 s[6:7], 0x2e00
	v_mul_f32_e32 v149, 0x45800000, v2
	v_lshl_add_u64 v[220:221], v[4:5], 0, s[6:7]
	s_mov_b64 s[6:7], 0x2f00
	v_cndmask_b32_e32 v2, v2, v149, vcc
	v_lshl_add_u64 v[222:223], v[4:5], 0, s[6:7]
	v_cmp_gt_f32_e64 s[6:7], s53, v148
	v_mul_f32_e32 v160, 0x3f4ccccd, v2
	global_load_dword v164, v[152:153], off
	global_load_dword v163, v[154:155], off
	global_load_dword v162, v[156:157], off
	global_load_dword v161, v[158:159], off
	s_nop 0
	global_load_dword v159, v[166:167], off
	global_load_dword v158, v[192:193], off
	global_load_dword v157, v[194:195], off
	global_load_dword v156, v[196:197], off
	global_load_dword v155, v[202:203], off
	global_load_dword v154, v[204:205], off
	global_load_dword v153, v[206:207], off
	global_load_dword v152, v[208:209], off
	global_load_dword v151, v[214:215], off
	global_load_dword v150, v[218:219], off
	global_load_dword v149, v[220:221], off
	global_load_dword v2, v[222:223], off
	s_waitcnt vmcnt(15)
	v_lshlrev_b32_e32 v166, 16, v164
	v_mul_f32 v167, v138, v175
	s_nop 0
	v_fma_f32 v166, v212, v167, v166
	s_nop 0
	v_mul_f32 v166, v166, v160
	s_nop 0
	v_mul_f32 v166, v166, v190
	s_nop 0
	v_max_f32_e32 v166, v166, v166
	v_max_f32_e32 v166, 0xc3e00000, v166
	v_min_f32_e32 v167, 0x43e00000, v166
	s_nop 1
	v_mov_b32_dpp v191, v167 quad_perm:[1,0,3,2] row_mask:0xf bank_mask:0xf
	v_mov_b32_e32 v166, v3
	s_waitcnt lgkmcnt(0)
	v_cvt_pk_fp8_f32 v166, v167, v191
	s_nop 1
	v_mov_b32_dpp v167, v166 quad_perm:[2,3,0,1] row_mask:0xf bank_mask:0xf
	s_and_saveexec_b64 s[8:9], s[4:5]
	s_cbranch_execz .LBB0_1423
	v_and_b32_e32 v166, 0xffff, v166
	s_waitcnt lgkmcnt(0)
	v_lshl_or_b32 v191, v167, 16, v166
	v_add_co_u32_e32 v166, vcc, 0x10000, v6
	s_nop 1
	v_addc_co_u32_e32 v167, vcc, 0, v7, vcc
	global_store_dword v[166:167], v191, off
.LBB0_1423:
	s_or_b64 exec, exec, s[8:9]
	v_and_b32_e32 v164, 0xffff0000, v164
	v_mul_f32 v166, v122, v175
	s_nop 0
	v_fma_f32 v164, v212, v166, v164
	s_nop 0
	v_mul_f32 v164, v164, v160
	s_nop 0
	v_mul_f32 v164, v164, v189
	s_nop 0
	v_max_f32_e32 v164, v164, v164
	v_max_f32_e32 v164, 0xc3e00000, v164
	v_min_f32_e32 v166, 0x43e00000, v164
	s_waitcnt lgkmcnt(0)
	s_nop 1
	v_mov_b32_dpp v167, v166 quad_perm:[1,0,3,2] row_mask:0xf bank_mask:0xf
	v_mov_b32_e32 v164, v3
	s_waitcnt lgkmcnt(0)
	v_cvt_pk_fp8_f32 v164, v166, v167
	s_nop 1
	v_mov_b32_dpp v166, v164 quad_perm:[2,3,0,1] row_mask:0xf bank_mask:0xf
	s_and_saveexec_b64 s[8:9], s[4:5]
	s_cbranch_execz .LBB0_1425
	v_and_b32_e32 v164, 0xffff, v164
	s_waitcnt lgkmcnt(0)
	v_lshl_or_b32 v164, v166, 16, v164
	v_add_co_u32_e32 v166, vcc, 0x10000, v6
	s_nop 1
	v_addc_co_u32_e32 v167, vcc, 0, v7, vcc
	global_store_dword v[166:167], v164, off offset:32
.LBB0_1425:
	s_or_b64 exec, exec, s[8:9]
	s_waitcnt vmcnt(14)
	v_lshlrev_b32_e32 v164, 16, v163
	s_waitcnt lgkmcnt(0)
	v_mul_f32 v166, v106, v175
	s_nop 0
	v_fma_f32 v164, v212, v166, v164
	s_nop 0
	v_mul_f32 v164, v164, v160
	s_nop 0
	v_mul_f32 v164, v164, v188
	s_nop 0
	v_max_f32_e32 v164, v164, v164
	v_max_f32_e32 v164, 0xc3e00000, v164
	v_min_f32_e32 v166, 0x43e00000, v164
	s_nop 1
	v_mov_b32_dpp v167, v166 quad_perm:[1,0,3,2] row_mask:0xf bank_mask:0xf
	v_mov_b32_e32 v164, v3
	s_waitcnt lgkmcnt(0)
	v_cvt_pk_fp8_f32 v164, v166, v167
	s_nop 1
	v_mov_b32_dpp v166, v164 quad_perm:[2,3,0,1] row_mask:0xf bank_mask:0xf
	s_and_saveexec_b64 s[8:9], s[4:5]
	s_cbranch_execz .LBB0_1427
	v_and_b32_e32 v164, 0xffff, v164
	s_waitcnt lgkmcnt(0)
	v_lshl_or_b32 v164, v166, 16, v164
	v_add_co_u32_e32 v166, vcc, 0x10000, v6
	s_nop 1
	v_addc_co_u32_e32 v167, vcc, 0, v7, vcc
	global_store_dword v[166:167], v164, off offset:64
; __device__ __forceinline__ int crow(int r, int hi) { return (r & 3) + 8 * (r >> 2) + 4 * hi; }
; __device__ __forceinline__ float mul_ns(float a, float b) { float r; asm("v_mul_f32 %0, %1, %2" : "=v"(r) : "v"(a), "v"(b)); return r; }
; __device__ __forceinline__ float fma_ns(float a, float b, float c) { float r; asm("v_fma_f32 %0, %1, %2, %3" : "=v"(r) : "v"(a), "v"(b), "v"(c)); return r; }
; __device__ __forceinline__ void store_quad8(unsigned char* p, float v, int r32) {
;     v = fminf(fmaxf(v, -448.f), 448.f);
;     const float v1 = swz_xor<1>(v);
;     const int w = __builtin_amdgcn_cvt_pk_fp8_f32(v, v1, 0, false);
;     const int w2 = __builtin_amdgcn_ds_swizzle(w, (2 << 10) | 0x1f);
;     if ((r32 & 3) == 0) *(unsigned*)p = ((unsigned)w & 0xffffu) | ((unsigned)w2 << 16);
; }
;     __device__ __forceinline__ void operator()(f32x16 (&o)[8], const float (&rli)[16], int wid, int lane, int r32, int hi) const {
;     ...
;                 for (int q = 0; q < 4; ++q) { const int r = rb + q;
; #pragma unroll
;                     for (int d0 = 0; d0 < 8; ++d0) { const float t = __uint_as_float((d0 & 1) ? (tw[q][d0 >> 1] & 0xffff0000u) : (tw[q][d0 >> 1] << 16));
;                         const float dd = fma_ns(nlam, mul_ns(o[d0][r], rli[r]), t);
;                         store_quad8(base + (crow(r, 0) * 4096 + d0 * 32) + uo, mul_ns(mul_ns(dd, rn[r]), g[d0]), r32); } }
.LBB0_1427:
	s_or_b64 exec, exec, s[8:9]
	v_and_b32_e32 v163, 0xffff0000, v163
	v_mul_f32 v164, v90, v175
	s_nop 0
	v_fma_f32 v163, v212, v164, v163
	s_nop 0
	v_mul_f32 v163, v163, v160
	s_nop 0
	v_mul_f32 v163, v163, v187
	s_nop 0
	v_max_f32_e32 v163, v163, v163
	v_max_f32_e32 v163, 0xc3e00000, v163
	v_min_f32_e32 v164, 0x43e00000, v163
	s_waitcnt lgkmcnt(0)
	s_nop 1
	v_mov_b32_dpp v166, v164 quad_perm:[1,0,3,2] row_mask:0xf bank_mask:0xf
	v_mov_b32_e32 v163, v3
	s_waitcnt lgkmcnt(0)
	v_cvt_pk_fp8_f32 v163, v164, v166
	s_nop 1
	v_mov_b32_dpp v164, v163 quad_perm:[2,3,0,1] row_mask:0xf bank_mask:0xf
	s_and_saveexec_b64 s[8:9], s[4:5]
	s_cbranch_execz .LBB0_1429
	v_and_b32_e32 v163, 0xffff, v163
	v_add_co_u32_e32 v166, vcc, 0x10000, v6
	s_waitcnt lgkmcnt(0)
	v_lshl_or_b32 v163, v164, 16, v163
	v_addc_co_u32_e32 v167, vcc, 0, v7, vcc
	global_store_dword v[166:167], v163, off offset:96
.LBB0_1429:
	s_or_b64 exec, exec, s[8:9]
	s_waitcnt vmcnt(13)
	v_lshlrev_b32_e32 v163, 16, v162
	s_waitcnt lgkmcnt(0)
	v_mul_f32 v164, v74, v175
	s_nop 0
	v_fma_f32 v163, v212, v164, v163
	s_nop 0
	v_mul_f32 v163, v163, v160
	s_nop 0
	v_mul_f32 v163, v163, v186
	s_nop 0
	v_max_f32_e32 v163, v163, v163
	v_max_f32_e32 v163, 0xc3e00000, v163
	v_min_f32_e32 v164, 0x43e00000, v163
	s_nop 1
	v_mov_b32_dpp v166, v164 quad_perm:[1,0,3,2] row_mask:0xf bank_mask:0xf
	v_mov_b32_e32 v163, v3
	s_waitcnt lgkmcnt(0)
	v_cvt_pk_fp8_f32 v163, v164, v166
	s_nop 1
	v_mov_b32_dpp v164, v163 quad_perm:[2,3,0,1] row_mask:0xf bank_mask:0xf
	s_and_saveexec_b64 s[8:9], s[4:5]
	s_cbranch_execz .LBB0_1431
	v_and_b32_e32 v163, 0xffff, v163
	v_add_co_u32_e32 v166, vcc, 0x10000, v6
	s_waitcnt lgkmcnt(0)
	v_lshl_or_b32 v163, v164, 16, v163
	v_addc_co_u32_e32 v167, vcc, 0, v7, vcc
	global_store_dword v[166:167], v163, off offset:128
.LBB0_1431:
	s_or_b64 exec, exec, s[8:9]
	v_and_b32_e32 v162, 0xffff0000, v162
	v_mul_f32 v163, v58, v175
	s_nop 0
	v_fma_f32 v162, v212, v163, v162
	s_nop 0
	v_mul_f32 v162, v162, v160
	s_nop 0
	v_mul_f32 v162, v162, v185
	s_nop 0
	v_max_f32_e32 v162, v162, v162
	v_max_f32_e32 v162, 0xc3e00000, v162
	v_min_f32_e32 v163, 0x43e00000, v162
	s_waitcnt lgkmcnt(0)
	s_nop 1
	v_mov_b32_dpp v164, v163 quad_perm:[1,0,3,2] row_mask:0xf bank_mask:0xf
	v_mov_b32_e32 v162, v3
	s_waitcnt lgkmcnt(0)
	v_cvt_pk_fp8_f32 v162, v163, v164
	s_nop 1
	v_mov_b32_dpp v163, v162 quad_perm:[2,3,0,1] row_mask:0xf bank_mask:0xf
	s_and_saveexec_b64 s[8:9], s[4:5]
	s_cbranch_execz .LBB0_1433
	v_and_b32_e32 v162, 0xffff, v162
	s_waitcnt lgkmcnt(0)
	v_lshl_or_b32 v164, v163, 16, v162
	v_add_co_u32_e32 v162, vcc, 0x10000, v6
	s_nop 1
	v_addc_co_u32_e32 v163, vcc, 0, v7, vcc
	global_store_dword v[162:163], v164, off offset:160
.LBB0_1433:
	s_or_b64 exec, exec, s[8:9]
	s_waitcnt vmcnt(12)
	v_lshlrev_b32_e32 v162, 16, v161
	s_waitcnt lgkmcnt(0)
	v_mul_f32 v163, v42, v175
	s_nop 0
	v_fma_f32 v162, v212, v163, v162
	s_nop 0
	v_mul_f32 v162, v162, v160
	s_nop 0
	v_mul_f32 v162, v162, v184
	s_nop 0
	v_max_f32_e32 v162, v162, v162
	v_max_f32_e32 v162, 0xc3e00000, v162
	v_min_f32_e32 v163, 0x43e00000, v162
	s_nop 1
	v_mov_b32_dpp v164, v163 quad_perm:[1,0,3,2] row_mask:0xf bank_mask:0xf
	v_mov_b32_e32 v162, v3
	s_waitcnt lgkmcnt(0)
	v_cvt_pk_fp8_f32 v162, v163, v164
	s_nop 1
	v_mov_b32_dpp v163, v162 quad_perm:[2,3,0,1] row_mask:0xf bank_mask:0xf
	s_and_saveexec_b64 s[8:9], s[4:5]
	s_cbranch_execz .LBB0_1435
	v_and_b32_e32 v162, 0xffff, v162
	s_waitcnt lgkmcnt(0)
	v_lshl_or_b32 v164, v163, 16, v162
	v_add_co_u32_e32 v162, vcc, 0x10000, v6
	s_nop 1
	v_addc_co_u32_e32 v163, vcc, 0, v7, vcc
	global_store_dword v[162:163], v164, off offset:192
.LBB0_1435:
	s_or_b64 exec, exec, s[8:9]
	v_and_b32_e32 v161, 0xffff0000, v161
	v_mul_f32 v162, v26, v175
	s_nop 0
	v_fma_f32 v161, v212, v162, v161
	s_nop 0
	v_mul_f32 v160, v161, v160
	s_nop 0
	v_mul_f32 v160, v160, v165
	s_nop 0
	v_max_f32_e32 v160, v160, v160
	v_max_f32_e32 v160, 0xc3e00000, v160
	v_min_f32_e32 v161, 0x43e00000, v160
	s_nop 1
	v_mov_b32_dpp v162, v161 quad_perm:[1,0,3,2] row_mask:0xf bank_mask:0xf
	v_mov_b32_e32 v160, v3
	s_waitcnt lgkmcnt(0)
	v_cvt_pk_fp8_f32 v160, v161, v162
	s_nop 1
	v_mov_b32_dpp v161, v160 quad_perm:[2,3,0,1] row_mask:0xf bank_mask:0xf
	s_and_saveexec_b64 s[8:9], s[4:5]
	s_cbranch_execz .LBB0_1437
	v_and_b32_e32 v160, 0xffff, v160
	s_waitcnt lgkmcnt(0)
	v_lshl_or_b32 v162, v161, 16, v160
	v_add_co_u32_e32 v160, vcc, 0x10000, v6
	s_nop 1
	v_addc_co_u32_e32 v161, vcc, 0, v7, vcc
	global_store_dword v[160:161], v162, off offset:224
.LBB0_1437:
	s_or_b64 exec, exec, s[8:9]
	v_mul_f32_e32 v160, 0x4b800000, v148
	v_cndmask_b32_e64 v148, v148, v160, s[6:7]
	v_rsq_f32_e32 v148, v148
	s_waitcnt lgkmcnt(0)
	v_mul_f32 v161, v139, v174
	v_mul_f32_e32 v160, 0x45800000, v148
	v_cndmask_b32_e64 v148, v148, v160, s[6:7]
	s_waitcnt vmcnt(11)
	v_lshlrev_b32_e32 v160, 16, v159
	v_fma_f32 v160, v212, v161, v160
	v_mul_f32_e32 v148, 0x3f4ccccd, v148
	v_mul_f32 v160, v160, v148
	s_nop 0
	v_mul_f32 v160, v160, v190
	s_nop 0
	v_max_f32_e32 v160, v160, v160
	v_max_f32_e32 v160, 0xc3e00000, v160
	v_min_f32_e32 v161, 0x43e00000, v160
	s_nop 1
	v_mov_b32_dpp v162, v161 quad_perm:[1,0,3,2] row_mask:0xf bank_mask:0xf
	v_mov_b32_e32 v160, v3
	s_waitcnt lgkmcnt(0)
	v_cvt_pk_fp8_f32 v160, v161, v162
	s_nop 1
	v_mov_b32_dpp v161, v160 quad_perm:[2,3,0,1] row_mask:0xf bank_mask:0xf
	s_and_saveexec_b64 s[6:7], s[4:5]
	s_cbranch_execz .LBB0_1439
	v_and_b32_e32 v160, 0xffff, v160
	s_waitcnt lgkmcnt(0)
	v_lshl_or_b32 v162, v161, 16, v160
	v_add_co_u32_e32 v160, vcc, 0x11000, v6
	s_nop 1
	v_addc_co_u32_e32 v161, vcc, 0, v7, vcc
	global_store_dword v[160:161], v162, off
; __device__ __forceinline__ int crow(int r, int hi) { return (r & 3) + 8 * (r >> 2) + 4 * hi; }
; __device__ __forceinline__ float mul_ns(float a, float b) { float r; asm("v_mul_f32 %0, %1, %2" : "=v"(r) : "v"(a), "v"(b)); return r; }
; __device__ __forceinline__ float fma_ns(float a, float b, float c) { float r; asm("v_fma_f32 %0, %1, %2, %3" : "=v"(r) : "v"(a), "v"(b), "v"(c)); return r; }
; __device__ __forceinline__ void store_quad8(unsigned char* p, float v, int r32) {
;     v = fminf(fmaxf(v, -448.f), 448.f);
;     const float v1 = swz_xor<1>(v);
;     const int w = __builtin_amdgcn_cvt_pk_fp8_f32(v, v1, 0, false);
;     const int w2 = __builtin_amdgcn_ds_swizzle(w, (2 << 10) | 0x1f);
;     if ((r32 & 3) == 0) *(unsigned*)p = ((unsigned)w & 0xffffu) | ((unsigned)w2 << 16);
; }
;     __device__ __forceinline__ void operator()(f32x16 (&o)[8], const float (&rli)[16], int wid, int lane, int r32, int hi) const {
;     ...
;                 for (int q = 0; q < 4; ++q) { const int r = rb + q;
; #pragma unroll
;                     for (int d0 = 0; d0 < 8; ++d0) { const float t = __uint_as_float((d0 & 1) ? (tw[q][d0 >> 1] & 0xffff0000u) : (tw[q][d0 >> 1] << 16));
;                         const float dd = fma_ns(nlam, mul_ns(o[d0][r], rli[r]), t);
;                         store_quad8(base + (crow(r, 0) * 4096 + d0 * 32) + uo, mul_ns(mul_ns(dd, rn[r]), g[d0]), r32); } }
.LBB0_1439:
	s_or_b64 exec, exec, s[6:7]
	v_and_b32_e32 v159, 0xffff0000, v159
	v_mul_f32 v160, v123, v174
	s_nop 0
	v_fma_f32 v159, v212, v160, v159
	s_nop 0
	v_mul_f32 v159, v159, v148
	s_nop 0
	v_mul_f32 v159, v159, v189
	s_nop 0
	v_max_f32_e32 v159, v159, v159
	v_max_f32_e32 v159, 0xc3e00000, v159
	v_min_f32_e32 v160, 0x43e00000, v159
	s_waitcnt lgkmcnt(0)
	s_nop 1
	v_mov_b32_dpp v161, v160 quad_perm:[1,0,3,2] row_mask:0xf bank_mask:0xf
	v_mov_b32_e32 v159, v3
	s_waitcnt lgkmcnt(0)
	v_cvt_pk_fp8_f32 v159, v160, v161
	s_nop 1
	v_mov_b32_dpp v160, v159 quad_perm:[2,3,0,1] row_mask:0xf bank_mask:0xf
	s_and_saveexec_b64 s[6:7], s[4:5]
	s_cbranch_execz .LBB0_1441
	v_and_b32_e32 v159, 0xffff, v159
	s_waitcnt lgkmcnt(0)
	v_lshl_or_b32 v159, v160, 16, v159
	v_add_co_u32_e32 v160, vcc, 0x11000, v6
	s_nop 1
	v_addc_co_u32_e32 v161, vcc, 0, v7, vcc
	global_store_dword v[160:161], v159, off offset:32
.LBB0_1441:
	s_or_b64 exec, exec, s[6:7]
	s_waitcnt vmcnt(10)
	v_lshlrev_b32_e32 v159, 16, v158
	s_waitcnt lgkmcnt(0)
	v_mul_f32 v160, v107, v174
	s_nop 0
	v_fma_f32 v159, v212, v160, v159
	s_nop 0
	v_mul_f32 v159, v159, v148
	s_nop 0
	v_mul_f32 v159, v159, v188
	s_nop 0
	v_max_f32_e32 v159, v159, v159
	v_max_f32_e32 v159, 0xc3e00000, v159
	v_min_f32_e32 v160, 0x43e00000, v159
	s_nop 1
	v_mov_b32_dpp v161, v160 quad_perm:[1,0,3,2] row_mask:0xf bank_mask:0xf
	v_mov_b32_e32 v159, v3
	s_waitcnt lgkmcnt(0)
	v_cvt_pk_fp8_f32 v159, v160, v161
	s_nop 1
	v_mov_b32_dpp v160, v159 quad_perm:[2,3,0,1] row_mask:0xf bank_mask:0xf
	s_and_saveexec_b64 s[6:7], s[4:5]
	s_cbranch_execz .LBB0_1443
	v_and_b32_e32 v159, 0xffff, v159
	s_waitcnt lgkmcnt(0)
	v_lshl_or_b32 v159, v160, 16, v159
	v_add_co_u32_e32 v160, vcc, 0x11000, v6
	s_nop 1
	v_addc_co_u32_e32 v161, vcc, 0, v7, vcc
	global_store_dword v[160:161], v159, off offset:64
.LBB0_1443:
	s_or_b64 exec, exec, s[6:7]
	v_and_b32_e32 v158, 0xffff0000, v158
	v_mul_f32 v159, v91, v174
	s_nop 0
	v_fma_f32 v158, v212, v159, v158
	s_nop 0
	v_mul_f32 v158, v158, v148
	s_nop 0
	v_mul_f32 v158, v158, v187
	s_nop 0
	v_max_f32_e32 v158, v158, v158
	v_max_f32_e32 v158, 0xc3e00000, v158
	v_min_f32_e32 v159, 0x43e00000, v158
	s_waitcnt lgkmcnt(0)
	s_nop 1
	v_mov_b32_dpp v160, v159 quad_perm:[1,0,3,2] row_mask:0xf bank_mask:0xf
	v_mov_b32_e32 v158, v3
	s_waitcnt lgkmcnt(0)
	v_cvt_pk_fp8_f32 v158, v159, v160
	s_nop 1
	v_mov_b32_dpp v159, v158 quad_perm:[2,3,0,1] row_mask:0xf bank_mask:0xf
	s_and_saveexec_b64 s[6:7], s[4:5]
	s_cbranch_execz .LBB0_1445
	v_and_b32_e32 v158, 0xffff, v158
	s_waitcnt lgkmcnt(0)
	v_lshl_or_b32 v160, v159, 16, v158
	v_add_co_u32_e32 v158, vcc, 0x11000, v6
	s_nop 1
	v_addc_co_u32_e32 v159, vcc, 0, v7, vcc
	global_store_dword v[158:159], v160, off offset:96
.LBB0_1445:
	s_or_b64 exec, exec, s[6:7]
	s_waitcnt vmcnt(9)
	v_lshlrev_b32_e32 v158, 16, v157
	s_waitcnt lgkmcnt(0)
	v_mul_f32 v159, v75, v174
	s_nop 0
	v_fma_f32 v158, v212, v159, v158
	s_nop 0
	v_mul_f32 v158, v158, v148
	s_nop 0
	v_mul_f32 v158, v158, v186
	s_nop 0
	v_max_f32_e32 v158, v158, v158
	v_max_f32_e32 v158, 0xc3e00000, v158
	v_min_f32_e32 v159, 0x43e00000, v158
	s_nop 1
	v_mov_b32_dpp v160, v159 quad_perm:[1,0,3,2] row_mask:0xf bank_mask:0xf
	v_mov_b32_e32 v158, v3
	s_waitcnt lgkmcnt(0)
	v_cvt_pk_fp8_f32 v158, v159, v160
	s_nop 1
	v_mov_b32_dpp v159, v158 quad_perm:[2,3,0,1] row_mask:0xf bank_mask:0xf
	s_and_saveexec_b64 s[6:7], s[4:5]
	s_cbranch_execz .LBB0_1447
	v_and_b32_e32 v158, 0xffff, v158
	s_waitcnt lgkmcnt(0)
	v_lshl_or_b32 v160, v159, 16, v158
	v_add_co_u32_e32 v158, vcc, 0x11000, v6
	s_nop 1
	v_addc_co_u32_e32 v159, vcc, 0, v7, vcc
	global_store_dword v[158:159], v160, off offset:128
.LBB0_1447:
	s_or_b64 exec, exec, s[6:7]
	v_and_b32_e32 v157, 0xffff0000, v157
	v_mul_f32 v158, v59, v174
	s_nop 0
	v_fma_f32 v157, v212, v158, v157
	s_nop 0
	v_mul_f32 v157, v157, v148
	s_nop 0
	v_mul_f32 v157, v157, v185
	s_nop 0
	v_max_f32_e32 v157, v157, v157
	v_max_f32_e32 v157, 0xc3e00000, v157
	v_min_f32_e32 v158, 0x43e00000, v157
	s_waitcnt lgkmcnt(0)
	s_nop 1
	v_mov_b32_dpp v159, v158 quad_perm:[1,0,3,2] row_mask:0xf bank_mask:0xf
	v_mov_b32_e32 v157, v3
	s_waitcnt lgkmcnt(0)
	v_cvt_pk_fp8_f32 v157, v158, v159
	s_nop 1
	v_mov_b32_dpp v158, v157 quad_perm:[2,3,0,1] row_mask:0xf bank_mask:0xf
	s_and_saveexec_b64 s[6:7], s[4:5]
	s_cbranch_execz .LBB0_1449
	v_and_b32_e32 v157, 0xffff, v157
	s_waitcnt lgkmcnt(0)
	v_lshl_or_b32 v157, v158, 16, v157
	v_add_co_u32_e32 v158, vcc, 0x11000, v6
	s_nop 1
	v_addc_co_u32_e32 v159, vcc, 0, v7, vcc
	global_store_dword v[158:159], v157, off offset:160
.LBB0_1449:
	s_or_b64 exec, exec, s[6:7]
	s_waitcnt vmcnt(8)
	v_lshlrev_b32_e32 v157, 16, v156
	s_waitcnt lgkmcnt(0)
	v_mul_f32 v158, v43, v174
	s_nop 0
	v_fma_f32 v157, v212, v158, v157
	s_nop 0
	v_mul_f32 v157, v157, v148
	s_nop 0
	v_mul_f32 v157, v157, v184
	s_nop 0
	v_max_f32_e32 v157, v157, v157
	v_max_f32_e32 v157, 0xc3e00000, v157
	v_min_f32_e32 v158, 0x43e00000, v157
	s_nop 1
	v_mov_b32_dpp v159, v158 quad_perm:[1,0,3,2] row_mask:0xf bank_mask:0xf
	v_mov_b32_e32 v157, v3
	s_waitcnt lgkmcnt(0)
	v_cvt_pk_fp8_f32 v157, v158, v159
	s_nop 1
	v_mov_b32_dpp v158, v157 quad_perm:[2,3,0,1] row_mask:0xf bank_mask:0xf
	s_and_saveexec_b64 s[6:7], s[4:5]
	s_cbranch_execz .LBB0_1451
	v_and_b32_e32 v157, 0xffff, v157
	s_waitcnt lgkmcnt(0)
	v_lshl_or_b32 v157, v158, 16, v157
	v_add_co_u32_e32 v158, vcc, 0x11000, v6
	s_nop 1
	v_addc_co_u32_e32 v159, vcc, 0, v7, vcc
	global_store_dword v[158:159], v157, off offset:192
; __device__ __forceinline__ int crow(int r, int hi) { return (r & 3) + 8 * (r >> 2) + 4 * hi; }
; __device__ __forceinline__ float mul_ns(float a, float b) { float r; asm("v_mul_f32 %0, %1, %2" : "=v"(r) : "v"(a), "v"(b)); return r; }
; __device__ __forceinline__ float fma_ns(float a, float b, float c) { float r; asm("v_fma_f32 %0, %1, %2, %3" : "=v"(r) : "v"(a), "v"(b), "v"(c)); return r; }
; __device__ __forceinline__ void store_quad8(unsigned char* p, float v, int r32) {
;     v = fminf(fmaxf(v, -448.f), 448.f);
;     const float v1 = swz_xor<1>(v);
;     const int w = __builtin_amdgcn_cvt_pk_fp8_f32(v, v1, 0, false);
;     const int w2 = __builtin_amdgcn_ds_swizzle(w, (2 << 10) | 0x1f);
;     if ((r32 & 3) == 0) *(unsigned*)p = ((unsigned)w & 0xffffu) | ((unsigned)w2 << 16);
; }
;     __device__ __forceinline__ void operator()(f32x16 (&o)[8], const float (&rli)[16], int wid, int lane, int r32, int hi) const {
;     ...
;                 for (int q = 0; q < 4; ++q) { const int r = rb + q;
; #pragma unroll
;                     for (int d0 = 0; d0 < 8; ++d0) { const float t = __uint_as_float((d0 & 1) ? (tw[q][d0 >> 1] & 0xffff0000u) : (tw[q][d0 >> 1] << 16));
;                         const float dd = fma_ns(nlam, mul_ns(o[d0][r], rli[r]), t);
;                         store_quad8(base + (crow(r, 0) * 4096 + d0 * 32) + uo, mul_ns(mul_ns(dd, rn[r]), g[d0]), r32); } }
.LBB0_1451:
	s_or_b64 exec, exec, s[6:7]
	v_and_b32_e32 v156, 0xffff0000, v156
	v_mul_f32 v157, v27, v174
	s_nop 0
	v_fma_f32 v156, v212, v157, v156
	s_nop 0
	v_mul_f32 v148, v156, v148
	s_nop 0
	v_mul_f32 v148, v148, v165
	s_nop 0
	v_max_f32_e32 v148, v148, v148
	v_max_f32_e32 v148, 0xc3e00000, v148
	v_min_f32_e32 v156, 0x43e00000, v148
	s_nop 1
	v_mov_b32_dpp v157, v156 quad_perm:[1,0,3,2] row_mask:0xf bank_mask:0xf
	v_mov_b32_e32 v148, v3
	s_waitcnt lgkmcnt(0)
	v_cvt_pk_fp8_f32 v148, v156, v157
	s_nop 1
	v_mov_b32_dpp v156, v148 quad_perm:[2,3,0,1] row_mask:0xf bank_mask:0xf
	s_and_saveexec_b64 s[6:7], s[4:5]
	s_cbranch_execz .LBB0_1453
	v_and_b32_e32 v148, 0xffff, v148
	s_waitcnt lgkmcnt(0)
	v_lshl_or_b32 v148, v156, 16, v148
	v_add_co_u32_e32 v156, vcc, 0x11000, v6
	s_nop 1
	v_addc_co_u32_e32 v157, vcc, 0, v7, vcc
	global_store_dword v[156:157], v148, off offset:224
.LBB0_1453:
	s_or_b64 exec, exec, s[6:7]
	v_pk_add_f32 v[16:17], v[16:17], v[146:147]
	v_mul_f32 v147, v140, v173
	s_nop 0
	v_pk_fma_f32 v[16:17], v[16:17], s[54:55], v[198:199] op_sel_hi:[1,0,0]
	s_nop 0
	v_mul_f32_e32 v146, 0x4b800000, v17
	v_cmp_gt_f32_e32 vcc, s53, v17
	v_cmp_gt_f32_e64 s[6:7], s53, v16
	s_nop 0
	v_cndmask_b32_e32 v17, v17, v146, vcc
	v_rsq_f32_e32 v17, v17
	s_waitcnt vmcnt(7)
	v_lshlrev_b32_e32 v146, 16, v155
	v_fma_f32 v146, v212, v147, v146
	v_mul_f32_e32 v148, 0x45800000, v17
	v_cndmask_b32_e32 v17, v17, v148, vcc
	v_mul_f32_e32 v17, 0x3f4ccccd, v17
	v_mul_f32 v146, v146, v17
	s_nop 0
	v_mul_f32 v146, v146, v190
	s_nop 0
	v_max_f32_e32 v146, v146, v146
	v_max_f32_e32 v146, 0xc3e00000, v146
	v_min_f32_e32 v147, 0x43e00000, v146
	s_nop 1
	v_mov_b32_dpp v148, v147 quad_perm:[1,0,3,2] row_mask:0xf bank_mask:0xf
	v_mov_b32_e32 v146, v3
	s_waitcnt lgkmcnt(0)
	v_cvt_pk_fp8_f32 v146, v147, v148
	s_nop 1
	v_mov_b32_dpp v147, v146 quad_perm:[2,3,0,1] row_mask:0xf bank_mask:0xf
	s_and_saveexec_b64 s[8:9], s[4:5]
	s_cbranch_execz .LBB0_1455
	v_and_b32_e32 v146, 0xffff, v146
	s_waitcnt lgkmcnt(0)
	v_lshl_or_b32 v148, v147, 16, v146
	v_add_co_u32_e32 v146, vcc, 0x12000, v6
	s_nop 1
	v_addc_co_u32_e32 v147, vcc, 0, v7, vcc
	global_store_dword v[146:147], v148, off
.LBB0_1455:
	s_or_b64 exec, exec, s[8:9]
	v_and_b32_e32 v146, 0xffff0000, v155
	s_waitcnt lgkmcnt(0)
	v_mul_f32 v147, v124, v173
	s_nop 0
	v_fma_f32 v146, v212, v147, v146
	s_nop 0
	v_mul_f32 v146, v146, v17
	s_nop 0
	v_mul_f32 v146, v146, v189
	s_nop 0
	v_max_f32_e32 v146, v146, v146
	v_max_f32_e32 v146, 0xc3e00000, v146
	v_min_f32_e32 v147, 0x43e00000, v146
	s_nop 1
	v_mov_b32_dpp v148, v147 quad_perm:[1,0,3,2] row_mask:0xf bank_mask:0xf
	v_mov_b32_e32 v146, v3
	s_waitcnt lgkmcnt(0)
	v_cvt_pk_fp8_f32 v146, v147, v148
	s_nop 1
	v_mov_b32_dpp v147, v146 quad_perm:[2,3,0,1] row_mask:0xf bank_mask:0xf
	s_and_saveexec_b64 s[8:9], s[4:5]
	s_cbranch_execz .LBB0_1457
	v_and_b32_e32 v146, 0xffff, v146
	s_waitcnt lgkmcnt(0)
	v_lshl_or_b32 v148, v147, 16, v146
	v_add_co_u32_e32 v146, vcc, 0x12000, v6
	s_nop 1
	v_addc_co_u32_e32 v147, vcc, 0, v7, vcc
	global_store_dword v[146:147], v148, off offset:32
.LBB0_1457:
	s_or_b64 exec, exec, s[8:9]
	s_waitcnt vmcnt(6)
	v_lshlrev_b32_e32 v146, 16, v154
	s_waitcnt lgkmcnt(0)
	v_mul_f32 v147, v108, v173
	s_nop 0
	v_fma_f32 v146, v212, v147, v146
	s_nop 0
	v_mul_f32 v146, v146, v17
	s_nop 0
	v_mul_f32 v146, v146, v188
	s_nop 0
	v_max_f32_e32 v146, v146, v146
	v_max_f32_e32 v146, 0xc3e00000, v146
	v_min_f32_e32 v147, 0x43e00000, v146
	s_nop 1
	v_mov_b32_dpp v148, v147 quad_perm:[1,0,3,2] row_mask:0xf bank_mask:0xf
	v_mov_b32_e32 v146, v3
	s_waitcnt lgkmcnt(0)
	v_cvt_pk_fp8_f32 v146, v147, v148
	s_nop 1
	v_mov_b32_dpp v147, v146 quad_perm:[2,3,0,1] row_mask:0xf bank_mask:0xf
	s_and_saveexec_b64 s[8:9], s[4:5]
	s_cbranch_execz .LBB0_1459
	v_and_b32_e32 v146, 0xffff, v146
	s_waitcnt lgkmcnt(0)
	v_lshl_or_b32 v148, v147, 16, v146
	v_add_co_u32_e32 v146, vcc, 0x12000, v6
	s_nop 1
	v_addc_co_u32_e32 v147, vcc, 0, v7, vcc
	global_store_dword v[146:147], v148, off offset:64
.LBB0_1459:
	s_or_b64 exec, exec, s[8:9]
	v_and_b32_e32 v146, 0xffff0000, v154
	s_waitcnt lgkmcnt(0)
	v_mul_f32 v147, v92, v173
	s_nop 0
	v_fma_f32 v146, v212, v147, v146
	s_nop 0
	v_mul_f32 v146, v146, v17
	s_nop 0
	v_mul_f32 v146, v146, v187
	s_nop 0
	v_max_f32_e32 v146, v146, v146
	v_max_f32_e32 v146, 0xc3e00000, v146
	v_min_f32_e32 v147, 0x43e00000, v146
	s_nop 1
	v_mov_b32_dpp v148, v147 quad_perm:[1,0,3,2] row_mask:0xf bank_mask:0xf
	v_mov_b32_e32 v146, v3
	s_waitcnt lgkmcnt(0)
	v_cvt_pk_fp8_f32 v146, v147, v148
	s_nop 1
	v_mov_b32_dpp v147, v146 quad_perm:[2,3,0,1] row_mask:0xf bank_mask:0xf
	s_and_saveexec_b64 s[8:9], s[4:5]
	s_cbranch_execz .LBB0_1461
	v_and_b32_e32 v146, 0xffff, v146
	s_waitcnt lgkmcnt(0)
	v_lshl_or_b32 v148, v147, 16, v146
	v_add_co_u32_e32 v146, vcc, 0x12000, v6
	s_nop 1
	v_addc_co_u32_e32 v147, vcc, 0, v7, vcc
	global_store_dword v[146:147], v148, off offset:96
.LBB0_1461:
	s_or_b64 exec, exec, s[8:9]
	s_waitcnt vmcnt(5)
	v_lshlrev_b32_e32 v146, 16, v153
	s_waitcnt lgkmcnt(0)
	v_mul_f32 v147, v76, v173
	s_nop 0
	v_fma_f32 v146, v212, v147, v146
	s_nop 0
	v_mul_f32 v146, v146, v17
	s_nop 0
	v_mul_f32 v146, v146, v186
	s_nop 0
	v_max_f32_e32 v146, v146, v146
	v_max_f32_e32 v146, 0xc3e00000, v146
	v_min_f32_e32 v147, 0x43e00000, v146
	s_nop 1
	v_mov_b32_dpp v148, v147 quad_perm:[1,0,3,2] row_mask:0xf bank_mask:0xf
	v_mov_b32_e32 v146, v3
	s_waitcnt lgkmcnt(0)
	v_cvt_pk_fp8_f32 v146, v147, v148
	s_nop 1
	v_mov_b32_dpp v147, v146 quad_perm:[2,3,0,1] row_mask:0xf bank_mask:0xf
	s_and_saveexec_b64 s[8:9], s[4:5]
	s_cbranch_execz .LBB0_1463
	v_and_b32_e32 v146, 0xffff, v146
	s_waitcnt lgkmcnt(0)
	v_lshl_or_b32 v148, v147, 16, v146
	v_add_co_u32_e32 v146, vcc, 0x12000, v6
	s_nop 1
	v_addc_co_u32_e32 v147, vcc, 0, v7, vcc
	global_store_dword v[146:147], v148, off offset:128
; __device__ __forceinline__ int crow(int r, int hi) { return (r & 3) + 8 * (r >> 2) + 4 * hi; }
; __device__ __forceinline__ float mul_ns(float a, float b) { float r; asm("v_mul_f32 %0, %1, %2" : "=v"(r) : "v"(a), "v"(b)); return r; }
; __device__ __forceinline__ float fma_ns(float a, float b, float c) { float r; asm("v_fma_f32 %0, %1, %2, %3" : "=v"(r) : "v"(a), "v"(b), "v"(c)); return r; }
; __device__ __forceinline__ void store_quad8(unsigned char* p, float v, int r32) {
;     v = fminf(fmaxf(v, -448.f), 448.f);
;     const float v1 = swz_xor<1>(v);
;     const int w = __builtin_amdgcn_cvt_pk_fp8_f32(v, v1, 0, false);
;     const int w2 = __builtin_amdgcn_ds_swizzle(w, (2 << 10) | 0x1f);
;     if ((r32 & 3) == 0) *(unsigned*)p = ((unsigned)w & 0xffffu) | ((unsigned)w2 << 16);
; }
;     __device__ __forceinline__ void operator()(f32x16 (&o)[8], const float (&rli)[16], int wid, int lane, int r32, int hi) const {
;     ...
;                 for (int q = 0; q < 4; ++q) { const int r = rb + q;
; #pragma unroll
;                     for (int d0 = 0; d0 < 8; ++d0) { const float t = __uint_as_float((d0 & 1) ? (tw[q][d0 >> 1] & 0xffff0000u) : (tw[q][d0 >> 1] << 16));
;                         const float dd = fma_ns(nlam, mul_ns(o[d0][r], rli[r]), t);
;                         store_quad8(base + (crow(r, 0) * 4096 + d0 * 32) + uo, mul_ns(mul_ns(dd, rn[r]), g[d0]), r32); } }
.LBB0_1463:
	s_or_b64 exec, exec, s[8:9]
	v_and_b32_e32 v146, 0xffff0000, v153
	s_waitcnt lgkmcnt(0)
	v_mul_f32 v147, v60, v173
	s_nop 0
	v_fma_f32 v146, v212, v147, v146
	s_nop 0
	v_mul_f32 v146, v146, v17
	s_nop 0
	v_mul_f32 v146, v146, v185
	s_nop 0
	v_max_f32_e32 v146, v146, v146
	v_max_f32_e32 v146, 0xc3e00000, v146
	v_min_f32_e32 v147, 0x43e00000, v146
	s_nop 1
	v_mov_b32_dpp v148, v147 quad_perm:[1,0,3,2] row_mask:0xf bank_mask:0xf
	v_mov_b32_e32 v146, v3
	s_waitcnt lgkmcnt(0)
	v_cvt_pk_fp8_f32 v146, v147, v148
	s_nop 1
	v_mov_b32_dpp v147, v146 quad_perm:[2,3,0,1] row_mask:0xf bank_mask:0xf
	s_and_saveexec_b64 s[8:9], s[4:5]
	s_cbranch_execz .LBB0_1465
	v_and_b32_e32 v146, 0xffff, v146
	s_waitcnt lgkmcnt(0)
	v_lshl_or_b32 v148, v147, 16, v146
	v_add_co_u32_e32 v146, vcc, 0x12000, v6
	s_nop 1
	v_addc_co_u32_e32 v147, vcc, 0, v7, vcc
	global_store_dword v[146:147], v148, off offset:160
.LBB0_1465:
	s_or_b64 exec, exec, s[8:9]
	s_waitcnt vmcnt(4)
	v_lshlrev_b32_e32 v146, 16, v152
	s_waitcnt lgkmcnt(0)
	v_mul_f32 v147, v44, v173
	s_nop 0
	v_fma_f32 v146, v212, v147, v146
	s_nop 0
	v_mul_f32 v146, v146, v17
	s_nop 0
	v_mul_f32 v146, v146, v184
	s_nop 0
	v_max_f32_e32 v146, v146, v146
	v_max_f32_e32 v146, 0xc3e00000, v146
	v_min_f32_e32 v147, 0x43e00000, v146
	s_nop 1
	v_mov_b32_dpp v148, v147 quad_perm:[1,0,3,2] row_mask:0xf bank_mask:0xf
	v_mov_b32_e32 v146, v3
	s_waitcnt lgkmcnt(0)
	v_cvt_pk_fp8_f32 v146, v147, v148
	s_nop 1
	v_mov_b32_dpp v147, v146 quad_perm:[2,3,0,1] row_mask:0xf bank_mask:0xf
	s_and_saveexec_b64 s[8:9], s[4:5]
	s_cbranch_execz .LBB0_1467
	v_and_b32_e32 v146, 0xffff, v146
	s_waitcnt lgkmcnt(0)
	v_lshl_or_b32 v148, v147, 16, v146
	v_add_co_u32_e32 v146, vcc, 0x12000, v6
	s_nop 1
	v_addc_co_u32_e32 v147, vcc, 0, v7, vcc
	global_store_dword v[146:147], v148, off offset:192
.LBB0_1467:
	s_or_b64 exec, exec, s[8:9]
	v_and_b32_e32 v146, 0xffff0000, v152
	s_waitcnt lgkmcnt(0)
	v_mul_f32 v147, v28, v173
	s_nop 0
	v_fma_f32 v146, v212, v147, v146
	s_nop 0
	v_mul_f32 v17, v146, v17
	s_nop 0
	v_mul_f32 v17, v17, v165
	s_nop 0
	v_max_f32_e32 v17, v17, v17
	v_max_f32_e32 v17, 0xc3e00000, v17
	v_min_f32_e32 v146, 0x43e00000, v17
	s_nop 1
	v_mov_b32_dpp v147, v146 quad_perm:[1,0,3,2] row_mask:0xf bank_mask:0xf
	v_mov_b32_e32 v17, v3
	s_waitcnt lgkmcnt(0)
	v_cvt_pk_fp8_f32 v17, v146, v147
	s_nop 1
	v_mov_b32_dpp v146, v17 quad_perm:[2,3,0,1] row_mask:0xf bank_mask:0xf
	s_and_saveexec_b64 s[8:9], s[4:5]
	s_cbranch_execz .LBB0_1469
	v_and_b32_e32 v17, 0xffff, v17
	s_waitcnt lgkmcnt(0)
	v_lshl_or_b32 v17, v146, 16, v17
	v_add_co_u32_e32 v146, vcc, 0x12000, v6
	s_nop 1
	v_addc_co_u32_e32 v147, vcc, 0, v7, vcc
	global_store_dword v[146:147], v17, off offset:224
.LBB0_1469:
	s_or_b64 exec, exec, s[8:9]
	v_mul_f32_e32 v17, 0x4b800000, v16
	v_cndmask_b32_e64 v16, v16, v17, s[6:7]
	v_rsq_f32_e32 v16, v16
	s_waitcnt lgkmcnt(0)
	v_mul_f32 v146, v141, v172
	v_mul_f32_e32 v17, 0x45800000, v16
	v_cndmask_b32_e64 v16, v16, v17, s[6:7]
	s_waitcnt vmcnt(3)
	v_lshlrev_b32_e32 v17, 16, v151
	v_fma_f32 v17, v212, v146, v17
	v_mul_f32_e32 v16, 0x3f4ccccd, v16
	v_mul_f32 v17, v17, v16
	s_nop 0
	v_mul_f32 v17, v17, v190
	s_nop 0
	v_max_f32_e32 v17, v17, v17
	v_max_f32_e32 v17, 0xc3e00000, v17
	v_min_f32_e32 v146, 0x43e00000, v17
	s_nop 1
	v_mov_b32_dpp v147, v146 quad_perm:[1,0,3,2] row_mask:0xf bank_mask:0xf
	v_mov_b32_e32 v17, v3
	s_waitcnt lgkmcnt(0)
	v_cvt_pk_fp8_f32 v17, v146, v147
	s_nop 1
	v_mov_b32_dpp v146, v17 quad_perm:[2,3,0,1] row_mask:0xf bank_mask:0xf
	s_and_saveexec_b64 s[6:7], s[4:5]
	s_cbranch_execz .LBB0_1471
	v_and_b32_e32 v17, 0xffff, v17
	s_waitcnt lgkmcnt(0)
	v_lshl_or_b32 v17, v146, 16, v17
	v_add_co_u32_e32 v146, vcc, 0x13000, v6
	s_nop 1
	v_addc_co_u32_e32 v147, vcc, 0, v7, vcc
	global_store_dword v[146:147], v17, off
.LBB0_1471:
	s_or_b64 exec, exec, s[6:7]
	v_and_b32_e32 v17, 0xffff0000, v151
	s_waitcnt lgkmcnt(0)
	v_mul_f32 v146, v125, v172
	s_nop 0
	v_fma_f32 v17, v212, v146, v17
	s_nop 0
	v_mul_f32 v17, v17, v16
	s_nop 0
	v_mul_f32 v17, v17, v189
	s_nop 0
	v_max_f32_e32 v17, v17, v17
	v_max_f32_e32 v17, 0xc3e00000, v17
	v_min_f32_e32 v146, 0x43e00000, v17
	s_nop 1
	v_mov_b32_dpp v147, v146 quad_perm:[1,0,3,2] row_mask:0xf bank_mask:0xf
	v_mov_b32_e32 v17, v3
	s_waitcnt lgkmcnt(0)
	v_cvt_pk_fp8_f32 v17, v146, v147
	s_nop 1
	v_mov_b32_dpp v146, v17 quad_perm:[2,3,0,1] row_mask:0xf bank_mask:0xf
	s_and_saveexec_b64 s[6:7], s[4:5]
	s_cbranch_execz .LBB0_1473
	v_and_b32_e32 v17, 0xffff, v17
	s_waitcnt lgkmcnt(0)
	v_lshl_or_b32 v17, v146, 16, v17
	v_add_co_u32_e32 v146, vcc, 0x13000, v6
	s_nop 1
	v_addc_co_u32_e32 v147, vcc, 0, v7, vcc
	global_store_dword v[146:147], v17, off offset:32
.LBB0_1473:
	s_or_b64 exec, exec, s[6:7]
	s_waitcnt vmcnt(2)
	v_lshlrev_b32_e32 v17, 16, v150
	s_waitcnt lgkmcnt(0)
	v_mul_f32 v146, v109, v172
	s_nop 0
	v_fma_f32 v17, v212, v146, v17
	s_nop 0
	v_mul_f32 v17, v17, v16
	s_nop 0
	v_mul_f32 v17, v17, v188
	s_nop 0
	v_max_f32_e32 v17, v17, v17
	v_max_f32_e32 v17, 0xc3e00000, v17
	v_min_f32_e32 v146, 0x43e00000, v17
	s_nop 1
	v_mov_b32_dpp v147, v146 quad_perm:[1,0,3,2] row_mask:0xf bank_mask:0xf
	v_mov_b32_e32 v17, v3
	s_waitcnt lgkmcnt(0)
	v_cvt_pk_fp8_f32 v17, v146, v147
	s_nop 1
	v_mov_b32_dpp v146, v17 quad_perm:[2,3,0,1] row_mask:0xf bank_mask:0xf
	s_and_saveexec_b64 s[6:7], s[4:5]
	s_cbranch_execz .LBB0_1475
	v_and_b32_e32 v17, 0xffff, v17
	s_waitcnt lgkmcnt(0)
	v_lshl_or_b32 v17, v146, 16, v17
	v_add_co_u32_e32 v146, vcc, 0x13000, v6
	s_nop 1
	v_addc_co_u32_e32 v147, vcc, 0, v7, vcc
	global_store_dword v[146:147], v17, off offset:64
; __device__ __forceinline__ int crow(int r, int hi) { return (r & 3) + 8 * (r >> 2) + 4 * hi; }
; __device__ __forceinline__ float mul_ns(float a, float b) { float r; asm("v_mul_f32 %0, %1, %2" : "=v"(r) : "v"(a), "v"(b)); return r; }
; __device__ __forceinline__ float fma_ns(float a, float b, float c) { float r; asm("v_fma_f32 %0, %1, %2, %3" : "=v"(r) : "v"(a), "v"(b), "v"(c)); return r; }
; __device__ __forceinline__ void store_quad8(unsigned char* p, float v, int r32) {
;     v = fminf(fmaxf(v, -448.f), 448.f);
;     const float v1 = swz_xor<1>(v);
;     const int w = __builtin_amdgcn_cvt_pk_fp8_f32(v, v1, 0, false);
;     const int w2 = __builtin_amdgcn_ds_swizzle(w, (2 << 10) | 0x1f);
;     if ((r32 & 3) == 0) *(unsigned*)p = ((unsigned)w & 0xffffu) | ((unsigned)w2 << 16);
; }
;     __device__ __forceinline__ void operator()(f32x16 (&o)[8], const float (&rli)[16], int wid, int lane, int r32, int hi) const {
;     ...
;                 for (int q = 0; q < 4; ++q) { const int r = rb + q;
; #pragma unroll
;                     for (int d0 = 0; d0 < 8; ++d0) { const float t = __uint_as_float((d0 & 1) ? (tw[q][d0 >> 1] & 0xffff0000u) : (tw[q][d0 >> 1] << 16));
;                         const float dd = fma_ns(nlam, mul_ns(o[d0][r], rli[r]), t);
;                         store_quad8(base + (crow(r, 0) * 4096 + d0 * 32) + uo, mul_ns(mul_ns(dd, rn[r]), g[d0]), r32); } }
.LBB0_1475:
	s_or_b64 exec, exec, s[6:7]
	v_and_b32_e32 v17, 0xffff0000, v150
	s_waitcnt lgkmcnt(0)
	v_mul_f32 v146, v93, v172
	s_nop 0
	v_fma_f32 v17, v212, v146, v17
	s_nop 0
	v_mul_f32 v17, v17, v16
	s_nop 0
	v_mul_f32 v17, v17, v187
	s_nop 0
	v_max_f32_e32 v17, v17, v17
	v_max_f32_e32 v17, 0xc3e00000, v17
	v_min_f32_e32 v146, 0x43e00000, v17
	s_nop 1
	v_mov_b32_dpp v147, v146 quad_perm:[1,0,3,2] row_mask:0xf bank_mask:0xf
	v_mov_b32_e32 v17, v3
	s_waitcnt lgkmcnt(0)
	v_cvt_pk_fp8_f32 v17, v146, v147
	s_nop 1
	v_mov_b32_dpp v146, v17 quad_perm:[2,3,0,1] row_mask:0xf bank_mask:0xf
	s_and_saveexec_b64 s[6:7], s[4:5]
	s_cbranch_execz .LBB0_1477
	v_and_b32_e32 v17, 0xffff, v17
	s_waitcnt lgkmcnt(0)
	v_lshl_or_b32 v17, v146, 16, v17
	v_add_co_u32_e32 v146, vcc, 0x13000, v6
	s_nop 1
	v_addc_co_u32_e32 v147, vcc, 0, v7, vcc
	global_store_dword v[146:147], v17, off offset:96
.LBB0_1477:
	s_or_b64 exec, exec, s[6:7]
	s_waitcnt vmcnt(1)
	v_lshlrev_b32_e32 v17, 16, v149
	s_waitcnt lgkmcnt(0)
	v_mul_f32 v146, v77, v172
	s_nop 0
	v_fma_f32 v17, v212, v146, v17
	s_nop 0
	v_mul_f32 v17, v17, v16
	s_nop 0
	v_mul_f32 v17, v17, v186
	s_nop 0
	v_max_f32_e32 v17, v17, v17
	v_max_f32_e32 v17, 0xc3e00000, v17
	v_min_f32_e32 v146, 0x43e00000, v17
	s_nop 1
	v_mov_b32_dpp v147, v146 quad_perm:[1,0,3,2] row_mask:0xf bank_mask:0xf
	v_mov_b32_e32 v17, v3
	s_waitcnt lgkmcnt(0)
	v_cvt_pk_fp8_f32 v17, v146, v147
	s_nop 1
	v_mov_b32_dpp v146, v17 quad_perm:[2,3,0,1] row_mask:0xf bank_mask:0xf
	s_and_saveexec_b64 s[6:7], s[4:5]
	s_cbranch_execz .LBB0_1479
	v_and_b32_e32 v17, 0xffff, v17
	s_waitcnt lgkmcnt(0)
	v_lshl_or_b32 v17, v146, 16, v17
	v_add_co_u32_e32 v146, vcc, 0x13000, v6
	s_nop 1
	v_addc_co_u32_e32 v147, vcc, 0, v7, vcc
	global_store_dword v[146:147], v17, off offset:128
.LBB0_1479:
	s_or_b64 exec, exec, s[6:7]
	v_and_b32_e32 v17, 0xffff0000, v149
	s_waitcnt lgkmcnt(0)
	v_mul_f32 v146, v61, v172
	s_nop 0
	v_fma_f32 v17, v212, v146, v17
	s_nop 0
	v_mul_f32 v17, v17, v16
	s_nop 0
	v_mul_f32 v17, v17, v185
	s_nop 0
	v_max_f32_e32 v17, v17, v17
	v_max_f32_e32 v17, 0xc3e00000, v17
	v_min_f32_e32 v146, 0x43e00000, v17
	s_nop 1
	v_mov_b32_dpp v147, v146 quad_perm:[1,0,3,2] row_mask:0xf bank_mask:0xf
	v_mov_b32_e32 v17, v3
	s_waitcnt lgkmcnt(0)
	v_cvt_pk_fp8_f32 v17, v146, v147
	s_nop 1
	v_mov_b32_dpp v146, v17 quad_perm:[2,3,0,1] row_mask:0xf bank_mask:0xf
	s_and_saveexec_b64 s[6:7], s[4:5]
	s_cbranch_execz .LBB0_1481
	v_and_b32_e32 v17, 0xffff, v17
	s_waitcnt lgkmcnt(0)
	v_lshl_or_b32 v17, v146, 16, v17
	v_add_co_u32_e32 v146, vcc, 0x13000, v6
	s_nop 1
	v_addc_co_u32_e32 v147, vcc, 0, v7, vcc
	global_store_dword v[146:147], v17, off offset:160
.LBB0_1481:
	s_or_b64 exec, exec, s[6:7]
	s_waitcnt vmcnt(0)
	v_lshlrev_b32_e32 v17, 16, v2
	s_waitcnt lgkmcnt(0)
	v_mul_f32 v146, v45, v172
	s_nop 0
	v_fma_f32 v17, v212, v146, v17
	s_nop 0
	v_mul_f32 v17, v17, v16
	s_nop 0
	v_mul_f32 v17, v17, v184
	s_nop 0
	v_max_f32_e32 v17, v17, v17
	v_max_f32_e32 v17, 0xc3e00000, v17
	v_min_f32_e32 v146, 0x43e00000, v17
	s_nop 1
	v_mov_b32_dpp v147, v146 quad_perm:[1,0,3,2] row_mask:0xf bank_mask:0xf
	v_mov_b32_e32 v17, v3
	s_waitcnt lgkmcnt(0)
	v_cvt_pk_fp8_f32 v17, v146, v147
	s_nop 1
	v_mov_b32_dpp v146, v17 quad_perm:[2,3,0,1] row_mask:0xf bank_mask:0xf
	s_and_saveexec_b64 s[6:7], s[4:5]
	s_cbranch_execz .LBB0_1483
	v_and_b32_e32 v17, 0xffff, v17
	s_waitcnt lgkmcnt(0)
	v_lshl_or_b32 v17, v146, 16, v17
	v_add_co_u32_e32 v146, vcc, 0x13000, v6
	s_nop 1
	v_addc_co_u32_e32 v147, vcc, 0, v7, vcc
	global_store_dword v[146:147], v17, off offset:192
.LBB0_1483:
	s_or_b64 exec, exec, s[6:7]
	v_and_b32_e32 v2, 0xffff0000, v2
	v_mul_f32 v17, v29, v172
	s_nop 0
	v_fma_f32 v2, v212, v17, v2
	s_nop 0
	v_mul_f32 v2, v2, v16
	s_nop 0
	v_mul_f32 v2, v2, v165
	s_nop 0
	v_max_f32_e32 v2, v2, v2
	v_max_f32_e32 v2, 0xc3e00000, v2
	v_min_f32_e32 v16, 0x43e00000, v2
	s_nop 1
	v_mov_b32_dpp v17, v16 quad_perm:[1,0,3,2] row_mask:0xf bank_mask:0xf
	v_mov_b32_e32 v2, v3
	s_waitcnt lgkmcnt(0)
	v_cvt_pk_fp8_f32 v2, v16, v17
	s_nop 1
	v_mov_b32_dpp v16, v2 quad_perm:[2,3,0,1] row_mask:0xf bank_mask:0xf
	s_and_saveexec_b64 s[6:7], s[4:5]
	s_cbranch_execz .LBB0_1485
	v_and_b32_e32 v2, 0xffff, v2
	s_waitcnt lgkmcnt(0)
	v_lshl_or_b32 v2, v16, 16, v2
	v_add_co_u32_e32 v16, vcc, 0x13000, v6
	s_nop 1
	v_addc_co_u32_e32 v17, vcc, 0, v7, vcc
	global_store_dword v[16:17], v2, off offset:224
; #define SBAR() __builtin_amdgcn_sched_barrier(0)
; __device__ __forceinline__ int crow(int r, int hi) { return (r & 3) + 8 * (r >> 2) + 4 * hi; }
; __device__ __forceinline__ float mul_ns(float a, float b) { float r; asm("v_mul_f32 %0, %1, %2" : "=v"(r) : "v"(a), "v"(b)); return r; }
; __device__ __forceinline__ void store_quad8(unsigned char* p, float v, int r32) {
;     v = fminf(fmaxf(v, -448.f), 448.f);
;     const float v1 = swz_xor<1>(v);
;     const int w = __builtin_amdgcn_cvt_pk_fp8_f32(v, v1, 0, false);
;     const int w2 = __builtin_amdgcn_ds_swizzle(w, (2 << 10) | 0x1f);
;     if ((r32 & 3) == 0) *(unsigned*)p = ((unsigned)w & 0xffffu) | ((unsigned)w2 << 16);
; }
;     __device__ __forceinline__ void operator()(f32x16 (&o)[8], const float (&rli)[16], int wid, int lane, int r32, int hi) const {
;     ...
;                 for (int q = 0; q < 4; ++q) { const int r = rb + q; float s = 0.f;
; #pragma unroll
;                     for (int d0 = 0; d0 < 8; ++d0) { const float t = __uint_as_float((d0 & 1) ? (tw[q][d0 >> 1] & 0xffff0000u) : (tw[q][d0 >> 1] << 16));
;                         const float dd = fma_ns(nlam, mul_ns(o[d0][r], rli[r]), t); s = fma_ns(dd, dd, s); }
;                     s = half_sum(s); rn[r] = rsqrtf(s * (1.0f / 256.0f) + 1e-5f) * 0.8f; }
;                 asm volatile("" ::: "memory"); SBAR(); }
;             float g[8];
; #pragma unroll
;             for (int d0 = 0; d0 < 8; ++d0) g[d0] = gain[d0 * 32 + r32];
; #pragma unroll
;             for (int rb = 0; rb < 16; rb += 4) { unsigned tw[4][4];
; #pragma unroll
;                 for (int q = 0; q < 4; ++q)
; #pragma unroll
;                     for (int k = 0; k < 4; ++k) tw[q][k] = (scw + ((rb + q) * 4 + k) * 64)[ul];
;                 asm volatile("" ::: "memory"); SBAR();
; #pragma unroll
;                 for (int q = 0; q < 4; ++q) { const int r = rb + q;
; #pragma unroll
;                     for (int d0 = 0; d0 < 8; ++d0) { const float t = __uint_as_float((d0 & 1) ? (tw[q][d0 >> 1] & 0xffff0000u) : (tw[q][d0 >> 1] << 16));
;                         const float dd = fma_ns(nlam, mul_ns(o[d0][r], rli[r]), t);
;                         store_quad8(base + (crow(r, 0) * 4096 + d0 * 32) + uo, mul_ns(mul_ns(dd, rn[r]), g[d0]), r32); } }
;                 asm volatile("" ::: "memory"); SBAR(); }
.LBB0_1485:
	s_or_b64 exec, exec, s[6:7]
	s_mov_b64 s[6:7], 0x3000
	s_waitcnt lgkmcnt(0)
	v_lshl_add_u64 v[16:17], v[4:5], 0, s[6:7]
	s_mov_b64 s[6:7], 0x3100
	v_lshl_add_u64 v[146:147], v[4:5], 0, s[6:7]
	s_mov_b64 s[6:7], 0x3200
	v_lshl_add_u64 v[148:149], v[4:5], 0, s[6:7]
	s_mov_b64 s[6:7], 0x3300
	v_lshl_add_u64 v[156:157], v[4:5], 0, s[6:7]
	s_mov_b64 s[6:7], 0x3400
	v_lshl_add_u64 v[158:159], v[4:5], 0, s[6:7]
	s_mov_b64 s[6:7], 0x3500
	v_lshl_add_u64 v[160:161], v[4:5], 0, s[6:7]
	s_mov_b64 s[6:7], 0x3600
	v_lshl_add_u64 v[162:163], v[4:5], 0, s[6:7]
	s_mov_b64 s[6:7], 0x3700
	v_lshl_add_u64 v[166:167], v[4:5], 0, s[6:7]
	s_mov_b64 s[6:7], 0x3800
	v_pk_add_f32 v[12:13], v[12:13], v[14:15]
	v_lshl_add_u64 v[192:193], v[4:5], 0, s[6:7]
	s_mov_b64 s[6:7], 0x3900
	v_pk_fma_f32 v[12:13], v[12:13], s[54:55], v[198:199] op_sel_hi:[1,0,0]
	v_lshl_add_u64 v[194:195], v[4:5], 0, s[6:7]
	s_mov_b64 s[6:7], 0x3a00
	v_mul_f32_e32 v2, 0x4b800000, v13
	v_cmp_gt_f32_e32 vcc, s53, v13
	v_lshl_add_u64 v[196:197], v[4:5], 0, s[6:7]
	s_mov_b64 s[6:7], 0x3b00
	v_cndmask_b32_e32 v2, v13, v2, vcc
	v_lshl_add_u64 v[202:203], v[4:5], 0, s[6:7]
	s_mov_b64 s[6:7], 0x3c00
	v_rsq_f32_e32 v2, v2
	v_lshl_add_u64 v[204:205], v[4:5], 0, s[6:7]
	s_mov_b64 s[6:7], 0x3d00
	v_lshl_add_u64 v[206:207], v[4:5], 0, s[6:7]
	s_mov_b64 s[6:7], 0x3e00
	v_lshl_add_u64 v[208:209], v[4:5], 0, s[6:7]
	s_mov_b64 s[6:7], 0x3f00
	v_lshl_add_u64 v[214:215], v[4:5], 0, s[6:7]
	v_mul_f32_e32 v4, 0x45800000, v2
	v_cndmask_b32_e32 v2, v2, v4, vcc
	v_cmp_gt_f32_e64 s[6:7], s53, v12
	v_mul_f32_e32 v150, 0x3f4ccccd, v2
	global_load_dword v154, v[16:17], off
	global_load_dword v153, v[146:147], off
	global_load_dword v152, v[148:149], off
	global_load_dword v151, v[156:157], off
	s_nop 0
	global_load_dword v149, v[158:159], off
	global_load_dword v148, v[160:161], off
	global_load_dword v5, v[162:163], off
	global_load_dword v4, v[166:167], off
	global_load_dword v147, v[192:193], off
	global_load_dword v146, v[194:195], off
	global_load_dword v17, v[196:197], off
	global_load_dword v16, v[202:203], off
	global_load_dword v15, v[204:205], off
	global_load_dword v14, v[206:207], off
	global_load_dword v13, v[208:209], off
	global_load_dword v2, v[214:215], off
	s_waitcnt vmcnt(15)
	v_lshlrev_b32_e32 v155, 16, v154
	v_mul_f32 v156, v142, v171
	s_nop 0
	v_fma_f32 v155, v212, v156, v155
	s_nop 0
	v_mul_f32 v155, v155, v150
	s_nop 0
	v_mul_f32 v155, v155, v190
	s_nop 0
	v_max_f32_e32 v155, v155, v155
	v_max_f32_e32 v155, 0xc3e00000, v155
	v_min_f32_e32 v156, 0x43e00000, v155
	s_nop 1
	v_mov_b32_dpp v157, v156 quad_perm:[1,0,3,2] row_mask:0xf bank_mask:0xf
	v_mov_b32_e32 v155, v3
	s_waitcnt lgkmcnt(0)
	v_cvt_pk_fp8_f32 v155, v156, v157
	s_nop 1
	v_mov_b32_dpp v156, v155 quad_perm:[2,3,0,1] row_mask:0xf bank_mask:0xf
	s_and_saveexec_b64 s[8:9], s[4:5]
	s_cbranch_execz .LBB0_1487
	v_and_b32_e32 v155, 0xffff, v155
	s_waitcnt lgkmcnt(0)
	v_lshl_or_b32 v155, v156, 16, v155
	v_add_co_u32_e32 v156, vcc, 0x18000, v6
	s_nop 1
	v_addc_co_u32_e32 v157, vcc, 0, v7, vcc
	global_store_dword v[156:157], v155, off
.LBB0_1487:
	s_or_b64 exec, exec, s[8:9]
	v_and_b32_e32 v154, 0xffff0000, v154
	v_mul_f32 v155, v126, v171
	s_nop 0
	v_fma_f32 v154, v212, v155, v154
	s_nop 0
	v_mul_f32 v154, v154, v150
	s_nop 0
	v_mul_f32 v154, v154, v189
	s_nop 0
	v_max_f32_e32 v154, v154, v154
	v_max_f32_e32 v154, 0xc3e00000, v154
	v_min_f32_e32 v155, 0x43e00000, v154
	s_waitcnt lgkmcnt(0)
	s_nop 1
	v_mov_b32_dpp v156, v155 quad_perm:[1,0,3,2] row_mask:0xf bank_mask:0xf
	v_mov_b32_e32 v154, v3
	s_waitcnt lgkmcnt(0)
	v_cvt_pk_fp8_f32 v154, v155, v156
	s_nop 1
	v_mov_b32_dpp v155, v154 quad_perm:[2,3,0,1] row_mask:0xf bank_mask:0xf
	s_and_saveexec_b64 s[8:9], s[4:5]
	s_cbranch_execz .LBB0_1489
	v_and_b32_e32 v154, 0xffff, v154
	s_waitcnt lgkmcnt(0)
	v_lshl_or_b32 v156, v155, 16, v154
	v_add_co_u32_e32 v154, vcc, 0x18000, v6
	s_nop 1
	v_addc_co_u32_e32 v155, vcc, 0, v7, vcc
	global_store_dword v[154:155], v156, off offset:32
.LBB0_1489:
	s_or_b64 exec, exec, s[8:9]
	s_waitcnt vmcnt(14)
	v_lshlrev_b32_e32 v154, 16, v153
	s_waitcnt lgkmcnt(0)
	v_mul_f32 v155, v110, v171
	s_nop 0
	v_fma_f32 v154, v212, v155, v154
	s_nop 0
	v_mul_f32 v154, v154, v150
	s_nop 0
	v_mul_f32 v154, v154, v188
	s_nop 0
	v_max_f32_e32 v154, v154, v154
	v_max_f32_e32 v154, 0xc3e00000, v154
	v_min_f32_e32 v155, 0x43e00000, v154
	s_nop 1
	v_mov_b32_dpp v156, v155 quad_perm:[1,0,3,2] row_mask:0xf bank_mask:0xf
	v_mov_b32_e32 v154, v3
	s_waitcnt lgkmcnt(0)
	v_cvt_pk_fp8_f32 v154, v155, v156
	s_nop 1
	v_mov_b32_dpp v155, v154 quad_perm:[2,3,0,1] row_mask:0xf bank_mask:0xf
	s_and_saveexec_b64 s[8:9], s[4:5]
	s_cbranch_execz .LBB0_1491
	v_and_b32_e32 v154, 0xffff, v154
	s_waitcnt lgkmcnt(0)
	v_lshl_or_b32 v156, v155, 16, v154
	v_add_co_u32_e32 v154, vcc, 0x18000, v6
	s_nop 1
	v_addc_co_u32_e32 v155, vcc, 0, v7, vcc
	global_store_dword v[154:155], v156, off offset:64
.LBB0_1491:
	s_or_b64 exec, exec, s[8:9]
	v_and_b32_e32 v153, 0xffff0000, v153
	v_mul_f32 v154, v94, v171
	s_nop 0
	v_fma_f32 v153, v212, v154, v153
	s_nop 0
	v_mul_f32 v153, v153, v150
	s_nop 0
	v_mul_f32 v153, v153, v187
	s_nop 0
	v_max_f32_e32 v153, v153, v153
	v_max_f32_e32 v153, 0xc3e00000, v153
	v_min_f32_e32 v154, 0x43e00000, v153
	s_waitcnt lgkmcnt(0)
	s_nop 1
	v_mov_b32_dpp v155, v154 quad_perm:[1,0,3,2] row_mask:0xf bank_mask:0xf
	v_mov_b32_e32 v153, v3
	s_waitcnt lgkmcnt(0)
	v_cvt_pk_fp8_f32 v153, v154, v155
	s_nop 1
	v_mov_b32_dpp v154, v153 quad_perm:[2,3,0,1] row_mask:0xf bank_mask:0xf
	s_and_saveexec_b64 s[8:9], s[4:5]
	s_cbranch_execz .LBB0_1493
	v_and_b32_e32 v153, 0xffff, v153
	s_waitcnt lgkmcnt(0)
	v_lshl_or_b32 v153, v154, 16, v153
	v_add_co_u32_e32 v154, vcc, 0x18000, v6
	s_nop 1
	v_addc_co_u32_e32 v155, vcc, 0, v7, vcc
	global_store_dword v[154:155], v153, off offset:96
; #define SBAR() __builtin_amdgcn_sched_barrier(0)
; __device__ __forceinline__ int crow(int r, int hi) { return (r & 3) + 8 * (r >> 2) + 4 * hi; }
; __device__ __forceinline__ float mul_ns(float a, float b) { float r; asm("v_mul_f32 %0, %1, %2" : "=v"(r) : "v"(a), "v"(b)); return r; }
; __device__ __forceinline__ float fma_ns(float a, float b, float c) { float r; asm("v_fma_f32 %0, %1, %2, %3" : "=v"(r) : "v"(a), "v"(b), "v"(c)); return r; }
; __device__ __forceinline__ void store_quad8(unsigned char* p, float v, int r32) {
;     v = fminf(fmaxf(v, -448.f), 448.f);
;     const float v1 = swz_xor<1>(v);
;     const int w = __builtin_amdgcn_cvt_pk_fp8_f32(v, v1, 0, false);
;     const int w2 = __builtin_amdgcn_ds_swizzle(w, (2 << 10) | 0x1f);
;     if ((r32 & 3) == 0) *(unsigned*)p = ((unsigned)w & 0xffffu) | ((unsigned)w2 << 16);
; }
;     __device__ __forceinline__ void operator()(f32x16 (&o)[8], const float (&rli)[16], int wid, int lane, int r32, int hi) const {
;     ...
;                 for (int q = 0; q < 4; ++q) { const int r = rb + q;
; #pragma unroll
;                     for (int d0 = 0; d0 < 8; ++d0) { const float t = __uint_as_float((d0 & 1) ? (tw[q][d0 >> 1] & 0xffff0000u) : (tw[q][d0 >> 1] << 16));
;                         const float dd = fma_ns(nlam, mul_ns(o[d0][r], rli[r]), t);
;                         store_quad8(base + (crow(r, 0) * 4096 + d0 * 32) + uo, mul_ns(mul_ns(dd, rn[r]), g[d0]), r32); } }
;                 asm volatile("" ::: "memory"); SBAR(); }
.LBB0_1493:
	s_or_b64 exec, exec, s[8:9]
	s_waitcnt vmcnt(13)
	v_lshlrev_b32_e32 v153, 16, v152
	s_waitcnt lgkmcnt(0)
	v_mul_f32 v154, v78, v171
	s_nop 0
	v_fma_f32 v153, v212, v154, v153
	s_nop 0
	v_mul_f32 v153, v153, v150
	s_nop 0
	v_mul_f32 v153, v153, v186
	s_nop 0
	v_max_f32_e32 v153, v153, v153
	v_max_f32_e32 v153, 0xc3e00000, v153
	v_min_f32_e32 v154, 0x43e00000, v153
	s_nop 1
	v_mov_b32_dpp v155, v154 quad_perm:[1,0,3,2] row_mask:0xf bank_mask:0xf
	v_mov_b32_e32 v153, v3
	s_waitcnt lgkmcnt(0)
	v_cvt_pk_fp8_f32 v153, v154, v155
	s_nop 1
	v_mov_b32_dpp v154, v153 quad_perm:[2,3,0,1] row_mask:0xf bank_mask:0xf
	s_and_saveexec_b64 s[8:9], s[4:5]
	s_cbranch_execz .LBB0_1495
	v_and_b32_e32 v153, 0xffff, v153
	s_waitcnt lgkmcnt(0)
	v_lshl_or_b32 v153, v154, 16, v153
	v_add_co_u32_e32 v154, vcc, 0x18000, v6
	s_nop 1
	v_addc_co_u32_e32 v155, vcc, 0, v7, vcc
	global_store_dword v[154:155], v153, off offset:128
.LBB0_1495:
	s_or_b64 exec, exec, s[8:9]
	v_and_b32_e32 v152, 0xffff0000, v152
	v_mul_f32 v153, v62, v171
	s_nop 0
	v_fma_f32 v152, v212, v153, v152
	s_nop 0
	v_mul_f32 v152, v152, v150
	s_nop 0
	v_mul_f32 v152, v152, v185
	s_nop 0
	v_max_f32_e32 v152, v152, v152
	v_max_f32_e32 v152, 0xc3e00000, v152
	v_min_f32_e32 v153, 0x43e00000, v152
	s_waitcnt lgkmcnt(0)
	s_nop 1
	v_mov_b32_dpp v154, v153 quad_perm:[1,0,3,2] row_mask:0xf bank_mask:0xf
	v_mov_b32_e32 v152, v3
	s_waitcnt lgkmcnt(0)
	v_cvt_pk_fp8_f32 v152, v153, v154
	s_nop 1
	v_mov_b32_dpp v153, v152 quad_perm:[2,3,0,1] row_mask:0xf bank_mask:0xf
	s_and_saveexec_b64 s[8:9], s[4:5]
	s_cbranch_execz .LBB0_1497
	v_and_b32_e32 v152, 0xffff, v152
	s_waitcnt lgkmcnt(0)
	v_lshl_or_b32 v154, v153, 16, v152
	v_add_co_u32_e32 v152, vcc, 0x18000, v6
	s_nop 1
	v_addc_co_u32_e32 v153, vcc, 0, v7, vcc
	global_store_dword v[152:153], v154, off offset:160
.LBB0_1497:
	s_or_b64 exec, exec, s[8:9]
	s_waitcnt vmcnt(12)
	v_lshlrev_b32_e32 v152, 16, v151
	s_waitcnt lgkmcnt(0)
	v_mul_f32 v153, v46, v171
	s_nop 0
	v_fma_f32 v152, v212, v153, v152
	s_nop 0
	v_mul_f32 v152, v152, v150
	s_nop 0
	v_mul_f32 v152, v152, v184
	s_nop 0
	v_max_f32_e32 v152, v152, v152
	v_max_f32_e32 v152, 0xc3e00000, v152
	v_min_f32_e32 v153, 0x43e00000, v152
	s_nop 1
	v_mov_b32_dpp v154, v153 quad_perm:[1,0,3,2] row_mask:0xf bank_mask:0xf
	v_mov_b32_e32 v152, v3
	s_waitcnt lgkmcnt(0)
	v_cvt_pk_fp8_f32 v152, v153, v154
	s_nop 1
	v_mov_b32_dpp v153, v152 quad_perm:[2,3,0,1] row_mask:0xf bank_mask:0xf
	s_and_saveexec_b64 s[8:9], s[4:5]
	s_cbranch_execz .LBB0_1499
	v_and_b32_e32 v152, 0xffff, v152
	s_waitcnt lgkmcnt(0)
	v_lshl_or_b32 v154, v153, 16, v152
	v_add_co_u32_e32 v152, vcc, 0x18000, v6
	s_nop 1
	v_addc_co_u32_e32 v153, vcc, 0, v7, vcc
	global_store_dword v[152:153], v154, off offset:192
.LBB0_1499:
	s_or_b64 exec, exec, s[8:9]
	v_and_b32_e32 v151, 0xffff0000, v151
	v_mul_f32 v152, v30, v171
	s_nop 0
	v_fma_f32 v151, v212, v152, v151
	s_nop 0
	v_mul_f32 v150, v151, v150
	s_nop 0
	v_mul_f32 v150, v150, v165
	s_nop 0
	v_max_f32_e32 v150, v150, v150
	v_max_f32_e32 v150, 0xc3e00000, v150
	v_min_f32_e32 v151, 0x43e00000, v150
	s_nop 1
	v_mov_b32_dpp v152, v151 quad_perm:[1,0,3,2] row_mask:0xf bank_mask:0xf
	v_mov_b32_e32 v150, v3
	s_waitcnt lgkmcnt(0)
	v_cvt_pk_fp8_f32 v150, v151, v152
	s_nop 1
	v_mov_b32_dpp v151, v150 quad_perm:[2,3,0,1] row_mask:0xf bank_mask:0xf
	s_and_saveexec_b64 s[8:9], s[4:5]
	s_cbranch_execz .LBB0_1501
	v_and_b32_e32 v150, 0xffff, v150
	s_waitcnt lgkmcnt(0)
	v_lshl_or_b32 v152, v151, 16, v150
	v_add_co_u32_e32 v150, vcc, 0x18000, v6
	s_nop 1
	v_addc_co_u32_e32 v151, vcc, 0, v7, vcc
	global_store_dword v[150:151], v152, off offset:224
.LBB0_1501:
	s_or_b64 exec, exec, s[8:9]
	v_mul_f32_e32 v150, 0x4b800000, v12
	v_cndmask_b32_e64 v12, v12, v150, s[6:7]
	v_rsq_f32_e32 v12, v12
	s_waitcnt lgkmcnt(0)
	v_mul_f32 v151, v143, v170
	v_mul_f32_e32 v150, 0x45800000, v12
	v_cndmask_b32_e64 v12, v12, v150, s[6:7]
	s_waitcnt vmcnt(11)
	v_lshlrev_b32_e32 v150, 16, v149
	v_fma_f32 v150, v212, v151, v150
	v_mul_f32_e32 v12, 0x3f4ccccd, v12
	v_mul_f32 v150, v150, v12
	s_nop 0
	v_mul_f32 v150, v150, v190
	s_nop 0
	v_max_f32_e32 v150, v150, v150
	v_max_f32_e32 v150, 0xc3e00000, v150
	v_min_f32_e32 v151, 0x43e00000, v150
	s_nop 1
	v_mov_b32_dpp v152, v151 quad_perm:[1,0,3,2] row_mask:0xf bank_mask:0xf
	v_mov_b32_e32 v150, v3
	s_waitcnt lgkmcnt(0)
	v_cvt_pk_fp8_f32 v150, v151, v152
	s_nop 1
	v_mov_b32_dpp v151, v150 quad_perm:[2,3,0,1] row_mask:0xf bank_mask:0xf
	s_and_saveexec_b64 s[6:7], s[4:5]
	s_cbranch_execz .LBB0_1503
	v_and_b32_e32 v150, 0xffff, v150
	s_waitcnt lgkmcnt(0)
	v_lshl_or_b32 v152, v151, 16, v150
	v_add_co_u32_e32 v150, vcc, 0x19000, v6
	s_nop 1
	v_addc_co_u32_e32 v151, vcc, 0, v7, vcc
	global_store_dword v[150:151], v152, off
.LBB0_1503:
	s_or_b64 exec, exec, s[6:7]
	v_and_b32_e32 v149, 0xffff0000, v149
	v_mul_f32 v150, v127, v170
	s_nop 0
	v_fma_f32 v149, v212, v150, v149
	s_nop 0
	v_mul_f32 v149, v149, v12
	s_nop 0
	v_mul_f32 v149, v149, v189
	s_nop 0
	v_max_f32_e32 v149, v149, v149
	v_max_f32_e32 v149, 0xc3e00000, v149
	v_min_f32_e32 v150, 0x43e00000, v149
	s_waitcnt lgkmcnt(0)
	s_nop 1
	v_mov_b32_dpp v151, v150 quad_perm:[1,0,3,2] row_mask:0xf bank_mask:0xf
	v_mov_b32_e32 v149, v3
	s_waitcnt lgkmcnt(0)
	v_cvt_pk_fp8_f32 v149, v150, v151
	s_nop 1
	v_mov_b32_dpp v150, v149 quad_perm:[2,3,0,1] row_mask:0xf bank_mask:0xf
	s_and_saveexec_b64 s[6:7], s[4:5]
	s_cbranch_execz .LBB0_1505
	v_and_b32_e32 v149, 0xffff, v149
	s_waitcnt lgkmcnt(0)
	v_lshl_or_b32 v149, v150, 16, v149
	v_add_co_u32_e32 v150, vcc, 0x19000, v6
	s_nop 1
	v_addc_co_u32_e32 v151, vcc, 0, v7, vcc
	global_store_dword v[150:151], v149, off offset:32
; #define SBAR() __builtin_amdgcn_sched_barrier(0)
; __device__ __forceinline__ int crow(int r, int hi) { return (r & 3) + 8 * (r >> 2) + 4 * hi; }
; __device__ __forceinline__ float mul_ns(float a, float b) { float r; asm("v_mul_f32 %0, %1, %2" : "=v"(r) : "v"(a), "v"(b)); return r; }
; __device__ __forceinline__ float fma_ns(float a, float b, float c) { float r; asm("v_fma_f32 %0, %1, %2, %3" : "=v"(r) : "v"(a), "v"(b), "v"(c)); return r; }
; __device__ __forceinline__ void store_quad8(unsigned char* p, float v, int r32) {
;     v = fminf(fmaxf(v, -448.f), 448.f);
;     const float v1 = swz_xor<1>(v);
;     const int w = __builtin_amdgcn_cvt_pk_fp8_f32(v, v1, 0, false);
;     const int w2 = __builtin_amdgcn_ds_swizzle(w, (2 << 10) | 0x1f);
;     if ((r32 & 3) == 0) *(unsigned*)p = ((unsigned)w & 0xffffu) | ((unsigned)w2 << 16);
; }
;     __device__ __forceinline__ void operator()(f32x16 (&o)[8], const float (&rli)[16], int wid, int lane, int r32, int hi) const {
;     ...
;                 for (int q = 0; q < 4; ++q) { const int r = rb + q;
; #pragma unroll
;                     for (int d0 = 0; d0 < 8; ++d0) { const float t = __uint_as_float((d0 & 1) ? (tw[q][d0 >> 1] & 0xffff0000u) : (tw[q][d0 >> 1] << 16));
;                         const float dd = fma_ns(nlam, mul_ns(o[d0][r], rli[r]), t);
;                         store_quad8(base + (crow(r, 0) * 4096 + d0 * 32) + uo, mul_ns(mul_ns(dd, rn[r]), g[d0]), r32); } }
;                 asm volatile("" ::: "memory"); SBAR(); }
.LBB0_1505:
	s_or_b64 exec, exec, s[6:7]
	s_waitcnt vmcnt(10)
	v_lshlrev_b32_e32 v149, 16, v148
	s_waitcnt lgkmcnt(0)
	v_mul_f32 v150, v111, v170
	s_nop 0
	v_fma_f32 v149, v212, v150, v149
	s_nop 0
	v_mul_f32 v149, v149, v12
	s_nop 0
	v_mul_f32 v149, v149, v188
	s_nop 0
	v_max_f32_e32 v149, v149, v149
	v_max_f32_e32 v149, 0xc3e00000, v149
	v_min_f32_e32 v150, 0x43e00000, v149
	s_nop 1
	v_mov_b32_dpp v151, v150 quad_perm:[1,0,3,2] row_mask:0xf bank_mask:0xf
	v_mov_b32_e32 v149, v3
	s_waitcnt lgkmcnt(0)
	v_cvt_pk_fp8_f32 v149, v150, v151
	s_nop 1
	v_mov_b32_dpp v150, v149 quad_perm:[2,3,0,1] row_mask:0xf bank_mask:0xf
	s_and_saveexec_b64 s[6:7], s[4:5]
	s_cbranch_execz .LBB0_1507
	v_and_b32_e32 v149, 0xffff, v149
	s_waitcnt lgkmcnt(0)
	v_lshl_or_b32 v149, v150, 16, v149
	v_add_co_u32_e32 v150, vcc, 0x19000, v6
	s_nop 1
	v_addc_co_u32_e32 v151, vcc, 0, v7, vcc
	global_store_dword v[150:151], v149, off offset:64
.LBB0_1507:
	s_or_b64 exec, exec, s[6:7]
	v_and_b32_e32 v148, 0xffff0000, v148
	v_mul_f32 v149, v95, v170
	s_nop 0
	v_fma_f32 v148, v212, v149, v148
	s_nop 0
	v_mul_f32 v148, v148, v12
	s_nop 0
	v_mul_f32 v148, v148, v187
	s_nop 0
	v_max_f32_e32 v148, v148, v148
	v_max_f32_e32 v148, 0xc3e00000, v148
	v_min_f32_e32 v149, 0x43e00000, v148
	s_waitcnt lgkmcnt(0)
	s_nop 1
	v_mov_b32_dpp v150, v149 quad_perm:[1,0,3,2] row_mask:0xf bank_mask:0xf
	v_mov_b32_e32 v148, v3
	s_waitcnt lgkmcnt(0)
	v_cvt_pk_fp8_f32 v148, v149, v150
	s_nop 1
	v_mov_b32_dpp v149, v148 quad_perm:[2,3,0,1] row_mask:0xf bank_mask:0xf
	s_and_saveexec_b64 s[6:7], s[4:5]
	s_cbranch_execz .LBB0_1509
	v_and_b32_e32 v148, 0xffff, v148
	s_waitcnt lgkmcnt(0)
	v_lshl_or_b32 v150, v149, 16, v148
	v_add_co_u32_e32 v148, vcc, 0x19000, v6
	s_nop 1
	v_addc_co_u32_e32 v149, vcc, 0, v7, vcc
	global_store_dword v[148:149], v150, off offset:96
.LBB0_1509:
	s_or_b64 exec, exec, s[6:7]
	s_waitcnt vmcnt(9)
	v_lshlrev_b32_e32 v148, 16, v5
	s_waitcnt lgkmcnt(0)
	v_mul_f32 v149, v79, v170
	s_nop 0
	v_fma_f32 v148, v212, v149, v148
	s_nop 0
	v_mul_f32 v148, v148, v12
	s_nop 0
	v_mul_f32 v148, v148, v186
	s_nop 0
	v_max_f32_e32 v148, v148, v148
	v_max_f32_e32 v148, 0xc3e00000, v148
	v_min_f32_e32 v149, 0x43e00000, v148
	s_nop 1
	v_mov_b32_dpp v150, v149 quad_perm:[1,0,3,2] row_mask:0xf bank_mask:0xf
	v_mov_b32_e32 v148, v3
	s_waitcnt lgkmcnt(0)
	v_cvt_pk_fp8_f32 v148, v149, v150
	s_nop 1
	v_mov_b32_dpp v149, v148 quad_perm:[2,3,0,1] row_mask:0xf bank_mask:0xf
	s_and_saveexec_b64 s[6:7], s[4:5]
	s_cbranch_execz .LBB0_1511
	v_and_b32_e32 v148, 0xffff, v148
	s_waitcnt lgkmcnt(0)
	v_lshl_or_b32 v150, v149, 16, v148
	v_add_co_u32_e32 v148, vcc, 0x19000, v6
	s_nop 1
	v_addc_co_u32_e32 v149, vcc, 0, v7, vcc
	global_store_dword v[148:149], v150, off offset:128
.LBB0_1511:
	s_or_b64 exec, exec, s[6:7]
	v_and_b32_e32 v5, 0xffff0000, v5
	v_mul_f32 v148, v63, v170
	s_nop 0
	v_fma_f32 v5, v212, v148, v5
	s_nop 0
	v_mul_f32 v5, v5, v12
	s_nop 0
	v_mul_f32 v5, v5, v185
	s_nop 0
	v_max_f32_e32 v5, v5, v5
	v_max_f32_e32 v5, 0xc3e00000, v5
	v_min_f32_e32 v148, 0x43e00000, v5
	s_waitcnt lgkmcnt(0)
	s_nop 1
	v_mov_b32_dpp v149, v148 quad_perm:[1,0,3,2] row_mask:0xf bank_mask:0xf
	v_mov_b32_e32 v5, v3
	s_waitcnt lgkmcnt(0)
	v_cvt_pk_fp8_f32 v5, v148, v149
	s_nop 1
	v_mov_b32_dpp v148, v5 quad_perm:[2,3,0,1] row_mask:0xf bank_mask:0xf
	s_and_saveexec_b64 s[6:7], s[4:5]
	s_cbranch_execz .LBB0_1513
	v_and_b32_e32 v5, 0xffff, v5
	s_waitcnt lgkmcnt(0)
	v_lshl_or_b32 v5, v148, 16, v5
	v_add_co_u32_e32 v148, vcc, 0x19000, v6
	s_nop 1
	v_addc_co_u32_e32 v149, vcc, 0, v7, vcc
	global_store_dword v[148:149], v5, off offset:160
.LBB0_1513:
	s_or_b64 exec, exec, s[6:7]
	s_waitcnt vmcnt(8)
	v_lshlrev_b32_e32 v5, 16, v4
	s_waitcnt lgkmcnt(0)
	v_mul_f32 v148, v47, v170
	s_nop 0
	v_fma_f32 v5, v212, v148, v5
	s_nop 0
	v_mul_f32 v5, v5, v12
	s_nop 0
	v_mul_f32 v5, v5, v184
	s_nop 0
	v_max_f32_e32 v5, v5, v5
	v_max_f32_e32 v5, 0xc3e00000, v5
	v_min_f32_e32 v148, 0x43e00000, v5
	s_nop 1
	v_mov_b32_dpp v149, v148 quad_perm:[1,0,3,2] row_mask:0xf bank_mask:0xf
	v_mov_b32_e32 v5, v3
	s_waitcnt lgkmcnt(0)
	v_cvt_pk_fp8_f32 v5, v148, v149
	s_nop 1
	v_mov_b32_dpp v148, v5 quad_perm:[2,3,0,1] row_mask:0xf bank_mask:0xf
	s_and_saveexec_b64 s[6:7], s[4:5]
	s_cbranch_execz .LBB0_1515
	v_and_b32_e32 v5, 0xffff, v5
	s_waitcnt lgkmcnt(0)
	v_lshl_or_b32 v5, v148, 16, v5
	v_add_co_u32_e32 v148, vcc, 0x19000, v6
	s_nop 1
	v_addc_co_u32_e32 v149, vcc, 0, v7, vcc
	global_store_dword v[148:149], v5, off offset:192
.LBB0_1515:
	s_or_b64 exec, exec, s[6:7]
	v_and_b32_e32 v4, 0xffff0000, v4
	v_mul_f32 v5, v31, v170
	s_nop 0
	v_fma_f32 v4, v212, v5, v4
	s_nop 0
	v_mul_f32 v4, v4, v12
	s_nop 0
	v_mul_f32 v4, v4, v165
	s_nop 0
	v_max_f32_e32 v4, v4, v4
	v_max_f32_e32 v4, 0xc3e00000, v4
	v_min_f32_e32 v5, 0x43e00000, v4
	s_nop 1
	v_mov_b32_dpp v12, v5 quad_perm:[1,0,3,2] row_mask:0xf bank_mask:0xf
	v_mov_b32_e32 v4, v3
	s_waitcnt lgkmcnt(0)
	v_cvt_pk_fp8_f32 v4, v5, v12
	s_nop 1
	v_mov_b32_dpp v5, v4 quad_perm:[2,3,0,1] row_mask:0xf bank_mask:0xf
	s_and_saveexec_b64 s[6:7], s[4:5]
	s_cbranch_execz .LBB0_1517
	v_and_b32_e32 v4, 0xffff, v4
	s_waitcnt lgkmcnt(0)
	v_lshl_or_b32 v12, v5, 16, v4
	v_add_co_u32_e32 v4, vcc, 0x19000, v6
	s_nop 1
	v_addc_co_u32_e32 v5, vcc, 0, v7, vcc
	global_store_dword v[4:5], v12, off offset:224
; #define SBAR() __builtin_amdgcn_sched_barrier(0)
; __device__ __forceinline__ int crow(int r, int hi) { return (r & 3) + 8 * (r >> 2) + 4 * hi; }
; __device__ __forceinline__ float mul_ns(float a, float b) { float r; asm("v_mul_f32 %0, %1, %2" : "=v"(r) : "v"(a), "v"(b)); return r; }
; __device__ __forceinline__ void store_quad8(unsigned char* p, float v, int r32) {
;     v = fminf(fmaxf(v, -448.f), 448.f);
;     const float v1 = swz_xor<1>(v);
;     const int w = __builtin_amdgcn_cvt_pk_fp8_f32(v, v1, 0, false);
;     const int w2 = __builtin_amdgcn_ds_swizzle(w, (2 << 10) | 0x1f);
;     if ((r32 & 3) == 0) *(unsigned*)p = ((unsigned)w & 0xffffu) | ((unsigned)w2 << 16);
; }
;     __device__ __forceinline__ void operator()(f32x16 (&o)[8], const float (&rli)[16], int wid, int lane, int r32, int hi) const {
;     ...
;                 for (int q = 0; q < 4; ++q) { const int r = rb + q; float s = 0.f;
; #pragma unroll
;                     for (int d0 = 0; d0 < 8; ++d0) { const float t = __uint_as_float((d0 & 1) ? (tw[q][d0 >> 1] & 0xffff0000u) : (tw[q][d0 >> 1] << 16));
;                         const float dd = fma_ns(nlam, mul_ns(o[d0][r], rli[r]), t); s = fma_ns(dd, dd, s); }
;                     s = half_sum(s); rn[r] = rsqrtf(s * (1.0f / 256.0f) + 1e-5f) * 0.8f; }
;                 asm volatile("" ::: "memory"); SBAR(); }
;             float g[8];
; #pragma unroll
;             for (int d0 = 0; d0 < 8; ++d0) g[d0] = gain[d0 * 32 + r32];
; #pragma unroll
;             for (int rb = 0; rb < 16; rb += 4) { unsigned tw[4][4];
; #pragma unroll
;                 for (int q = 0; q < 4; ++q)
; #pragma unroll
;                     for (int k = 0; k < 4; ++k) tw[q][k] = (scw + ((rb + q) * 4 + k) * 64)[ul];
;                 asm volatile("" ::: "memory"); SBAR();
; #pragma unroll
;                 for (int q = 0; q < 4; ++q) { const int r = rb + q;
; #pragma unroll
;                     for (int d0 = 0; d0 < 8; ++d0) { const float t = __uint_as_float((d0 & 1) ? (tw[q][d0 >> 1] & 0xffff0000u) : (tw[q][d0 >> 1] << 16));
;                         const float dd = fma_ns(nlam, mul_ns(o[d0][r], rli[r]), t);
;                         store_quad8(base + (crow(r, 0) * 4096 + d0 * 32) + uo, mul_ns(mul_ns(dd, rn[r]), g[d0]), r32); } }
;                 asm volatile("" ::: "memory"); SBAR(); }
.LBB0_1517:
	s_or_b64 exec, exec, s[6:7]
	s_waitcnt lgkmcnt(0)
	v_pk_add_f32 v[4:5], v[8:9], v[10:11]
	v_mul_f32 v9, v144, v169
	s_nop 0
	v_pk_fma_f32 v[4:5], v[4:5], s[54:55], v[198:199] op_sel_hi:[1,0,0]
	s_nop 0
	v_mul_f32_e32 v8, 0x4b800000, v5
	v_cmp_gt_f32_e32 vcc, s53, v5
	v_cmp_gt_f32_e64 s[6:7], s53, v4
	s_nop 0
	v_cndmask_b32_e32 v5, v5, v8, vcc
	v_rsq_f32_e32 v5, v5
	s_waitcnt vmcnt(7)
	v_lshlrev_b32_e32 v8, 16, v147
	v_fma_f32 v8, v212, v9, v8
	v_mul_f32_e32 v10, 0x45800000, v5
	v_cndmask_b32_e32 v5, v5, v10, vcc
	v_mul_f32_e32 v5, 0x3f4ccccd, v5
	v_mul_f32 v8, v8, v5
	s_nop 0
	v_mul_f32 v8, v8, v190
	s_nop 0
	v_max_f32_e32 v8, v8, v8
	v_max_f32_e32 v8, 0xc3e00000, v8
	v_min_f32_e32 v9, 0x43e00000, v8
	s_nop 1
	v_mov_b32_dpp v10, v9 quad_perm:[1,0,3,2] row_mask:0xf bank_mask:0xf
	v_mov_b32_e32 v8, v3
	s_waitcnt lgkmcnt(0)
	v_cvt_pk_fp8_f32 v8, v9, v10
	s_nop 1
	v_mov_b32_dpp v9, v8 quad_perm:[2,3,0,1] row_mask:0xf bank_mask:0xf
	s_and_saveexec_b64 s[8:9], s[4:5]
	s_cbranch_execz .LBB0_1519
	v_and_b32_e32 v8, 0xffff, v8
	s_waitcnt lgkmcnt(0)
	v_lshl_or_b32 v10, v9, 16, v8
	v_add_co_u32_e32 v8, vcc, 0x1a000, v6
	s_nop 1
	v_addc_co_u32_e32 v9, vcc, 0, v7, vcc
	global_store_dword v[8:9], v10, off
.LBB0_1519:
	s_or_b64 exec, exec, s[8:9]
	v_and_b32_e32 v8, 0xffff0000, v147
	s_waitcnt lgkmcnt(0)
	v_mul_f32 v9, v128, v169
	s_nop 0
	v_fma_f32 v8, v212, v9, v8
	s_nop 0
	v_mul_f32 v8, v8, v5
	s_nop 0
	v_mul_f32 v8, v8, v189
	s_nop 0
	v_max_f32_e32 v8, v8, v8
	v_max_f32_e32 v8, 0xc3e00000, v8
	v_min_f32_e32 v9, 0x43e00000, v8
	s_nop 1
	v_mov_b32_dpp v10, v9 quad_perm:[1,0,3,2] row_mask:0xf bank_mask:0xf
	v_mov_b32_e32 v8, v3
	s_waitcnt lgkmcnt(0)
	v_cvt_pk_fp8_f32 v8, v9, v10
	s_nop 1
	v_mov_b32_dpp v9, v8 quad_perm:[2,3,0,1] row_mask:0xf bank_mask:0xf
	s_and_saveexec_b64 s[8:9], s[4:5]
	s_cbranch_execz .LBB0_1521
	v_and_b32_e32 v8, 0xffff, v8
	s_waitcnt lgkmcnt(0)
	v_lshl_or_b32 v10, v9, 16, v8
	v_add_co_u32_e32 v8, vcc, 0x1a000, v6
	s_nop 1
	v_addc_co_u32_e32 v9, vcc, 0, v7, vcc
	global_store_dword v[8:9], v10, off offset:32
.LBB0_1521:
	s_or_b64 exec, exec, s[8:9]
	s_waitcnt vmcnt(6)
	v_lshlrev_b32_e32 v8, 16, v146
	s_waitcnt lgkmcnt(0)
	v_mul_f32 v9, v112, v169
	s_nop 0
	v_fma_f32 v8, v212, v9, v8
	s_nop 0
	v_mul_f32 v8, v8, v5
	s_nop 0
	v_mul_f32 v8, v8, v188
	s_nop 0
	v_max_f32_e32 v8, v8, v8
	v_max_f32_e32 v8, 0xc3e00000, v8
	v_min_f32_e32 v9, 0x43e00000, v8
	s_nop 1
	v_mov_b32_dpp v10, v9 quad_perm:[1,0,3,2] row_mask:0xf bank_mask:0xf
	v_mov_b32_e32 v8, v3
	s_waitcnt lgkmcnt(0)
	v_cvt_pk_fp8_f32 v8, v9, v10
	s_nop 1
	v_mov_b32_dpp v9, v8 quad_perm:[2,3,0,1] row_mask:0xf bank_mask:0xf
	s_and_saveexec_b64 s[8:9], s[4:5]
	s_cbranch_execz .LBB0_1523
	v_and_b32_e32 v8, 0xffff, v8
	s_waitcnt lgkmcnt(0)
	v_lshl_or_b32 v10, v9, 16, v8
	v_add_co_u32_e32 v8, vcc, 0x1a000, v6
	s_nop 1
	v_addc_co_u32_e32 v9, vcc, 0, v7, vcc
	global_store_dword v[8:9], v10, off offset:64
.LBB0_1523:
	s_or_b64 exec, exec, s[8:9]
	v_and_b32_e32 v8, 0xffff0000, v146
	s_waitcnt lgkmcnt(0)
	v_mul_f32 v9, v96, v169
	s_nop 0
	v_fma_f32 v8, v212, v9, v8
	s_nop 0
	v_mul_f32 v8, v8, v5
	s_nop 0
	v_mul_f32 v8, v8, v187
	s_nop 0
	v_max_f32_e32 v8, v8, v8
	v_max_f32_e32 v8, 0xc3e00000, v8
	v_min_f32_e32 v9, 0x43e00000, v8
	s_nop 1
	v_mov_b32_dpp v10, v9 quad_perm:[1,0,3,2] row_mask:0xf bank_mask:0xf
	v_mov_b32_e32 v8, v3
	s_waitcnt lgkmcnt(0)
	v_cvt_pk_fp8_f32 v8, v9, v10
	s_nop 1
	v_mov_b32_dpp v9, v8 quad_perm:[2,3,0,1] row_mask:0xf bank_mask:0xf
	s_and_saveexec_b64 s[8:9], s[4:5]
	s_cbranch_execz .LBB0_1525
	v_and_b32_e32 v8, 0xffff, v8
	s_waitcnt lgkmcnt(0)
	v_lshl_or_b32 v10, v9, 16, v8
	v_add_co_u32_e32 v8, vcc, 0x1a000, v6
	s_nop 1
	v_addc_co_u32_e32 v9, vcc, 0, v7, vcc
	global_store_dword v[8:9], v10, off offset:96
.LBB0_1525:
	s_or_b64 exec, exec, s[8:9]
	s_waitcnt vmcnt(5)
	v_lshlrev_b32_e32 v8, 16, v17
	s_waitcnt lgkmcnt(0)
	v_mul_f32 v9, v80, v169
	s_nop 0
	v_fma_f32 v8, v212, v9, v8
	s_nop 0
	v_mul_f32 v8, v8, v5
	s_nop 0
	v_mul_f32 v8, v8, v186
	s_nop 0
	v_max_f32_e32 v8, v8, v8
	v_max_f32_e32 v8, 0xc3e00000, v8
	v_min_f32_e32 v9, 0x43e00000, v8
	s_nop 1
	v_mov_b32_dpp v10, v9 quad_perm:[1,0,3,2] row_mask:0xf bank_mask:0xf
	v_mov_b32_e32 v8, v3
	s_waitcnt lgkmcnt(0)
	v_cvt_pk_fp8_f32 v8, v9, v10
	s_nop 1
	v_mov_b32_dpp v9, v8 quad_perm:[2,3,0,1] row_mask:0xf bank_mask:0xf
	s_and_saveexec_b64 s[8:9], s[4:5]
	s_cbranch_execz .LBB0_1527
	v_and_b32_e32 v8, 0xffff, v8
	s_waitcnt lgkmcnt(0)
	v_lshl_or_b32 v10, v9, 16, v8
	v_add_co_u32_e32 v8, vcc, 0x1a000, v6
	s_nop 1
	v_addc_co_u32_e32 v9, vcc, 0, v7, vcc
	global_store_dword v[8:9], v10, off offset:128
.LBB0_1527:
	s_or_b64 exec, exec, s[8:9]
	v_and_b32_e32 v8, 0xffff0000, v17
	s_waitcnt lgkmcnt(0)
	v_mul_f32 v9, v64, v169
	s_nop 0
	v_fma_f32 v8, v212, v9, v8
	s_nop 0
	v_mul_f32 v8, v8, v5
	s_nop 0
	v_mul_f32 v8, v8, v185
	s_nop 0
	v_max_f32_e32 v8, v8, v8
	v_max_f32_e32 v8, 0xc3e00000, v8
	v_min_f32_e32 v9, 0x43e00000, v8
	s_nop 1
	v_mov_b32_dpp v10, v9 quad_perm:[1,0,3,2] row_mask:0xf bank_mask:0xf
	v_mov_b32_e32 v8, v3
	s_waitcnt lgkmcnt(0)
	v_cvt_pk_fp8_f32 v8, v9, v10
	s_nop 1
	v_mov_b32_dpp v9, v8 quad_perm:[2,3,0,1] row_mask:0xf bank_mask:0xf
	s_and_saveexec_b64 s[8:9], s[4:5]
	s_cbranch_execz .LBB0_1529
	v_and_b32_e32 v8, 0xffff, v8
	s_waitcnt lgkmcnt(0)
	v_lshl_or_b32 v10, v9, 16, v8
	v_add_co_u32_e32 v8, vcc, 0x1a000, v6
	s_nop 1
	v_addc_co_u32_e32 v9, vcc, 0, v7, vcc
	global_store_dword v[8:9], v10, off offset:160
; #define SBAR() __builtin_amdgcn_sched_barrier(0)
; __device__ __forceinline__ int crow(int r, int hi) { return (r & 3) + 8 * (r >> 2) + 4 * hi; }
; __device__ __forceinline__ float mul_ns(float a, float b) { float r; asm("v_mul_f32 %0, %1, %2" : "=v"(r) : "v"(a), "v"(b)); return r; }
; __device__ __forceinline__ float fma_ns(float a, float b, float c) { float r; asm("v_fma_f32 %0, %1, %2, %3" : "=v"(r) : "v"(a), "v"(b), "v"(c)); return r; }
; __device__ __forceinline__ void store_quad8(unsigned char* p, float v, int r32) {
;     v = fminf(fmaxf(v, -448.f), 448.f);
;     const float v1 = swz_xor<1>(v);
;     const int w = __builtin_amdgcn_cvt_pk_fp8_f32(v, v1, 0, false);
;     const int w2 = __builtin_amdgcn_ds_swizzle(w, (2 << 10) | 0x1f);
;     if ((r32 & 3) == 0) *(unsigned*)p = ((unsigned)w & 0xffffu) | ((unsigned)w2 << 16);
; }
;     __device__ __forceinline__ void operator()(f32x16 (&o)[8], const float (&rli)[16], int wid, int lane, int r32, int hi) const {
;     ...
;                 for (int q = 0; q < 4; ++q) { const int r = rb + q;
; #pragma unroll
;                     for (int d0 = 0; d0 < 8; ++d0) { const float t = __uint_as_float((d0 & 1) ? (tw[q][d0 >> 1] & 0xffff0000u) : (tw[q][d0 >> 1] << 16));
;                         const float dd = fma_ns(nlam, mul_ns(o[d0][r], rli[r]), t);
;                         store_quad8(base + (crow(r, 0) * 4096 + d0 * 32) + uo, mul_ns(mul_ns(dd, rn[r]), g[d0]), r32); } }
;                 asm volatile("" ::: "memory"); SBAR(); }
.LBB0_1529:
	s_or_b64 exec, exec, s[8:9]
	s_waitcnt vmcnt(4)
	v_lshlrev_b32_e32 v8, 16, v16
	s_waitcnt lgkmcnt(0)
	v_mul_f32 v9, v48, v169
	s_nop 0
	v_fma_f32 v8, v212, v9, v8
	s_nop 0
	v_mul_f32 v8, v8, v5
	s_nop 0
	v_mul_f32 v8, v8, v184
	s_nop 0
	v_max_f32_e32 v8, v8, v8
	v_max_f32_e32 v8, 0xc3e00000, v8
	v_min_f32_e32 v9, 0x43e00000, v8
	s_nop 1
	v_mov_b32_dpp v10, v9 quad_perm:[1,0,3,2] row_mask:0xf bank_mask:0xf
	v_mov_b32_e32 v8, v3
	s_waitcnt lgkmcnt(0)
	v_cvt_pk_fp8_f32 v8, v9, v10
	s_nop 1
	v_mov_b32_dpp v9, v8 quad_perm:[2,3,0,1] row_mask:0xf bank_mask:0xf
	s_and_saveexec_b64 s[8:9], s[4:5]
	s_cbranch_execz .LBB0_1531
	v_and_b32_e32 v8, 0xffff, v8
	s_waitcnt lgkmcnt(0)
	v_lshl_or_b32 v10, v9, 16, v8
	v_add_co_u32_e32 v8, vcc, 0x1a000, v6
	s_nop 1
	v_addc_co_u32_e32 v9, vcc, 0, v7, vcc
	global_store_dword v[8:9], v10, off offset:192
.LBB0_1531:
	s_or_b64 exec, exec, s[8:9]
	v_and_b32_e32 v8, 0xffff0000, v16
	s_waitcnt lgkmcnt(0)
	v_mul_f32 v9, v32, v169
	s_nop 0
	v_fma_f32 v8, v212, v9, v8
	s_nop 0
	v_mul_f32 v5, v8, v5
	s_nop 0
	v_mul_f32 v5, v5, v165
	s_nop 0
	v_max_f32_e32 v5, v5, v5
	v_max_f32_e32 v5, 0xc3e00000, v5
	v_min_f32_e32 v8, 0x43e00000, v5
	s_nop 1
	v_mov_b32_dpp v9, v8 quad_perm:[1,0,3,2] row_mask:0xf bank_mask:0xf
	v_mov_b32_e32 v5, v3
	s_waitcnt lgkmcnt(0)
	v_cvt_pk_fp8_f32 v5, v8, v9
	s_nop 1
	v_mov_b32_dpp v8, v5 quad_perm:[2,3,0,1] row_mask:0xf bank_mask:0xf
	s_and_saveexec_b64 s[8:9], s[4:5]
	s_cbranch_execz .LBB0_1533
	v_and_b32_e32 v5, 0xffff, v5
	s_waitcnt lgkmcnt(0)
	v_lshl_or_b32 v5, v8, 16, v5
	v_add_co_u32_e32 v8, vcc, 0x1a000, v6
	s_nop 1
	v_addc_co_u32_e32 v9, vcc, 0, v7, vcc
	global_store_dword v[8:9], v5, off offset:224
.LBB0_1533:
	s_or_b64 exec, exec, s[8:9]
	v_mul_f32_e32 v5, 0x4b800000, v4
	v_cndmask_b32_e64 v4, v4, v5, s[6:7]
	v_rsq_f32_e32 v4, v4
	s_waitcnt lgkmcnt(0)
	v_mul_f32 v8, v145, v168
	v_mul_f32_e32 v5, 0x45800000, v4
	v_cndmask_b32_e64 v4, v4, v5, s[6:7]
	s_waitcnt vmcnt(3)
	v_lshlrev_b32_e32 v5, 16, v15
	v_fma_f32 v5, v212, v8, v5
	v_mul_f32_e32 v4, 0x3f4ccccd, v4
	v_mul_f32 v5, v5, v4
	s_nop 0
	v_mul_f32 v5, v5, v190
	s_nop 0
	v_max_f32_e32 v5, v5, v5
	v_max_f32_e32 v5, 0xc3e00000, v5
	v_min_f32_e32 v8, 0x43e00000, v5
	s_nop 1
	v_mov_b32_dpp v9, v8 quad_perm:[1,0,3,2] row_mask:0xf bank_mask:0xf
	v_mov_b32_e32 v5, v3
	s_waitcnt lgkmcnt(0)
	v_cvt_pk_fp8_f32 v5, v8, v9
	s_nop 1
	v_mov_b32_dpp v8, v5 quad_perm:[2,3,0,1] row_mask:0xf bank_mask:0xf
	s_and_saveexec_b64 s[6:7], s[4:5]
	s_cbranch_execz .LBB0_1535
	v_and_b32_e32 v5, 0xffff, v5
	s_waitcnt lgkmcnt(0)
	v_lshl_or_b32 v5, v8, 16, v5
	v_add_co_u32_e32 v8, vcc, 0x1b000, v6
	s_nop 1
	v_addc_co_u32_e32 v9, vcc, 0, v7, vcc
	global_store_dword v[8:9], v5, off
.LBB0_1535:
	s_or_b64 exec, exec, s[6:7]
	v_and_b32_e32 v5, 0xffff0000, v15
	s_waitcnt lgkmcnt(0)
	v_mul_f32 v8, v129, v168
	s_nop 0
	v_fma_f32 v5, v212, v8, v5
	s_nop 0
	v_mul_f32 v5, v5, v4
	s_nop 0
	v_mul_f32 v5, v5, v189
	s_nop 0
	v_max_f32_e32 v5, v5, v5
	v_max_f32_e32 v5, 0xc3e00000, v5
	v_min_f32_e32 v8, 0x43e00000, v5
	s_nop 1
	v_mov_b32_dpp v9, v8 quad_perm:[1,0,3,2] row_mask:0xf bank_mask:0xf
	v_mov_b32_e32 v5, v3
	s_waitcnt lgkmcnt(0)
	v_cvt_pk_fp8_f32 v5, v8, v9
	s_nop 1
	v_mov_b32_dpp v8, v5 quad_perm:[2,3,0,1] row_mask:0xf bank_mask:0xf
	s_and_saveexec_b64 s[6:7], s[4:5]
	s_cbranch_execz .LBB0_1537
	v_and_b32_e32 v5, 0xffff, v5
	s_waitcnt lgkmcnt(0)
	v_lshl_or_b32 v5, v8, 16, v5
	v_add_co_u32_e32 v8, vcc, 0x1b000, v6
	s_nop 1
	v_addc_co_u32_e32 v9, vcc, 0, v7, vcc
	global_store_dword v[8:9], v5, off offset:32
.LBB0_1537:
	s_or_b64 exec, exec, s[6:7]
	s_waitcnt vmcnt(2)
	v_lshlrev_b32_e32 v5, 16, v14
	s_waitcnt lgkmcnt(0)
	v_mul_f32 v8, v113, v168
	s_nop 0
	v_fma_f32 v5, v212, v8, v5
	s_nop 0
	v_mul_f32 v5, v5, v4
	s_nop 0
	v_mul_f32 v5, v5, v188
	s_nop 0
	v_max_f32_e32 v5, v5, v5
	v_max_f32_e32 v5, 0xc3e00000, v5
	v_min_f32_e32 v8, 0x43e00000, v5
	s_nop 1
	v_mov_b32_dpp v9, v8 quad_perm:[1,0,3,2] row_mask:0xf bank_mask:0xf
	v_mov_b32_e32 v5, v3
	s_waitcnt lgkmcnt(0)
	v_cvt_pk_fp8_f32 v5, v8, v9
	s_nop 1
	v_mov_b32_dpp v8, v5 quad_perm:[2,3,0,1] row_mask:0xf bank_mask:0xf
	s_and_saveexec_b64 s[6:7], s[4:5]
	s_cbranch_execz .LBB0_1539
	v_and_b32_e32 v5, 0xffff, v5
	s_waitcnt lgkmcnt(0)
	v_lshl_or_b32 v5, v8, 16, v5
	v_add_co_u32_e32 v8, vcc, 0x1b000, v6
	s_nop 1
	v_addc_co_u32_e32 v9, vcc, 0, v7, vcc
	global_store_dword v[8:9], v5, off offset:64
; #define SBAR() __builtin_amdgcn_sched_barrier(0)
; __device__ __forceinline__ int crow(int r, int hi) { return (r & 3) + 8 * (r >> 2) + 4 * hi; }
; __device__ __forceinline__ float mul_ns(float a, float b) { float r; asm("v_mul_f32 %0, %1, %2" : "=v"(r) : "v"(a), "v"(b)); return r; }
; __device__ __forceinline__ float fma_ns(float a, float b, float c) { float r; asm("v_fma_f32 %0, %1, %2, %3" : "=v"(r) : "v"(a), "v"(b), "v"(c)); return r; }
; __device__ __forceinline__ void store_quad8(unsigned char* p, float v, int r32) {
;     v = fminf(fmaxf(v, -448.f), 448.f);
;     const float v1 = swz_xor<1>(v);
;     const int w = __builtin_amdgcn_cvt_pk_fp8_f32(v, v1, 0, false);
;     const int w2 = __builtin_amdgcn_ds_swizzle(w, (2 << 10) | 0x1f);
;     if ((r32 & 3) == 0) *(unsigned*)p = ((unsigned)w & 0xffffu) | ((unsigned)w2 << 16);
; }
;     __device__ __forceinline__ void operator()(f32x16 (&o)[8], const float (&rli)[16], int wid, int lane, int r32, int hi) const {
;     ...
;                 for (int q = 0; q < 4; ++q) { const int r = rb + q;
; #pragma unroll
;                     for (int d0 = 0; d0 < 8; ++d0) { const float t = __uint_as_float((d0 & 1) ? (tw[q][d0 >> 1] & 0xffff0000u) : (tw[q][d0 >> 1] << 16));
;                         const float dd = fma_ns(nlam, mul_ns(o[d0][r], rli[r]), t);
;                         store_quad8(base + (crow(r, 0) * 4096 + d0 * 32) + uo, mul_ns(mul_ns(dd, rn[r]), g[d0]), r32); } }
;                 asm volatile("" ::: "memory"); SBAR(); }
.LBB0_1539:
	s_or_b64 exec, exec, s[6:7]
	v_and_b32_e32 v5, 0xffff0000, v14
	s_waitcnt lgkmcnt(0)
	v_mul_f32 v8, v97, v168
	s_nop 0
	v_fma_f32 v5, v212, v8, v5
	s_nop 0
	v_mul_f32 v5, v5, v4
	s_nop 0
	v_mul_f32 v5, v5, v187
	s_nop 0
	v_max_f32_e32 v5, v5, v5
	v_max_f32_e32 v5, 0xc3e00000, v5
	v_min_f32_e32 v8, 0x43e00000, v5
	s_nop 1
	v_mov_b32_dpp v9, v8 quad_perm:[1,0,3,2] row_mask:0xf bank_mask:0xf
	v_mov_b32_e32 v5, v3
	s_waitcnt lgkmcnt(0)
	v_cvt_pk_fp8_f32 v5, v8, v9
	s_nop 1
	v_mov_b32_dpp v8, v5 quad_perm:[2,3,0,1] row_mask:0xf bank_mask:0xf
	s_and_saveexec_b64 s[6:7], s[4:5]
	s_cbranch_execz .LBB0_1541
	v_and_b32_e32 v5, 0xffff, v5
	s_waitcnt lgkmcnt(0)
	v_lshl_or_b32 v5, v8, 16, v5
	v_add_co_u32_e32 v8, vcc, 0x1b000, v6
	s_nop 1
	v_addc_co_u32_e32 v9, vcc, 0, v7, vcc
	global_store_dword v[8:9], v5, off offset:96
.LBB0_1541:
	s_or_b64 exec, exec, s[6:7]
	s_waitcnt vmcnt(1)
	v_lshlrev_b32_e32 v5, 16, v13
	s_waitcnt lgkmcnt(0)
	v_mul_f32 v8, v81, v168
	s_nop 0
	v_fma_f32 v5, v212, v8, v5
	s_nop 0
	v_mul_f32 v5, v5, v4
	s_nop 0
	v_mul_f32 v5, v5, v186
	s_nop 0
	v_max_f32_e32 v5, v5, v5
	v_max_f32_e32 v5, 0xc3e00000, v5
	v_min_f32_e32 v8, 0x43e00000, v5
	s_nop 1
	v_mov_b32_dpp v9, v8 quad_perm:[1,0,3,2] row_mask:0xf bank_mask:0xf
	v_mov_b32_e32 v5, v3
	s_waitcnt lgkmcnt(0)
	v_cvt_pk_fp8_f32 v5, v8, v9
	s_nop 1
	v_mov_b32_dpp v8, v5 quad_perm:[2,3,0,1] row_mask:0xf bank_mask:0xf
	s_and_saveexec_b64 s[6:7], s[4:5]
	s_cbranch_execz .LBB0_1543
	v_and_b32_e32 v5, 0xffff, v5
	s_waitcnt lgkmcnt(0)
	v_lshl_or_b32 v5, v8, 16, v5
	v_add_co_u32_e32 v8, vcc, 0x1b000, v6
	s_nop 1
	v_addc_co_u32_e32 v9, vcc, 0, v7, vcc
	global_store_dword v[8:9], v5, off offset:128
.LBB0_1543:
	s_or_b64 exec, exec, s[6:7]
	v_and_b32_e32 v5, 0xffff0000, v13
	s_waitcnt lgkmcnt(0)
	v_mul_f32 v8, v65, v168
	s_nop 0
	v_fma_f32 v5, v212, v8, v5
	s_nop 0
	v_mul_f32 v5, v5, v4
	s_nop 0
	v_mul_f32 v5, v5, v185
	s_nop 0
	v_max_f32_e32 v5, v5, v5
	v_max_f32_e32 v5, 0xc3e00000, v5
	v_min_f32_e32 v8, 0x43e00000, v5
	s_nop 1
	v_mov_b32_dpp v9, v8 quad_perm:[1,0,3,2] row_mask:0xf bank_mask:0xf
	v_mov_b32_e32 v5, v3
	s_waitcnt lgkmcnt(0)
	v_cvt_pk_fp8_f32 v5, v8, v9
	s_nop 1
	v_mov_b32_dpp v8, v5 quad_perm:[2,3,0,1] row_mask:0xf bank_mask:0xf
	s_and_saveexec_b64 s[6:7], s[4:5]
	s_cbranch_execz .LBB0_1545
	v_and_b32_e32 v5, 0xffff, v5
	s_waitcnt lgkmcnt(0)
	v_lshl_or_b32 v5, v8, 16, v5
	v_add_co_u32_e32 v8, vcc, 0x1b000, v6
	s_nop 1
	v_addc_co_u32_e32 v9, vcc, 0, v7, vcc
	global_store_dword v[8:9], v5, off offset:160
.LBB0_1545:
	s_or_b64 exec, exec, s[6:7]
	s_waitcnt vmcnt(0)
	v_lshlrev_b32_e32 v5, 16, v2
	s_waitcnt lgkmcnt(0)
	v_mul_f32 v8, v49, v168
	s_nop 0
	v_fma_f32 v5, v212, v8, v5
	s_nop 0
	v_mul_f32 v5, v5, v4
	s_nop 0
	v_mul_f32 v5, v5, v184
	s_nop 0
	v_max_f32_e32 v5, v5, v5
	v_max_f32_e32 v5, 0xc3e00000, v5
	v_min_f32_e32 v8, 0x43e00000, v5
	s_nop 1
	v_mov_b32_dpp v9, v8 quad_perm:[1,0,3,2] row_mask:0xf bank_mask:0xf
	v_mov_b32_e32 v5, v3
	s_waitcnt lgkmcnt(0)
	v_cvt_pk_fp8_f32 v5, v8, v9
	s_nop 1
	v_mov_b32_dpp v8, v5 quad_perm:[2,3,0,1] row_mask:0xf bank_mask:0xf
	s_and_saveexec_b64 s[6:7], s[4:5]
	s_cbranch_execz .LBB0_1547
	v_and_b32_e32 v5, 0xffff, v5
	s_waitcnt lgkmcnt(0)
	v_lshl_or_b32 v5, v8, 16, v5
	v_add_co_u32_e32 v8, vcc, 0x1b000, v6
	s_nop 1
	v_addc_co_u32_e32 v9, vcc, 0, v7, vcc
	global_store_dword v[8:9], v5, off offset:192
.LBB0_1547:
	s_or_b64 exec, exec, s[6:7]
	v_and_b32_e32 v2, 0xffff0000, v2
	v_mul_f32 v5, v33, v168
	s_nop 0
	v_fma_f32 v2, v212, v5, v2
	s_nop 0
	v_mul_f32 v2, v2, v4
	s_nop 0
	v_mul_f32 v2, v2, v165
	s_nop 0
	v_max_f32_e32 v2, v2, v2
	v_max_f32_e32 v2, 0xc3e00000, v2
	v_min_f32_e32 v4, 0x43e00000, v2
	s_nop 1
	v_mov_b32_dpp v5, v4 quad_perm:[1,0,3,2] row_mask:0xf bank_mask:0xf
	v_mov_b32_e32 v2, v3
	s_waitcnt lgkmcnt(0)
	v_cvt_pk_fp8_f32 v2, v4, v5
	s_nop 1
	v_mov_b32_dpp v4, v2 quad_perm:[2,3,0,1] row_mask:0xf bank_mask:0xf
	s_and_saveexec_b64 s[6:7], s[4:5]
	s_cbranch_execz .LBB0_1549
	v_and_b32_e32 v2, 0xffff, v2
	s_waitcnt lgkmcnt(0)
	v_lshl_or_b32 v2, v4, 16, v2
	v_add_co_u32_e32 v4, vcc, 0x1b000, v6
	s_nop 1
	v_addc_co_u32_e32 v5, vcc, 0, v7, vcc
	global_store_dword v[4:5], v2, off offset:224

; __device__ __forceinline__ int crow(int r, int hi) { return (r & 3) + 8 * (r >> 2) + 4 * hi; }
; template <class Epi, bool F8 = false>
; __device__ __forceinline__ void block(const BlockRef& cur, int skv, char* lds, Seam& S, bool moba, unsigned selmask, const Epi& E) {
;     ...
;     if (hi == 0) li_l[r32] = l_reg; asm volatile("s_waitcnt lgkmcnt(0)" ::: "memory");
;     float rli[16];
; #pragma unroll
;     for (int r = 0; r < 16; ++r) rli[r] = __builtin_amdgcn_rcpf(li_l[crow(r, hi)]) * (F8 ? 1.0f / 16.0f : 1.0f);
;     __device__ __forceinline__ void operator()(f32x16 (&o)[4], const float (&rli)[16], int wid, int lane, int r32, int hi) const {
;         asm volatile("" : "+v"(lane), "+v"(r32), "+v"(hi));
;         unsigned char* base = out + (size_t)(wid * QBLK) * 512;
; #pragma unroll
;         for (int r = 0; r < 16; ++r)
; #pragma unroll
;             for (int d0 = 0; d0 < 4; ++d0) store_quad8(base + (size_t)crow(r, hi) * 512 + d0 * 32 + r32, o[d0][r] * rli[r] * 16.f, r32);
;     }
.LBB0_1960:
	s_or_b64 exec, exec, s[6:7]
	s_waitcnt lgkmcnt(0)
	ds_read_b128 v[78:81], v161
	ds_read_b128 v[74:77], v161 offset:32
	s_lshl_b32 s0, s36, 12
	s_or_b32 s0, s0, s37
	s_ashr_i32 s1, s0, 31
	s_waitcnt lgkmcnt(1)
	v_rcp_f32_e32 v78, v78
	s_lshl_b64 s[0:1], s[0:1], 9
	s_add_u32 s0, s33, s0
	s_addc_u32 s1, s52, s1
	v_mul_f32_e32 v2, v2, v78
	v_mul_f32_e32 v2, 0x41800000, v2
	v_max_f32_e32 v2, 0xc3e00000, v2
	v_min_f32_e32 v82, 0x43e00000, v2
	s_nop 1
	v_mov_b32_dpp v83, v82 quad_perm:[1,0,3,2] row_mask:0xf bank_mask:0xf
	v_mov_b32_e32 v2, v147
	s_lshl_b32 s4, s21, 7
	s_add_u32 s4, s0, s4
	s_addc_u32 s5, s1, 0
	s_waitcnt lgkmcnt(0)
	v_cvt_pk_fp8_f32 v2, v82, v83
	s_ashr_i32 s21, s20, 31
	ds_read_b128 v[70:73], v161 offset:64
	ds_read_b128 v[66:69], v161 offset:96
	s_lshl_b64 s[0:1], s[20:21], 9
	v_and_b32_e32 v84, 3, v148
	s_nop 1
	v_mov_b32_dpp v88, v2 quad_perm:[2,3,0,1] row_mask:0xf bank_mask:0xf
	s_add_u32 s0, s4, s0
	v_cmp_eq_u32_e32 vcc, 0, v84
	v_lshlrev_b32_e32 v84, 2, v149
	s_addc_u32 s1, s5, s1
	v_ashrrev_i32_e32 v149, 31, v148
	v_ashrrev_i32_e32 v85, 31, v84
	v_lshl_add_u64 v[82:83], s[0:1], 0, v[148:149]
	v_lshlrev_b64 v[86:87], 9, v[84:85]
	v_lshl_add_u64 v[86:87], v[82:83], 0, v[86:87]
	s_and_saveexec_b64 s[0:1], vcc
	s_cbranch_execz .LBB0_1962
	v_and_b32_e32 v2, 0xffff, v2
	s_waitcnt lgkmcnt(0)
	v_lshl_or_b32 v2, v88, 16, v2
	global_store_dword v[86:87], v2, off
.LBB0_1962:
	s_or_b64 exec, exec, s[0:1]
	v_mul_f32_e32 v2, v18, v78
	v_mul_f32_e32 v2, 0x41800000, v2
	v_max_f32_e32 v2, 0xc3e00000, v2
	v_min_f32_e32 v18, 0x43e00000, v2
	s_nop 1
	v_mov_b32_dpp v85, v18 quad_perm:[1,0,3,2] row_mask:0xf bank_mask:0xf
	v_mov_b32_e32 v2, v147
	s_waitcnt lgkmcnt(0)
	v_cvt_pk_fp8_f32 v2, v18, v85
	s_nop 1
	v_mov_b32_dpp v18, v2 quad_perm:[2,3,0,1] row_mask:0xf bank_mask:0xf
	s_and_saveexec_b64 s[0:1], vcc
	s_cbranch_execz .LBB0_1964
	v_and_b32_e32 v2, 0xffff, v2
	s_waitcnt lgkmcnt(0)
	v_lshl_or_b32 v2, v18, 16, v2
	global_store_dword v[86:87], v2, off offset:32
.LBB0_1964:
	s_or_b64 exec, exec, s[0:1]
	v_mul_f32_e32 v2, v34, v78
	v_mul_f32_e32 v2, 0x41800000, v2
	v_max_f32_e32 v2, 0xc3e00000, v2
	s_waitcnt lgkmcnt(0)
	v_min_f32_e32 v18, 0x43e00000, v2
	s_nop 1
	v_mov_b32_dpp v34, v18 quad_perm:[1,0,3,2] row_mask:0xf bank_mask:0xf
	v_mov_b32_e32 v2, v147
	s_waitcnt lgkmcnt(0)
	v_cvt_pk_fp8_f32 v2, v18, v34
	s_nop 1
	v_mov_b32_dpp v18, v2 quad_perm:[2,3,0,1] row_mask:0xf bank_mask:0xf
	s_and_saveexec_b64 s[0:1], vcc
	s_cbranch_execz .LBB0_1966
	v_and_b32_e32 v2, 0xffff, v2
	s_waitcnt lgkmcnt(0)
	v_lshl_or_b32 v2, v18, 16, v2
	global_store_dword v[86:87], v2, off offset:64
.LBB0_1966:
	s_or_b64 exec, exec, s[0:1]
	v_mul_f32_e32 v2, v50, v78
	v_mul_f32_e32 v2, 0x41800000, v2
	v_max_f32_e32 v2, 0xc3e00000, v2
	s_waitcnt lgkmcnt(0)
	v_min_f32_e32 v18, 0x43e00000, v2
	s_nop 1
	v_mov_b32_dpp v34, v18 quad_perm:[1,0,3,2] row_mask:0xf bank_mask:0xf
	v_mov_b32_e32 v2, v147
	s_waitcnt lgkmcnt(0)
	v_cvt_pk_fp8_f32 v2, v18, v34
	s_nop 1
	v_mov_b32_dpp v18, v2 quad_perm:[2,3,0,1] row_mask:0xf bank_mask:0xf
	s_and_saveexec_b64 s[0:1], vcc
	s_cbranch_execz .LBB0_1968
	v_and_b32_e32 v2, 0xffff, v2
	s_waitcnt lgkmcnt(0)
	v_lshl_or_b32 v2, v18, 16, v2
	global_store_dword v[86:87], v2, off offset:96
.LBB0_1968:
	s_or_b64 exec, exec, s[0:1]
	s_waitcnt lgkmcnt(0)
	v_rcp_f32_e32 v18, v79
	v_mov_b32_e32 v34, v147
	v_mul_f32_e32 v2, v3, v18
	v_mul_f32_e32 v2, 0x41800000, v2
	v_max_f32_e32 v2, 0xc3e00000, v2
	v_min_f32_e32 v2, 0x43e00000, v2
	s_nop 1
	v_mov_b32_dpp v3, v2 quad_perm:[1,0,3,2] row_mask:0xf bank_mask:0xf
	s_waitcnt lgkmcnt(0)
	v_cvt_pk_fp8_f32 v34, v2, v3
	v_or_b32_e32 v2, 1, v84
	v_ashrrev_i32_e32 v3, 31, v2
	v_lshlrev_b64 v[2:3], 9, v[2:3]
	s_nop 1
	v_mov_b32_dpp v50, v34 quad_perm:[2,3,0,1] row_mask:0xf bank_mask:0xf
	v_lshl_add_u64 v[2:3], v[82:83], 0, v[2:3]
	s_and_saveexec_b64 s[0:1], vcc
	s_cbranch_execz .LBB0_1970
	v_and_b32_e32 v34, 0xffff, v34
	s_waitcnt lgkmcnt(0)
	v_lshl_or_b32 v34, v50, 16, v34
	global_store_dword v[2:3], v34, off
.LBB0_1970:
	s_or_b64 exec, exec, s[0:1]
	v_mul_f32_e32 v19, v19, v18
	v_mul_f32_e32 v19, 0x41800000, v19
	v_max_f32_e32 v19, 0xc3e00000, v19
	v_min_f32_e32 v34, 0x43e00000, v19
	s_waitcnt lgkmcnt(0)
	s_nop 1
	v_mov_b32_dpp v50, v34 quad_perm:[1,0,3,2] row_mask:0xf bank_mask:0xf
	v_mov_b32_e32 v19, v147
	s_waitcnt lgkmcnt(0)
	v_cvt_pk_fp8_f32 v19, v34, v50
	s_nop 1
	v_mov_b32_dpp v34, v19 quad_perm:[2,3,0,1] row_mask:0xf bank_mask:0xf
	s_and_saveexec_b64 s[0:1], vcc
	s_cbranch_execz .LBB0_1972
	v_and_b32_e32 v19, 0xffff, v19
	s_waitcnt lgkmcnt(0)
	v_lshl_or_b32 v19, v34, 16, v19
	global_store_dword v[2:3], v19, off offset:32
.LBB0_1972:
	s_or_b64 exec, exec, s[0:1]
	v_mul_f32_e32 v19, v35, v18
	v_mul_f32_e32 v19, 0x41800000, v19
	v_max_f32_e32 v19, 0xc3e00000, v19
	s_waitcnt lgkmcnt(0)
	v_min_f32_e32 v34, 0x43e00000, v19
	s_nop 1
	v_mov_b32_dpp v35, v34 quad_perm:[1,0,3,2] row_mask:0xf bank_mask:0xf
	v_mov_b32_e32 v19, v147
	s_waitcnt lgkmcnt(0)
	v_cvt_pk_fp8_f32 v19, v34, v35
	s_nop 1
	v_mov_b32_dpp v34, v19 quad_perm:[2,3,0,1] row_mask:0xf bank_mask:0xf
	s_and_saveexec_b64 s[0:1], vcc
	s_cbranch_execz .LBB0_1974
	v_and_b32_e32 v19, 0xffff, v19
	s_waitcnt lgkmcnt(0)
	v_lshl_or_b32 v19, v34, 16, v19
	global_store_dword v[2:3], v19, off offset:64
.LBB0_1974:
	s_or_b64 exec, exec, s[0:1]
	v_mul_f32_e32 v18, v51, v18
	v_mul_f32_e32 v18, 0x41800000, v18
	v_max_f32_e32 v18, 0xc3e00000, v18
	v_min_f32_e32 v19, 0x43e00000, v18
	s_waitcnt lgkmcnt(0)
	s_nop 1
	v_mov_b32_dpp v34, v19 quad_perm:[1,0,3,2] row_mask:0xf bank_mask:0xf
	v_mov_b32_e32 v18, v147
	s_waitcnt lgkmcnt(0)
	v_cvt_pk_fp8_f32 v18, v19, v34
	s_nop 1
	v_mov_b32_dpp v19, v18 quad_perm:[2,3,0,1] row_mask:0xf bank_mask:0xf
	s_and_saveexec_b64 s[0:1], vcc
	s_cbranch_execz .LBB0_1976
	v_and_b32_e32 v18, 0xffff, v18
	s_waitcnt lgkmcnt(0)
	v_lshl_or_b32 v18, v19, 16, v18
	global_store_dword v[2:3], v18, off offset:96
; __device__ __forceinline__ int crow(int r, int hi) { return (r & 3) + 8 * (r >> 2) + 4 * hi; }
; __device__ __forceinline__ void store_quad8(unsigned char* p, float v, int r32) {
;     v = fminf(fmaxf(v, -448.f), 448.f);
;     const float v1 = swz_xor<1>(v);
;     const int w = __builtin_amdgcn_cvt_pk_fp8_f32(v, v1, 0, false);
;     const int w2 = __builtin_amdgcn_ds_swizzle(w, (2 << 10) | 0x1f);
;     if ((r32 & 3) == 0) *(unsigned*)p = ((unsigned)w & 0xffffu) | ((unsigned)w2 << 16);
; }
;     __device__ __forceinline__ void operator()(f32x16 (&o)[4], const float (&rli)[16], int wid, int lane, int r32, int hi) const {
;         asm volatile("" : "+v"(lane), "+v"(r32), "+v"(hi));
;         unsigned char* base = out + (size_t)(wid * QBLK) * 512;
; #pragma unroll
;         for (int r = 0; r < 16; ++r)
; #pragma unroll
;             for (int d0 = 0; d0 < 4; ++d0) store_quad8(base + (size_t)crow(r, hi) * 512 + d0 * 32 + r32, o[d0][r] * rli[r] * 16.f, r32);
;     }
.LBB0_1976:
	s_or_b64 exec, exec, s[0:1]
	v_rcp_f32_e32 v18, v80
	s_nop 0
	v_mul_f32_e32 v2, v4, v18
	v_mul_f32_e32 v2, 0x41800000, v2
	v_max_f32_e32 v2, 0xc3e00000, v2
	v_min_f32_e32 v2, 0x43e00000, v2
	s_nop 1
	v_mov_b32_dpp v3, v2 quad_perm:[1,0,3,2] row_mask:0xf bank_mask:0xf
	v_mov_b32_e32 v4, v147
	s_waitcnt lgkmcnt(0)
	v_cvt_pk_fp8_f32 v4, v2, v3
	v_or_b32_e32 v2, 2, v84
	v_ashrrev_i32_e32 v3, 31, v2
	v_lshlrev_b64 v[2:3], 9, v[2:3]
	s_nop 1
	v_mov_b32_dpp v19, v4 quad_perm:[2,3,0,1] row_mask:0xf bank_mask:0xf
	v_lshl_add_u64 v[2:3], v[82:83], 0, v[2:3]
	s_and_saveexec_b64 s[0:1], vcc
	s_cbranch_execz .LBB0_1978
	v_and_b32_e32 v4, 0xffff, v4
	s_waitcnt lgkmcnt(0)
	v_lshl_or_b32 v4, v19, 16, v4
	global_store_dword v[2:3], v4, off
.LBB0_1978:
	s_or_b64 exec, exec, s[0:1]
	v_mul_f32_e32 v4, v20, v18
	v_mul_f32_e32 v4, 0x41800000, v4
	v_max_f32_e32 v4, 0xc3e00000, v4
	s_waitcnt lgkmcnt(0)
	v_min_f32_e32 v19, 0x43e00000, v4
	s_nop 1
	v_mov_b32_dpp v20, v19 quad_perm:[1,0,3,2] row_mask:0xf bank_mask:0xf
	v_mov_b32_e32 v4, v147
	s_waitcnt lgkmcnt(0)
	v_cvt_pk_fp8_f32 v4, v19, v20
	s_nop 1
	v_mov_b32_dpp v19, v4 quad_perm:[2,3,0,1] row_mask:0xf bank_mask:0xf
	s_and_saveexec_b64 s[0:1], vcc
	s_cbranch_execz .LBB0_1980
	v_and_b32_e32 v4, 0xffff, v4
	s_waitcnt lgkmcnt(0)
	v_lshl_or_b32 v4, v19, 16, v4
	global_store_dword v[2:3], v4, off offset:32
.LBB0_1980:
	s_or_b64 exec, exec, s[0:1]
	v_mul_f32_e32 v4, v36, v18
	v_mul_f32_e32 v4, 0x41800000, v4
	v_max_f32_e32 v4, 0xc3e00000, v4
	s_waitcnt lgkmcnt(0)
	v_min_f32_e32 v19, 0x43e00000, v4
	s_nop 1
	v_mov_b32_dpp v20, v19 quad_perm:[1,0,3,2] row_mask:0xf bank_mask:0xf
	v_mov_b32_e32 v4, v147
	s_waitcnt lgkmcnt(0)
	v_cvt_pk_fp8_f32 v4, v19, v20
	s_nop 1
	v_mov_b32_dpp v19, v4 quad_perm:[2,3,0,1] row_mask:0xf bank_mask:0xf
	s_and_saveexec_b64 s[0:1], vcc
	s_cbranch_execz .LBB0_1982
	v_and_b32_e32 v4, 0xffff, v4
	s_waitcnt lgkmcnt(0)
	v_lshl_or_b32 v4, v19, 16, v4
	global_store_dword v[2:3], v4, off offset:64
.LBB0_1982:
	s_or_b64 exec, exec, s[0:1]
	v_mul_f32_e32 v4, v52, v18
	v_mul_f32_e32 v4, 0x41800000, v4
	v_max_f32_e32 v4, 0xc3e00000, v4
	v_min_f32_e32 v18, 0x43e00000, v4
	s_waitcnt lgkmcnt(0)
	s_nop 1
	v_mov_b32_dpp v19, v18 quad_perm:[1,0,3,2] row_mask:0xf bank_mask:0xf
	v_mov_b32_e32 v4, v147
	s_waitcnt lgkmcnt(0)
	v_cvt_pk_fp8_f32 v4, v18, v19
	s_nop 1
	v_mov_b32_dpp v18, v4 quad_perm:[2,3,0,1] row_mask:0xf bank_mask:0xf
	s_and_saveexec_b64 s[0:1], vcc
	s_cbranch_execz .LBB0_1984
	v_and_b32_e32 v4, 0xffff, v4
	s_waitcnt lgkmcnt(0)
	v_lshl_or_b32 v4, v18, 16, v4
	global_store_dword v[2:3], v4, off offset:96
.LBB0_1984:
	s_or_b64 exec, exec, s[0:1]
	v_rcp_f32_e32 v4, v81
	s_nop 0
	v_mul_f32_e32 v2, v5, v4
	v_mul_f32_e32 v2, 0x41800000, v2
	v_max_f32_e32 v2, 0xc3e00000, v2
	v_min_f32_e32 v2, 0x43e00000, v2
	s_nop 1
	v_mov_b32_dpp v3, v2 quad_perm:[1,0,3,2] row_mask:0xf bank_mask:0xf
	v_mov_b32_e32 v5, v147
	s_waitcnt lgkmcnt(0)
	v_cvt_pk_fp8_f32 v5, v2, v3
	v_or_b32_e32 v2, 3, v84
	v_ashrrev_i32_e32 v3, 31, v2
	v_lshlrev_b64 v[2:3], 9, v[2:3]
	s_nop 1
	v_mov_b32_dpp v18, v5 quad_perm:[2,3,0,1] row_mask:0xf bank_mask:0xf
	v_lshl_add_u64 v[2:3], v[82:83], 0, v[2:3]
	s_and_saveexec_b64 s[0:1], vcc
	s_cbranch_execz .LBB0_1986
	v_and_b32_e32 v5, 0xffff, v5
	s_waitcnt lgkmcnt(0)
	v_lshl_or_b32 v5, v18, 16, v5
	global_store_dword v[2:3], v5, off
.LBB0_1986:
	s_or_b64 exec, exec, s[0:1]
	v_mul_f32_e32 v5, v21, v4
	v_mul_f32_e32 v5, 0x41800000, v5
	v_max_f32_e32 v5, 0xc3e00000, v5
	s_waitcnt lgkmcnt(0)
	v_min_f32_e32 v18, 0x43e00000, v5
	s_nop 1
	v_mov_b32_dpp v19, v18 quad_perm:[1,0,3,2] row_mask:0xf bank_mask:0xf
	v_mov_b32_e32 v5, v147
	s_waitcnt lgkmcnt(0)
	v_cvt_pk_fp8_f32 v5, v18, v19
	s_nop 1
	v_mov_b32_dpp v18, v5 quad_perm:[2,3,0,1] row_mask:0xf bank_mask:0xf
	s_and_saveexec_b64 s[0:1], vcc
	s_cbranch_execz .LBB0_1988
	v_and_b32_e32 v5, 0xffff, v5
	s_waitcnt lgkmcnt(0)
	v_lshl_or_b32 v5, v18, 16, v5
	global_store_dword v[2:3], v5, off offset:32
.LBB0_1988:
	s_or_b64 exec, exec, s[0:1]
	v_mul_f32_e32 v5, v37, v4
	v_mul_f32_e32 v5, 0x41800000, v5
	v_max_f32_e32 v5, 0xc3e00000, v5
	s_waitcnt lgkmcnt(0)
	v_min_f32_e32 v18, 0x43e00000, v5
	s_nop 1
	v_mov_b32_dpp v19, v18 quad_perm:[1,0,3,2] row_mask:0xf bank_mask:0xf
	v_mov_b32_e32 v5, v147
	s_waitcnt lgkmcnt(0)
	v_cvt_pk_fp8_f32 v5, v18, v19
	s_nop 1
	v_mov_b32_dpp v18, v5 quad_perm:[2,3,0,1] row_mask:0xf bank_mask:0xf
	s_and_saveexec_b64 s[0:1], vcc
	s_cbranch_execz .LBB0_1990
	v_and_b32_e32 v5, 0xffff, v5
	s_waitcnt lgkmcnt(0)
	v_lshl_or_b32 v5, v18, 16, v5
	global_store_dword v[2:3], v5, off offset:64
.LBB0_1990:
	s_or_b64 exec, exec, s[0:1]
	v_mul_f32_e32 v4, v53, v4
	v_mul_f32_e32 v4, 0x41800000, v4
	v_max_f32_e32 v4, 0xc3e00000, v4
	v_min_f32_e32 v5, 0x43e00000, v4
	s_waitcnt lgkmcnt(0)
	s_nop 1
	v_mov_b32_dpp v18, v5 quad_perm:[1,0,3,2] row_mask:0xf bank_mask:0xf
	v_mov_b32_e32 v4, v147
	s_waitcnt lgkmcnt(0)
	v_cvt_pk_fp8_f32 v4, v5, v18
	s_nop 1
	v_mov_b32_dpp v5, v4 quad_perm:[2,3,0,1] row_mask:0xf bank_mask:0xf
	s_and_saveexec_b64 s[0:1], vcc
	s_cbranch_execz .LBB0_1992
	v_and_b32_e32 v4, 0xffff, v4
	s_waitcnt lgkmcnt(0)
	v_lshl_or_b32 v4, v5, 16, v4
	global_store_dword v[2:3], v4, off offset:96
.LBB0_1992:
	s_or_b64 exec, exec, s[0:1]
	v_rcp_f32_e32 v4, v74
	s_waitcnt lgkmcnt(0)
	v_mov_b32_e32 v5, v147
	v_mul_f32_e32 v2, v6, v4
	v_mul_f32_e32 v2, 0x41800000, v2
	v_max_f32_e32 v2, 0xc3e00000, v2
	v_min_f32_e32 v2, 0x43e00000, v2
	s_nop 1
	v_mov_b32_dpp v3, v2 quad_perm:[1,0,3,2] row_mask:0xf bank_mask:0xf
	s_waitcnt lgkmcnt(0)
	v_cvt_pk_fp8_f32 v5, v2, v3
	v_add_u32_e32 v2, 8, v84
	v_ashrrev_i32_e32 v3, 31, v2
	v_lshlrev_b64 v[2:3], 9, v[2:3]
	s_nop 1
	v_mov_b32_dpp v6, v5 quad_perm:[2,3,0,1] row_mask:0xf bank_mask:0xf
	v_lshl_add_u64 v[2:3], v[82:83], 0, v[2:3]
	s_and_saveexec_b64 s[0:1], vcc
	s_cbranch_execz .LBB0_1994
	v_and_b32_e32 v5, 0xffff, v5
	s_waitcnt lgkmcnt(0)
	v_lshl_or_b32 v5, v6, 16, v5
	global_store_dword v[2:3], v5, off
; __device__ __forceinline__ int crow(int r, int hi) { return (r & 3) + 8 * (r >> 2) + 4 * hi; }
; __device__ __forceinline__ void store_quad8(unsigned char* p, float v, int r32) {
;     v = fminf(fmaxf(v, -448.f), 448.f);
;     const float v1 = swz_xor<1>(v);
;     const int w = __builtin_amdgcn_cvt_pk_fp8_f32(v, v1, 0, false);
;     const int w2 = __builtin_amdgcn_ds_swizzle(w, (2 << 10) | 0x1f);
;     if ((r32 & 3) == 0) *(unsigned*)p = ((unsigned)w & 0xffffu) | ((unsigned)w2 << 16);
; }
;     __device__ __forceinline__ void operator()(f32x16 (&o)[4], const float (&rli)[16], int wid, int lane, int r32, int hi) const {
;         asm volatile("" : "+v"(lane), "+v"(r32), "+v"(hi));
;         unsigned char* base = out + (size_t)(wid * QBLK) * 512;
; #pragma unroll
;         for (int r = 0; r < 16; ++r)
; #pragma unroll
;             for (int d0 = 0; d0 < 4; ++d0) store_quad8(base + (size_t)crow(r, hi) * 512 + d0 * 32 + r32, o[d0][r] * rli[r] * 16.f, r32);
;     }
.LBB0_1994:
	s_or_b64 exec, exec, s[0:1]
	v_mul_f32_e32 v5, v22, v4
	v_mul_f32_e32 v5, 0x41800000, v5
	v_max_f32_e32 v5, 0xc3e00000, v5
	s_waitcnt lgkmcnt(0)
	v_min_f32_e32 v6, 0x43e00000, v5
	s_nop 1
	v_mov_b32_dpp v18, v6 quad_perm:[1,0,3,2] row_mask:0xf bank_mask:0xf
	v_mov_b32_e32 v5, v147
	s_waitcnt lgkmcnt(0)
	v_cvt_pk_fp8_f32 v5, v6, v18
	s_nop 1
	v_mov_b32_dpp v6, v5 quad_perm:[2,3,0,1] row_mask:0xf bank_mask:0xf
	s_and_saveexec_b64 s[0:1], vcc
	s_cbranch_execz .LBB0_1996
	v_and_b32_e32 v5, 0xffff, v5
	s_waitcnt lgkmcnt(0)
	v_lshl_or_b32 v5, v6, 16, v5
	global_store_dword v[2:3], v5, off offset:32
.LBB0_1996:
	s_or_b64 exec, exec, s[0:1]
	v_mul_f32_e32 v5, v38, v4
	v_mul_f32_e32 v5, 0x41800000, v5
	v_max_f32_e32 v5, 0xc3e00000, v5
	s_waitcnt lgkmcnt(0)
	v_min_f32_e32 v6, 0x43e00000, v5
	s_nop 1
	v_mov_b32_dpp v18, v6 quad_perm:[1,0,3,2] row_mask:0xf bank_mask:0xf
	v_mov_b32_e32 v5, v147
	s_waitcnt lgkmcnt(0)
	v_cvt_pk_fp8_f32 v5, v6, v18
	s_nop 1
	v_mov_b32_dpp v6, v5 quad_perm:[2,3,0,1] row_mask:0xf bank_mask:0xf
	s_and_saveexec_b64 s[0:1], vcc
	s_cbranch_execz .LBB0_1998
	v_and_b32_e32 v5, 0xffff, v5
	s_waitcnt lgkmcnt(0)
	v_lshl_or_b32 v5, v6, 16, v5
	global_store_dword v[2:3], v5, off offset:64
.LBB0_1998:
	s_or_b64 exec, exec, s[0:1]
	v_mul_f32_e32 v4, v54, v4
	v_mul_f32_e32 v4, 0x41800000, v4
	v_max_f32_e32 v4, 0xc3e00000, v4
	v_min_f32_e32 v5, 0x43e00000, v4
	s_waitcnt lgkmcnt(0)
	s_nop 1
	v_mov_b32_dpp v6, v5 quad_perm:[1,0,3,2] row_mask:0xf bank_mask:0xf
	v_mov_b32_e32 v4, v147
	s_waitcnt lgkmcnt(0)
	v_cvt_pk_fp8_f32 v4, v5, v6
	s_nop 1
	v_mov_b32_dpp v5, v4 quad_perm:[2,3,0,1] row_mask:0xf bank_mask:0xf
	s_and_saveexec_b64 s[0:1], vcc
	s_cbranch_execz .LBB0_2000
	v_and_b32_e32 v4, 0xffff, v4
	s_waitcnt lgkmcnt(0)
	v_lshl_or_b32 v4, v5, 16, v4
	global_store_dword v[2:3], v4, off offset:96
.LBB0_2000:
	s_or_b64 exec, exec, s[0:1]
	v_rcp_f32_e32 v4, v75
	s_waitcnt lgkmcnt(0)
	v_mov_b32_e32 v5, v147
	v_mul_f32_e32 v2, v7, v4
	v_mul_f32_e32 v2, 0x41800000, v2
	v_max_f32_e32 v2, 0xc3e00000, v2
	v_min_f32_e32 v2, 0x43e00000, v2
	s_nop 1
	v_mov_b32_dpp v3, v2 quad_perm:[1,0,3,2] row_mask:0xf bank_mask:0xf
	s_waitcnt lgkmcnt(0)
	v_cvt_pk_fp8_f32 v5, v2, v3
	v_add_u32_e32 v2, 9, v84
	v_ashrrev_i32_e32 v3, 31, v2
	v_lshlrev_b64 v[2:3], 9, v[2:3]
	s_nop 1
	v_mov_b32_dpp v6, v5 quad_perm:[2,3,0,1] row_mask:0xf bank_mask:0xf
	v_lshl_add_u64 v[2:3], v[82:83], 0, v[2:3]
	s_and_saveexec_b64 s[0:1], vcc
	s_cbranch_execz .LBB0_2002
	v_and_b32_e32 v5, 0xffff, v5
	s_waitcnt lgkmcnt(0)
	v_lshl_or_b32 v5, v6, 16, v5
	global_store_dword v[2:3], v5, off
.LBB0_2002:
	s_or_b64 exec, exec, s[0:1]
	v_mul_f32_e32 v5, v23, v4
	v_mul_f32_e32 v5, 0x41800000, v5
	v_max_f32_e32 v5, 0xc3e00000, v5
	s_waitcnt lgkmcnt(0)
	v_min_f32_e32 v6, 0x43e00000, v5
	s_nop 1
	v_mov_b32_dpp v7, v6 quad_perm:[1,0,3,2] row_mask:0xf bank_mask:0xf
	v_mov_b32_e32 v5, v147
	s_waitcnt lgkmcnt(0)
	v_cvt_pk_fp8_f32 v5, v6, v7
	s_nop 1
	v_mov_b32_dpp v6, v5 quad_perm:[2,3,0,1] row_mask:0xf bank_mask:0xf
	s_and_saveexec_b64 s[0:1], vcc
	s_cbranch_execz .LBB0_2004
	v_and_b32_e32 v5, 0xffff, v5
	s_waitcnt lgkmcnt(0)
	v_lshl_or_b32 v5, v6, 16, v5
	global_store_dword v[2:3], v5, off offset:32
.LBB0_2004:
	s_or_b64 exec, exec, s[0:1]
	v_mul_f32_e32 v5, v39, v4
	v_mul_f32_e32 v5, 0x41800000, v5
	v_max_f32_e32 v5, 0xc3e00000, v5
	s_waitcnt lgkmcnt(0)
	v_min_f32_e32 v6, 0x43e00000, v5
	s_nop 1
	v_mov_b32_dpp v7, v6 quad_perm:[1,0,3,2] row_mask:0xf bank_mask:0xf
	v_mov_b32_e32 v5, v147
	s_waitcnt lgkmcnt(0)
	v_cvt_pk_fp8_f32 v5, v6, v7
	s_nop 1
	v_mov_b32_dpp v6, v5 quad_perm:[2,3,0,1] row_mask:0xf bank_mask:0xf
	s_and_saveexec_b64 s[0:1], vcc
	s_cbranch_execz .LBB0_2006
	v_and_b32_e32 v5, 0xffff, v5
	s_waitcnt lgkmcnt(0)
	v_lshl_or_b32 v5, v6, 16, v5
	global_store_dword v[2:3], v5, off offset:64
.LBB0_2006:
	s_or_b64 exec, exec, s[0:1]
	v_mul_f32_e32 v4, v55, v4
	v_mul_f32_e32 v4, 0x41800000, v4
	v_max_f32_e32 v4, 0xc3e00000, v4
	v_min_f32_e32 v5, 0x43e00000, v4
	s_waitcnt lgkmcnt(0)
	s_nop 1
	v_mov_b32_dpp v6, v5 quad_perm:[1,0,3,2] row_mask:0xf bank_mask:0xf
	v_mov_b32_e32 v4, v147
	s_waitcnt lgkmcnt(0)
	v_cvt_pk_fp8_f32 v4, v5, v6
	s_nop 1
	v_mov_b32_dpp v5, v4 quad_perm:[2,3,0,1] row_mask:0xf bank_mask:0xf
	s_and_saveexec_b64 s[0:1], vcc
	s_cbranch_execz .LBB0_2008
	v_and_b32_e32 v4, 0xffff, v4
	s_waitcnt lgkmcnt(0)
	v_lshl_or_b32 v4, v5, 16, v4
	global_store_dword v[2:3], v4, off offset:96
.LBB0_2008:
	s_or_b64 exec, exec, s[0:1]
	v_rcp_f32_e32 v4, v76
	s_waitcnt lgkmcnt(0)
	v_mov_b32_e32 v5, v147
	v_mul_f32_e32 v2, v8, v4
	v_mul_f32_e32 v2, 0x41800000, v2
	v_max_f32_e32 v2, 0xc3e00000, v2
	v_min_f32_e32 v2, 0x43e00000, v2
	s_nop 1
	v_mov_b32_dpp v3, v2 quad_perm:[1,0,3,2] row_mask:0xf bank_mask:0xf
	s_waitcnt lgkmcnt(0)
	v_cvt_pk_fp8_f32 v5, v2, v3
	v_add_u32_e32 v2, 10, v84
	v_ashrrev_i32_e32 v3, 31, v2
	v_lshlrev_b64 v[2:3], 9, v[2:3]
	s_nop 1
	v_mov_b32_dpp v6, v5 quad_perm:[2,3,0,1] row_mask:0xf bank_mask:0xf
	v_lshl_add_u64 v[2:3], v[82:83], 0, v[2:3]
	s_and_saveexec_b64 s[0:1], vcc
	s_cbranch_execz .LBB0_2010
	v_and_b32_e32 v5, 0xffff, v5
	s_waitcnt lgkmcnt(0)
	v_lshl_or_b32 v5, v6, 16, v5
	global_store_dword v[2:3], v5, off
.LBB0_2010:
	s_or_b64 exec, exec, s[0:1]
	v_mul_f32_e32 v5, v24, v4
	v_mul_f32_e32 v5, 0x41800000, v5
	v_max_f32_e32 v5, 0xc3e00000, v5
	s_waitcnt lgkmcnt(0)
	v_min_f32_e32 v6, 0x43e00000, v5
	s_nop 1
	v_mov_b32_dpp v7, v6 quad_perm:[1,0,3,2] row_mask:0xf bank_mask:0xf
	v_mov_b32_e32 v5, v147
	s_waitcnt lgkmcnt(0)
	v_cvt_pk_fp8_f32 v5, v6, v7
	s_nop 1
	v_mov_b32_dpp v6, v5 quad_perm:[2,3,0,1] row_mask:0xf bank_mask:0xf
	s_and_saveexec_b64 s[0:1], vcc
	s_cbranch_execz .LBB0_2012
	v_and_b32_e32 v5, 0xffff, v5
	s_waitcnt lgkmcnt(0)
	v_lshl_or_b32 v5, v6, 16, v5
	global_store_dword v[2:3], v5, off offset:32
; __device__ __forceinline__ int crow(int r, int hi) { return (r & 3) + 8 * (r >> 2) + 4 * hi; }
; __device__ __forceinline__ void store_quad8(unsigned char* p, float v, int r32) {
;     v = fminf(fmaxf(v, -448.f), 448.f);
;     const float v1 = swz_xor<1>(v);
;     const int w = __builtin_amdgcn_cvt_pk_fp8_f32(v, v1, 0, false);
;     const int w2 = __builtin_amdgcn_ds_swizzle(w, (2 << 10) | 0x1f);
;     if ((r32 & 3) == 0) *(unsigned*)p = ((unsigned)w & 0xffffu) | ((unsigned)w2 << 16);
; }
;     __device__ __forceinline__ void operator()(f32x16 (&o)[4], const float (&rli)[16], int wid, int lane, int r32, int hi) const {
;         asm volatile("" : "+v"(lane), "+v"(r32), "+v"(hi));
;         unsigned char* base = out + (size_t)(wid * QBLK) * 512;
; #pragma unroll
;         for (int r = 0; r < 16; ++r)
; #pragma unroll
;             for (int d0 = 0; d0 < 4; ++d0) store_quad8(base + (size_t)crow(r, hi) * 512 + d0 * 32 + r32, o[d0][r] * rli[r] * 16.f, r32);
;     }
.LBB0_2012:
	s_or_b64 exec, exec, s[0:1]
	v_mul_f32_e32 v5, v40, v4
	v_mul_f32_e32 v5, 0x41800000, v5
	v_max_f32_e32 v5, 0xc3e00000, v5
	s_waitcnt lgkmcnt(0)
	v_min_f32_e32 v6, 0x43e00000, v5
	s_nop 1
	v_mov_b32_dpp v7, v6 quad_perm:[1,0,3,2] row_mask:0xf bank_mask:0xf
	v_mov_b32_e32 v5, v147
	s_waitcnt lgkmcnt(0)
	v_cvt_pk_fp8_f32 v5, v6, v7
	s_nop 1
	v_mov_b32_dpp v6, v5 quad_perm:[2,3,0,1] row_mask:0xf bank_mask:0xf
	s_and_saveexec_b64 s[0:1], vcc
	s_cbranch_execz .LBB0_2014
	v_and_b32_e32 v5, 0xffff, v5
	s_waitcnt lgkmcnt(0)
	v_lshl_or_b32 v5, v6, 16, v5
	global_store_dword v[2:3], v5, off offset:64
.LBB0_2014:
	s_or_b64 exec, exec, s[0:1]
	v_mul_f32_e32 v4, v56, v4
	v_mul_f32_e32 v4, 0x41800000, v4
	v_max_f32_e32 v4, 0xc3e00000, v4
	v_min_f32_e32 v5, 0x43e00000, v4
	s_waitcnt lgkmcnt(0)
	s_nop 1
	v_mov_b32_dpp v6, v5 quad_perm:[1,0,3,2] row_mask:0xf bank_mask:0xf
	v_mov_b32_e32 v4, v147
	s_waitcnt lgkmcnt(0)
	v_cvt_pk_fp8_f32 v4, v5, v6
	s_nop 1
	v_mov_b32_dpp v5, v4 quad_perm:[2,3,0,1] row_mask:0xf bank_mask:0xf
	s_and_saveexec_b64 s[0:1], vcc
	s_cbranch_execz .LBB0_2016
	v_and_b32_e32 v4, 0xffff, v4
	s_waitcnt lgkmcnt(0)
	v_lshl_or_b32 v4, v5, 16, v4
	global_store_dword v[2:3], v4, off offset:96
.LBB0_2016:
	s_or_b64 exec, exec, s[0:1]
	v_rcp_f32_e32 v4, v77
	s_waitcnt lgkmcnt(0)
	v_mov_b32_e32 v5, v147
	v_mul_f32_e32 v2, v9, v4
	v_mul_f32_e32 v2, 0x41800000, v2
	v_max_f32_e32 v2, 0xc3e00000, v2
	v_min_f32_e32 v2, 0x43e00000, v2
	s_nop 1
	v_mov_b32_dpp v3, v2 quad_perm:[1,0,3,2] row_mask:0xf bank_mask:0xf
	s_waitcnt lgkmcnt(0)
	v_cvt_pk_fp8_f32 v5, v2, v3
	v_add_u32_e32 v2, 11, v84
	v_ashrrev_i32_e32 v3, 31, v2
	v_lshlrev_b64 v[2:3], 9, v[2:3]
	s_nop 1
	v_mov_b32_dpp v6, v5 quad_perm:[2,3,0,1] row_mask:0xf bank_mask:0xf
	v_lshl_add_u64 v[2:3], v[82:83], 0, v[2:3]
	s_and_saveexec_b64 s[0:1], vcc
	s_cbranch_execz .LBB0_2018
	v_and_b32_e32 v5, 0xffff, v5
	s_waitcnt lgkmcnt(0)
	v_lshl_or_b32 v5, v6, 16, v5
	global_store_dword v[2:3], v5, off
.LBB0_2018:
	s_or_b64 exec, exec, s[0:1]
	v_mul_f32_e32 v5, v25, v4
	v_mul_f32_e32 v5, 0x41800000, v5
	v_max_f32_e32 v5, 0xc3e00000, v5
	s_waitcnt lgkmcnt(0)
	v_min_f32_e32 v6, 0x43e00000, v5
	s_nop 1
	v_mov_b32_dpp v7, v6 quad_perm:[1,0,3,2] row_mask:0xf bank_mask:0xf
	v_mov_b32_e32 v5, v147
	s_waitcnt lgkmcnt(0)
	v_cvt_pk_fp8_f32 v5, v6, v7
	s_nop 1
	v_mov_b32_dpp v6, v5 quad_perm:[2,3,0,1] row_mask:0xf bank_mask:0xf
	s_and_saveexec_b64 s[0:1], vcc
	s_cbranch_execz .LBB0_2020
	v_and_b32_e32 v5, 0xffff, v5
	s_waitcnt lgkmcnt(0)
	v_lshl_or_b32 v5, v6, 16, v5
	global_store_dword v[2:3], v5, off offset:32
.LBB0_2020:
	s_or_b64 exec, exec, s[0:1]
	v_mul_f32_e32 v5, v41, v4
	v_mul_f32_e32 v5, 0x41800000, v5
	v_max_f32_e32 v5, 0xc3e00000, v5
	s_waitcnt lgkmcnt(0)
	v_min_f32_e32 v6, 0x43e00000, v5
	s_nop 1
	v_mov_b32_dpp v7, v6 quad_perm:[1,0,3,2] row_mask:0xf bank_mask:0xf
	v_mov_b32_e32 v5, v147
	s_waitcnt lgkmcnt(0)
	v_cvt_pk_fp8_f32 v5, v6, v7
	s_nop 1
	v_mov_b32_dpp v6, v5 quad_perm:[2,3,0,1] row_mask:0xf bank_mask:0xf
	s_and_saveexec_b64 s[0:1], vcc
	s_cbranch_execz .LBB0_2022
	v_and_b32_e32 v5, 0xffff, v5
	s_waitcnt lgkmcnt(0)
	v_lshl_or_b32 v5, v6, 16, v5
	global_store_dword v[2:3], v5, off offset:64
.LBB0_2022:
	s_or_b64 exec, exec, s[0:1]
	v_mul_f32_e32 v4, v57, v4
	v_mul_f32_e32 v4, 0x41800000, v4
	v_max_f32_e32 v4, 0xc3e00000, v4
	v_min_f32_e32 v5, 0x43e00000, v4
	s_waitcnt lgkmcnt(0)
	s_nop 1
	v_mov_b32_dpp v6, v5 quad_perm:[1,0,3,2] row_mask:0xf bank_mask:0xf
	v_mov_b32_e32 v4, v147
	s_waitcnt lgkmcnt(0)
	v_cvt_pk_fp8_f32 v4, v5, v6
	s_nop 1
	v_mov_b32_dpp v5, v4 quad_perm:[2,3,0,1] row_mask:0xf bank_mask:0xf
	s_and_saveexec_b64 s[0:1], vcc
	s_cbranch_execz .LBB0_2024
	v_and_b32_e32 v4, 0xffff, v4
	s_waitcnt lgkmcnt(0)
	v_lshl_or_b32 v4, v5, 16, v4
	global_store_dword v[2:3], v4, off offset:96
.LBB0_2024:
	s_or_b64 exec, exec, s[0:1]
	v_rcp_f32_e32 v4, v70
	s_waitcnt lgkmcnt(0)
	v_mov_b32_e32 v5, v147
	v_mul_f32_e32 v2, v10, v4
	v_mul_f32_e32 v2, 0x41800000, v2
	v_max_f32_e32 v2, 0xc3e00000, v2
	v_min_f32_e32 v2, 0x43e00000, v2
	s_nop 1
	v_mov_b32_dpp v3, v2 quad_perm:[1,0,3,2] row_mask:0xf bank_mask:0xf
	s_waitcnt lgkmcnt(0)
	v_cvt_pk_fp8_f32 v5, v2, v3
	v_add_u32_e32 v2, 16, v84
	v_ashrrev_i32_e32 v3, 31, v2
	v_lshlrev_b64 v[2:3], 9, v[2:3]
	s_nop 1
	v_mov_b32_dpp v6, v5 quad_perm:[2,3,0,1] row_mask:0xf bank_mask:0xf
	v_lshl_add_u64 v[2:3], v[82:83], 0, v[2:3]
	s_and_saveexec_b64 s[0:1], vcc
	s_cbranch_execz .LBB0_2026
	v_and_b32_e32 v5, 0xffff, v5
	s_waitcnt lgkmcnt(0)
	v_lshl_or_b32 v5, v6, 16, v5
	global_store_dword v[2:3], v5, off
.LBB0_2026:
	s_or_b64 exec, exec, s[0:1]
	v_mul_f32_e32 v5, v26, v4
	v_mul_f32_e32 v5, 0x41800000, v5
	v_max_f32_e32 v5, 0xc3e00000, v5
	s_waitcnt lgkmcnt(0)
	v_min_f32_e32 v6, 0x43e00000, v5
	s_nop 1
	v_mov_b32_dpp v7, v6 quad_perm:[1,0,3,2] row_mask:0xf bank_mask:0xf
	v_mov_b32_e32 v5, v147
	s_waitcnt lgkmcnt(0)
	v_cvt_pk_fp8_f32 v5, v6, v7
	s_nop 1
	v_mov_b32_dpp v6, v5 quad_perm:[2,3,0,1] row_mask:0xf bank_mask:0xf
	s_and_saveexec_b64 s[0:1], vcc
	s_cbranch_execz .LBB0_2028
	v_and_b32_e32 v5, 0xffff, v5
	s_waitcnt lgkmcnt(0)
	v_lshl_or_b32 v5, v6, 16, v5
	global_store_dword v[2:3], v5, off offset:32
.LBB0_2028:
	s_or_b64 exec, exec, s[0:1]
	v_mul_f32_e32 v5, v42, v4
	v_mul_f32_e32 v5, 0x41800000, v5
	v_max_f32_e32 v5, 0xc3e00000, v5
	s_waitcnt lgkmcnt(0)
	v_min_f32_e32 v6, 0x43e00000, v5
	s_nop 1
	v_mov_b32_dpp v7, v6 quad_perm:[1,0,3,2] row_mask:0xf bank_mask:0xf
	v_mov_b32_e32 v5, v147
	s_waitcnt lgkmcnt(0)
	v_cvt_pk_fp8_f32 v5, v6, v7
	s_nop 1
	v_mov_b32_dpp v6, v5 quad_perm:[2,3,0,1] row_mask:0xf bank_mask:0xf
	s_and_saveexec_b64 s[0:1], vcc
	s_cbranch_execz .LBB0_2030
	v_and_b32_e32 v5, 0xffff, v5
	s_waitcnt lgkmcnt(0)
	v_lshl_or_b32 v5, v6, 16, v5
	global_store_dword v[2:3], v5, off offset:64
; __device__ __forceinline__ int crow(int r, int hi) { return (r & 3) + 8 * (r >> 2) + 4 * hi; }
; __device__ __forceinline__ void store_quad8(unsigned char* p, float v, int r32) {
;     v = fminf(fmaxf(v, -448.f), 448.f);
;     const float v1 = swz_xor<1>(v);
;     const int w = __builtin_amdgcn_cvt_pk_fp8_f32(v, v1, 0, false);
;     const int w2 = __builtin_amdgcn_ds_swizzle(w, (2 << 10) | 0x1f);
;     if ((r32 & 3) == 0) *(unsigned*)p = ((unsigned)w & 0xffffu) | ((unsigned)w2 << 16);
; }
;     __device__ __forceinline__ void operator()(f32x16 (&o)[4], const float (&rli)[16], int wid, int lane, int r32, int hi) const {
;         asm volatile("" : "+v"(lane), "+v"(r32), "+v"(hi));
;         unsigned char* base = out + (size_t)(wid * QBLK) * 512;
; #pragma unroll
;         for (int r = 0; r < 16; ++r)
; #pragma unroll
;             for (int d0 = 0; d0 < 4; ++d0) store_quad8(base + (size_t)crow(r, hi) * 512 + d0 * 32 + r32, o[d0][r] * rli[r] * 16.f, r32);
;     }
.LBB0_2030:
	s_or_b64 exec, exec, s[0:1]
	v_mul_f32_e32 v4, v58, v4
	v_mul_f32_e32 v4, 0x41800000, v4
	v_max_f32_e32 v4, 0xc3e00000, v4
	v_min_f32_e32 v5, 0x43e00000, v4
	s_waitcnt lgkmcnt(0)
	s_nop 1
	v_mov_b32_dpp v6, v5 quad_perm:[1,0,3,2] row_mask:0xf bank_mask:0xf
	v_mov_b32_e32 v4, v147
	s_waitcnt lgkmcnt(0)
	v_cvt_pk_fp8_f32 v4, v5, v6
	s_nop 1
	v_mov_b32_dpp v5, v4 quad_perm:[2,3,0,1] row_mask:0xf bank_mask:0xf
	s_and_saveexec_b64 s[0:1], vcc
	s_cbranch_execz .LBB0_2032
	v_and_b32_e32 v4, 0xffff, v4
	s_waitcnt lgkmcnt(0)
	v_lshl_or_b32 v4, v5, 16, v4
	global_store_dword v[2:3], v4, off offset:96
.LBB0_2032:
	s_or_b64 exec, exec, s[0:1]
	v_rcp_f32_e32 v4, v71
	s_waitcnt lgkmcnt(0)
	v_mov_b32_e32 v5, v147
	v_mul_f32_e32 v2, v11, v4
	v_mul_f32_e32 v2, 0x41800000, v2
	v_max_f32_e32 v2, 0xc3e00000, v2
	v_min_f32_e32 v2, 0x43e00000, v2
	s_nop 1
	v_mov_b32_dpp v3, v2 quad_perm:[1,0,3,2] row_mask:0xf bank_mask:0xf
	s_waitcnt lgkmcnt(0)
	v_cvt_pk_fp8_f32 v5, v2, v3
	v_add_u32_e32 v2, 17, v84
	v_ashrrev_i32_e32 v3, 31, v2
	v_lshlrev_b64 v[2:3], 9, v[2:3]
	s_nop 1
	v_mov_b32_dpp v6, v5 quad_perm:[2,3,0,1] row_mask:0xf bank_mask:0xf
	v_lshl_add_u64 v[2:3], v[82:83], 0, v[2:3]
	s_and_saveexec_b64 s[0:1], vcc
	s_cbranch_execz .LBB0_2034
	v_and_b32_e32 v5, 0xffff, v5
	s_waitcnt lgkmcnt(0)
	v_lshl_or_b32 v5, v6, 16, v5
	global_store_dword v[2:3], v5, off
.LBB0_2034:
	s_or_b64 exec, exec, s[0:1]
	v_mul_f32_e32 v5, v27, v4
	v_mul_f32_e32 v5, 0x41800000, v5
	v_max_f32_e32 v5, 0xc3e00000, v5
	s_waitcnt lgkmcnt(0)
	v_min_f32_e32 v6, 0x43e00000, v5
	s_nop 1
	v_mov_b32_dpp v7, v6 quad_perm:[1,0,3,2] row_mask:0xf bank_mask:0xf
	v_mov_b32_e32 v5, v147
	s_waitcnt lgkmcnt(0)
	v_cvt_pk_fp8_f32 v5, v6, v7
	s_nop 1
	v_mov_b32_dpp v6, v5 quad_perm:[2,3,0,1] row_mask:0xf bank_mask:0xf
	s_and_saveexec_b64 s[0:1], vcc
	s_cbranch_execz .LBB0_2036
	v_and_b32_e32 v5, 0xffff, v5
	s_waitcnt lgkmcnt(0)
	v_lshl_or_b32 v5, v6, 16, v5
	global_store_dword v[2:3], v5, off offset:32
.LBB0_2036:
	s_or_b64 exec, exec, s[0:1]
	v_mul_f32_e32 v5, v43, v4
	v_mul_f32_e32 v5, 0x41800000, v5
	v_max_f32_e32 v5, 0xc3e00000, v5
	s_waitcnt lgkmcnt(0)
	v_min_f32_e32 v6, 0x43e00000, v5
	s_nop 1
	v_mov_b32_dpp v7, v6 quad_perm:[1,0,3,2] row_mask:0xf bank_mask:0xf
	v_mov_b32_e32 v5, v147
	s_waitcnt lgkmcnt(0)
	v_cvt_pk_fp8_f32 v5, v6, v7
	s_nop 1
	v_mov_b32_dpp v6, v5 quad_perm:[2,3,0,1] row_mask:0xf bank_mask:0xf
	s_and_saveexec_b64 s[0:1], vcc
	s_cbranch_execz .LBB0_2038
	v_and_b32_e32 v5, 0xffff, v5
	s_waitcnt lgkmcnt(0)
	v_lshl_or_b32 v5, v6, 16, v5
	global_store_dword v[2:3], v5, off offset:64
.LBB0_2038:
	s_or_b64 exec, exec, s[0:1]
	v_mul_f32_e32 v4, v59, v4
	v_mul_f32_e32 v4, 0x41800000, v4
	v_max_f32_e32 v4, 0xc3e00000, v4
	v_min_f32_e32 v5, 0x43e00000, v4
	s_waitcnt lgkmcnt(0)
	s_nop 1
	v_mov_b32_dpp v6, v5 quad_perm:[1,0,3,2] row_mask:0xf bank_mask:0xf
	v_mov_b32_e32 v4, v147
	s_waitcnt lgkmcnt(0)
	v_cvt_pk_fp8_f32 v4, v5, v6
	s_nop 1
	v_mov_b32_dpp v5, v4 quad_perm:[2,3,0,1] row_mask:0xf bank_mask:0xf
	s_and_saveexec_b64 s[0:1], vcc
	s_cbranch_execz .LBB0_2040
	v_and_b32_e32 v4, 0xffff, v4
	s_waitcnt lgkmcnt(0)
	v_lshl_or_b32 v4, v5, 16, v4
	global_store_dword v[2:3], v4, off offset:96
.LBB0_2040:
	s_or_b64 exec, exec, s[0:1]
	v_rcp_f32_e32 v4, v72
	s_waitcnt lgkmcnt(0)
	v_mov_b32_e32 v5, v147
	v_mul_f32_e32 v2, v12, v4
	v_mul_f32_e32 v2, 0x41800000, v2
	v_max_f32_e32 v2, 0xc3e00000, v2
	v_min_f32_e32 v2, 0x43e00000, v2
	s_nop 1
	v_mov_b32_dpp v3, v2 quad_perm:[1,0,3,2] row_mask:0xf bank_mask:0xf
	s_waitcnt lgkmcnt(0)
	v_cvt_pk_fp8_f32 v5, v2, v3
	v_add_u32_e32 v2, 18, v84
	v_ashrrev_i32_e32 v3, 31, v2
	v_lshlrev_b64 v[2:3], 9, v[2:3]
	s_nop 1
	v_mov_b32_dpp v6, v5 quad_perm:[2,3,0,1] row_mask:0xf bank_mask:0xf
	v_lshl_add_u64 v[2:3], v[82:83], 0, v[2:3]
	s_and_saveexec_b64 s[0:1], vcc
	s_cbranch_execz .LBB0_2042
	v_and_b32_e32 v5, 0xffff, v5
	s_waitcnt lgkmcnt(0)
	v_lshl_or_b32 v5, v6, 16, v5
	global_store_dword v[2:3], v5, off
.LBB0_2042:
	s_or_b64 exec, exec, s[0:1]
	v_mul_f32_e32 v5, v28, v4
	v_mul_f32_e32 v5, 0x41800000, v5
	v_max_f32_e32 v5, 0xc3e00000, v5
	s_waitcnt lgkmcnt(0)
	v_min_f32_e32 v6, 0x43e00000, v5
	s_nop 1
	v_mov_b32_dpp v7, v6 quad_perm:[1,0,3,2] row_mask:0xf bank_mask:0xf
	v_mov_b32_e32 v5, v147
	s_waitcnt lgkmcnt(0)
	v_cvt_pk_fp8_f32 v5, v6, v7
	s_nop 1
	v_mov_b32_dpp v6, v5 quad_perm:[2,3,0,1] row_mask:0xf bank_mask:0xf
	s_and_saveexec_b64 s[0:1], vcc
	s_cbranch_execz .LBB0_2044
	v_and_b32_e32 v5, 0xffff, v5
	s_waitcnt lgkmcnt(0)
	v_lshl_or_b32 v5, v6, 16, v5
	global_store_dword v[2:3], v5, off offset:32
.LBB0_2044:
	s_or_b64 exec, exec, s[0:1]
	v_mul_f32_e32 v5, v44, v4
	v_mul_f32_e32 v5, 0x41800000, v5
	v_max_f32_e32 v5, 0xc3e00000, v5
	s_waitcnt lgkmcnt(0)
	v_min_f32_e32 v6, 0x43e00000, v5
	s_nop 1
	v_mov_b32_dpp v7, v6 quad_perm:[1,0,3,2] row_mask:0xf bank_mask:0xf
	v_mov_b32_e32 v5, v147
	s_waitcnt lgkmcnt(0)
	v_cvt_pk_fp8_f32 v5, v6, v7
	s_nop 1
	v_mov_b32_dpp v6, v5 quad_perm:[2,3,0,1] row_mask:0xf bank_mask:0xf
	s_and_saveexec_b64 s[0:1], vcc
	s_cbranch_execz .LBB0_2046
	v_and_b32_e32 v5, 0xffff, v5
	s_waitcnt lgkmcnt(0)
	v_lshl_or_b32 v5, v6, 16, v5
	global_store_dword v[2:3], v5, off offset:64
.LBB0_2046:
	s_or_b64 exec, exec, s[0:1]
	v_mul_f32_e32 v4, v60, v4
	v_mul_f32_e32 v4, 0x41800000, v4
	v_max_f32_e32 v4, 0xc3e00000, v4
	v_min_f32_e32 v5, 0x43e00000, v4
	s_waitcnt lgkmcnt(0)
	s_nop 1
	v_mov_b32_dpp v6, v5 quad_perm:[1,0,3,2] row_mask:0xf bank_mask:0xf
	v_mov_b32_e32 v4, v147
	s_waitcnt lgkmcnt(0)
	v_cvt_pk_fp8_f32 v4, v5, v6
	s_nop 1
	v_mov_b32_dpp v5, v4 quad_perm:[2,3,0,1] row_mask:0xf bank_mask:0xf
	s_and_saveexec_b64 s[0:1], vcc
	s_cbranch_execz .LBB0_2048
	v_and_b32_e32 v4, 0xffff, v4
	s_waitcnt lgkmcnt(0)
	v_lshl_or_b32 v4, v5, 16, v4
	global_store_dword v[2:3], v4, off offset:96
; __device__ __forceinline__ int crow(int r, int hi) { return (r & 3) + 8 * (r >> 2) + 4 * hi; }
; __device__ __forceinline__ void store_quad8(unsigned char* p, float v, int r32) {
;     v = fminf(fmaxf(v, -448.f), 448.f);
;     const float v1 = swz_xor<1>(v);
;     const int w = __builtin_amdgcn_cvt_pk_fp8_f32(v, v1, 0, false);
;     const int w2 = __builtin_amdgcn_ds_swizzle(w, (2 << 10) | 0x1f);
;     if ((r32 & 3) == 0) *(unsigned*)p = ((unsigned)w & 0xffffu) | ((unsigned)w2 << 16);
; }
;     __device__ __forceinline__ void operator()(f32x16 (&o)[4], const float (&rli)[16], int wid, int lane, int r32, int hi) const {
;         asm volatile("" : "+v"(lane), "+v"(r32), "+v"(hi));
;         unsigned char* base = out + (size_t)(wid * QBLK) * 512;
; #pragma unroll
;         for (int r = 0; r < 16; ++r)
; #pragma unroll
;             for (int d0 = 0; d0 < 4; ++d0) store_quad8(base + (size_t)crow(r, hi) * 512 + d0 * 32 + r32, o[d0][r] * rli[r] * 16.f, r32);
;     }
.LBB0_2048:
	s_or_b64 exec, exec, s[0:1]
	v_rcp_f32_e32 v4, v73
	s_waitcnt lgkmcnt(0)
	v_mov_b32_e32 v5, v147
	v_mul_f32_e32 v2, v13, v4
	v_mul_f32_e32 v2, 0x41800000, v2
	v_max_f32_e32 v2, 0xc3e00000, v2
	v_min_f32_e32 v2, 0x43e00000, v2
	s_nop 1
	v_mov_b32_dpp v3, v2 quad_perm:[1,0,3,2] row_mask:0xf bank_mask:0xf
	s_waitcnt lgkmcnt(0)
	v_cvt_pk_fp8_f32 v5, v2, v3
	v_add_u32_e32 v2, 19, v84
	v_ashrrev_i32_e32 v3, 31, v2
	v_lshlrev_b64 v[2:3], 9, v[2:3]
	s_nop 1
	v_mov_b32_dpp v6, v5 quad_perm:[2,3,0,1] row_mask:0xf bank_mask:0xf
	v_lshl_add_u64 v[2:3], v[82:83], 0, v[2:3]
	s_and_saveexec_b64 s[0:1], vcc
	s_cbranch_execz .LBB0_2050
	v_and_b32_e32 v5, 0xffff, v5
	s_waitcnt lgkmcnt(0)
	v_lshl_or_b32 v5, v6, 16, v5
	global_store_dword v[2:3], v5, off
.LBB0_2050:
	s_or_b64 exec, exec, s[0:1]
	v_mul_f32_e32 v5, v29, v4
	v_mul_f32_e32 v5, 0x41800000, v5
	v_max_f32_e32 v5, 0xc3e00000, v5
	s_waitcnt lgkmcnt(0)
	v_min_f32_e32 v6, 0x43e00000, v5
	s_nop 1
	v_mov_b32_dpp v7, v6 quad_perm:[1,0,3,2] row_mask:0xf bank_mask:0xf
	v_mov_b32_e32 v5, v147
	s_waitcnt lgkmcnt(0)
	v_cvt_pk_fp8_f32 v5, v6, v7
	s_nop 1
	v_mov_b32_dpp v6, v5 quad_perm:[2,3,0,1] row_mask:0xf bank_mask:0xf
	s_and_saveexec_b64 s[0:1], vcc
	s_cbranch_execz .LBB0_2052
	v_and_b32_e32 v5, 0xffff, v5
	s_waitcnt lgkmcnt(0)
	v_lshl_or_b32 v5, v6, 16, v5
	global_store_dword v[2:3], v5, off offset:32
.LBB0_2052:
	s_or_b64 exec, exec, s[0:1]
	v_mul_f32_e32 v5, v45, v4
	v_mul_f32_e32 v5, 0x41800000, v5
	v_max_f32_e32 v5, 0xc3e00000, v5
	s_waitcnt lgkmcnt(0)
	v_min_f32_e32 v6, 0x43e00000, v5
	s_nop 1
	v_mov_b32_dpp v7, v6 quad_perm:[1,0,3,2] row_mask:0xf bank_mask:0xf
	v_mov_b32_e32 v5, v147
	s_waitcnt lgkmcnt(0)
	v_cvt_pk_fp8_f32 v5, v6, v7
	s_nop 1
	v_mov_b32_dpp v6, v5 quad_perm:[2,3,0,1] row_mask:0xf bank_mask:0xf
	s_and_saveexec_b64 s[0:1], vcc
	s_cbranch_execz .LBB0_2054
	v_and_b32_e32 v5, 0xffff, v5
	s_waitcnt lgkmcnt(0)
	v_lshl_or_b32 v5, v6, 16, v5
	global_store_dword v[2:3], v5, off offset:64
.LBB0_2054:
	s_or_b64 exec, exec, s[0:1]
	v_mul_f32_e32 v4, v61, v4
	v_mul_f32_e32 v4, 0x41800000, v4
	v_max_f32_e32 v4, 0xc3e00000, v4
	v_min_f32_e32 v5, 0x43e00000, v4
	s_waitcnt lgkmcnt(0)
	s_nop 1
	v_mov_b32_dpp v6, v5 quad_perm:[1,0,3,2] row_mask:0xf bank_mask:0xf
	v_mov_b32_e32 v4, v147
	s_waitcnt lgkmcnt(0)
	v_cvt_pk_fp8_f32 v4, v5, v6
	s_nop 1
	v_mov_b32_dpp v5, v4 quad_perm:[2,3,0,1] row_mask:0xf bank_mask:0xf
	s_and_saveexec_b64 s[0:1], vcc
	s_cbranch_execz .LBB0_2056
	v_and_b32_e32 v4, 0xffff, v4
	s_waitcnt lgkmcnt(0)
	v_lshl_or_b32 v4, v5, 16, v4
	global_store_dword v[2:3], v4, off offset:96
.LBB0_2056:
	s_or_b64 exec, exec, s[0:1]
	v_rcp_f32_e32 v4, v66
	s_waitcnt lgkmcnt(0)
	v_mov_b32_e32 v5, v147
	v_mul_f32_e32 v2, v14, v4
	v_mul_f32_e32 v2, 0x41800000, v2
	v_max_f32_e32 v2, 0xc3e00000, v2
	v_min_f32_e32 v2, 0x43e00000, v2
	s_nop 1
	v_mov_b32_dpp v3, v2 quad_perm:[1,0,3,2] row_mask:0xf bank_mask:0xf
	s_waitcnt lgkmcnt(0)
	v_cvt_pk_fp8_f32 v5, v2, v3
	v_add_u32_e32 v2, 24, v84
	v_ashrrev_i32_e32 v3, 31, v2
	v_lshlrev_b64 v[2:3], 9, v[2:3]
	s_nop 1
	v_mov_b32_dpp v6, v5 quad_perm:[2,3,0,1] row_mask:0xf bank_mask:0xf
	v_lshl_add_u64 v[2:3], v[82:83], 0, v[2:3]
	s_and_saveexec_b64 s[0:1], vcc
	s_cbranch_execz .LBB0_2058
	v_and_b32_e32 v5, 0xffff, v5
	s_waitcnt lgkmcnt(0)
	v_lshl_or_b32 v5, v6, 16, v5
	global_store_dword v[2:3], v5, off
.LBB0_2058:
	s_or_b64 exec, exec, s[0:1]
	v_mul_f32_e32 v5, v30, v4
	v_mul_f32_e32 v5, 0x41800000, v5
	v_max_f32_e32 v5, 0xc3e00000, v5
	s_waitcnt lgkmcnt(0)
	v_min_f32_e32 v6, 0x43e00000, v5
	s_nop 1
	v_mov_b32_dpp v7, v6 quad_perm:[1,0,3,2] row_mask:0xf bank_mask:0xf
	v_mov_b32_e32 v5, v147
	s_waitcnt lgkmcnt(0)
	v_cvt_pk_fp8_f32 v5, v6, v7
	s_nop 1
	v_mov_b32_dpp v6, v5 quad_perm:[2,3,0,1] row_mask:0xf bank_mask:0xf
	s_and_saveexec_b64 s[0:1], vcc
	s_cbranch_execz .LBB0_2060
	v_and_b32_e32 v5, 0xffff, v5
	s_waitcnt lgkmcnt(0)
	v_lshl_or_b32 v5, v6, 16, v5
	global_store_dword v[2:3], v5, off offset:32
.LBB0_2060:
	s_or_b64 exec, exec, s[0:1]
	v_mul_f32_e32 v5, v46, v4
	v_mul_f32_e32 v5, 0x41800000, v5
	v_max_f32_e32 v5, 0xc3e00000, v5
	s_waitcnt lgkmcnt(0)
	v_min_f32_e32 v6, 0x43e00000, v5
	s_nop 1
	v_mov_b32_dpp v7, v6 quad_perm:[1,0,3,2] row_mask:0xf bank_mask:0xf
	v_mov_b32_e32 v5, v147
	s_waitcnt lgkmcnt(0)
	v_cvt_pk_fp8_f32 v5, v6, v7
	s_nop 1
	v_mov_b32_dpp v6, v5 quad_perm:[2,3,0,1] row_mask:0xf bank_mask:0xf
	s_and_saveexec_b64 s[0:1], vcc
	s_cbranch_execz .LBB0_2062
	v_and_b32_e32 v5, 0xffff, v5
	s_waitcnt lgkmcnt(0)
	v_lshl_or_b32 v5, v6, 16, v5
	global_store_dword v[2:3], v5, off offset:64
.LBB0_2062:
	s_or_b64 exec, exec, s[0:1]
	v_mul_f32_e32 v4, v62, v4
	v_mul_f32_e32 v4, 0x41800000, v4
	v_max_f32_e32 v4, 0xc3e00000, v4
	v_min_f32_e32 v5, 0x43e00000, v4
	s_waitcnt lgkmcnt(0)
	s_nop 1
	v_mov_b32_dpp v6, v5 quad_perm:[1,0,3,2] row_mask:0xf bank_mask:0xf
	v_mov_b32_e32 v4, v147
	s_waitcnt lgkmcnt(0)
	v_cvt_pk_fp8_f32 v4, v5, v6
	s_nop 1
	v_mov_b32_dpp v5, v4 quad_perm:[2,3,0,1] row_mask:0xf bank_mask:0xf
	s_and_saveexec_b64 s[0:1], vcc
	s_cbranch_execz .LBB0_2064
	v_and_b32_e32 v4, 0xffff, v4
	s_waitcnt lgkmcnt(0)
	v_lshl_or_b32 v4, v5, 16, v4
	global_store_dword v[2:3], v4, off offset:96
.LBB0_2064:
	s_or_b64 exec, exec, s[0:1]
	v_rcp_f32_e32 v4, v67
	s_waitcnt lgkmcnt(0)
	v_mov_b32_e32 v5, v147
	v_mul_f32_e32 v2, v15, v4
	v_mul_f32_e32 v2, 0x41800000, v2
	v_max_f32_e32 v2, 0xc3e00000, v2
	v_min_f32_e32 v2, 0x43e00000, v2
	s_nop 1
	v_mov_b32_dpp v3, v2 quad_perm:[1,0,3,2] row_mask:0xf bank_mask:0xf
	s_waitcnt lgkmcnt(0)
	v_cvt_pk_fp8_f32 v5, v2, v3
	v_add_u32_e32 v2, 25, v84
	v_ashrrev_i32_e32 v3, 31, v2
	v_lshlrev_b64 v[2:3], 9, v[2:3]
	s_nop 1
	v_mov_b32_dpp v6, v5 quad_perm:[2,3,0,1] row_mask:0xf bank_mask:0xf
	v_lshl_add_u64 v[2:3], v[82:83], 0, v[2:3]
	s_and_saveexec_b64 s[0:1], vcc
	s_cbranch_execz .LBB0_2066
	v_and_b32_e32 v5, 0xffff, v5
	s_waitcnt lgkmcnt(0)
	v_lshl_or_b32 v5, v6, 16, v5
	global_store_dword v[2:3], v5, off
; __device__ __forceinline__ int crow(int r, int hi) { return (r & 3) + 8 * (r >> 2) + 4 * hi; }
; __device__ __forceinline__ void store_quad8(unsigned char* p, float v, int r32) {
;     v = fminf(fmaxf(v, -448.f), 448.f);
;     const float v1 = swz_xor<1>(v);
;     const int w = __builtin_amdgcn_cvt_pk_fp8_f32(v, v1, 0, false);
;     const int w2 = __builtin_amdgcn_ds_swizzle(w, (2 << 10) | 0x1f);
;     if ((r32 & 3) == 0) *(unsigned*)p = ((unsigned)w & 0xffffu) | ((unsigned)w2 << 16);
; }
;     __device__ __forceinline__ void operator()(f32x16 (&o)[4], const float (&rli)[16], int wid, int lane, int r32, int hi) const {
;         asm volatile("" : "+v"(lane), "+v"(r32), "+v"(hi));
;         unsigned char* base = out + (size_t)(wid * QBLK) * 512;
; #pragma unroll
;         for (int r = 0; r < 16; ++r)
; #pragma unroll
;             for (int d0 = 0; d0 < 4; ++d0) store_quad8(base + (size_t)crow(r, hi) * 512 + d0 * 32 + r32, o[d0][r] * rli[r] * 16.f, r32);
;     }
.LBB0_2066:
	s_or_b64 exec, exec, s[0:1]
	v_mul_f32_e32 v5, v31, v4
	v_mul_f32_e32 v5, 0x41800000, v5
	v_max_f32_e32 v5, 0xc3e00000, v5
	s_waitcnt lgkmcnt(0)
	v_min_f32_e32 v6, 0x43e00000, v5
	s_nop 1
	v_mov_b32_dpp v7, v6 quad_perm:[1,0,3,2] row_mask:0xf bank_mask:0xf
	v_mov_b32_e32 v5, v147
	s_waitcnt lgkmcnt(0)
	v_cvt_pk_fp8_f32 v5, v6, v7
	s_nop 1
	v_mov_b32_dpp v6, v5 quad_perm:[2,3,0,1] row_mask:0xf bank_mask:0xf
	s_and_saveexec_b64 s[0:1], vcc
	s_cbranch_execz .LBB0_2068
	v_and_b32_e32 v5, 0xffff, v5
	s_waitcnt lgkmcnt(0)
	v_lshl_or_b32 v5, v6, 16, v5
	global_store_dword v[2:3], v5, off offset:32
.LBB0_2068:
	s_or_b64 exec, exec, s[0:1]
	v_mul_f32_e32 v5, v47, v4
	v_mul_f32_e32 v5, 0x41800000, v5
	v_max_f32_e32 v5, 0xc3e00000, v5
	s_waitcnt lgkmcnt(0)
	v_min_f32_e32 v6, 0x43e00000, v5
	s_nop 1
	v_mov_b32_dpp v7, v6 quad_perm:[1,0,3,2] row_mask:0xf bank_mask:0xf
	v_mov_b32_e32 v5, v147
	s_waitcnt lgkmcnt(0)
	v_cvt_pk_fp8_f32 v5, v6, v7
	s_nop 1
	v_mov_b32_dpp v6, v5 quad_perm:[2,3,0,1] row_mask:0xf bank_mask:0xf
	s_and_saveexec_b64 s[0:1], vcc
	s_cbranch_execz .LBB0_2070
	v_and_b32_e32 v5, 0xffff, v5
	s_waitcnt lgkmcnt(0)
	v_lshl_or_b32 v5, v6, 16, v5
	global_store_dword v[2:3], v5, off offset:64
.LBB0_2070:
	s_or_b64 exec, exec, s[0:1]
	v_mul_f32_e32 v4, v63, v4
	v_mul_f32_e32 v4, 0x41800000, v4
	v_max_f32_e32 v4, 0xc3e00000, v4
	v_min_f32_e32 v5, 0x43e00000, v4
	s_waitcnt lgkmcnt(0)
	s_nop 1
	v_mov_b32_dpp v6, v5 quad_perm:[1,0,3,2] row_mask:0xf bank_mask:0xf
	v_mov_b32_e32 v4, v147
	s_waitcnt lgkmcnt(0)
	v_cvt_pk_fp8_f32 v4, v5, v6
	s_nop 1
	v_mov_b32_dpp v5, v4 quad_perm:[2,3,0,1] row_mask:0xf bank_mask:0xf
	s_and_saveexec_b64 s[0:1], vcc
	s_cbranch_execz .LBB0_2072
	v_and_b32_e32 v4, 0xffff, v4
	s_waitcnt lgkmcnt(0)
	v_lshl_or_b32 v4, v5, 16, v4
	global_store_dword v[2:3], v4, off offset:96
.LBB0_2072:
	s_or_b64 exec, exec, s[0:1]
	v_rcp_f32_e32 v4, v68
	s_waitcnt lgkmcnt(0)
	v_mov_b32_e32 v5, v147
	v_mul_f32_e32 v2, v16, v4
	v_mul_f32_e32 v2, 0x41800000, v2
	v_max_f32_e32 v2, 0xc3e00000, v2
	v_min_f32_e32 v2, 0x43e00000, v2
	s_nop 1
	v_mov_b32_dpp v3, v2 quad_perm:[1,0,3,2] row_mask:0xf bank_mask:0xf
	s_waitcnt lgkmcnt(0)
	v_cvt_pk_fp8_f32 v5, v2, v3
	v_add_u32_e32 v2, 26, v84
	v_ashrrev_i32_e32 v3, 31, v2
	v_lshlrev_b64 v[2:3], 9, v[2:3]
	s_nop 1
	v_mov_b32_dpp v6, v5 quad_perm:[2,3,0,1] row_mask:0xf bank_mask:0xf
	v_lshl_add_u64 v[2:3], v[82:83], 0, v[2:3]
	s_and_saveexec_b64 s[0:1], vcc
	s_cbranch_execz .LBB0_2074
	v_and_b32_e32 v5, 0xffff, v5
	s_waitcnt lgkmcnt(0)
	v_lshl_or_b32 v5, v6, 16, v5
	global_store_dword v[2:3], v5, off
.LBB0_2074:
	s_or_b64 exec, exec, s[0:1]
	v_mul_f32_e32 v5, v32, v4
	v_mul_f32_e32 v5, 0x41800000, v5
	v_max_f32_e32 v5, 0xc3e00000, v5
	s_waitcnt lgkmcnt(0)
	v_min_f32_e32 v6, 0x43e00000, v5
	s_nop 1
	v_mov_b32_dpp v7, v6 quad_perm:[1,0,3,2] row_mask:0xf bank_mask:0xf
	v_mov_b32_e32 v5, v147
	s_waitcnt lgkmcnt(0)
	v_cvt_pk_fp8_f32 v5, v6, v7
	s_nop 1
	v_mov_b32_dpp v6, v5 quad_perm:[2,3,0,1] row_mask:0xf bank_mask:0xf
	s_and_saveexec_b64 s[0:1], vcc
	s_cbranch_execz .LBB0_2076
	v_and_b32_e32 v5, 0xffff, v5
	s_waitcnt lgkmcnt(0)
	v_lshl_or_b32 v5, v6, 16, v5
	global_store_dword v[2:3], v5, off offset:32
.LBB0_2076:
	s_or_b64 exec, exec, s[0:1]
	v_mul_f32_e32 v5, v48, v4
	v_mul_f32_e32 v5, 0x41800000, v5
	v_max_f32_e32 v5, 0xc3e00000, v5
	s_waitcnt lgkmcnt(0)
	v_min_f32_e32 v6, 0x43e00000, v5
	s_nop 1
	v_mov_b32_dpp v7, v6 quad_perm:[1,0,3,2] row_mask:0xf bank_mask:0xf
	v_mov_b32_e32 v5, v147
	s_waitcnt lgkmcnt(0)
	v_cvt_pk_fp8_f32 v5, v6, v7
	s_nop 1
	v_mov_b32_dpp v6, v5 quad_perm:[2,3,0,1] row_mask:0xf bank_mask:0xf
	s_and_saveexec_b64 s[0:1], vcc
	s_cbranch_execz .LBB0_2078
	v_and_b32_e32 v5, 0xffff, v5
	s_waitcnt lgkmcnt(0)
	v_lshl_or_b32 v5, v6, 16, v5
	global_store_dword v[2:3], v5, off offset:64
.LBB0_2078:
	s_or_b64 exec, exec, s[0:1]
	v_mul_f32_e32 v4, v64, v4
	v_mul_f32_e32 v4, 0x41800000, v4
	v_max_f32_e32 v4, 0xc3e00000, v4
	v_min_f32_e32 v5, 0x43e00000, v4
	s_waitcnt lgkmcnt(0)
	s_nop 1
	v_mov_b32_dpp v6, v5 quad_perm:[1,0,3,2] row_mask:0xf bank_mask:0xf
	v_mov_b32_e32 v4, v147
	s_waitcnt lgkmcnt(0)
	v_cvt_pk_fp8_f32 v4, v5, v6
	s_nop 1
	v_mov_b32_dpp v5, v4 quad_perm:[2,3,0,1] row_mask:0xf bank_mask:0xf
	s_and_saveexec_b64 s[0:1], vcc
	s_cbranch_execz .LBB0_2080
	v_and_b32_e32 v4, 0xffff, v4
	s_waitcnt lgkmcnt(0)
	v_lshl_or_b32 v4, v5, 16, v4
	global_store_dword v[2:3], v4, off offset:96
; __device__ __forceinline__ int crow(int r, int hi) { return (r & 3) + 8 * (r >> 2) + 4 * hi; }
;     __device__ __forceinline__ void operator()(f32x16 (&o)[4], const float (&rli)[16], int wid, int lane, int r32, int hi) const {
;         asm volatile("" : "+v"(lane), "+v"(r32), "+v"(hi));
;         unsigned char* base = out + (size_t)(wid * QBLK) * 512;
; #pragma unroll
;         for (int r = 0; r < 16; ++r)
; #pragma unroll
;             for (int d0 = 0; d0 < 4; ++d0) store_quad8(base + (size_t)crow(r, hi) * 512 + d0 * 32 + r32, o[d0][r] * rli[r] * 16.f, r32);
;     }
; __device__ __forceinline__ void xcd_barrier(const XcdBarrier& b) {
;     asm volatile("s_waitcnt vmcnt(0)" ::: "memory");
;     __syncthreads();
;     if (threadIdx.x == 0) {
;         unsigned* bar = b.bar;
;         __builtin_amdgcn_s_waitcnt(0);
;         unsigned nloc = b.st[0], nx = b.st[1];
;         if (nloc == 0u) { xcd_barrier_complete(bar, b.x, nloc, nx); b.st[0] = nloc; b.st[1] = nx; }
.LBB0_2080:
	s_or_b64 exec, exec, s[0:1]
	v_rcp_f32_e32 v4, v69
	s_waitcnt lgkmcnt(0)
	v_mov_b32_e32 v5, v147
	v_mul_f32_e32 v2, v17, v4
	v_mul_f32_e32 v2, 0x41800000, v2
	v_max_f32_e32 v2, 0xc3e00000, v2
	v_min_f32_e32 v2, 0x43e00000, v2
	s_nop 1
	v_mov_b32_dpp v3, v2 quad_perm:[1,0,3,2] row_mask:0xf bank_mask:0xf
	s_waitcnt lgkmcnt(0)
	v_cvt_pk_fp8_f32 v5, v2, v3
	v_add_u32_e32 v2, 27, v84
	v_ashrrev_i32_e32 v3, 31, v2
	v_lshlrev_b64 v[2:3], 9, v[2:3]
	s_nop 1
	v_mov_b32_dpp v6, v5 quad_perm:[2,3,0,1] row_mask:0xf bank_mask:0xf
	v_lshl_add_u64 v[2:3], v[82:83], 0, v[2:3]
	s_and_saveexec_b64 s[0:1], vcc
	s_cbranch_execz .LBB0_2082
	v_and_b32_e32 v5, 0xffff, v5
	s_waitcnt lgkmcnt(0)
	v_lshl_or_b32 v5, v6, 16, v5
	global_store_dword v[2:3], v5, off
.LBB0_2082:
	s_or_b64 exec, exec, s[0:1]
	v_mul_f32_e32 v5, v33, v4
	v_mul_f32_e32 v5, 0x41800000, v5
	v_max_f32_e32 v5, 0xc3e00000, v5
	s_waitcnt lgkmcnt(0)
	v_min_f32_e32 v6, 0x43e00000, v5
	s_nop 1
	v_mov_b32_dpp v7, v6 quad_perm:[1,0,3,2] row_mask:0xf bank_mask:0xf
	v_mov_b32_e32 v5, v147
	s_waitcnt lgkmcnt(0)
	v_cvt_pk_fp8_f32 v5, v6, v7
	s_nop 1
	v_mov_b32_dpp v6, v5 quad_perm:[2,3,0,1] row_mask:0xf bank_mask:0xf
	s_and_saveexec_b64 s[0:1], vcc
	s_cbranch_execz .LBB0_2084
	v_and_b32_e32 v5, 0xffff, v5
	s_waitcnt lgkmcnt(0)
	v_lshl_or_b32 v5, v6, 16, v5
	global_store_dword v[2:3], v5, off offset:32
.LBB0_2084:
	s_or_b64 exec, exec, s[0:1]
	v_mul_f32_e32 v5, v49, v4
	v_mul_f32_e32 v5, 0x41800000, v5
	v_max_f32_e32 v5, 0xc3e00000, v5
	s_waitcnt lgkmcnt(0)
	v_min_f32_e32 v6, 0x43e00000, v5
	s_nop 1
	v_mov_b32_dpp v7, v6 quad_perm:[1,0,3,2] row_mask:0xf bank_mask:0xf
	v_mov_b32_e32 v5, v147
	s_waitcnt lgkmcnt(0)
	v_cvt_pk_fp8_f32 v5, v6, v7
	s_nop 1
	v_mov_b32_dpp v6, v5 quad_perm:[2,3,0,1] row_mask:0xf bank_mask:0xf
	s_and_saveexec_b64 s[0:1], vcc
	s_cbranch_execz .LBB0_2086
	v_and_b32_e32 v5, 0xffff, v5
	s_waitcnt lgkmcnt(0)
	v_lshl_or_b32 v5, v6, 16, v5
	global_store_dword v[2:3], v5, off offset:64
.LBB0_2086:
	s_or_b64 exec, exec, s[0:1]
	v_mul_f32_e32 v4, v65, v4
	v_mul_f32_e32 v4, 0x41800000, v4
	v_max_f32_e32 v4, 0xc3e00000, v4
	v_min_f32_e32 v5, 0x43e00000, v4
	s_waitcnt lgkmcnt(0)
	s_nop 1
	v_mov_b32_dpp v6, v5 quad_perm:[1,0,3,2] row_mask:0xf bank_mask:0xf
	v_mov_b32_e32 v4, v147
	s_waitcnt lgkmcnt(0)
	v_cvt_pk_fp8_f32 v4, v5, v6
	s_nop 1
	v_mov_b32_dpp v5, v4 quad_perm:[2,3,0,1] row_mask:0xf bank_mask:0xf
	s_and_saveexec_b64 s[0:1], vcc
	s_cbranch_execz .LBB0_1937
	v_and_b32_e32 v4, 0xffff, v4
	s_waitcnt lgkmcnt(0)
	v_lshl_or_b32 v4, v5, 16, v4
	global_store_dword v[2:3], v4, off offset:96
	s_branch .LBB0_1937
.LBB0_2088:
	s_cmp_gt_i32 s81, 7
	s_cbranch_scc0 .LBB0_2138
	s_waitcnt vmcnt(0)
	v_cmp_eq_u32_e32 vcc, 0, v0
	s_waitcnt vmcnt(0) lgkmcnt(0)
	s_barrier
	s_and_saveexec_b64 s[0:1], vcc
	s_cbranch_execz .LBB0_2137
	v_readlane_b32 s2, v253, 29
	s_waitcnt vmcnt(0) expcnt(0) lgkmcnt(0)
	s_nop 0
	v_mov_b32_e32 v1, s2
	ds_read_b32 v3, v1
	ds_read_b32 v1, v1 offset:4
	s_waitcnt lgkmcnt(0)
	v_cmp_ne_u32_e32 vcc, 0, v3
	s_cbranch_vccnz .LBB0_2105
	v_readlane_b32 s2, v253, 8
	v_readlane_b32 s3, v253, 9
	s_load_dwordx2 s[6:7], s[2:3], 0x4
	s_add_u32 s2, s78, 0x4200
	s_addc_u32 s3, s79, 0
	s_add_u32 s4, s78, 0x4400
	s_addc_u32 s5, s79, 0
	s_waitcnt lgkmcnt(0)
	s_mul_i32 s44, s6, s75
	s_add_u32 s6, s78, 0x4500
	s_mul_i32 s44, s44, s7
	s_addc_u32 s7, s79, 0
	s_add_u32 s8, s78, 0x4600
	s_addc_u32 s9, s79, 0
	s_add_u32 s10, s78, 0x4700
	s_addc_u32 s11, s79, 0
	s_add_u32 s12, s78, 0x4800
	s_addc_u32 s13, s79, 0
	s_add_u32 s14, s78, 0x4900
	s_addc_u32 s15, s79, 0
	s_add_u32 s16, s78, 0x4a00
	s_addc_u32 s17, s79, 0
	s_add_u32 s18, s78, 0x4b00
	s_addc_u32 s19, s79, 0
	s_add_u32 s20, s78, 0x4c00
	s_addc_u32 s21, s79, 0
	s_add_u32 s22, s78, 0x4d00
	s_addc_u32 s23, s79, 0
	s_add_u32 s24, s78, 0x4e00
	s_addc_u32 s25, s79, 0
	s_add_u32 s26, s78, 0x4f00
	s_addc_u32 s27, s79, 0
	s_add_u32 s28, s78, 0x5000
	s_addc_u32 s29, s79, 0
	s_add_u32 s30, s78, 0x5100
	s_addc_u32 s31, s79, 0
	s_add_u32 s34, s78, 0x5200
	s_addc_u32 s35, s79, 0
	s_add_u32 s36, s78, 0x5300
	s_addc_u32 s37, s79, 0
	s_mov_b32 s45, 1
	v_mov_b32_e32 v17, 0
	s_branch .LBB0_2093
